# LDS-DMA issue blocks: dropped the m0 save/restore and inter-block pads (3 instrs per DMA instead of 6)
# speedup vs baseline: 1.0012x; 1.0002x over previous
;     __device__ __forceinline__ const char* a_base(const Unit& u) const { return (const char*)A + (size_t)u.pm * BM * lda * 2; }
;     __device__ __forceinline__ const char* b_base(const Unit& u) const { return (const char*)Bt + (size_t)u.pn * BM * K * 2; }
;     __device__ __forceinline__ const char* b_base(const Unit& u) const { return (const char*)Bt + ((size_t)u.e * NB + (size_t)u.pn * BM) * K * 2; }
; #define PG8_RC() int R[2], C[2]; { int t_ = threadIdx.x; asm volatile("" : "+v"(t_)); _Pragma("unroll") for (int i = 0; i < 2; ++i) stage_rc(t_ * 16 + i * 8192, R[i], C[i]); }
;     ...
;     { int R[2], C[2];
; #pragma unroll
;       for (int i = 0; i < 2; ++i) { stage_rc(tid * 16 + i * 8192, R[i], C[i]); voffB[i] = (unsigned)(R[i] * K + C[i]) * 2u; } }
;     ...
;     const size_t kstep = (size_t)(BK * 2);
;     const size_t hstepB = (size_t)HALF * K * 2;
;     const unsigned ldsbase = (unsigned)__builtin_amdgcn_readfirstlane((int)((unsigned)(size_t)lds + (unsigned)wid * 1024u));
;     const int aoff = lds_byte(wr * 64 + fr, fq * 8), boff = lds_byte(wc * 32 + fr, fq * 8);
;     ...
;     constexpr int EST = HM ? Epi::kStoresHM : Epi::kStores;
;     ...
;     Unit cur, nxt; int ui = 0;
;     if (!S.next(0, cur)) return;
;     unsigned voffA[2][2];
;     { PG8_RC(); S.a_offs(cur, R, C, voffA); }
;     f32x4 acc[2][2][4][2];
; #pragma unroll
;     for (int a = 0; a < 2; ++a)
; #pragma unroll
;         for (int b = 0; b < 2; ++b)
; #pragma unroll
;             for (int m = 0; m < 4; ++m)
; #pragma unroll
;                 for (int n = 0; n < 2; ++n) acc[a][b][m][n] = (f32x4){0.f, 0.f, 0.f, 0.f};
;     bf16x8 At[4][2], B0[2][2], B1[2][2];
;     const char* cA = S.a_base(cur); const char* cB = S.b_base(cur);
;     const unsigned bias_lds = (unsigned)__builtin_amdgcn_readfirstlane((int)((unsigned)(size_t)lds + (unsigned)(AUX_OFF + 8192) + (unsigned)wid * 256u));
;     if constexpr (Epi::kBiasDMA) { if (lane < 16) glds16(E.bias_base(cur), E.bias_off(cur, wc, lane), bias_lds); }
;     const unsigned rowid_lds = (unsigned)__builtin_amdgcn_readfirstlane((int)((unsigned)(size_t)lds + (unsigned)AUX_OFF + (unsigned)wid * 512u));
;     if constexpr (Epi::kRowDMA) { if (lane < 32) glds16(E.row_base(cur), E.row_off(cur, wr, lane), rowid_lds); }
;     PG8_STAGEB(PG8_SB(0, 0), cB); PG8_STAGEB(PG8_SB(0, 1), cB + hstepB); PG8_STAGEA(PG8_SA(0, 0), cA, 0); if constexpr (!HM) PG8_STAGEA(PG8_SA(0, 1), cA, 1);
.LBB0_129:
	s_andn2_b64 vcc, exec, s[0:1]
	s_cbranch_vccnz .LBB0_282
	v_bfe_i32 v4, v2, 27, 1
	v_lshlrev_b32_e32 v3, 4, v2
	v_lshrrev_b32_e32 v4, 22, v4
	v_add_u32_e32 v4, v3, v4
	v_and_b32_e32 v4, 0xfffffc00, v4
	v_sub_u32_e32 v4, v3, v4
	v_lshrrev_b32_e32 v5, 4, v4
	v_ashrrev_i32_e32 v1, 31, v2
	v_bitop3_b32 v4, v5, v4, 32 bitop3:0x6c
	v_lshrrev_b32_e32 v1, 26, v1
	s_waitcnt vmcnt(1)
	v_ashrrev_i32_e32 v6, 31, v4
	v_add_u32_e32 v1, v2, v1
	v_lshrrev_b32_e32 v6, 26, v6
	v_ashrrev_i32_e32 v1, 6, v1
	v_add_u32_e32 v6, v4, v6
	v_lshlrev_b32_e32 v5, 3, v1
	v_lshrrev_b32_e32 v7, 6, v6
	v_and_b32_e32 v6, 0xc0, v6
	v_and_b32_e32 v5, 0xffff0, v5
	v_lshlrev_b32_e32 v1, 5, v1
	v_sub_u32_e32 v4, v4, v6
	v_mov_b32_e32 v6, 1
	v_add_u32_e32 v5, v7, v5
	v_and_b32_e32 v1, 32, v1
	v_ashrrev_i16_sdwa v4, v6, sext(v4) dst_sel:DWORD dst_unused:UNUSED_PAD src0_sel:DWORD src1_sel:BYTE_0
	v_bfe_i32 v4, v4, 0, 16
	v_lshl_or_b32 v1, v5, 11, v1
	v_add_u32_e32 v3, 0x2000, v3
	v_add_lshl_u32 v1, v1, v4, 1
	v_ashrrev_i32_e32 v4, 31, v3
	v_lshrrev_b32_e32 v4, 22, v4
	v_add_u32_e32 v4, v3, v4
	v_ashrrev_i32_e32 v4, 10, v4
	v_mul_i32_i24_e32 v5, 0x400, v4
	v_sub_u32_e32 v3, v3, v5
	v_lshrrev_b32_e32 v5, 4, v3
	v_bitop3_b32 v3, v5, v3, 32 bitop3:0x6c
	v_ashrrev_i32_e32 v7, 31, v3
	v_lshrrev_b32_e32 v7, 26, v7
	v_add_u32_e32 v7, v3, v7
	v_lshlrev_b32_e32 v5, 3, v4
	v_lshrrev_b32_e32 v8, 6, v7
	v_and_b32_e32 v7, 0xc0, v7
	v_and_b32_e32 v5, 0xffff0, v5
	v_lshlrev_b32_e32 v4, 5, v4
	v_sub_u32_e32 v3, v3, v7
	v_add_u32_e32 v5, v8, v5
	v_and_b32_e32 v4, 32, v4
	v_ashrrev_i16_sdwa v3, v6, sext(v3) dst_sel:DWORD dst_unused:UNUSED_PAD src0_sel:DWORD src1_sel:BYTE_0
	v_bfe_i32 v3, v3, 0, 16
	v_lshl_or_b32 v4, v5, 11, v4
	v_add_lshl_u32 v156, v4, v3, 1
	v_mov_b32_e32 v3, v0
	s_lshl_b32 s1, s6, 10
	v_ashrrev_i32_e32 v5, 31, v3
	v_lshrrev_b32_e32 v5, 26, v5
	v_lshlrev_b32_e32 v4, 4, v3
	v_add_u32_e32 v5, v3, v5
	v_bfe_i32 v3, v3, 27, 1
	v_lshrrev_b32_e32 v3, 22, v3
	v_add_u32_e32 v3, v4, v3
	v_and_b32_e32 v3, 0xfffffc00, v3
	v_sub_u32_e32 v3, v4, v3
	v_lshrrev_b32_e32 v7, 4, v3
	v_bitop3_b32 v3, v7, v3, 32 bitop3:0x6c
	v_ashrrev_i32_e32 v8, 31, v3
	v_lshrrev_b32_e32 v8, 26, v8
	v_add_u32_e32 v8, v3, v8
	v_ashrrev_i32_e32 v5, 6, v5
	v_ashrrev_i32_e32 v9, 6, v8
	v_and_b32_e32 v8, 0xc0, v8
	v_lshlrev_b32_e32 v7, 3, v5
	v_lshlrev_b32_e32 v5, 5, v5
	v_sub_u32_e32 v3, v3, v8
	v_and_b32_e32 v5, 32, v5
	v_ashrrev_i16_sdwa v3, v6, sext(v3) dst_sel:DWORD dst_unused:UNUSED_PAD src0_sel:DWORD src1_sel:BYTE_0
	v_add_u32_e32 v4, 0x2000, v4
	v_add_u32_sdwa v3, v5, sext(v3) dst_sel:DWORD dst_unused:UNUSED_PAD src0_sel:DWORD src1_sel:WORD_0
	v_ashrrev_i32_e32 v5, 31, v4
	s_ashr_i32 s0, s4, 8
	s_add_i32 s29, s1, 0
	v_lshrrev_b32_e32 v5, 22, v5
	s_add_u32 s31, s94, 0x34600000
	v_add_u32_e32 v5, v4, v5
	s_addc_u32 s35, s95, 0
	v_ashrrev_i32_e32 v5, 10, v5
	s_add_u32 s37, s94, 0x200000
	v_mul_i32_i24_e32 v8, 0x400, v5
	s_addc_u32 s39, s95, 0
	v_sub_u32_e32 v4, v4, v8
	s_ashr_i32 s11, s10, 31
	v_lshrrev_b32_e32 v8, 4, v4
	s_lshl_b64 s[8:9], s[10:11], 20
	v_and_b32_e32 v7, -16, v7
	v_bitop3_b32 v4, v8, v4, 32 bitop3:0x6c
	s_add_u32 s12, s31, s8
	v_add_u32_e32 v7, v9, v7
	v_ashrrev_i32_e32 v9, 31, v4
	s_addc_u32 s13, s35, s9
	s_ashr_i32 s53, s52, 31
	v_lshrrev_b32_e32 v9, 26, v9
	s_lshl_b64 s[8:9], s[52:53], 20
	v_add_u32_e32 v9, v4, v9
	s_add_u32 s54, s37, s8
	v_ashrrev_i32_e32 v10, 6, v9
	v_and_b32_e32 v9, 0xc0, v9
	s_addc_u32 s55, s39, s9
	s_add_i32 s41, s29, 0x10000
	s_mov_b32 m0, s41
	s_nop 0
	global_load_lds_dwordx4 v1, s[54:55]
	s_add_i32 s43, s29, 0x12000
	v_lshlrev_b32_e32 v8, 3, v5
	v_lshlrev_b32_e32 v5, 5, v5
	v_sub_u32_e32 v4, v4, v9
	s_mov_b32 m0, s43
	s_nop 0
	global_load_lds_dwordx4 v156, s[54:55]
	s_add_u32 s8, s54, 0x80000
	v_and_b32_e32 v8, -16, v8
	v_and_b32_e32 v5, 32, v5
	v_ashrrev_i16_sdwa v4, v6, sext(v4) dst_sel:DWORD dst_unused:UNUSED_PAD src0_sel:DWORD src1_sel:BYTE_0
	s_addc_u32 s9, s55, 0
	s_add_i32 s53, s29, 0x14000
	s_mov_b32 m0, s53
	s_nop 0
	global_load_lds_dwordx4 v1, s[8:9]
	v_add_u32_e32 v8, v10, v8
	v_add_u32_sdwa v4, v5, sext(v4) dst_sel:DWORD dst_unused:UNUSED_PAD src0_sel:DWORD src1_sel:WORD_0
	v_lshl_add_u32 v5, v7, 11, v3
	v_lshlrev_b32_e32 v7, 12, v7
	s_add_i32 s58, s29, 0x16000
	s_mov_b32 m0, s58
	s_nop 0
	global_load_lds_dwordx4 v156, s[8:9]
	v_lshl_add_u32 v157, v3, 1, v7
	v_lshlrev_b32_e32 v3, 12, v8
	s_mov_b32 m0, s29
	s_nop 0
	global_load_lds_dwordx4 v157, s[12:13]
	v_lshl_add_u32 v158, v4, 1, v3
	v_mov_b32_e32 v3, 0x80000
	s_add_i32 s59, s29, 0x2000
	s_mov_b32 m0, s59
	s_nop 0
	global_load_lds_dwordx4 v158, s[12:13]
	v_lshl_add_u32 v6, v8, 11, v4
	v_lshl_add_u32 v159, v5, 1, v3
	s_add_i32 s60, s29, 0x4000
	s_mov_b32 m0, s60
	s_nop 0
	global_load_lds_dwordx4 v159, s[12:13]
	v_lshl_add_u32 v160, v6, 1, v3
	s_add_i32 s61, s29, 0x6000
	s_mov_b32 m0, s61
	s_nop 0
	global_load_lds_dwordx4 v160, s[12:13]
	s_cmp_eq_u32 s0, 1
	s_mov_b32 s5, 0
	s_mov_b64 s[16:17], 0x80000
	s_cselect_b64 s[18:19], -1, 0
	s_cmp_lg_u32 s0, 1
	s_cbranch_scc1 .LBB0_132
	s_barrier
; #define PG8_STAGEB(bufoff, gbase) PG8_STAGE2(bufoff, gbase, voffB[0], voffB[1])
; #define PG8_STAGEA(bufoff, gbase, h) PG8_STAGE2(bufoff, gbase, voffA[h][0], voffA[h][1])
; #define PG8_WAIT_V(n) asm volatile("s_waitcnt vmcnt(" #n ")" ::: "memory")
; #define PG8_BAR __builtin_amdgcn_s_barrier()
;     ...
;     if (wr == 1) PG8_BAR;
;     if constexpr (HM) PG8_WAIT_V(0); else PG8_WAIT_V(2);
;     PG8_BAR;
;     PG8_STAGEB(PG8_SB(1, 0), cB + kstep); PG8_STAGEA(PG8_SA(1, 0), cA + kstep, 0); PG8_STAGEB(PG8_SB(1, 1), cB + hstepB + kstep);
;     PG8_WAIT_V(6); PG8_BAR;
.LBB0_132:
	v_bfe_u32 v6, v2, 4, 2
	v_and_b32_e32 v3, 15, v2
	v_lshlrev_b32_e32 v4, 4, v6
	v_lshlrev_b32_e32 v2, 2, v2
	s_and_b32 s8, s6, 3
	v_lshl_or_b32 v161, s0, 6, v3
	v_lshl_or_b32 v3, v3, 6, v4
	s_lshl_b32 s0, s0, 13
	v_and_b32_e32 v2, 32, v2
	v_bitop3_b32 v8, v3, s0, v2 bitop3:0xde
	s_lshl_b32 s0, s8, 12
	s_add_u32 s62, s94, 0x50600000
	s_addc_u32 s63, s95, 0
	s_ashr_i32 s64, s3, 31
	s_ashr_i32 s65, s92, 31
	v_bitop3_b32 v3, v3, s0, v2 bitop3:0xde
	s_add_u32 s0, s54, 0x80
	s_waitcnt vmcnt(2)
	s_barrier
	s_addc_u32 s1, s55, 0
	s_add_i32 s66, s29, 0x18000
	s_mov_b32 m0, s66
	s_nop 0
	global_load_lds_dwordx4 v1, s[0:1]
	s_add_i32 s67, s29, 0x1a000
	s_mov_b32 m0, s67
	s_nop 0
	global_load_lds_dwordx4 v156, s[0:1]
	s_add_u32 s0, s12, 0x80
	s_addc_u32 s1, s13, 0
	s_add_i32 s68, s29, 0x8000
	s_mov_b32 m0, s68
	s_nop 0
	global_load_lds_dwordx4 v157, s[0:1]
	s_add_i32 s69, s29, 0xa000
	s_mov_b32 m0, s69
	s_nop 0
	global_load_lds_dwordx4 v158, s[0:1]
	s_add_u32 s0, s54, 0x80080
	v_lshlrev_b32_e32 v2, 2, v6
	s_addc_u32 s1, s55, 0
	s_add_i32 s70, s29, 0x1c000
	s_mov_b32 m0, s70
	s_nop 0
	global_load_lds_dwordx4 v1, s[0:1]
	v_lshl_or_b32 v2, s8, 4, v2
	s_add_i32 s71, s29, 0x1e000
	s_mov_b32 m0, s71
	s_nop 0
	global_load_lds_dwordx4 v156, s[0:1]
	s_add_i32 s72, s29, 0xc000
	s_add_i32 s73, s29, 0xe000
	v_mov_b32_e32 v131, 0
	v_lshlrev_b32_e32 v130, 2, v2
	s_waitcnt vmcnt(6)
	s_cmpk_lt_u32 s4, 0x100
	v_lshl_add_u64 v[4:5], s[94:95], 0, v[130:131]
	s_mov_b64 s[0:1], 0x50800000
	v_lshlrev_b32_e32 v7, 3, v6
	s_cselect_b64 s[20:21], -1, 0
	v_lshl_add_u64 v[132:133], v[4:5], 0, s[0:1]
	s_mov_b64 s[0:1], 0x50c00000
	s_lshl_b32 s74, s8, 1
	v_add_u32_e32 v3, 0, v3
	v_lshlrev_b32_e32 v140, 1, v2
	v_mbcnt_lo_u32_b32 v2, -1, 0
	v_lshl_add_u64 v[134:135], v[4:5], 0, s[0:1]
	v_cmp_eq_u32_e64 s[6:7], 0, v6
	s_orn2_b32 s74, s74, 31
	v_lshl_or_b32 v162, s8, 5, v7
	v_mov_b64_e32 v[136:137], 0xc00
	v_mov_b64_e32 v[138:139], 0xbff
	s_movk_i32 s75, 0x181
	v_add_u32_e32 v163, 0x10000, v3
	v_add_u32_e32 v164, 0x14000, v3
	v_add_u32_e32 v165, 0, v8
	v_add_u32_e32 v166, 0x18000, v3
	v_add_u32_e32 v167, 0x1c000, v3
	s_mov_b32 s76, 0x48600000
	s_mov_b64 s[22:23], 0x90000
	s_mov_b64 s[24:25], 0xa0000
	s_mov_b64 s[26:27], 0xb0000
	s_mov_b32 s77, 0x3c600000
	s_mov_b32 s78, 0x38600000
	s_mov_b32 s28, 0x3e6d3388
	s_mov_b32 s30, 0x3f07dc22
	s_mov_b32 s34, 0xbf3a00e3
	s_mov_b32 s36, 0x3f35f0e3
	s_mov_b32 s38, 0xbe11a98e
	s_mov_b32 s40, 0x3e027906
	s_mov_b32 s42, 0xbf38aa3b
	v_mov_b32_e32 v168, 0x3db504f3
	v_mbcnt_hi_u32_b32 v169, -1, v2
	s_mov_b32 s79, 0
	s_barrier
	s_branch .LBB0_135

; #define LAS __attribute__((address_space(3)))
; #define PG8_STAGEB(bufoff, gbase) PG8_STAGE2(bufoff, gbase, voffB[0], voffB[1])
; #define PG8_STAGEA(bufoff, gbase, h) PG8_STAGE2(bufoff, gbase, voffA[h][0], voffA[h][1])
; #define PG8_STAGEAS(bufoff, gbase, h) PG8_STAGE2(bufoff, gbase, voffA[h][0], voffA[h][1])
; #define PG8_LDA(dst, b, h) do { _Pragma("unroll") for (int m = 0; m < 4; ++m) _Pragma("unroll") for (int k = 0; k < 2; ++k) dst[m][k] = *(const LAS bf16x8*)(lds + PG8_SA(b, h) + aoff + m * 2048 + k * 1024); } while (0)
; #define PG8_LDB(dst, b, h) do { _Pragma("unroll") for (int n = 0; n < 2; ++n) _Pragma("unroll") for (int k = 0; k < 2; ++k) dst[n][k] = *(const LAS bf16x8*)(lds + PG8_SB(b, h) + boff + n * 2048 + k * 1024); } while (0)
;     ...
;             const char* a1 = cA + (size_t)(t + 1) * kstep;
;             const char* a2 = last ? nA : cA + (size_t)(t + 2) * kstep; const char* b2 = last ? nB : cB + (size_t)(t + 2) * kstep;
;             const char* a3 = a2 + kstep; const char* b3 = b2 + kstep;
;             PG8_LDB(B0, 0, 0); PG8_LDB(B1, 0, 1); PG8_SCHED; PG8_LDA(At, 0, 0); if constexpr (!HM) PG8_STAGEA(PG8_SA(1, 1), a1, 1);
;             if constexpr (Sched::kGather) { if (last && has_next) { const u32x4 tn = *(const LAS u32x4*)(S.aux + tid * 16); voffA[0][0] = tn.x; voffA[0][1] = tn.y; voffA[1][0] = tn.z; voffA[1][1] = tn.w; } }
;             PG8_WAIT_K0(); PG8_WAIT_L(0); PG8_BAR; PG8_MMA(0, 0, At, B0); PG8_MMA(0, 1, At, B1); PG8_BAR; PG8_SCHED;
;             if constexpr (!HM) PG8_LDA(At, 0, 1);
;             PG8_STAGEB(PG8_SB(0, 0), b2); PG8_STAGEB(PG8_SB(0, 1), b2 + hstepB); PG8_STAGEAS(PG8_SA(0, 0), a2, 0);
;             PG8_WAIT_K0(); PG8_WAIT_L(0); PG8_BAR; if constexpr (!HM) { PG8_MMA(1, 0, At, B0); PG8_MMA(1, 1, At, B1); } PG8_BAR; PG8_SCHED;
;             PG8_LDB(B0, 1, 0); PG8_LDB(B1, 1, 1); PG8_SCHED; PG8_LDA(At, 1, 0); if constexpr (!HM) PG8_STAGEAS(PG8_SA(0, 1), a2, 1);
;             PG8_WAIT_K(); PG8_WAIT_L(0); PG8_BAR; PG8_MMA(0, 0, At, B0); PG8_MMA(0, 1, At, B1); PG8_BAR; PG8_SCHED;
;             if constexpr (!HM) PG8_LDA(At, 1, 1);
;             PG8_STAGEB(PG8_SB(1, 0), b3); PG8_STAGEB(PG8_SB(1, 1), b3 + hstepB); PG8_STAGEAS(PG8_SA(1, 0), a3, 0);
;             PG8_WAIT_K(); PG8_WAIT_L(0); PG8_BAR; if constexpr (!HM) { PG8_MMA(1, 0, At, B0); PG8_MMA(1, 1, At, B1); } PG8_BAR; PG8_SCHED;
.LBB0_140:
	ds_read_b128 v[142:145], v163
	ds_read_b128 v[146:149], v163 offset:1024
	ds_read_b128 v[150:153], v163 offset:2048
	ds_read_b128 v[170:173], v163 offset:3072
	ds_read_b128 v[174:177], v164
	ds_read_b128 v[178:181], v164 offset:1024
	ds_read_b128 v[182:185], v164 offset:2048
	ds_read_b128 v[186:189], v164 offset:3072
	s_cmp_eq_u32 s47, 28
	s_cselect_b32 s56, s48, s4
	s_cselect_b32 s57, s49, s11
	s_cselect_b32 s54, s50, s33
	s_cselect_b32 s55, s51, s45
	s_add_u32 s12, s56, 0x80
	s_addc_u32 s13, s57, 0
	ds_read_b128 v[190:193], v165
	ds_read_b128 v[194:197], v165 offset:1024
	ds_read_b128 v[198:201], v165 offset:2048
	ds_read_b128 v[202:205], v165 offset:3072
	ds_read_b128 v[206:209], v165 offset:4096
	ds_read_b128 v[210:213], v165 offset:5120
	ds_read_b128 v[214:217], v165 offset:6144
	ds_read_b128 v[218:221], v165 offset:7168
	s_mov_b32 m0, s72
	s_nop 0
	global_load_lds_dwordx4 v159, s[0:1]
	s_mov_b32 m0, s73
	s_nop 0
	global_load_lds_dwordx4 v160, s[0:1]
	s_waitcnt vmcnt(8)
	s_waitcnt lgkmcnt(0)
	s_barrier
	s_setprio 1
	s_waitcnt lgkmcnt(7)
	v_mfma_f32_16x16x32_bf16 v[126:129], v[142:145], v[190:193], v[126:129]
	v_mfma_f32_16x16x32_bf16 v[122:125], v[150:153], v[190:193], v[122:125]
	s_waitcnt lgkmcnt(5)
	v_mfma_f32_16x16x32_bf16 v[110:113], v[142:145], v[198:201], v[110:113]
	v_mfma_f32_16x16x32_bf16 v[106:109], v[150:153], v[198:201], v[106:109]
	s_waitcnt lgkmcnt(3)
	v_mfma_f32_16x16x32_bf16 v[94:97], v[142:145], v[206:209], v[94:97]
	v_mfma_f32_16x16x32_bf16 v[90:93], v[150:153], v[206:209], v[90:93]
	s_waitcnt lgkmcnt(1)
	v_mfma_f32_16x16x32_bf16 v[78:81], v[142:145], v[214:217], v[78:81]
	v_mfma_f32_16x16x32_bf16 v[74:77], v[150:153], v[214:217], v[74:77]
	v_mfma_f32_16x16x32_bf16 v[126:129], v[146:149], v[194:197], v[126:129]
	v_mfma_f32_16x16x32_bf16 v[122:125], v[170:173], v[194:197], v[122:125]
	v_mfma_f32_16x16x32_bf16 v[110:113], v[146:149], v[202:205], v[110:113]
	v_mfma_f32_16x16x32_bf16 v[106:109], v[170:173], v[202:205], v[106:109]
	v_mfma_f32_16x16x32_bf16 v[94:97], v[146:149], v[210:213], v[94:97]
	v_mfma_f32_16x16x32_bf16 v[90:93], v[170:173], v[210:213], v[90:93]
	s_waitcnt lgkmcnt(0)
	v_mfma_f32_16x16x32_bf16 v[78:81], v[146:149], v[218:221], v[78:81]
	v_mfma_f32_16x16x32_bf16 v[74:77], v[170:173], v[218:221], v[74:77]
	s_setprio 0
	s_setprio 1
	v_mfma_f32_16x16x32_bf16 v[118:121], v[174:177], v[190:193], v[118:121]
	v_mfma_f32_16x16x32_bf16 v[114:117], v[182:185], v[190:193], v[114:117]
	v_mfma_f32_16x16x32_bf16 v[102:105], v[174:177], v[198:201], v[102:105]
	v_mfma_f32_16x16x32_bf16 v[98:101], v[182:185], v[198:201], v[98:101]
	v_mfma_f32_16x16x32_bf16 v[86:89], v[174:177], v[206:209], v[86:89]
	v_mfma_f32_16x16x32_bf16 v[82:85], v[182:185], v[206:209], v[82:85]
	v_mfma_f32_16x16x32_bf16 v[70:73], v[174:177], v[214:217], v[70:73]
	v_mfma_f32_16x16x32_bf16 v[66:69], v[182:185], v[214:217], v[66:69]
	v_mfma_f32_16x16x32_bf16 v[118:121], v[178:181], v[194:197], v[118:121]
	v_mfma_f32_16x16x32_bf16 v[114:117], v[186:189], v[194:197], v[114:117]
	v_mfma_f32_16x16x32_bf16 v[102:105], v[178:181], v[202:205], v[102:105]
	v_mfma_f32_16x16x32_bf16 v[98:101], v[186:189], v[202:205], v[98:101]
	v_mfma_f32_16x16x32_bf16 v[86:89], v[178:181], v[210:213], v[86:89]
	v_mfma_f32_16x16x32_bf16 v[82:85], v[186:189], v[210:213], v[82:85]
	v_mfma_f32_16x16x32_bf16 v[70:73], v[178:181], v[218:221], v[70:73]
	v_mfma_f32_16x16x32_bf16 v[66:69], v[186:189], v[218:221], v[66:69]
	s_setprio 0
	s_barrier
	ds_read_b128 v[190:193], v165 offset:16384
	ds_read_b128 v[194:197], v165 offset:17408
	ds_read_b128 v[198:201], v165 offset:18432
	ds_read_b128 v[202:205], v165 offset:19456
	ds_read_b128 v[206:209], v165 offset:20480
	ds_read_b128 v[210:213], v165 offset:21504
	ds_read_b128 v[214:217], v165 offset:22528
	ds_read_b128 v[218:221], v165 offset:23552
	s_mov_b32 m0, s41
	s_nop 0
	global_load_lds_dwordx4 v1, s[54:55]
	s_mov_b32 m0, s43
	s_nop 0
	global_load_lds_dwordx4 v156, s[54:55]
	s_add_u32 s80, s54, 0x80000
	s_addc_u32 s81, s55, 0
	s_mov_b32 m0, s53
	s_nop 0
	global_load_lds_dwordx4 v1, s[80:81]
	s_mov_b32 m0, s58
	s_nop 0
	global_load_lds_dwordx4 v156, s[80:81]
	s_mov_b32 m0, s29
	s_nop 0
	global_load_lds_dwordx4 v157, s[56:57]
	s_mov_b32 m0, s59
	s_nop 0
	global_load_lds_dwordx4 v158, s[56:57]
	s_waitcnt vmcnt(8)
	s_waitcnt lgkmcnt(0)
	s_barrier
	s_setprio 1
	s_waitcnt lgkmcnt(7)
	v_mfma_f32_16x16x32_bf16 v[62:65], v[142:145], v[190:193], v[62:65]
	v_mfma_f32_16x16x32_bf16 v[58:61], v[150:153], v[190:193], v[58:61]
	s_waitcnt lgkmcnt(5)
	v_mfma_f32_16x16x32_bf16 v[46:49], v[142:145], v[198:201], v[46:49]
	v_mfma_f32_16x16x32_bf16 v[42:45], v[150:153], v[198:201], v[42:45]
	s_waitcnt lgkmcnt(3)
	v_mfma_f32_16x16x32_bf16 v[30:33], v[142:145], v[206:209], v[30:33]
	v_mfma_f32_16x16x32_bf16 v[26:29], v[150:153], v[206:209], v[26:29]
	s_waitcnt lgkmcnt(1)
	v_mfma_f32_16x16x32_bf16 v[14:17], v[142:145], v[214:217], v[14:17]
	v_mfma_f32_16x16x32_bf16 v[10:13], v[150:153], v[214:217], v[10:13]
	v_mfma_f32_16x16x32_bf16 v[62:65], v[146:149], v[194:197], v[62:65]
	v_mfma_f32_16x16x32_bf16 v[58:61], v[170:173], v[194:197], v[58:61]
	v_mfma_f32_16x16x32_bf16 v[46:49], v[146:149], v[202:205], v[46:49]
	v_mfma_f32_16x16x32_bf16 v[42:45], v[170:173], v[202:205], v[42:45]
	v_mfma_f32_16x16x32_bf16 v[30:33], v[146:149], v[210:213], v[30:33]
	v_mfma_f32_16x16x32_bf16 v[26:29], v[170:173], v[210:213], v[26:29]
	s_waitcnt lgkmcnt(0)
	v_mfma_f32_16x16x32_bf16 v[14:17], v[146:149], v[218:221], v[14:17]
	v_mfma_f32_16x16x32_bf16 v[10:13], v[170:173], v[218:221], v[10:13]
	s_setprio 0
	s_setprio 1
	v_mfma_f32_16x16x32_bf16 v[54:57], v[174:177], v[190:193], v[54:57]
	v_mfma_f32_16x16x32_bf16 v[50:53], v[182:185], v[190:193], v[50:53]
	v_mfma_f32_16x16x32_bf16 v[38:41], v[174:177], v[198:201], v[38:41]
	v_mfma_f32_16x16x32_bf16 v[34:37], v[182:185], v[198:201], v[34:37]
	v_mfma_f32_16x16x32_bf16 v[22:25], v[174:177], v[206:209], v[22:25]
	v_mfma_f32_16x16x32_bf16 v[18:21], v[182:185], v[206:209], v[18:21]
	v_mfma_f32_16x16x32_bf16 v[6:9], v[174:177], v[214:217], v[6:9]
	v_mfma_f32_16x16x32_bf16 v[2:5], v[182:185], v[214:217], v[2:5]
	v_mfma_f32_16x16x32_bf16 v[54:57], v[178:181], v[194:197], v[54:57]
	v_mfma_f32_16x16x32_bf16 v[50:53], v[186:189], v[194:197], v[50:53]
	v_mfma_f32_16x16x32_bf16 v[38:41], v[178:181], v[202:205], v[38:41]
	v_mfma_f32_16x16x32_bf16 v[34:37], v[186:189], v[202:205], v[34:37]
	v_mfma_f32_16x16x32_bf16 v[22:25], v[178:181], v[210:213], v[22:25]
	v_mfma_f32_16x16x32_bf16 v[18:21], v[186:189], v[210:213], v[18:21]
	v_mfma_f32_16x16x32_bf16 v[6:9], v[178:181], v[218:221], v[6:9]
	v_mfma_f32_16x16x32_bf16 v[2:5], v[186:189], v[218:221], v[2:5]
	s_setprio 0
	s_barrier
; #define PG8_STAGEB(bufoff, gbase) PG8_STAGE2(bufoff, gbase, voffB[0], voffB[1])
; #define PG8_STAGEAS(bufoff, gbase, h) PG8_STAGE2(bufoff, gbase, voffA[h][0], voffA[h][1])
; #define PG8_LDA(dst, b, h) do { _Pragma("unroll") for (int m = 0; m < 4; ++m) _Pragma("unroll") for (int k = 0; k < 2; ++k) dst[m][k] = *(const LAS bf16x8*)(lds + PG8_SA(b, h) + aoff + m * 2048 + k * 1024); } while (0)
; #define PG8_LDB(dst, b, h) do { _Pragma("unroll") for (int n = 0; n < 2; ++n) _Pragma("unroll") for (int k = 0; k < 2; ++k) dst[n][k] = *(const LAS bf16x8*)(lds + PG8_SB(b, h) + boff + n * 2048 + k * 1024); } while (0)
; #define PG8_WAIT_K() do { if constexpr (HM) PG8_WAIT_V(6); else PG8_WAIT_V(8); } while (0)
; #define PG8_WAIT_L(n) asm volatile("s_waitcnt lgkmcnt(" #n ")" ::: "memory")
; #define PG8_BAR __builtin_amdgcn_s_barrier()
; #define PG8_SCHED __builtin_amdgcn_sched_barrier(0)
;     ...
;             PG8_LDB(B0, 1, 0); PG8_LDB(B1, 1, 1); PG8_SCHED; PG8_LDA(At, 1, 0); if constexpr (!HM) PG8_STAGEAS(PG8_SA(0, 1), a2, 1);
;             PG8_WAIT_K(); PG8_WAIT_L(0); PG8_BAR; PG8_MMA(0, 0, At, B0); PG8_MMA(0, 1, At, B1); PG8_BAR; PG8_SCHED;
;             if constexpr (!HM) PG8_LDA(At, 1, 1);
;             PG8_STAGEB(PG8_SB(1, 0), b3); PG8_STAGEB(PG8_SB(1, 1), b3 + hstepB); PG8_STAGEAS(PG8_SA(1, 0), a3, 0);
;             PG8_WAIT_K(); PG8_WAIT_L(0); PG8_BAR; if constexpr (!HM) { PG8_MMA(1, 0, At, B0); PG8_MMA(1, 1, At, B1); } PG8_BAR; PG8_SCHED;
	ds_read_b128 v[142:145], v166
	ds_read_b128 v[146:149], v166 offset:1024
	ds_read_b128 v[150:153], v166 offset:2048
	ds_read_b128 v[170:173], v166 offset:3072
	ds_read_b128 v[174:177], v167
	ds_read_b128 v[178:181], v167 offset:1024
	ds_read_b128 v[182:185], v167 offset:2048
	ds_read_b128 v[186:189], v167 offset:3072
	ds_read_b128 v[190:193], v165 offset:32768
	ds_read_b128 v[194:197], v165 offset:33792
	ds_read_b128 v[198:201], v165 offset:34816
	ds_read_b128 v[202:205], v165 offset:35840
	ds_read_b128 v[206:209], v165 offset:36864
	ds_read_b128 v[210:213], v165 offset:37888
	ds_read_b128 v[214:217], v165 offset:38912
	ds_read_b128 v[218:221], v165 offset:39936
	s_mov_b32 m0, s60
	s_nop 0
	global_load_lds_dwordx4 v159, s[56:57]
	s_mov_b32 m0, s61
	s_nop 0
	global_load_lds_dwordx4 v160, s[56:57]
	s_waitcnt vmcnt(8)
	s_waitcnt lgkmcnt(0)
	s_barrier
	s_setprio 1
	s_waitcnt lgkmcnt(7)
	v_mfma_f32_16x16x32_bf16 v[126:129], v[142:145], v[190:193], v[126:129]
	v_mfma_f32_16x16x32_bf16 v[122:125], v[150:153], v[190:193], v[122:125]
	s_waitcnt lgkmcnt(5)
	v_mfma_f32_16x16x32_bf16 v[110:113], v[142:145], v[198:201], v[110:113]
	v_mfma_f32_16x16x32_bf16 v[106:109], v[150:153], v[198:201], v[106:109]
	s_waitcnt lgkmcnt(3)
	v_mfma_f32_16x16x32_bf16 v[94:97], v[142:145], v[206:209], v[94:97]
	v_mfma_f32_16x16x32_bf16 v[90:93], v[150:153], v[206:209], v[90:93]
	s_waitcnt lgkmcnt(1)
	v_mfma_f32_16x16x32_bf16 v[78:81], v[142:145], v[214:217], v[78:81]
	v_mfma_f32_16x16x32_bf16 v[74:77], v[150:153], v[214:217], v[74:77]
	v_mfma_f32_16x16x32_bf16 v[126:129], v[146:149], v[194:197], v[126:129]
	v_mfma_f32_16x16x32_bf16 v[122:125], v[170:173], v[194:197], v[122:125]
	v_mfma_f32_16x16x32_bf16 v[110:113], v[146:149], v[202:205], v[110:113]
	v_mfma_f32_16x16x32_bf16 v[106:109], v[170:173], v[202:205], v[106:109]
	v_mfma_f32_16x16x32_bf16 v[94:97], v[146:149], v[210:213], v[94:97]
	v_mfma_f32_16x16x32_bf16 v[90:93], v[170:173], v[210:213], v[90:93]
	s_waitcnt lgkmcnt(0)
	v_mfma_f32_16x16x32_bf16 v[78:81], v[146:149], v[218:221], v[78:81]
	v_mfma_f32_16x16x32_bf16 v[74:77], v[170:173], v[218:221], v[74:77]
	s_setprio 0
	s_setprio 1
	v_mfma_f32_16x16x32_bf16 v[118:121], v[174:177], v[190:193], v[118:121]
	v_mfma_f32_16x16x32_bf16 v[114:117], v[182:185], v[190:193], v[114:117]
	v_mfma_f32_16x16x32_bf16 v[102:105], v[174:177], v[198:201], v[102:105]
	v_mfma_f32_16x16x32_bf16 v[98:101], v[182:185], v[198:201], v[98:101]
	v_mfma_f32_16x16x32_bf16 v[86:89], v[174:177], v[206:209], v[86:89]
	v_mfma_f32_16x16x32_bf16 v[82:85], v[182:185], v[206:209], v[82:85]
	v_mfma_f32_16x16x32_bf16 v[70:73], v[174:177], v[214:217], v[70:73]
	v_mfma_f32_16x16x32_bf16 v[66:69], v[182:185], v[214:217], v[66:69]
	v_mfma_f32_16x16x32_bf16 v[118:121], v[178:181], v[194:197], v[118:121]
	v_mfma_f32_16x16x32_bf16 v[114:117], v[186:189], v[194:197], v[114:117]
	v_mfma_f32_16x16x32_bf16 v[102:105], v[178:181], v[202:205], v[102:105]
	v_mfma_f32_16x16x32_bf16 v[98:101], v[186:189], v[202:205], v[98:101]
	v_mfma_f32_16x16x32_bf16 v[86:89], v[178:181], v[210:213], v[86:89]
	v_mfma_f32_16x16x32_bf16 v[82:85], v[186:189], v[210:213], v[82:85]
	v_mfma_f32_16x16x32_bf16 v[70:73], v[178:181], v[218:221], v[70:73]
	v_mfma_f32_16x16x32_bf16 v[66:69], v[186:189], v[218:221], v[66:69]
	s_setprio 0
	s_barrier
	ds_read_b128 v[190:193], v165 offset:49152
	ds_read_b128 v[194:197], v165 offset:50176
	ds_read_b128 v[198:201], v165 offset:51200
	ds_read_b128 v[202:205], v165 offset:52224
	ds_read_b128 v[206:209], v165 offset:53248
	ds_read_b128 v[210:213], v165 offset:54272
	ds_read_b128 v[214:217], v165 offset:55296
	ds_read_b128 v[218:221], v165 offset:56320
	s_add_u32 s56, s54, 0x80
	s_addc_u32 s57, s55, 0
	s_mov_b32 m0, s66
	s_nop 0
	global_load_lds_dwordx4 v1, s[56:57]
	s_add_u32 s54, s54, 0x80080
	s_mov_b32 m0, s67
	s_nop 0
	global_load_lds_dwordx4 v156, s[56:57]
	s_addc_u32 s55, s55, 0
	s_mov_b32 m0, s70
	s_nop 0
	global_load_lds_dwordx4 v1, s[54:55]
	s_mov_b32 m0, s71
	s_nop 0
	global_load_lds_dwordx4 v156, s[54:55]
	s_mov_b32 m0, s68
	s_nop 0
	global_load_lds_dwordx4 v157, s[12:13]
	s_mov_b32 m0, s69
	s_nop 0
	global_load_lds_dwordx4 v158, s[12:13]
	s_waitcnt vmcnt(8)
	s_waitcnt lgkmcnt(0)
	s_barrier
	s_setprio 1
	s_waitcnt lgkmcnt(7)
	v_mfma_f32_16x16x32_bf16 v[62:65], v[142:145], v[190:193], v[62:65]
	v_mfma_f32_16x16x32_bf16 v[58:61], v[150:153], v[190:193], v[58:61]
	s_waitcnt lgkmcnt(5)
	v_mfma_f32_16x16x32_bf16 v[46:49], v[142:145], v[198:201], v[46:49]
	v_mfma_f32_16x16x32_bf16 v[42:45], v[150:153], v[198:201], v[42:45]
	s_waitcnt lgkmcnt(3)
	v_mfma_f32_16x16x32_bf16 v[30:33], v[142:145], v[206:209], v[30:33]
	v_mfma_f32_16x16x32_bf16 v[26:29], v[150:153], v[206:209], v[26:29]
	s_waitcnt lgkmcnt(1)
	v_mfma_f32_16x16x32_bf16 v[14:17], v[142:145], v[214:217], v[14:17]
	v_mfma_f32_16x16x32_bf16 v[10:13], v[150:153], v[214:217], v[10:13]
	v_mfma_f32_16x16x32_bf16 v[62:65], v[146:149], v[194:197], v[62:65]
	v_mfma_f32_16x16x32_bf16 v[58:61], v[170:173], v[194:197], v[58:61]
	v_mfma_f32_16x16x32_bf16 v[46:49], v[146:149], v[202:205], v[46:49]
	v_mfma_f32_16x16x32_bf16 v[42:45], v[170:173], v[202:205], v[42:45]
	v_mfma_f32_16x16x32_bf16 v[30:33], v[146:149], v[210:213], v[30:33]
	v_mfma_f32_16x16x32_bf16 v[26:29], v[170:173], v[210:213], v[26:29]
	s_waitcnt lgkmcnt(0)
	v_mfma_f32_16x16x32_bf16 v[14:17], v[146:149], v[218:221], v[14:17]
	v_mfma_f32_16x16x32_bf16 v[10:13], v[170:173], v[218:221], v[10:13]
	s_setprio 0
	s_setprio 1
	v_mfma_f32_16x16x32_bf16 v[54:57], v[174:177], v[190:193], v[54:57]
	v_mfma_f32_16x16x32_bf16 v[50:53], v[182:185], v[190:193], v[50:53]
	v_mfma_f32_16x16x32_bf16 v[38:41], v[174:177], v[198:201], v[38:41]
	v_mfma_f32_16x16x32_bf16 v[34:37], v[182:185], v[198:201], v[34:37]
	v_mfma_f32_16x16x32_bf16 v[22:25], v[174:177], v[206:209], v[22:25]
	v_mfma_f32_16x16x32_bf16 v[18:21], v[182:185], v[206:209], v[18:21]
	v_mfma_f32_16x16x32_bf16 v[6:9], v[174:177], v[214:217], v[6:9]
	v_mfma_f32_16x16x32_bf16 v[2:5], v[182:185], v[214:217], v[2:5]
	v_mfma_f32_16x16x32_bf16 v[54:57], v[178:181], v[194:197], v[54:57]
	v_mfma_f32_16x16x32_bf16 v[50:53], v[186:189], v[194:197], v[50:53]
	v_mfma_f32_16x16x32_bf16 v[38:41], v[178:181], v[202:205], v[38:41]
	v_mfma_f32_16x16x32_bf16 v[34:37], v[186:189], v[202:205], v[34:37]
	v_mfma_f32_16x16x32_bf16 v[22:25], v[178:181], v[210:213], v[22:25]
	v_mfma_f32_16x16x32_bf16 v[18:21], v[186:189], v[210:213], v[18:21]
	v_mfma_f32_16x16x32_bf16 v[6:9], v[178:181], v[218:221], v[6:9]
	v_mfma_f32_16x16x32_bf16 v[2:5], v[186:189], v[218:221], v[2:5]
	s_setprio 0
	s_barrier
	s_add_i32 s47, s47, 2
	s_add_u32 s4, s4, 0x100
	s_addc_u32 s11, s11, 0
	s_add_u32 s33, s33, 0x100
	s_addc_u32 s45, s45, 0
	s_add_u32 s0, s0, 0x100
	s_addc_u32 s1, s1, 0
	s_cmp_gt_u32 s47, 29
	s_cbranch_scc0 .LBB0_140
	s_and_b64 vcc, exec, s[20:21]
	s_cbranch_vccnz .LBB0_144
	v_lshl_add_u32 v142, s10, 8, v161
	s_cmp_gt_i32 s52, 7
	s_mov_b64 s[0:1], -1
	s_cbranch_scc1 .LBB0_145

;     __device__ __forceinline__ const char* a_base(const Unit& u) const { return (const char*)A + (size_t)u.pm * BM * lda * 2; }
;     __device__ __forceinline__ const char* b_base(const Unit& u) const { return (const char*)Bt + (size_t)u.pn * BM * K * 2; }
;     __device__ __forceinline__ const char* b_base(const Unit& u) const { return (const char*)Bt + ((size_t)u.e * NB + (size_t)u.pn * BM) * K * 2; }
; #define PG8_RC() int R[2], C[2]; { int t_ = threadIdx.x; asm volatile("" : "+v"(t_)); _Pragma("unroll") for (int i = 0; i < 2; ++i) stage_rc(t_ * 16 + i * 8192, R[i], C[i]); }
;     __device__ __forceinline__ bool next(int i, Unit& u) const {
;         const long L = (long)i * G + c; if (L >= nwg) return false;
;         int wgid = (int)L; { const int q = nwg / NXCD, r = nwg % NXCD, xcd = wgid % NXCD, off = wgid / NXCD; wgid = (xcd < r ? xcd * (q + 1) : r * (q + 1) + (xcd - r) * q) + off; }
;         const int nig = WGM * nN, gid = wgid / nig, fm = gid * WGM, gsz = (nM - fm) < WGM ? (nM - fm) : WGM;
;         u.pm = fm + ((wgid % nig) % gsz); u.pn = (wgid % nig) / gsz; u.e = 0; u.mt = u.pm; u.hx = 0; return true;
;     }
;     ...
;     if (!S.next(0, cur)) return;
;     unsigned voffA[2][2];
;     { PG8_RC(); S.a_offs(cur, R, C, voffA); }
;     f32x4 acc[2][2][4][2];
; #pragma unroll
;     for (int a = 0; a < 2; ++a)
; #pragma unroll
;         for (int b = 0; b < 2; ++b)
; #pragma unroll
;             for (int m = 0; m < 4; ++m)
; #pragma unroll
;                 for (int n = 0; n < 2; ++n) acc[a][b][m][n] = (f32x4){0.f, 0.f, 0.f, 0.f};
;     bf16x8 At[4][2], B0[2][2], B1[2][2];
;     const char* cA = S.a_base(cur); const char* cB = S.b_base(cur);
;     const unsigned bias_lds = (unsigned)__builtin_amdgcn_readfirstlane((int)((unsigned)(size_t)lds + (unsigned)(AUX_OFF + 8192) + (unsigned)wid * 256u));
;     if constexpr (Epi::kBiasDMA) { if (lane < 16) glds16(E.bias_base(cur), E.bias_off(cur, wc, lane), bias_lds); }
;     const unsigned rowid_lds = (unsigned)__builtin_amdgcn_readfirstlane((int)((unsigned)(size_t)lds + (unsigned)AUX_OFF + (unsigned)wid * 512u));
;     if constexpr (Epi::kRowDMA) { if (lane < 32) glds16(E.row_base(cur), E.row_off(cur, wr, lane), rowid_lds); }
;     PG8_STAGEB(PG8_SB(0, 0), cB); PG8_STAGEB(PG8_SB(0, 1), cB + hstepB); PG8_STAGEA(PG8_SA(0, 0), cA, 0); if constexpr (!HM) PG8_STAGEA(PG8_SA(0, 1), cA, 1);
.LBB0_559:
	s_cmp_lt_i32 s88, 6
	s_cselect_b64 s[4:5], -1, 0
	s_and_b64 s[4:5], s[4:5], s[0:1]
	s_andn2_b64 vcc, exec, s[4:5]
	s_cbranch_vccnz .LBB0_620
	s_cmpk_lt_i32 s92, 0x200
	s_cselect_b64 s[12:13], -1, 0
	s_waitcnt lgkmcnt(0)
	s_add_u32 s8, s94, 0x63000000
	s_addc_u32 s9, s95, 0
	s_ashr_i32 s33, s92, 31
	s_lshr_b32 s0, s33, 29
	v_mov_b32_e32 v1, v0
	s_add_i32 s0, s92, s0
	s_waitcnt vmcnt(2)
	v_mov_b32_e32 v2, 0x7f7f7f7f
	v_mov_b32_e32 v3, 0x7f7f7f7f
	s_ashr_i32 s48, s0, 3
	s_and_b32 s0, s0, -8
	s_ashr_i32 s3, s2, 31
	s_sub_i32 s50, s92, s0
	v_mov_b32_e32 v2, v0
	s_cmp_lt_i32 s50, 0
	s_cselect_b64 s[10:11], -1, 0
	v_readfirstlane_b32 s1, v2
	s_lshl_b32 s49, s50, 6
	s_ashr_i32 s6, s1, 6
	v_mov_b32_e32 v1, 0x7f7f7f7f
	s_cmpk_gt_i32 s92, 0x1ff
	s_mulk_i32 s50, 0x41
	s_cbranch_scc1 .LBB0_590
	v_bfe_i32 v5, v2, 27, 1
	v_lshlrev_b32_e32 v3, 4, v2
	v_lshrrev_b32_e32 v5, 22, v5
	v_add_u32_e32 v5, v3, v5
	v_and_b32_e32 v5, 0xfffffc00, v5
	v_sub_u32_e32 v5, v3, v5
	s_waitcnt vmcnt(1)
	v_lshrrev_b32_e32 v6, 4, v5
	v_ashrrev_i32_e32 v4, 31, v2
	v_bitop3_b32 v5, v6, v5, 32 bitop3:0x6c
	v_lshrrev_b32_e32 v4, 26, v4
	v_ashrrev_i32_e32 v7, 31, v5
	v_add_u32_e32 v4, v2, v4
	v_lshrrev_b32_e32 v7, 26, v7
	v_ashrrev_i32_e32 v4, 6, v4
	v_add_u32_e32 v7, v5, v7
	v_lshlrev_b32_e32 v6, 3, v4
	v_lshrrev_b32_e32 v8, 6, v7
	v_and_b32_e32 v7, 0xc0, v7
	v_and_b32_e32 v6, 0x1ffff0, v6
	v_lshlrev_b32_e32 v4, 5, v4
	v_sub_u32_e32 v5, v5, v7
	v_mov_b32_e32 v7, 1
	v_add_u32_e32 v6, v8, v6
	v_and_b32_e32 v4, 32, v4
	v_ashrrev_i16_sdwa v5, v7, sext(v5) dst_sel:DWORD dst_unused:UNUSED_PAD src0_sel:DWORD src1_sel:BYTE_0
	v_bfe_i32 v5, v5, 0, 16
	v_lshl_or_b32 v4, v6, 10, v4
	v_add_u32_e32 v3, 0x2000, v3
	v_add_lshl_u32 v158, v4, v5, 1
	v_ashrrev_i32_e32 v4, 31, v3
	v_lshrrev_b32_e32 v4, 22, v4
	v_add_u32_e32 v4, v3, v4
	v_ashrrev_i32_e32 v4, 10, v4
	v_mul_i32_i24_e32 v5, 0x400, v4
	v_sub_u32_e32 v3, v3, v5
	v_lshrrev_b32_e32 v5, 4, v3
	v_bitop3_b32 v3, v5, v3, 32 bitop3:0x6c
	v_ashrrev_i32_e32 v6, 31, v3
	v_lshrrev_b32_e32 v6, 26, v6
	v_add_u32_e32 v6, v3, v6
	v_lshlrev_b32_e32 v5, 3, v4
	v_lshrrev_b32_e32 v8, 6, v6
	v_and_b32_e32 v6, 0xc0, v6
	v_and_b32_e32 v5, 0x1ffff0, v5
	v_lshlrev_b32_e32 v4, 5, v4
	v_sub_u32_e32 v3, v3, v6
	v_add_u32_e32 v5, v8, v5
	v_and_b32_e32 v4, 32, v4
	v_ashrrev_i16_sdwa v3, v7, sext(v3) dst_sel:DWORD dst_unused:UNUSED_PAD src0_sel:DWORD src1_sel:BYTE_0
	v_bfe_i32 v3, v3, 0, 16
	v_lshl_or_b32 v4, v5, 10, v4
	s_add_u32 s51, s94, 0x51000000
	v_add_lshl_u32 v159, v4, v3, 1
	v_mov_b32_e32 v3, v0
	s_addc_u32 s52, s95, 0
	s_add_u32 s53, s94, 0x3200000
	v_ashrrev_i32_e32 v5, 31, v3
	v_lshrrev_b32_e32 v5, 26, v5
	s_addc_u32 s54, s95, 0
	s_lshl_b32 s0, s6, 10
	v_lshlrev_b32_e32 v4, 4, v3
	v_add_u32_e32 v5, v3, v5
	v_bfe_i32 v3, v3, 27, 1
	s_ashr_i32 s7, s1, 8
	s_add_i32 s55, s0, 0
	v_lshrrev_b32_e32 v3, 22, v3
	s_and_b64 s[14:15], s[10:11], exec
	v_add_u32_e32 v3, v4, v3
	s_cselect_b32 s0, s50, s49
	v_and_b32_e32 v3, 0xfffffc00, v3
	s_add_i32 s0, s0, s48
	v_sub_u32_e32 v3, v4, v3
	s_ashr_i32 s14, s0, 31
	v_lshrrev_b32_e32 v6, 4, v3
	s_lshr_b32 s14, s14, 27
	v_bitop3_b32 v3, v6, v3, 32 bitop3:0x6c
	s_add_i32 s14, s0, s14
	v_ashrrev_i32_e32 v8, 31, v3
	s_ashr_i32 s15, s14, 5
	s_andn2_b32 s14, s14, 31
	v_lshrrev_b32_e32 v8, 26, v8
	s_sub_i32 s14, s0, s14
	v_add_u32_e32 v8, v3, v8
	s_bfe_i32 s0, s14, 0x80000
	v_ashrrev_i32_e32 v5, 6, v5
	v_ashrrev_i32_e32 v9, 6, v8
	v_and_b32_e32 v8, 0xc0, v8
	s_bfe_u32 s0, s0, 0x2000d
	v_lshlrev_b32_e32 v6, 3, v5
	v_lshlrev_b32_e32 v5, 5, v5
	v_sub_u32_e32 v3, v3, v8
	s_add_i32 s16, s14, s0
	v_and_b32_e32 v5, 32, v5
	v_ashrrev_i16_sdwa v3, v7, sext(v3) dst_sel:DWORD dst_unused:UNUSED_PAD src0_sel:DWORD src1_sel:BYTE_0
	v_add_u32_e32 v4, 0x2000, v4
	s_bfe_i32 s0, s16, 0x80000
	s_and_b32 s16, s16, 0xfc
	v_add_u32_sdwa v3, v5, sext(v3) dst_sel:DWORD dst_unused:UNUSED_PAD src0_sel:DWORD src1_sel:WORD_0
	v_ashrrev_i32_e32 v5, 31, v4
	s_sub_i32 s14, s14, s16
	v_lshrrev_b32_e32 v5, 22, v5
	s_lshl_b32 s15, s15, 2
	s_sext_i32_i8 s14, s14
	v_add_u32_e32 v5, v4, v5
	s_add_i32 s36, s15, s14
	v_ashrrev_i32_e32 v5, 10, v5
	s_sext_i32_i16 s0, s0
	v_mul_i32_i24_e32 v8, 0x400, v5
	s_ashr_i32 s37, s36, 31
	s_lshr_b32 s0, s0, 2
	v_sub_u32_e32 v4, v4, v8
	s_lshl_b64 s[14:15], s[36:37], 19
	v_lshrrev_b32_e32 v8, 4, v4
	s_add_u32 s38, s51, s14
	v_and_b32_e32 v6, -16, v6
	v_bitop3_b32 v4, v8, v4, 32 bitop3:0x6c
	s_addc_u32 s39, s52, s15
	s_bfe_i64 s[14:15], s[0:1], 0x100000
	v_add_u32_e32 v6, v9, v6
	v_ashrrev_i32_e32 v9, 31, v4
	s_lshl_b64 s[14:15], s[14:15], 19
	v_lshrrev_b32_e32 v9, 26, v9
	s_add_u32 s40, s53, s14
	v_add_u32_e32 v9, v4, v9
	s_addc_u32 s41, s54, s15
	s_add_i32 s37, s55, 0x10000
	s_mov_b32 m0, s37
	s_nop 0
	global_load_lds_dwordx4 v158, s[40:41]
	v_ashrrev_i32_e32 v10, 6, v9
	v_and_b32_e32 v9, 0xc0, v9
	s_add_i32 s56, s55, 0x12000
	s_mov_b32 m0, s56
	s_nop 0
	global_load_lds_dwordx4 v159, s[40:41]
	v_lshlrev_b32_e32 v8, 3, v5
	v_lshlrev_b32_e32 v5, 5, v5
	v_sub_u32_e32 v4, v4, v9
	s_add_u32 s14, s40, 0x40000
	v_and_b32_e32 v8, -16, v8
	v_and_b32_e32 v5, 32, v5
	v_ashrrev_i16_sdwa v4, v7, sext(v4) dst_sel:DWORD dst_unused:UNUSED_PAD src0_sel:DWORD src1_sel:BYTE_0
	s_addc_u32 s15, s41, 0
	s_add_i32 s57, s55, 0x14000
	s_mov_b32 m0, s57
	s_nop 0
	global_load_lds_dwordx4 v158, s[14:15]
	v_add_u32_e32 v8, v10, v8
	v_add_u32_sdwa v4, v5, sext(v4) dst_sel:DWORD dst_unused:UNUSED_PAD src0_sel:DWORD src1_sel:WORD_0
	v_lshl_add_u32 v5, v6, 10, v3
	v_lshlrev_b32_e32 v6, 11, v6
	s_add_i32 s58, s55, 0x16000
	s_mov_b32 m0, s58
	s_nop 0
	global_load_lds_dwordx4 v159, s[14:15]
	v_lshl_add_u32 v160, v3, 1, v6
	v_lshlrev_b32_e32 v3, 11, v8
	s_mov_b32 m0, s55
	s_nop 0
	global_load_lds_dwordx4 v160, s[38:39]
	v_lshl_add_u32 v161, v4, 1, v3
	v_mov_b32_e32 v3, 0x40000
	s_add_i32 s59, s55, 0x2000
	s_mov_b32 m0, s59
	s_nop 0
	global_load_lds_dwordx4 v161, s[38:39]
	v_lshl_add_u32 v7, v8, 10, v4
	v_lshl_add_u32 v162, v5, 1, v3
	s_add_i32 s60, s55, 0x4000
	s_mov_b32 m0, s60
	s_nop 0
	global_load_lds_dwordx4 v162, s[38:39]
	v_lshl_add_u32 v163, v7, 1, v3
	s_add_i32 s61, s55, 0x6000
	s_mov_b32 m0, s61
	s_nop 0
	global_load_lds_dwordx4 v163, s[38:39]
	s_cmp_eq_u32 s7, 1
	s_cselect_b64 s[14:15], -1, 0
	s_cmp_lg_u32 s7, 1
	s_cbranch_scc1 .LBB0_563
	s_barrier
; #define PG8_STAGEB(bufoff, gbase) PG8_STAGE2(bufoff, gbase, voffB[0], voffB[1])
; #define PG8_STAGEA(bufoff, gbase, h) PG8_STAGE2(bufoff, gbase, voffA[h][0], voffA[h][1])
; #define PG8_WAIT_V(n) asm volatile("s_waitcnt vmcnt(" #n ")" ::: "memory")
; #define PG8_BAR __builtin_amdgcn_s_barrier()
;     ...
;     if (wr == 1) PG8_BAR;
;     if constexpr (HM) PG8_WAIT_V(0); else PG8_WAIT_V(2);
;     PG8_BAR;
;     PG8_STAGEB(PG8_SB(1, 0), cB + kstep); PG8_STAGEA(PG8_SA(1, 0), cA + kstep, 0); PG8_STAGEB(PG8_SB(1, 1), cB + hstepB + kstep);
;     PG8_WAIT_V(6); PG8_BAR;
.LBB0_563:
	v_lshrrev_b32_e32 v4, 1, v2
	v_and_b32_e32 v4, 24, v4
	s_add_u32 s16, s94, 0x48600000
	v_and_b32_e32 v3, 15, v2
	v_lshlrev_b32_e32 v5, 1, v4
	v_lshlrev_b32_e32 v2, 2, v2
	s_sext_i32_i8 s71, s0
	s_addc_u32 s17, s95, 0
	v_lshl_or_b32 v164, s7, 6, v3
	v_lshl_or_b32 v3, v3, 6, v5
	s_lshl_b32 s0, s7, 13
	v_and_b32_e32 v2, 32, v2
	v_bitop3_b32 v5, v3, s0, v2 bitop3:0xde
	s_lshl_b32 s0, s6, 5
	s_and_b32 s0, s0, 0x60
	s_lshl_b32 s6, s0, 7
	v_bitop3_b32 v2, v3, s6, v2 bitop3:0xde
	s_add_u32 s6, s40, 0x80
	s_waitcnt vmcnt(2)
	s_barrier
	s_addc_u32 s7, s41, 0
	s_add_i32 s62, s55, 0x18000
	s_mov_b32 m0, s62
	s_nop 0
	global_load_lds_dwordx4 v158, s[6:7]
	s_add_i32 s63, s55, 0x1a000
	s_mov_b32 m0, s63
	s_nop 0
	global_load_lds_dwordx4 v159, s[6:7]
	s_add_u32 s6, s38, 0x80
	s_addc_u32 s7, s39, 0
	s_add_i32 s64, s55, 0x8000
	s_mov_b32 m0, s64
	s_nop 0
	global_load_lds_dwordx4 v160, s[6:7]
	s_add_i32 s65, s55, 0xa000
	s_mov_b32 m0, s65
	s_nop 0
	global_load_lds_dwordx4 v161, s[6:7]
	s_add_u32 s6, s40, 0x40080
	s_addc_u32 s7, s41, 0
	s_add_i32 s66, s55, 0x1c000
	s_mov_b32 m0, s66
	s_nop 0
	global_load_lds_dwordx4 v158, s[6:7]
	s_add_i32 s67, s55, 0x1e000
	s_mov_b32 m0, s67
	s_nop 0
	global_load_lds_dwordx4 v159, s[6:7]
	s_waitcnt vmcnt(6)
	s_add_i32 s68, s55, 0xc000
	s_add_i32 s69, s55, 0xe000
	s_cmpk_lt_u32 s1, 0x100
	v_add_u32_e32 v166, 0, v2
	s_mov_b32 s42, 0
	s_cselect_b64 s[18:19], -1, 0
	v_or_b32_e32 v165, s0, v4
	v_mov_b64_e32 v[146:147], 0x200
	v_mov_b64_e32 v[148:149], 0x1ff
	v_add_u32_e32 v167, 0x10000, v166
	v_add_u32_e32 v168, 0x14000, v166
	v_add_u32_e32 v169, 0, v5
	s_mov_b64 s[20:21], 0x80000
	s_mov_b64 s[22:23], 0x90000
	s_mov_b64 s[24:25], 0xa0000
	s_mov_b64 s[26:27], 0xb0000
	s_barrier
	s_branch .LBB0_566

; #define LAS __attribute__((address_space(3)))
; #define PG8_STAGEA(bufoff, gbase, h) PG8_STAGE2(bufoff, gbase, voffA[h][0], voffA[h][1])
; #define PG8_LDA(dst, b, h) do { _Pragma("unroll") for (int m = 0; m < 4; ++m) _Pragma("unroll") for (int k = 0; k < 2; ++k) dst[m][k] = *(const LAS bf16x8*)(lds + PG8_SA(b, h) + aoff + m * 2048 + k * 1024); } while (0)
; #define PG8_LDB(dst, b, h) do { _Pragma("unroll") for (int n = 0; n < 2; ++n) _Pragma("unroll") for (int k = 0; k < 2; ++k) dst[n][k] = *(const LAS bf16x8*)(lds + PG8_SB(b, h) + boff + n * 2048 + k * 1024); } while (0)
; #define PG8_WAIT_K0() do { if (EST > 0 && t == 0 && ui > 0) asm volatile("s_waitcnt vmcnt(%0)" :: "n"((HM ? 6 : 8) + EST) : "memory"); else PG8_WAIT_K(); } while (0)
; #define PG8_WAIT_L(n) asm volatile("s_waitcnt lgkmcnt(" #n ")" ::: "memory")
; #define PG8_BAR __builtin_amdgcn_s_barrier()
; #define PG8_SCHED __builtin_amdgcn_sched_barrier(0)
;     ...
;             PG8_LDB(B0, 0, 0); PG8_LDB(B1, 0, 1); PG8_SCHED; PG8_LDA(At, 0, 0); if constexpr (!HM) PG8_STAGEA(PG8_SA(1, 1), a1, 1);
;             if constexpr (Sched::kGather) { if (last && has_next) { const u32x4 tn = *(const LAS u32x4*)(S.aux + tid * 16); voffA[0][0] = tn.x; voffA[0][1] = tn.y; voffA[1][0] = tn.z; voffA[1][1] = tn.w; } }
;             PG8_WAIT_K0(); PG8_WAIT_L(0); PG8_BAR; PG8_MMA(0, 0, At, B0); PG8_MMA(0, 1, At, B1); PG8_BAR; PG8_SCHED;
.LBB0_574:
	ds_read_b128 v[18:21], v167
	ds_read_b128 v[22:25], v167 offset:1024
	ds_read_b128 v[26:29], v167 offset:2048
	ds_read_b128 v[30:33], v167 offset:3072
	ds_read_b128 v[2:5], v168
	ds_read_b128 v[6:9], v168 offset:1024
	ds_read_b128 v[10:13], v168 offset:2048
	s_waitcnt vmcnt(0)
	ds_read_b128 v[14:17], v168 offset:3072
	s_cmp_lg_u32 s42, 0
	s_cselect_b64 s[42:43], -1, 0
	s_add_u32 s44, s38, 0x80
	s_addc_u32 s45, s39, 0
	ds_read_b128 v[74:77], v169
	ds_read_b128 v[78:81], v169 offset:1024
	ds_read_b128 v[82:85], v169 offset:2048
	ds_read_b128 v[90:93], v169 offset:3072
	ds_read_b128 v[94:97], v169 offset:4096
	ds_read_b128 v[98:101], v169 offset:5120
	ds_read_b128 v[70:73], v169 offset:6144
	ds_read_b128 v[86:89], v169 offset:7168
	s_mov_b32 m0, s68
	s_nop 0
	global_load_lds_dwordx4 v162, s[44:45]
	s_and_b64 vcc, exec, s[42:43]
	s_mov_b32 m0, s69
	s_nop 0
	global_load_lds_dwordx4 v163, s[44:45]
	s_cbranch_vccz .LBB0_587
	s_waitcnt vmcnt(24)
	s_cbranch_execnz .LBB0_577

; #define PG8_STAGEB(bufoff, gbase) PG8_STAGE2(bufoff, gbase, voffB[0], voffB[1])
; #define PG8_STAGEAS(bufoff, gbase, h) PG8_STAGE2(bufoff, gbase, voffA[h][0], voffA[h][1])
; #define PG8_LDA(dst, b, h) do { _Pragma("unroll") for (int m = 0; m < 4; ++m) _Pragma("unroll") for (int k = 0; k < 2; ++k) dst[m][k] = *(const LAS bf16x8*)(lds + PG8_SA(b, h) + aoff + m * 2048 + k * 1024); } while (0)
; #define PG8_WAIT_K0() do { if (EST > 0 && t == 0 && ui > 0) asm volatile("s_waitcnt vmcnt(%0)" :: "n"((HM ? 6 : 8) + EST) : "memory"); else PG8_WAIT_K(); } while (0)
; #define PG8_WAIT_L(n) asm volatile("s_waitcnt lgkmcnt(" #n ")" ::: "memory")
; #define PG8_BAR __builtin_amdgcn_s_barrier()
; #define PG8_SCHED __builtin_amdgcn_sched_barrier(0)
;     ...
;             PG8_WAIT_K0(); PG8_WAIT_L(0); PG8_BAR; PG8_MMA(0, 0, At, B0); PG8_MMA(0, 1, At, B1); PG8_BAR; PG8_SCHED;
;             if constexpr (!HM) PG8_LDA(At, 0, 1);
;             PG8_STAGEB(PG8_SB(0, 0), b2); PG8_STAGEB(PG8_SB(0, 1), b2 + hstepB); PG8_STAGEAS(PG8_SA(0, 0), a2, 0);
;             PG8_WAIT_K0(); PG8_WAIT_L(0); PG8_BAR; if constexpr (!HM) { PG8_MMA(1, 0, At, B0); PG8_MMA(1, 1, At, B1); } PG8_BAR; PG8_SCHED;
.LBB0_577:
	s_add_u32 s44, s38, 0x100
	s_waitcnt lgkmcnt(0)
	s_addc_u32 s45, s39, 0
	s_add_u32 s46, s40, 0x100
	s_addc_u32 s47, s41, 0
	s_barrier
	s_setprio 1
	s_waitcnt lgkmcnt(7)
	v_mfma_f32_16x16x32_bf16 v[34:37], v[18:21], v[74:77], 0
	v_mfma_f32_16x16x32_bf16 v[38:41], v[26:29], v[74:77], 0
	s_waitcnt lgkmcnt(5)
	v_mfma_f32_16x16x32_bf16 v[42:45], v[18:21], v[82:85], 0
	v_mfma_f32_16x16x32_bf16 v[46:49], v[26:29], v[82:85], 0
	s_waitcnt lgkmcnt(3)
	v_mfma_f32_16x16x32_bf16 v[50:53], v[18:21], v[94:97], 0
	v_mfma_f32_16x16x32_bf16 v[54:57], v[26:29], v[94:97], 0
	s_waitcnt lgkmcnt(1)
	v_mfma_f32_16x16x32_bf16 v[58:61], v[18:21], v[70:73], 0
	v_mfma_f32_16x16x32_bf16 v[62:65], v[26:29], v[70:73], 0
	v_mfma_f32_16x16x32_bf16 v[34:37], v[22:25], v[78:81], v[34:37]
	v_mfma_f32_16x16x32_bf16 v[38:41], v[30:33], v[78:81], v[38:41]
	v_mfma_f32_16x16x32_bf16 v[42:45], v[22:25], v[90:93], v[42:45]
	v_mfma_f32_16x16x32_bf16 v[46:49], v[30:33], v[90:93], v[46:49]
	v_mfma_f32_16x16x32_bf16 v[50:53], v[22:25], v[98:101], v[50:53]
	v_mfma_f32_16x16x32_bf16 v[54:57], v[30:33], v[98:101], v[54:57]
	s_waitcnt lgkmcnt(0)
	v_mfma_f32_16x16x32_bf16 v[58:61], v[22:25], v[86:89], v[58:61]
	v_mfma_f32_16x16x32_bf16 v[62:65], v[30:33], v[86:89], v[62:65]
	s_setprio 0
	s_setprio 1
	v_mfma_f32_16x16x32_bf16 v[66:69], v[2:5], v[74:77], 0
	v_mfma_f32_16x16x32_bf16 v[74:77], v[10:13], v[74:77], 0
	v_mfma_f32_16x16x32_bf16 v[66:69], v[6:9], v[78:81], v[66:69]
	v_mfma_f32_16x16x32_bf16 v[74:77], v[14:17], v[78:81], v[74:77]
	v_mfma_f32_16x16x32_bf16 v[78:81], v[2:5], v[82:85], 0
	v_mfma_f32_16x16x32_bf16 v[82:85], v[10:13], v[82:85], 0
	v_mfma_f32_16x16x32_bf16 v[78:81], v[6:9], v[90:93], v[78:81]
	v_mfma_f32_16x16x32_bf16 v[82:85], v[14:17], v[90:93], v[82:85]
	v_mfma_f32_16x16x32_bf16 v[90:93], v[2:5], v[94:97], 0
	v_mfma_f32_16x16x32_bf16 v[94:97], v[10:13], v[94:97], 0
	v_mfma_f32_16x16x32_bf16 v[130:133], v[14:17], v[98:101], v[94:97]
	v_mfma_f32_16x16x32_bf16 v[94:97], v[2:5], v[70:73], 0
	v_mfma_f32_16x16x32_bf16 v[70:73], v[10:13], v[70:73], 0
	v_mfma_f32_16x16x32_bf16 v[90:93], v[6:9], v[98:101], v[90:93]
	v_mfma_f32_16x16x32_bf16 v[134:137], v[6:9], v[86:89], v[94:97]
	v_mfma_f32_16x16x32_bf16 v[138:141], v[14:17], v[86:89], v[70:73]
	s_setprio 0
	s_barrier
	ds_read_b128 v[110:113], v169 offset:16384
	ds_read_b128 v[114:117], v169 offset:17408
	ds_read_b128 v[102:105], v169 offset:18432
	ds_read_b128 v[106:109], v169 offset:19456
	ds_read_b128 v[94:97], v169 offset:20480
	ds_read_b128 v[98:101], v169 offset:21504
	ds_read_b128 v[70:73], v169 offset:22528
	ds_read_b128 v[86:89], v169 offset:23552
	s_mov_b32 m0, s37
	s_nop 0
	global_load_lds_dwordx4 v158, s[46:47]
	s_mov_b32 m0, s56
	s_nop 0
	global_load_lds_dwordx4 v159, s[46:47]
	s_add_u32 s46, s40, 0x40100
	s_addc_u32 s47, s41, 0
	s_mov_b32 m0, s57
	s_nop 0
	global_load_lds_dwordx4 v158, s[46:47]
	s_and_b64 vcc, exec, s[42:43]
	s_mov_b32 m0, s58
	s_nop 0
	global_load_lds_dwordx4 v159, s[46:47]
	s_mov_b32 m0, s55
	s_nop 0
	global_load_lds_dwordx4 v160, s[44:45]
	s_mov_b32 m0, s59
	s_nop 0
	global_load_lds_dwordx4 v161, s[44:45]
	s_cbranch_vccz .LBB0_588
	s_waitcnt vmcnt(24)
	s_cbranch_execnz .LBB0_580

; #define PG8_STAGEAS(bufoff, gbase, h) PG8_STAGE2(bufoff, gbase, voffA[h][0], voffA[h][1])
; #define PG8_LDA(dst, b, h) do { _Pragma("unroll") for (int m = 0; m < 4; ++m) _Pragma("unroll") for (int k = 0; k < 2; ++k) dst[m][k] = *(const LAS bf16x8*)(lds + PG8_SA(b, h) + aoff + m * 2048 + k * 1024); } while (0)
; #define PG8_LDB(dst, b, h) do { _Pragma("unroll") for (int n = 0; n < 2; ++n) _Pragma("unroll") for (int k = 0; k < 2; ++k) dst[n][k] = *(const LAS bf16x8*)(lds + PG8_SB(b, h) + boff + n * 2048 + k * 1024); } while (0)
; #define PG8_WAIT_K() do { if constexpr (HM) PG8_WAIT_V(6); else PG8_WAIT_V(8); } while (0)
; #define PG8_WAIT_K0() do { if (EST > 0 && t == 0 && ui > 0) asm volatile("s_waitcnt vmcnt(%0)" :: "n"((HM ? 6 : 8) + EST) : "memory"); else PG8_WAIT_K(); } while (0)
; #define PG8_WAIT_L(n) asm volatile("s_waitcnt lgkmcnt(" #n ")" ::: "memory")
; #define PG8_BAR __builtin_amdgcn_s_barrier()
; #define PG8_SCHED __builtin_amdgcn_sched_barrier(0)
;     ...
;             PG8_WAIT_K0(); PG8_WAIT_L(0); PG8_BAR; if constexpr (!HM) { PG8_MMA(1, 0, At, B0); PG8_MMA(1, 1, At, B1); } PG8_BAR; PG8_SCHED;
;             PG8_LDB(B0, 1, 0); PG8_LDB(B1, 1, 1); PG8_SCHED; PG8_LDA(At, 1, 0); if constexpr (!HM) PG8_STAGEAS(PG8_SA(0, 1), a2, 1);
;             PG8_WAIT_K(); PG8_WAIT_L(0); PG8_BAR; PG8_MMA(0, 0, At, B0); PG8_MMA(0, 1, At, B1); PG8_BAR; PG8_SCHED;
;             if constexpr (!HM) PG8_LDA(At, 1, 1);
.LBB0_580:
	s_add_u32 s42, s38, 0x180
	s_waitcnt lgkmcnt(0)
	s_addc_u32 s43, s39, 0
	s_add_u32 s46, s40, 0x180
	s_addc_u32 s47, s41, 0
	s_barrier
	s_setprio 1
	s_waitcnt lgkmcnt(7)
	v_mfma_f32_16x16x32_bf16 v[118:121], v[18:21], v[110:113], 0
	s_waitcnt lgkmcnt(6)
	v_mfma_f32_16x16x32_bf16 v[150:153], v[22:25], v[114:117], v[118:121]
	v_mfma_f32_16x16x32_bf16 v[118:121], v[26:29], v[110:113], 0
	v_mfma_f32_16x16x32_bf16 v[154:157], v[30:33], v[114:117], v[118:121]
	s_waitcnt lgkmcnt(5)
	v_mfma_f32_16x16x32_bf16 v[118:121], v[18:21], v[102:105], 0
	s_waitcnt lgkmcnt(4)
	v_mfma_f32_16x16x32_bf16 v[170:173], v[22:25], v[106:109], v[118:121]
	v_mfma_f32_16x16x32_bf16 v[118:121], v[26:29], v[102:105], 0
	v_mfma_f32_16x16x32_bf16 v[174:177], v[30:33], v[106:109], v[118:121]
	s_waitcnt lgkmcnt(3)
	v_mfma_f32_16x16x32_bf16 v[118:121], v[18:21], v[94:97], 0
	s_waitcnt lgkmcnt(1)
	v_mfma_f32_16x16x32_bf16 v[18:21], v[18:21], v[70:73], 0
	v_mfma_f32_16x16x32_bf16 v[178:181], v[22:25], v[98:101], v[118:121]
	s_waitcnt lgkmcnt(0)
	v_mfma_f32_16x16x32_bf16 v[18:21], v[22:25], v[86:89], v[18:21]
	v_mfma_f32_16x16x32_bf16 v[22:25], v[26:29], v[70:73], 0
	v_mfma_f32_16x16x32_bf16 v[118:121], v[26:29], v[94:97], 0
	v_mfma_f32_16x16x32_bf16 v[22:25], v[30:33], v[86:89], v[22:25]
	v_mfma_f32_16x16x32_bf16 v[182:185], v[30:33], v[98:101], v[118:121]
	s_setprio 0
	s_setprio 1
	v_mfma_f32_16x16x32_bf16 v[26:29], v[2:5], v[110:113], 0
	v_mfma_f32_16x16x32_bf16 v[186:189], v[6:9], v[114:117], v[26:29]
	v_mfma_f32_16x16x32_bf16 v[26:29], v[10:13], v[110:113], 0
	v_mfma_f32_16x16x32_bf16 v[190:193], v[14:17], v[114:117], v[26:29]
	v_mfma_f32_16x16x32_bf16 v[26:29], v[2:5], v[102:105], 0
	v_mfma_f32_16x16x32_bf16 v[194:197], v[6:9], v[106:109], v[26:29]
	v_mfma_f32_16x16x32_bf16 v[26:29], v[10:13], v[102:105], 0
	v_mfma_f32_16x16x32_bf16 v[198:201], v[14:17], v[106:109], v[26:29]
	v_mfma_f32_16x16x32_bf16 v[26:29], v[2:5], v[94:97], 0
	v_mfma_f32_16x16x32_bf16 v[2:5], v[2:5], v[70:73], 0
	v_mfma_f32_16x16x32_bf16 v[202:205], v[6:9], v[98:101], v[26:29]
	v_mfma_f32_16x16x32_bf16 v[26:29], v[10:13], v[94:97], 0
	v_mfma_f32_16x16x32_bf16 v[2:5], v[6:9], v[86:89], v[2:5]
	v_mfma_f32_16x16x32_bf16 v[6:9], v[10:13], v[70:73], 0
	v_mfma_f32_16x16x32_bf16 v[206:209], v[14:17], v[98:101], v[26:29]
	v_mfma_f32_16x16x32_bf16 v[210:213], v[14:17], v[86:89], v[6:9]
	s_setprio 0
	s_barrier
	v_add_u32_e32 v142, 0x18000, v166
	v_add_u32_e32 v143, 0x1c000, v166
	s_nop 1
	ds_read_b128 v[6:9], v142
	ds_read_b128 v[10:13], v142 offset:1024
	ds_read_b128 v[214:217], v142 offset:2048
	ds_read_b128 v[218:221], v142 offset:3072
	ds_read_b128 v[222:225], v143
	ds_read_b128 v[226:229], v143 offset:1024
	ds_read_b128 v[230:233], v143 offset:2048
	ds_read_b128 v[234:237], v143 offset:3072
	ds_read_b128 v[14:17], v169 offset:32768
	ds_read_b128 v[26:29], v169 offset:33792
	ds_read_b128 v[30:33], v169 offset:34816
	ds_read_b128 v[98:101], v169 offset:35840
	ds_read_b128 v[238:241], v169 offset:36864
	ds_read_b128 v[242:245], v169 offset:37888
	ds_read_b128 v[246:249], v169 offset:38912
	ds_read_b128 v[250:253], v169 offset:39936
	s_mov_b32 m0, s60
	s_nop 0
	global_load_lds_dwordx4 v162, s[44:45]
	s_mov_b32 m0, s61
	s_nop 0
	global_load_lds_dwordx4 v163, s[44:45]
	s_waitcnt vmcnt(8)
	s_waitcnt lgkmcnt(0)
	s_barrier
	s_setprio 1
	s_waitcnt lgkmcnt(7)
	v_mfma_f32_16x16x32_bf16 v[34:37], v[6:9], v[14:17], v[34:37]
	s_waitcnt lgkmcnt(6)
	v_mfma_f32_16x16x32_bf16 v[114:117], v[10:13], v[26:29], v[34:37]
	v_mfma_f32_16x16x32_bf16 v[34:37], v[214:217], v[14:17], v[38:41]
	v_mfma_f32_16x16x32_bf16 v[110:113], v[218:221], v[26:29], v[34:37]
	s_waitcnt lgkmcnt(5)
	v_mfma_f32_16x16x32_bf16 v[34:37], v[6:9], v[30:33], v[42:45]
	s_waitcnt lgkmcnt(4)
	v_mfma_f32_16x16x32_bf16 v[106:109], v[10:13], v[98:101], v[34:37]
	v_mfma_f32_16x16x32_bf16 v[34:37], v[214:217], v[30:33], v[46:49]
	v_mfma_f32_16x16x32_bf16 v[102:105], v[218:221], v[98:101], v[34:37]
	s_waitcnt lgkmcnt(3)
	v_mfma_f32_16x16x32_bf16 v[34:37], v[6:9], v[238:241], v[50:53]
	s_waitcnt lgkmcnt(2)
	v_mfma_f32_16x16x32_bf16 v[94:97], v[10:13], v[242:245], v[34:37]
	v_mfma_f32_16x16x32_bf16 v[34:37], v[214:217], v[238:241], v[54:57]
	v_mfma_f32_16x16x32_bf16 v[86:89], v[218:221], v[242:245], v[34:37]
	s_waitcnt lgkmcnt(1)
	v_mfma_f32_16x16x32_bf16 v[34:37], v[6:9], v[246:249], v[58:61]
	s_waitcnt lgkmcnt(0)
	v_mfma_f32_16x16x32_bf16 v[70:73], v[10:13], v[250:253], v[34:37]
	v_mfma_f32_16x16x32_bf16 v[34:37], v[214:217], v[246:249], v[62:65]
	v_mfma_f32_16x16x32_bf16 v[58:61], v[218:221], v[250:253], v[34:37]
	s_setprio 0
	s_setprio 1
	v_mfma_f32_16x16x32_bf16 v[34:37], v[222:225], v[14:17], v[66:69]
	v_mfma_f32_16x16x32_bf16 v[14:17], v[230:233], v[14:17], v[74:77]
	v_mfma_f32_16x16x32_bf16 v[122:125], v[234:237], v[26:29], v[14:17]
	v_mfma_f32_16x16x32_bf16 v[14:17], v[222:225], v[30:33], v[78:81]
	v_mfma_f32_16x16x32_bf16 v[118:121], v[226:229], v[98:101], v[14:17]
	v_mfma_f32_16x16x32_bf16 v[14:17], v[230:233], v[30:33], v[82:85]
	v_mfma_f32_16x16x32_bf16 v[98:101], v[234:237], v[98:101], v[14:17]
	v_mfma_f32_16x16x32_bf16 v[14:17], v[222:225], v[238:241], v[90:93]
	v_mfma_f32_16x16x32_bf16 v[90:93], v[226:229], v[242:245], v[14:17]
	v_mfma_f32_16x16x32_bf16 v[14:17], v[230:233], v[238:241], v[130:133]
	v_mfma_f32_16x16x32_bf16 v[82:85], v[234:237], v[242:245], v[14:17]
	v_mfma_f32_16x16x32_bf16 v[14:17], v[222:225], v[246:249], v[134:137]
	v_mfma_f32_16x16x32_bf16 v[66:69], v[226:229], v[250:253], v[14:17]
	v_mfma_f32_16x16x32_bf16 v[14:17], v[230:233], v[246:249], v[138:141]
	v_mfma_f32_16x16x32_bf16 v[126:129], v[226:229], v[26:29], v[34:37]
	v_mfma_f32_16x16x32_bf16 v[54:57], v[234:237], v[250:253], v[14:17]
	s_setprio 0
	s_barrier
; #define LAS __attribute__((address_space(3)))
; #define PG8_STAGEB(bufoff, gbase) PG8_STAGE2(bufoff, gbase, voffB[0], voffB[1])
; #define PG8_STAGEA(bufoff, gbase, h) PG8_STAGE2(bufoff, gbase, voffA[h][0], voffA[h][1])
; #define PG8_STAGEAS(bufoff, gbase, h) PG8_STAGE2(bufoff, gbase, voffA[h][0], voffA[h][1])
; #define PG8_LDA(dst, b, h) do { _Pragma("unroll") for (int m = 0; m < 4; ++m) _Pragma("unroll") for (int k = 0; k < 2; ++k) dst[m][k] = *(const LAS bf16x8*)(lds + PG8_SA(b, h) + aoff + m * 2048 + k * 1024); } while (0)
; #define PG8_LDB(dst, b, h) do { _Pragma("unroll") for (int n = 0; n < 2; ++n) _Pragma("unroll") for (int k = 0; k < 2; ++k) dst[n][k] = *(const LAS bf16x8*)(lds + PG8_SB(b, h) + boff + n * 2048 + k * 1024); } while (0)
; #define PG8_WAIT_K() do { if constexpr (HM) PG8_WAIT_V(6); else PG8_WAIT_V(8); } while (0)
; #define PG8_WAIT_K0() do { if (EST > 0 && t == 0 && ui > 0) asm volatile("s_waitcnt vmcnt(%0)" :: "n"((HM ? 6 : 8) + EST) : "memory"); else PG8_WAIT_K(); } while (0)
; #define PG8_WAIT_L(n) asm volatile("s_waitcnt lgkmcnt(" #n ")" ::: "memory")
; #define PG8_BAR __builtin_amdgcn_s_barrier()
; #define PG8_SCHED __builtin_amdgcn_sched_barrier(0)
;     ...
;             const char* a1 = cA + (size_t)(t + 1) * kstep;
;             const char* a2 = last ? nA : cA + (size_t)(t + 2) * kstep; const char* b2 = last ? nB : cB + (size_t)(t + 2) * kstep;
;             const char* a3 = a2 + kstep; const char* b3 = b2 + kstep;
;             PG8_LDB(B0, 0, 0); PG8_LDB(B1, 0, 1); PG8_SCHED; PG8_LDA(At, 0, 0); if constexpr (!HM) PG8_STAGEA(PG8_SA(1, 1), a1, 1);
;             if constexpr (Sched::kGather) { if (last && has_next) { const u32x4 tn = *(const LAS u32x4*)(S.aux + tid * 16); voffA[0][0] = tn.x; voffA[0][1] = tn.y; voffA[1][0] = tn.z; voffA[1][1] = tn.w; } }
;             PG8_WAIT_K0(); PG8_WAIT_L(0); PG8_BAR; PG8_MMA(0, 0, At, B0); PG8_MMA(0, 1, At, B1); PG8_BAR; PG8_SCHED;
;     ...
;             PG8_STAGEB(PG8_SB(1, 0), b3); PG8_STAGEB(PG8_SB(1, 1), b3 + hstepB); PG8_STAGEAS(PG8_SA(1, 0), a3, 0);
;             PG8_WAIT_K(); PG8_WAIT_L(0); PG8_BAR; if constexpr (!HM) { PG8_MMA(1, 0, At, B0); PG8_MMA(1, 1, At, B1); } PG8_BAR; PG8_SCHED;
	ds_read_b128 v[34:37], v169 offset:49152
	ds_read_b128 v[38:41], v169 offset:50176
	ds_read_b128 v[130:133], v169 offset:51200
	ds_read_b128 v[134:137], v169 offset:52224
	ds_read_b128 v[138:141], v169 offset:53248
	ds_read_b128 v[238:241], v169 offset:54272
	ds_read_b128 v[242:245], v169 offset:55296
	ds_read_b128 v[246:249], v169 offset:56320
	s_mov_b32 m0, s62
	s_nop 0
	global_load_lds_dwordx4 v158, s[46:47]
	s_add_u32 s44, s40, 0x40180
	s_mov_b32 m0, s63
	s_nop 0
	global_load_lds_dwordx4 v159, s[46:47]
	s_addc_u32 s45, s41, 0
	s_mov_b32 m0, s66
	s_nop 0
	global_load_lds_dwordx4 v158, s[44:45]
	s_mov_b32 m0, s67
	s_nop 0
	global_load_lds_dwordx4 v159, s[44:45]
	s_mov_b32 m0, s64
	s_nop 0
	global_load_lds_dwordx4 v160, s[42:43]
	s_mov_b32 m0, s65
	s_nop 0
	global_load_lds_dwordx4 v161, s[42:43]
	s_waitcnt vmcnt(8)
	s_waitcnt lgkmcnt(0)
	s_barrier
	s_setprio 1
	s_waitcnt lgkmcnt(7)
	v_mfma_f32_16x16x32_bf16 v[14:17], v[6:9], v[34:37], v[150:153]
	s_waitcnt lgkmcnt(6)
	v_mfma_f32_16x16x32_bf16 v[78:81], v[10:13], v[38:41], v[14:17]
	v_mfma_f32_16x16x32_bf16 v[14:17], v[214:217], v[34:37], v[154:157]
	v_mfma_f32_16x16x32_bf16 v[74:77], v[218:221], v[38:41], v[14:17]
	s_waitcnt lgkmcnt(5)
	v_mfma_f32_16x16x32_bf16 v[14:17], v[6:9], v[130:133], v[170:173]
	s_waitcnt lgkmcnt(4)
	v_mfma_f32_16x16x32_bf16 v[46:49], v[10:13], v[134:137], v[14:17]
	v_mfma_f32_16x16x32_bf16 v[14:17], v[214:217], v[130:133], v[174:177]
	v_mfma_f32_16x16x32_bf16 v[42:45], v[218:221], v[134:137], v[14:17]
	s_waitcnt lgkmcnt(3)
	v_mfma_f32_16x16x32_bf16 v[14:17], v[6:9], v[138:141], v[178:181]
	s_waitcnt lgkmcnt(2)
	v_mfma_f32_16x16x32_bf16 v[30:33], v[10:13], v[238:241], v[14:17]
	v_mfma_f32_16x16x32_bf16 v[14:17], v[214:217], v[138:141], v[182:185]
	s_waitcnt lgkmcnt(1)
	v_mfma_f32_16x16x32_bf16 v[6:9], v[6:9], v[242:245], v[18:21]
	v_mfma_f32_16x16x32_bf16 v[26:29], v[218:221], v[238:241], v[14:17]
	s_waitcnt lgkmcnt(0)
	v_mfma_f32_16x16x32_bf16 v[14:17], v[10:13], v[246:249], v[6:9]
	v_mfma_f32_16x16x32_bf16 v[6:9], v[214:217], v[242:245], v[22:25]
	v_mfma_f32_16x16x32_bf16 v[10:13], v[218:221], v[246:249], v[6:9]
	s_setprio 0
	s_setprio 1
	v_mfma_f32_16x16x32_bf16 v[6:9], v[222:225], v[34:37], v[186:189]
	v_mfma_f32_16x16x32_bf16 v[62:65], v[226:229], v[38:41], v[6:9]
	v_mfma_f32_16x16x32_bf16 v[6:9], v[230:233], v[34:37], v[190:193]
	v_mfma_f32_16x16x32_bf16 v[50:53], v[234:237], v[38:41], v[6:9]
	v_mfma_f32_16x16x32_bf16 v[6:9], v[222:225], v[130:133], v[194:197]
	v_mfma_f32_16x16x32_bf16 v[38:41], v[226:229], v[134:137], v[6:9]
	v_mfma_f32_16x16x32_bf16 v[6:9], v[230:233], v[130:133], v[198:201]
	v_mfma_f32_16x16x32_bf16 v[34:37], v[234:237], v[134:137], v[6:9]
	v_mfma_f32_16x16x32_bf16 v[6:9], v[222:225], v[138:141], v[202:205]
	v_mfma_f32_16x16x32_bf16 v[22:25], v[226:229], v[238:241], v[6:9]
	v_mfma_f32_16x16x32_bf16 v[6:9], v[230:233], v[138:141], v[206:209]
	v_mfma_f32_16x16x32_bf16 v[2:5], v[222:225], v[242:245], v[2:5]
	v_mfma_f32_16x16x32_bf16 v[18:21], v[234:237], v[238:241], v[6:9]
	v_mfma_f32_16x16x32_bf16 v[6:9], v[226:229], v[246:249], v[2:5]
	v_mfma_f32_16x16x32_bf16 v[2:5], v[230:233], v[242:245], v[210:213]
	v_mfma_f32_16x16x32_bf16 v[2:5], v[234:237], v[246:249], v[2:5]
	s_setprio 0
	s_barrier
	s_add_u32 s29, s38, 0x200
	s_addc_u32 s31, s39, 0
	s_add_u32 s72, s40, 0x200
	s_addc_u32 s73, s41, 0
	s_mov_b32 s74, 0
.LBB0_581:
	ds_read_b128 v[130:133], v167
	ds_read_b128 v[134:137], v167 offset:1024
	ds_read_b128 v[138:141], v167 offset:2048
	ds_read_b128 v[150:153], v167 offset:3072
	ds_read_b128 v[154:157], v168
	ds_read_b128 v[170:173], v168 offset:1024
	ds_read_b128 v[174:177], v168 offset:2048
	ds_read_b128 v[178:181], v168 offset:3072
	s_cmp_eq_u32 s74, 12
	s_cselect_b32 s46, s0, s29
	s_cselect_b32 s47, s1, s31
	s_cselect_b32 s40, s34, s72
	s_cselect_b32 s41, s35, s73
	s_add_u32 s38, s46, 0x80
	s_addc_u32 s39, s47, 0
	ds_read_b128 v[182:185], v169
	ds_read_b128 v[186:189], v169 offset:1024
	ds_read_b128 v[190:193], v169 offset:2048
	ds_read_b128 v[194:197], v169 offset:3072
	ds_read_b128 v[198:201], v169 offset:4096
	ds_read_b128 v[202:205], v169 offset:5120
	ds_read_b128 v[206:209], v169 offset:6144
	ds_read_b128 v[210:213], v169 offset:7168
	s_mov_b32 m0, s68
	s_nop 0
	global_load_lds_dwordx4 v162, s[42:43]
	s_add_u32 s44, s40, 0x80
	s_mov_b32 m0, s69
	s_nop 0
	global_load_lds_dwordx4 v163, s[42:43]
	s_waitcnt vmcnt(8)
	s_waitcnt lgkmcnt(0)
	s_addc_u32 s45, s41, 0
	s_barrier
; #define PG8_STAGEB(bufoff, gbase) PG8_STAGE2(bufoff, gbase, voffB[0], voffB[1])
; #define PG8_STAGEAS(bufoff, gbase, h) PG8_STAGE2(bufoff, gbase, voffA[h][0], voffA[h][1])
; #define PG8_LDA(dst, b, h) do { _Pragma("unroll") for (int m = 0; m < 4; ++m) _Pragma("unroll") for (int k = 0; k < 2; ++k) dst[m][k] = *(const LAS bf16x8*)(lds + PG8_SA(b, h) + aoff + m * 2048 + k * 1024); } while (0)
; #define PG8_WAIT_K0() do { if (EST > 0 && t == 0 && ui > 0) asm volatile("s_waitcnt vmcnt(%0)" :: "n"((HM ? 6 : 8) + EST) : "memory"); else PG8_WAIT_K(); } while (0)
; #define PG8_WAIT_L(n) asm volatile("s_waitcnt lgkmcnt(" #n ")" ::: "memory")
; #define PG8_BAR __builtin_amdgcn_s_barrier()
; #define PG8_SCHED __builtin_amdgcn_sched_barrier(0)
;     ...
;             PG8_WAIT_K0(); PG8_WAIT_L(0); PG8_BAR; PG8_MMA(0, 0, At, B0); PG8_MMA(0, 1, At, B1); PG8_BAR; PG8_SCHED;
;             if constexpr (!HM) PG8_LDA(At, 0, 1);
;             PG8_STAGEB(PG8_SB(0, 0), b2); PG8_STAGEB(PG8_SB(0, 1), b2 + hstepB); PG8_STAGEAS(PG8_SA(0, 0), a2, 0);
;             PG8_WAIT_K0(); PG8_WAIT_L(0); PG8_BAR; if constexpr (!HM) { PG8_MMA(1, 0, At, B0); PG8_MMA(1, 1, At, B1); } PG8_BAR; PG8_SCHED;
	s_setprio 1
	s_waitcnt lgkmcnt(7)
	v_mfma_f32_16x16x32_bf16 v[114:117], v[130:133], v[182:185], v[114:117]
	v_mfma_f32_16x16x32_bf16 v[110:113], v[138:141], v[182:185], v[110:113]
	s_waitcnt lgkmcnt(5)
	v_mfma_f32_16x16x32_bf16 v[106:109], v[130:133], v[190:193], v[106:109]
	v_mfma_f32_16x16x32_bf16 v[102:105], v[138:141], v[190:193], v[102:105]
	s_waitcnt lgkmcnt(3)
	v_mfma_f32_16x16x32_bf16 v[94:97], v[130:133], v[198:201], v[94:97]
	v_mfma_f32_16x16x32_bf16 v[86:89], v[138:141], v[198:201], v[86:89]
	s_waitcnt lgkmcnt(1)
	v_mfma_f32_16x16x32_bf16 v[70:73], v[130:133], v[206:209], v[70:73]
	v_mfma_f32_16x16x32_bf16 v[58:61], v[138:141], v[206:209], v[58:61]
	v_mfma_f32_16x16x32_bf16 v[114:117], v[134:137], v[186:189], v[114:117]
	v_mfma_f32_16x16x32_bf16 v[110:113], v[150:153], v[186:189], v[110:113]
	v_mfma_f32_16x16x32_bf16 v[106:109], v[134:137], v[194:197], v[106:109]
	v_mfma_f32_16x16x32_bf16 v[102:105], v[150:153], v[194:197], v[102:105]
	v_mfma_f32_16x16x32_bf16 v[94:97], v[134:137], v[202:205], v[94:97]
	v_mfma_f32_16x16x32_bf16 v[86:89], v[150:153], v[202:205], v[86:89]
	s_waitcnt lgkmcnt(0)
	v_mfma_f32_16x16x32_bf16 v[70:73], v[134:137], v[210:213], v[70:73]
	v_mfma_f32_16x16x32_bf16 v[58:61], v[150:153], v[210:213], v[58:61]
	s_setprio 0
	s_setprio 1
	v_mfma_f32_16x16x32_bf16 v[126:129], v[154:157], v[182:185], v[126:129]
	v_mfma_f32_16x16x32_bf16 v[122:125], v[174:177], v[182:185], v[122:125]
	v_mfma_f32_16x16x32_bf16 v[118:121], v[154:157], v[190:193], v[118:121]
	v_mfma_f32_16x16x32_bf16 v[98:101], v[174:177], v[190:193], v[98:101]
	v_mfma_f32_16x16x32_bf16 v[90:93], v[154:157], v[198:201], v[90:93]
	v_mfma_f32_16x16x32_bf16 v[82:85], v[174:177], v[198:201], v[82:85]
	v_mfma_f32_16x16x32_bf16 v[66:69], v[154:157], v[206:209], v[66:69]
	v_mfma_f32_16x16x32_bf16 v[54:57], v[174:177], v[206:209], v[54:57]
	v_mfma_f32_16x16x32_bf16 v[126:129], v[170:173], v[186:189], v[126:129]
	v_mfma_f32_16x16x32_bf16 v[122:125], v[178:181], v[186:189], v[122:125]
	v_mfma_f32_16x16x32_bf16 v[118:121], v[170:173], v[194:197], v[118:121]
	v_mfma_f32_16x16x32_bf16 v[98:101], v[178:181], v[194:197], v[98:101]
	v_mfma_f32_16x16x32_bf16 v[90:93], v[170:173], v[202:205], v[90:93]
	v_mfma_f32_16x16x32_bf16 v[82:85], v[178:181], v[202:205], v[82:85]
	v_mfma_f32_16x16x32_bf16 v[66:69], v[170:173], v[210:213], v[66:69]
	v_mfma_f32_16x16x32_bf16 v[54:57], v[178:181], v[210:213], v[54:57]
	s_setprio 0
	s_barrier
	ds_read_b128 v[182:185], v169 offset:16384
	ds_read_b128 v[186:189], v169 offset:17408
	ds_read_b128 v[190:193], v169 offset:18432
	ds_read_b128 v[194:197], v169 offset:19456
	ds_read_b128 v[198:201], v169 offset:20480
	ds_read_b128 v[202:205], v169 offset:21504
	ds_read_b128 v[206:209], v169 offset:22528
	ds_read_b128 v[210:213], v169 offset:23552
	s_mov_b32 m0, s37
	s_nop 0
	global_load_lds_dwordx4 v158, s[40:41]
	s_add_u32 s76, s40, 0x40000
	s_mov_b32 m0, s56
	s_nop 0
	global_load_lds_dwordx4 v159, s[40:41]
	s_addc_u32 s77, s41, 0
	s_mov_b32 m0, s57
	s_nop 0
	global_load_lds_dwordx4 v158, s[76:77]
	s_mov_b32 m0, s58
	s_nop 0
	global_load_lds_dwordx4 v159, s[76:77]
	s_mov_b32 m0, s55
	s_nop 0
	global_load_lds_dwordx4 v160, s[46:47]
	s_mov_b32 m0, s59
	s_nop 0
	global_load_lds_dwordx4 v161, s[46:47]
	s_waitcnt vmcnt(8)
	s_waitcnt lgkmcnt(0)
	s_barrier
	s_setprio 1
	s_waitcnt lgkmcnt(7)
	v_mfma_f32_16x16x32_bf16 v[78:81], v[130:133], v[182:185], v[78:81]
	v_mfma_f32_16x16x32_bf16 v[74:77], v[138:141], v[182:185], v[74:77]
	s_waitcnt lgkmcnt(5)
	v_mfma_f32_16x16x32_bf16 v[46:49], v[130:133], v[190:193], v[46:49]
	v_mfma_f32_16x16x32_bf16 v[42:45], v[138:141], v[190:193], v[42:45]
	s_waitcnt lgkmcnt(3)
	v_mfma_f32_16x16x32_bf16 v[30:33], v[130:133], v[198:201], v[30:33]
	v_mfma_f32_16x16x32_bf16 v[26:29], v[138:141], v[198:201], v[26:29]
	s_waitcnt lgkmcnt(1)
	v_mfma_f32_16x16x32_bf16 v[14:17], v[130:133], v[206:209], v[14:17]
	v_mfma_f32_16x16x32_bf16 v[10:13], v[138:141], v[206:209], v[10:13]
	v_mfma_f32_16x16x32_bf16 v[78:81], v[134:137], v[186:189], v[78:81]
	v_mfma_f32_16x16x32_bf16 v[74:77], v[150:153], v[186:189], v[74:77]
	v_mfma_f32_16x16x32_bf16 v[46:49], v[134:137], v[194:197], v[46:49]
	v_mfma_f32_16x16x32_bf16 v[42:45], v[150:153], v[194:197], v[42:45]
	v_mfma_f32_16x16x32_bf16 v[30:33], v[134:137], v[202:205], v[30:33]
	v_mfma_f32_16x16x32_bf16 v[26:29], v[150:153], v[202:205], v[26:29]
	s_waitcnt lgkmcnt(0)
	v_mfma_f32_16x16x32_bf16 v[14:17], v[134:137], v[210:213], v[14:17]
	v_mfma_f32_16x16x32_bf16 v[10:13], v[150:153], v[210:213], v[10:13]
	s_setprio 0
	s_setprio 1
	v_mfma_f32_16x16x32_bf16 v[62:65], v[154:157], v[182:185], v[62:65]
	v_mfma_f32_16x16x32_bf16 v[50:53], v[174:177], v[182:185], v[50:53]
	v_mfma_f32_16x16x32_bf16 v[38:41], v[154:157], v[190:193], v[38:41]
	v_mfma_f32_16x16x32_bf16 v[34:37], v[174:177], v[190:193], v[34:37]
	v_mfma_f32_16x16x32_bf16 v[22:25], v[154:157], v[198:201], v[22:25]
	v_mfma_f32_16x16x32_bf16 v[18:21], v[174:177], v[198:201], v[18:21]
	v_mfma_f32_16x16x32_bf16 v[6:9], v[154:157], v[206:209], v[6:9]
	v_mfma_f32_16x16x32_bf16 v[2:5], v[174:177], v[206:209], v[2:5]
	v_mfma_f32_16x16x32_bf16 v[62:65], v[170:173], v[186:189], v[62:65]
	v_mfma_f32_16x16x32_bf16 v[50:53], v[178:181], v[186:189], v[50:53]
	v_mfma_f32_16x16x32_bf16 v[38:41], v[170:173], v[194:197], v[38:41]
	v_mfma_f32_16x16x32_bf16 v[34:37], v[178:181], v[194:197], v[34:37]
	v_mfma_f32_16x16x32_bf16 v[22:25], v[170:173], v[202:205], v[22:25]
	v_mfma_f32_16x16x32_bf16 v[18:21], v[178:181], v[202:205], v[18:21]
	v_mfma_f32_16x16x32_bf16 v[6:9], v[170:173], v[210:213], v[6:9]
	v_mfma_f32_16x16x32_bf16 v[2:5], v[178:181], v[210:213], v[2:5]
	s_setprio 0
	s_barrier
; #define PG8_STAGEB(bufoff, gbase) PG8_STAGE2(bufoff, gbase, voffB[0], voffB[1])
; #define PG8_STAGEAS(bufoff, gbase, h) PG8_STAGE2(bufoff, gbase, voffA[h][0], voffA[h][1])
; #define PG8_LDA(dst, b, h) do { _Pragma("unroll") for (int m = 0; m < 4; ++m) _Pragma("unroll") for (int k = 0; k < 2; ++k) dst[m][k] = *(const LAS bf16x8*)(lds + PG8_SA(b, h) + aoff + m * 2048 + k * 1024); } while (0)
; #define PG8_LDB(dst, b, h) do { _Pragma("unroll") for (int n = 0; n < 2; ++n) _Pragma("unroll") for (int k = 0; k < 2; ++k) dst[n][k] = *(const LAS bf16x8*)(lds + PG8_SB(b, h) + boff + n * 2048 + k * 1024); } while (0)
; #define PG8_WAIT_K() do { if constexpr (HM) PG8_WAIT_V(6); else PG8_WAIT_V(8); } while (0)
; #define PG8_WAIT_L(n) asm volatile("s_waitcnt lgkmcnt(" #n ")" ::: "memory")
; #define PG8_BAR __builtin_amdgcn_s_barrier()
; #define PG8_SCHED __builtin_amdgcn_sched_barrier(0)
;     ...
;             PG8_LDB(B0, 1, 0); PG8_LDB(B1, 1, 1); PG8_SCHED; PG8_LDA(At, 1, 0); if constexpr (!HM) PG8_STAGEAS(PG8_SA(0, 1), a2, 1);
;             PG8_WAIT_K(); PG8_WAIT_L(0); PG8_BAR; PG8_MMA(0, 0, At, B0); PG8_MMA(0, 1, At, B1); PG8_BAR; PG8_SCHED;
;             if constexpr (!HM) PG8_LDA(At, 1, 1);
;             PG8_STAGEB(PG8_SB(1, 0), b3); PG8_STAGEB(PG8_SB(1, 1), b3 + hstepB); PG8_STAGEAS(PG8_SA(1, 0), a3, 0);
;             PG8_WAIT_K(); PG8_WAIT_L(0); PG8_BAR; if constexpr (!HM) { PG8_MMA(1, 0, At, B0); PG8_MMA(1, 1, At, B1); } PG8_BAR; PG8_SCHED;
	ds_read_b128 v[130:133], v142
	ds_read_b128 v[134:137], v142 offset:1024
	ds_read_b128 v[138:141], v142 offset:2048
	ds_read_b128 v[150:153], v142 offset:3072
	ds_read_b128 v[154:157], v143
	ds_read_b128 v[170:173], v143 offset:1024
	ds_read_b128 v[174:177], v143 offset:2048
	ds_read_b128 v[178:181], v143 offset:3072
	ds_read_b128 v[182:185], v169 offset:32768
	ds_read_b128 v[186:189], v169 offset:33792
	ds_read_b128 v[190:193], v169 offset:34816
	ds_read_b128 v[194:197], v169 offset:35840
	ds_read_b128 v[198:201], v169 offset:36864
	ds_read_b128 v[202:205], v169 offset:37888
	ds_read_b128 v[206:209], v169 offset:38912
	ds_read_b128 v[210:213], v169 offset:39936
	s_mov_b32 m0, s60
	s_nop 0
	global_load_lds_dwordx4 v162, s[46:47]
	s_mov_b32 m0, s61
	s_nop 0
	global_load_lds_dwordx4 v163, s[46:47]
	s_waitcnt vmcnt(8)
	s_waitcnt lgkmcnt(0)
	s_barrier
	s_setprio 1
	s_waitcnt lgkmcnt(7)
	v_mfma_f32_16x16x32_bf16 v[114:117], v[130:133], v[182:185], v[114:117]
	v_mfma_f32_16x16x32_bf16 v[110:113], v[138:141], v[182:185], v[110:113]
	s_waitcnt lgkmcnt(5)
	v_mfma_f32_16x16x32_bf16 v[106:109], v[130:133], v[190:193], v[106:109]
	v_mfma_f32_16x16x32_bf16 v[102:105], v[138:141], v[190:193], v[102:105]
	s_waitcnt lgkmcnt(3)
	v_mfma_f32_16x16x32_bf16 v[94:97], v[130:133], v[198:201], v[94:97]
	v_mfma_f32_16x16x32_bf16 v[86:89], v[138:141], v[198:201], v[86:89]
	s_waitcnt lgkmcnt(1)
	v_mfma_f32_16x16x32_bf16 v[70:73], v[130:133], v[206:209], v[70:73]
	v_mfma_f32_16x16x32_bf16 v[58:61], v[138:141], v[206:209], v[58:61]
	v_mfma_f32_16x16x32_bf16 v[114:117], v[134:137], v[186:189], v[114:117]
	v_mfma_f32_16x16x32_bf16 v[110:113], v[150:153], v[186:189], v[110:113]
	v_mfma_f32_16x16x32_bf16 v[106:109], v[134:137], v[194:197], v[106:109]
	v_mfma_f32_16x16x32_bf16 v[102:105], v[150:153], v[194:197], v[102:105]
	v_mfma_f32_16x16x32_bf16 v[94:97], v[134:137], v[202:205], v[94:97]
	v_mfma_f32_16x16x32_bf16 v[86:89], v[150:153], v[202:205], v[86:89]
	s_waitcnt lgkmcnt(0)
	v_mfma_f32_16x16x32_bf16 v[70:73], v[134:137], v[210:213], v[70:73]
	v_mfma_f32_16x16x32_bf16 v[58:61], v[150:153], v[210:213], v[58:61]
	s_setprio 0
	s_setprio 1
	v_mfma_f32_16x16x32_bf16 v[126:129], v[154:157], v[182:185], v[126:129]
	v_mfma_f32_16x16x32_bf16 v[122:125], v[174:177], v[182:185], v[122:125]
	v_mfma_f32_16x16x32_bf16 v[118:121], v[154:157], v[190:193], v[118:121]
	v_mfma_f32_16x16x32_bf16 v[98:101], v[174:177], v[190:193], v[98:101]
	v_mfma_f32_16x16x32_bf16 v[90:93], v[154:157], v[198:201], v[90:93]
	v_mfma_f32_16x16x32_bf16 v[82:85], v[174:177], v[198:201], v[82:85]
	v_mfma_f32_16x16x32_bf16 v[66:69], v[154:157], v[206:209], v[66:69]
	v_mfma_f32_16x16x32_bf16 v[54:57], v[174:177], v[206:209], v[54:57]
	v_mfma_f32_16x16x32_bf16 v[126:129], v[170:173], v[186:189], v[126:129]
	v_mfma_f32_16x16x32_bf16 v[122:125], v[178:181], v[186:189], v[122:125]
	v_mfma_f32_16x16x32_bf16 v[118:121], v[170:173], v[194:197], v[118:121]
	v_mfma_f32_16x16x32_bf16 v[98:101], v[178:181], v[194:197], v[98:101]
	v_mfma_f32_16x16x32_bf16 v[90:93], v[170:173], v[202:205], v[90:93]
	v_mfma_f32_16x16x32_bf16 v[82:85], v[178:181], v[202:205], v[82:85]
	v_mfma_f32_16x16x32_bf16 v[66:69], v[170:173], v[210:213], v[66:69]
	v_mfma_f32_16x16x32_bf16 v[54:57], v[178:181], v[210:213], v[54:57]
	s_setprio 0
	s_barrier
	ds_read_b128 v[182:185], v169 offset:49152
	ds_read_b128 v[186:189], v169 offset:50176
	ds_read_b128 v[190:193], v169 offset:51200
	ds_read_b128 v[194:197], v169 offset:52224
	ds_read_b128 v[198:201], v169 offset:53248
	ds_read_b128 v[202:205], v169 offset:54272
	ds_read_b128 v[206:209], v169 offset:55296
	ds_read_b128 v[210:213], v169 offset:56320
	s_mov_b32 m0, s62
	s_nop 0
	global_load_lds_dwordx4 v158, s[44:45]
	s_add_u32 s40, s40, 0x40080
	s_mov_b32 m0, s63
	s_nop 0
	global_load_lds_dwordx4 v159, s[44:45]
	s_addc_u32 s41, s41, 0
	s_mov_b32 m0, s66
	s_nop 0
	global_load_lds_dwordx4 v158, s[40:41]
	s_mov_b32 m0, s67
	s_nop 0
	global_load_lds_dwordx4 v159, s[40:41]
	s_mov_b32 m0, s64
	s_nop 0
	global_load_lds_dwordx4 v160, s[38:39]
	s_mov_b32 m0, s65
	s_nop 0
	global_load_lds_dwordx4 v161, s[38:39]
	s_waitcnt vmcnt(8)
	s_waitcnt lgkmcnt(0)
	s_barrier
	s_setprio 1
	s_waitcnt lgkmcnt(7)
	v_mfma_f32_16x16x32_bf16 v[78:81], v[130:133], v[182:185], v[78:81]
	v_mfma_f32_16x16x32_bf16 v[74:77], v[138:141], v[182:185], v[74:77]
	s_waitcnt lgkmcnt(5)
	v_mfma_f32_16x16x32_bf16 v[46:49], v[130:133], v[190:193], v[46:49]
	v_mfma_f32_16x16x32_bf16 v[42:45], v[138:141], v[190:193], v[42:45]
	s_waitcnt lgkmcnt(3)
	v_mfma_f32_16x16x32_bf16 v[30:33], v[130:133], v[198:201], v[30:33]
	v_mfma_f32_16x16x32_bf16 v[26:29], v[138:141], v[198:201], v[26:29]
	s_waitcnt lgkmcnt(1)
	v_mfma_f32_16x16x32_bf16 v[14:17], v[130:133], v[206:209], v[14:17]
	v_mfma_f32_16x16x32_bf16 v[10:13], v[138:141], v[206:209], v[10:13]
	v_mfma_f32_16x16x32_bf16 v[78:81], v[134:137], v[186:189], v[78:81]
	v_mfma_f32_16x16x32_bf16 v[74:77], v[150:153], v[186:189], v[74:77]
	v_mfma_f32_16x16x32_bf16 v[46:49], v[134:137], v[194:197], v[46:49]
	v_mfma_f32_16x16x32_bf16 v[42:45], v[150:153], v[194:197], v[42:45]
	v_mfma_f32_16x16x32_bf16 v[30:33], v[134:137], v[202:205], v[30:33]
	v_mfma_f32_16x16x32_bf16 v[26:29], v[150:153], v[202:205], v[26:29]
	s_waitcnt lgkmcnt(0)
	v_mfma_f32_16x16x32_bf16 v[14:17], v[134:137], v[210:213], v[14:17]
	v_mfma_f32_16x16x32_bf16 v[10:13], v[150:153], v[210:213], v[10:13]
	s_setprio 0
	s_setprio 1
	v_mfma_f32_16x16x32_bf16 v[62:65], v[154:157], v[182:185], v[62:65]
	v_mfma_f32_16x16x32_bf16 v[50:53], v[174:177], v[182:185], v[50:53]
	v_mfma_f32_16x16x32_bf16 v[38:41], v[154:157], v[190:193], v[38:41]
	v_mfma_f32_16x16x32_bf16 v[34:37], v[174:177], v[190:193], v[34:37]
	v_mfma_f32_16x16x32_bf16 v[22:25], v[154:157], v[198:201], v[22:25]
	v_mfma_f32_16x16x32_bf16 v[18:21], v[174:177], v[198:201], v[18:21]
	v_mfma_f32_16x16x32_bf16 v[6:9], v[154:157], v[206:209], v[6:9]
	v_mfma_f32_16x16x32_bf16 v[2:5], v[174:177], v[206:209], v[2:5]
	v_mfma_f32_16x16x32_bf16 v[62:65], v[170:173], v[186:189], v[62:65]
	v_mfma_f32_16x16x32_bf16 v[50:53], v[178:181], v[186:189], v[50:53]
	v_mfma_f32_16x16x32_bf16 v[38:41], v[170:173], v[194:197], v[38:41]
	v_mfma_f32_16x16x32_bf16 v[34:37], v[178:181], v[194:197], v[34:37]
	v_mfma_f32_16x16x32_bf16 v[22:25], v[170:173], v[202:205], v[22:25]
	v_mfma_f32_16x16x32_bf16 v[18:21], v[178:181], v[202:205], v[18:21]
	v_mfma_f32_16x16x32_bf16 v[6:9], v[170:173], v[210:213], v[6:9]
	v_mfma_f32_16x16x32_bf16 v[2:5], v[178:181], v[210:213], v[2:5]
	s_setprio 0
	s_barrier
	s_add_i32 s74, s74, 2
	s_add_u32 s29, s29, 0x100
	s_addc_u32 s31, s31, 0
	s_add_u32 s72, s72, 0x100
	s_addc_u32 s73, s73, 0
	s_add_u32 s42, s42, 0x100
	s_addc_u32 s43, s43, 0
	s_cmp_gt_u32 s74, 13
	s_cbranch_scc0 .LBB0_581
	s_and_b64 vcc, exec, s[18:19]
	s_cbranch_vccz .LBB0_584
	s_barrier

;     __device__ __forceinline__ const char* a_base(const Unit& u) const { return (const char*)A + (size_t)u.pm * BM * lda * 2; }
;     __device__ __forceinline__ const char* b_base(const Unit& u) const { return (const char*)Bt + (size_t)u.pn * BM * K * 2; }
;     __device__ __forceinline__ const char* b_base(const Unit& u) const { return (const char*)Bt + ((size_t)u.e * NB + (size_t)u.pn * BM) * K * 2; }
; #define PG8_RC() int R[2], C[2]; { int t_ = threadIdx.x; asm volatile("" : "+v"(t_)); _Pragma("unroll") for (int i = 0; i < 2; ++i) stage_rc(t_ * 16 + i * 8192, R[i], C[i]); }
;     __device__ __forceinline__ bool next(int i, Unit& u) const {
;         const long L = (long)i * G + c; if (L >= nwg) return false;
;         int wgid = (int)L; { const int q = nwg / NXCD, r = nwg % NXCD, xcd = wgid % NXCD, off = wgid / NXCD; wgid = (xcd < r ? xcd * (q + 1) : r * (q + 1) + (xcd - r) * q) + off; }
;         const int nig = WGM * nN, gid = wgid / nig, fm = gid * WGM, gsz = (nM - fm) < WGM ? (nM - fm) : WGM;
;         u.pm = fm + ((wgid % nig) % gsz); u.pn = (wgid % nig) / gsz; u.e = 0; u.mt = u.pm; u.hx = 0; return true;
;     }
;     ...
;     if (!S.next(0, cur)) return;
;     unsigned voffA[2][2];
;     { PG8_RC(); S.a_offs(cur, R, C, voffA); }
;     f32x4 acc[2][2][4][2];
; #pragma unroll
;     for (int a = 0; a < 2; ++a)
; #pragma unroll
;         for (int b = 0; b < 2; ++b)
; #pragma unroll
;             for (int m = 0; m < 4; ++m)
; #pragma unroll
;                 for (int n = 0; n < 2; ++n) acc[a][b][m][n] = (f32x4){0.f, 0.f, 0.f, 0.f};
;     bf16x8 At[4][2], B0[2][2], B1[2][2];
;     const char* cA = S.a_base(cur); const char* cB = S.b_base(cur);
;     const unsigned bias_lds = (unsigned)__builtin_amdgcn_readfirstlane((int)((unsigned)(size_t)lds + (unsigned)(AUX_OFF + 8192) + (unsigned)wid * 256u));
;     if constexpr (Epi::kBiasDMA) { if (lane < 16) glds16(E.bias_base(cur), E.bias_off(cur, wc, lane), bias_lds); }
;     const unsigned rowid_lds = (unsigned)__builtin_amdgcn_readfirstlane((int)((unsigned)(size_t)lds + (unsigned)AUX_OFF + (unsigned)wid * 512u));
;     if constexpr (Epi::kRowDMA) { if (lane < 32) glds16(E.row_base(cur), E.row_off(cur, wr, lane), rowid_lds); }
;     PG8_STAGEB(PG8_SB(0, 0), cB); PG8_STAGEB(PG8_SB(0, 1), cB + hstepB); PG8_STAGEA(PG8_SA(0, 0), cA, 0); if constexpr (!HM) PG8_STAGEA(PG8_SA(0, 1), cA, 1);
.LBB0_590:
	v_mov_b32_e32 v2, 0x7f7f7f7f
	s_barrier
	s_andn2_b64 vcc, exec, s[12:13]
	v_mov_b32_e32 v2, v0
	s_nop 0
	v_readfirstlane_b32 s1, v2
	s_ashr_i32 s6, s1, 6
	s_cbranch_vccnz .LBB0_620
	v_bfe_i32 v4, v2, 27, 1
	v_lshlrev_b32_e32 v3, 4, v2
	v_lshrrev_b32_e32 v4, 22, v4
	v_add_u32_e32 v4, v3, v4
	v_and_b32_e32 v4, 0xfffffc00, v4
	v_sub_u32_e32 v4, v3, v4
	v_lshrrev_b32_e32 v5, 4, v4
	v_ashrrev_i32_e32 v1, 31, v2
	v_bitop3_b32 v4, v5, v4, 32 bitop3:0x6c
	v_lshrrev_b32_e32 v1, 26, v1
	s_waitcnt vmcnt(1)
	v_ashrrev_i32_e32 v6, 31, v4
	v_add_u32_e32 v1, v2, v1
	v_lshrrev_b32_e32 v6, 26, v6
	v_ashrrev_i32_e32 v1, 6, v1
	v_add_u32_e32 v6, v4, v6
	v_lshlrev_b32_e32 v5, 3, v1
	v_lshrrev_b32_e32 v7, 6, v6
	v_and_b32_e32 v6, 0xc0, v6
	v_and_b32_e32 v5, 0xffff0, v5
	v_lshlrev_b32_e32 v1, 5, v1
	v_sub_u32_e32 v4, v4, v6
	v_mov_b32_e32 v6, 1
	v_add_u32_e32 v5, v7, v5
	v_and_b32_e32 v1, 32, v1
	v_ashrrev_i16_sdwa v4, v6, sext(v4) dst_sel:DWORD dst_unused:UNUSED_PAD src0_sel:DWORD src1_sel:BYTE_0
	v_bfe_i32 v4, v4, 0, 16
	v_lshl_or_b32 v1, v5, 11, v1
	v_add_u32_e32 v3, 0x2000, v3
	v_add_lshl_u32 v1, v1, v4, 1
	v_ashrrev_i32_e32 v4, 31, v3
	v_lshrrev_b32_e32 v4, 22, v4
	v_add_u32_e32 v4, v3, v4
	v_ashrrev_i32_e32 v4, 10, v4
	v_mul_i32_i24_e32 v5, 0x400, v4
	v_sub_u32_e32 v3, v3, v5
	v_lshrrev_b32_e32 v5, 4, v3
	v_bitop3_b32 v3, v5, v3, 32 bitop3:0x6c
	v_ashrrev_i32_e32 v7, 31, v3
	v_lshrrev_b32_e32 v7, 26, v7
	v_add_u32_e32 v7, v3, v7
	v_lshlrev_b32_e32 v5, 3, v4
	v_lshrrev_b32_e32 v8, 6, v7
	v_and_b32_e32 v7, 0xc0, v7
	v_and_b32_e32 v5, 0xffff0, v5
	v_lshlrev_b32_e32 v4, 5, v4
	v_sub_u32_e32 v3, v3, v7
	v_add_u32_e32 v5, v8, v5
	v_and_b32_e32 v4, 32, v4
	v_ashrrev_i16_sdwa v3, v6, sext(v3) dst_sel:DWORD dst_unused:UNUSED_PAD src0_sel:DWORD src1_sel:BYTE_0
	v_bfe_i32 v3, v3, 0, 16
	v_lshl_or_b32 v4, v5, 11, v4
	s_lshl_b32 s0, s6, 10
	s_ashr_i32 s7, s1, 8
	v_add_lshl_u32 v172, v4, v3, 1
	s_add_i32 s36, s0, 0
	v_mov_b32_e32 v3, v0
	s_add_u32 s37, s94, 0x5f000000
	s_addc_u32 s38, s95, 0
	v_ashrrev_i32_e32 v5, 31, v3
	v_lshrrev_b32_e32 v5, 26, v5
	s_add_u32 s39, s94, 0x3600000
	v_lshlrev_b32_e32 v4, 4, v3
	v_add_u32_e32 v5, v3, v5
	v_bfe_i32 v3, v3, 27, 1
	s_addc_u32 s40, s95, 0
	v_lshrrev_b32_e32 v3, 22, v3
	s_and_b64 s[10:11], s[10:11], exec
	v_add_u32_e32 v3, v4, v3
	s_cselect_b32 s0, s50, s49
	v_and_b32_e32 v3, 0xfffffc00, v3
	s_add_i32 s0, s0, s48
	v_sub_u32_e32 v3, v4, v3
	s_ashr_i32 s10, s0, 31
	v_lshrrev_b32_e32 v7, 4, v3
	s_lshr_b32 s10, s10, 27
	v_bitop3_b32 v3, v7, v3, 32 bitop3:0x6c
	s_add_i32 s10, s0, s10
	v_ashrrev_i32_e32 v8, 31, v3
	s_ashr_i32 s11, s10, 5
	s_andn2_b32 s10, s10, 31
	v_lshrrev_b32_e32 v8, 26, v8
	s_sub_i32 s10, s0, s10
	v_add_u32_e32 v8, v3, v8
	s_bfe_i32 s0, s10, 0x80000
	v_ashrrev_i32_e32 v5, 6, v5
	v_ashrrev_i32_e32 v9, 6, v8
	v_and_b32_e32 v8, 0xc0, v8
	s_bfe_u32 s0, s0, 0x2000d
	v_lshlrev_b32_e32 v7, 3, v5
	v_lshlrev_b32_e32 v5, 5, v5
	v_sub_u32_e32 v3, v3, v8
	s_add_i32 s12, s10, s0
	v_and_b32_e32 v5, 32, v5
	v_ashrrev_i16_sdwa v3, v6, sext(v3) dst_sel:DWORD dst_unused:UNUSED_PAD src0_sel:DWORD src1_sel:BYTE_0
	v_add_u32_e32 v4, 0x2000, v4
	s_bfe_i32 s0, s12, 0x80000
	s_and_b32 s12, s12, 0xfc
	v_add_u32_sdwa v3, v5, sext(v3) dst_sel:DWORD dst_unused:UNUSED_PAD src0_sel:DWORD src1_sel:WORD_0
	v_ashrrev_i32_e32 v5, 31, v4
	s_sub_i32 s10, s10, s12
	v_lshrrev_b32_e32 v5, 22, v5
	s_lshl_b32 s11, s11, 2
	s_sext_i32_i8 s10, s10
	v_add_u32_e32 v5, v4, v5
	s_add_i32 s22, s11, s10
	v_ashrrev_i32_e32 v5, 10, v5
	s_sext_i32_i16 s0, s0
	v_mul_i32_i24_e32 v8, 0x400, v5
	s_ashr_i32 s23, s22, 31
	s_lshr_b32 s0, s0, 2
	v_sub_u32_e32 v4, v4, v8
	s_lshl_b64 s[10:11], s[22:23], 20
	v_lshrrev_b32_e32 v8, 4, v4
	s_add_u32 s24, s37, s10
	v_and_b32_e32 v7, -16, v7
	v_bitop3_b32 v4, v8, v4, 32 bitop3:0x6c
	s_addc_u32 s25, s38, s11
	s_bfe_i64 s[10:11], s[0:1], 0x100000
	v_add_u32_e32 v7, v9, v7
	v_ashrrev_i32_e32 v9, 31, v4
	s_lshl_b64 s[10:11], s[10:11], 20
	v_lshrrev_b32_e32 v9, 26, v9
	s_add_u32 s26, s39, s10
	v_add_u32_e32 v9, v4, v9
	s_addc_u32 s27, s40, s11
	s_add_i32 s23, s36, 0x10000
	s_mov_b32 m0, s23
	s_nop 0
	global_load_lds_dwordx4 v1, s[26:27]
	v_ashrrev_i32_e32 v10, 6, v9
	v_and_b32_e32 v9, 0xc0, v9
	s_add_i32 s41, s36, 0x12000
	s_mov_b32 m0, s41
	s_nop 0
	global_load_lds_dwordx4 v172, s[26:27]
	v_lshlrev_b32_e32 v8, 3, v5
	v_lshlrev_b32_e32 v5, 5, v5
	v_sub_u32_e32 v4, v4, v9
	s_add_u32 s10, s26, 0x80000
	v_and_b32_e32 v8, -16, v8
	v_and_b32_e32 v5, 32, v5
	v_ashrrev_i16_sdwa v4, v6, sext(v4) dst_sel:DWORD dst_unused:UNUSED_PAD src0_sel:DWORD src1_sel:BYTE_0
	s_addc_u32 s11, s27, 0
	s_add_i32 s42, s36, 0x14000
	s_mov_b32 m0, s42
	s_nop 0
	global_load_lds_dwordx4 v1, s[10:11]
	v_add_u32_e32 v8, v10, v8
	v_add_u32_sdwa v4, v5, sext(v4) dst_sel:DWORD dst_unused:UNUSED_PAD src0_sel:DWORD src1_sel:WORD_0
	v_lshl_add_u32 v5, v7, 11, v3
	v_lshlrev_b32_e32 v7, 12, v7
	s_add_i32 s43, s36, 0x16000
	s_mov_b32 m0, s43
	s_nop 0
	global_load_lds_dwordx4 v172, s[10:11]
	v_lshl_add_u32 v173, v3, 1, v7
	v_lshlrev_b32_e32 v3, 12, v8
	s_mov_b32 m0, s36
	s_nop 0
	global_load_lds_dwordx4 v173, s[24:25]
	v_lshl_add_u32 v174, v4, 1, v3
	v_mov_b32_e32 v3, 0x80000
	s_add_i32 s44, s36, 0x2000
	s_mov_b32 m0, s44
	s_nop 0
	global_load_lds_dwordx4 v174, s[24:25]
	v_lshl_add_u32 v6, v8, 11, v4
	v_lshl_add_u32 v175, v5, 1, v3
	s_add_i32 s45, s36, 0x4000
	s_mov_b32 m0, s45
	s_nop 0
	global_load_lds_dwordx4 v175, s[24:25]
	v_lshl_add_u32 v176, v6, 1, v3
	s_add_i32 s46, s36, 0x6000
	s_mov_b32 m0, s46
	s_nop 0
	global_load_lds_dwordx4 v176, s[24:25]
	s_cmp_eq_u32 s7, 1
	s_mov_b32 s28, 0
	s_cselect_b64 s[10:11], -1, 0
	s_cmp_lg_u32 s7, 1
	s_cbranch_scc1 .LBB0_593
	s_barrier
; #define PG8_STAGEB(bufoff, gbase) PG8_STAGE2(bufoff, gbase, voffB[0], voffB[1])
; #define PG8_STAGEA(bufoff, gbase, h) PG8_STAGE2(bufoff, gbase, voffA[h][0], voffA[h][1])
; #define PG8_WAIT_V(n) asm volatile("s_waitcnt vmcnt(" #n ")" ::: "memory")
; #define PG8_BAR __builtin_amdgcn_s_barrier()
;     ...
;     const int aoff = lds_byte(wr * 64 + fr, fq * 8), boff = lds_byte(wc * 32 + fr, fq * 8);
;     ...
;     PG8_STAGEB(PG8_SB(0, 0), cB); PG8_STAGEB(PG8_SB(0, 1), cB + hstepB); PG8_STAGEA(PG8_SA(0, 0), cA, 0); if constexpr (!HM) PG8_STAGEA(PG8_SA(0, 1), cA, 1);
;     if (wr == 1) PG8_BAR;
;     if constexpr (HM) PG8_WAIT_V(0); else PG8_WAIT_V(2);
;     PG8_BAR;
;     PG8_STAGEB(PG8_SB(1, 0), cB + kstep); PG8_STAGEA(PG8_SA(1, 0), cA + kstep, 0); PG8_STAGEB(PG8_SB(1, 1), cB + hstepB + kstep);
;     PG8_WAIT_V(6); PG8_BAR;
.LBB0_593:
	v_lshrrev_b32_e32 v4, 1, v2
	v_and_b32_e32 v4, 24, v4
	v_and_b32_e32 v3, 15, v2
	v_lshlrev_b32_e32 v5, 1, v4
	v_lshlrev_b32_e32 v2, 2, v2
	s_sext_i32_i8 s56, s0
	v_lshl_or_b32 v177, s7, 6, v3
	v_lshl_or_b32 v3, v3, 6, v5
	s_lshl_b32 s0, s7, 13
	v_and_b32_e32 v2, 32, v2
	v_bitop3_b32 v5, v3, s0, v2 bitop3:0xde
	s_lshl_b32 s0, s6, 5
	s_and_b32 s0, s0, 0x60
	s_lshl_b32 s6, s0, 7
	s_add_u32 s12, s94, 0x4c600000
	s_addc_u32 s13, s95, 0
	v_bitop3_b32 v2, v3, s6, v2 bitop3:0xde
	s_add_u32 s6, s26, 0x80
	s_waitcnt vmcnt(2)
	s_barrier
	s_addc_u32 s7, s27, 0
	s_add_i32 s47, s36, 0x18000
	s_mov_b32 m0, s47
	s_nop 0
	global_load_lds_dwordx4 v1, s[6:7]
	s_add_i32 s48, s36, 0x1a000
	s_mov_b32 m0, s48
	s_nop 0
	global_load_lds_dwordx4 v172, s[6:7]
	s_add_u32 s6, s24, 0x80
	s_addc_u32 s7, s25, 0
	s_add_i32 s49, s36, 0x8000
	s_mov_b32 m0, s49
	s_nop 0
	global_load_lds_dwordx4 v173, s[6:7]
	s_add_i32 s50, s36, 0xa000
	s_mov_b32 m0, s50
	s_nop 0
	global_load_lds_dwordx4 v174, s[6:7]
	s_add_u32 s6, s26, 0x80080
	s_addc_u32 s7, s27, 0
	s_add_i32 s51, s36, 0x1c000
	s_mov_b32 m0, s51
	s_nop 0
	global_load_lds_dwordx4 v1, s[6:7]
	s_add_i32 s52, s36, 0x1e000
	s_mov_b32 m0, s52
	s_nop 0
	global_load_lds_dwordx4 v172, s[6:7]
	s_waitcnt vmcnt(6)
	s_add_i32 s53, s36, 0xc000
	s_add_i32 s54, s36, 0xe000
	s_cmpk_lt_u32 s1, 0x100
	v_add_u32_e32 v179, 0, v2
	s_cselect_b64 s[14:15], -1, 0
	v_or_b32_e32 v178, s0, v4
	v_mov_b64_e32 v[252:253], 0x200
	v_mov_b64_e32 v[160:161], 0x1ff
	v_add_u32_e32 v180, 0x10000, v179
	v_add_u32_e32 v181, 0x14000, v179
	v_add_u32_e32 v182, 0, v5
	s_barrier
	s_branch .LBB0_596

; #define LAS __attribute__((address_space(3)))
; #define PG8_STAGEA(bufoff, gbase, h) PG8_STAGE2(bufoff, gbase, voffA[h][0], voffA[h][1])
; #define PG8_LDA(dst, b, h) do { _Pragma("unroll") for (int m = 0; m < 4; ++m) _Pragma("unroll") for (int k = 0; k < 2; ++k) dst[m][k] = *(const LAS bf16x8*)(lds + PG8_SA(b, h) + aoff + m * 2048 + k * 1024); } while (0)
; #define PG8_LDB(dst, b, h) do { _Pragma("unroll") for (int n = 0; n < 2; ++n) _Pragma("unroll") for (int k = 0; k < 2; ++k) dst[n][k] = *(const LAS bf16x8*)(lds + PG8_SB(b, h) + boff + n * 2048 + k * 1024); } while (0)
; #define PG8_WAIT_K0() do { if (EST > 0 && t == 0 && ui > 0) asm volatile("s_waitcnt vmcnt(%0)" :: "n"((HM ? 6 : 8) + EST) : "memory"); else PG8_WAIT_K(); } while (0)
; #define PG8_WAIT_L(n) asm volatile("s_waitcnt lgkmcnt(" #n ")" ::: "memory")
; #define PG8_BAR __builtin_amdgcn_s_barrier()
; #define PG8_SCHED __builtin_amdgcn_sched_barrier(0)
;     ...
;             const char* a1 = cA + (size_t)(t + 1) * kstep;
;             const char* a2 = last ? nA : cA + (size_t)(t + 2) * kstep; const char* b2 = last ? nB : cB + (size_t)(t + 2) * kstep;
;             const char* a3 = a2 + kstep; const char* b3 = b2 + kstep;
;             PG8_LDB(B0, 0, 0); PG8_LDB(B1, 0, 1); PG8_SCHED; PG8_LDA(At, 0, 0); if constexpr (!HM) PG8_STAGEA(PG8_SA(1, 1), a1, 1);
;             if constexpr (Sched::kGather) { if (last && has_next) { const u32x4 tn = *(const LAS u32x4*)(S.aux + tid * 16); voffA[0][0] = tn.x; voffA[0][1] = tn.y; voffA[1][0] = tn.z; voffA[1][1] = tn.w; } }
;             PG8_WAIT_K0(); PG8_WAIT_L(0); PG8_BAR; PG8_MMA(0, 0, At, B0); PG8_MMA(0, 1, At, B1); PG8_BAR; PG8_SCHED;
.LBB0_604:
	ds_read_b128 v[18:21], v180
	ds_read_b128 v[22:25], v180 offset:1024
	ds_read_b128 v[26:29], v180 offset:2048
	ds_read_b128 v[30:33], v180 offset:3072
	ds_read_b128 v[2:5], v181
	ds_read_b128 v[6:9], v181 offset:1024
	ds_read_b128 v[10:13], v181 offset:2048
	s_waitcnt vmcnt(0)
	ds_read_b128 v[14:17], v181 offset:3072
	s_cmp_lg_u32 s28, 0
	s_cselect_b64 s[28:29], -1, 0
	s_add_u32 s30, s24, 0x80
	s_addc_u32 s31, s25, 0
	ds_read_b128 v[70:73], v182
	ds_read_b128 v[82:85], v182 offset:1024
	ds_read_b128 v[86:89], v182 offset:2048
	ds_read_b128 v[98:101], v182 offset:3072
	ds_read_b128 v[90:93], v182 offset:4096
	ds_read_b128 v[94:97], v182 offset:5120
	ds_read_b128 v[74:77], v182 offset:6144
	ds_read_b128 v[78:81], v182 offset:7168
	s_mov_b32 m0, s53
	s_nop 0
	global_load_lds_dwordx4 v175, s[30:31]
	s_and_b64 vcc, exec, s[28:29]
	s_mov_b32 m0, s54
	s_nop 0
	global_load_lds_dwordx4 v176, s[30:31]
	s_cbranch_vccz .LBB0_617
	s_waitcnt vmcnt(24)
	s_cbranch_execnz .LBB0_607

; #define PG8_STAGEB(bufoff, gbase) PG8_STAGE2(bufoff, gbase, voffB[0], voffB[1])
; #define PG8_STAGEAS(bufoff, gbase, h) PG8_STAGE2(bufoff, gbase, voffA[h][0], voffA[h][1])
; #define PG8_LDA(dst, b, h) do { _Pragma("unroll") for (int m = 0; m < 4; ++m) _Pragma("unroll") for (int k = 0; k < 2; ++k) dst[m][k] = *(const LAS bf16x8*)(lds + PG8_SA(b, h) + aoff + m * 2048 + k * 1024); } while (0)
; #define PG8_WAIT_K0() do { if (EST > 0 && t == 0 && ui > 0) asm volatile("s_waitcnt vmcnt(%0)" :: "n"((HM ? 6 : 8) + EST) : "memory"); else PG8_WAIT_K(); } while (0)
; #define PG8_WAIT_L(n) asm volatile("s_waitcnt lgkmcnt(" #n ")" ::: "memory")
; #define PG8_BAR __builtin_amdgcn_s_barrier()
; #define PG8_SCHED __builtin_amdgcn_sched_barrier(0)
;     ...
;             PG8_WAIT_K0(); PG8_WAIT_L(0); PG8_BAR; PG8_MMA(0, 0, At, B0); PG8_MMA(0, 1, At, B1); PG8_BAR; PG8_SCHED;
;             if constexpr (!HM) PG8_LDA(At, 0, 1);
;             PG8_STAGEB(PG8_SB(0, 0), b2); PG8_STAGEB(PG8_SB(0, 1), b2 + hstepB); PG8_STAGEAS(PG8_SA(0, 0), a2, 0);
;             PG8_WAIT_K0(); PG8_WAIT_L(0); PG8_BAR; if constexpr (!HM) { PG8_MMA(1, 0, At, B0); PG8_MMA(1, 1, At, B1); } PG8_BAR; PG8_SCHED;
.LBB0_607:
	s_add_u32 s30, s24, 0x100
	s_waitcnt lgkmcnt(0)
	s_addc_u32 s31, s25, 0
	s_add_u32 s34, s26, 0x100
	s_addc_u32 s35, s27, 0
	s_barrier
	s_setprio 1
	s_waitcnt lgkmcnt(7)
	v_mfma_f32_16x16x32_bf16 v[34:37], v[18:21], v[70:73], 0
	v_mfma_f32_16x16x32_bf16 v[38:41], v[26:29], v[70:73], 0
	s_waitcnt lgkmcnt(5)
	v_mfma_f32_16x16x32_bf16 v[42:45], v[18:21], v[86:89], 0
	v_mfma_f32_16x16x32_bf16 v[46:49], v[26:29], v[86:89], 0
	s_waitcnt lgkmcnt(3)
	v_mfma_f32_16x16x32_bf16 v[50:53], v[18:21], v[90:93], 0
	v_mfma_f32_16x16x32_bf16 v[54:57], v[26:29], v[90:93], 0
	s_waitcnt lgkmcnt(1)
	v_mfma_f32_16x16x32_bf16 v[58:61], v[18:21], v[74:77], 0
	v_mfma_f32_16x16x32_bf16 v[62:65], v[26:29], v[74:77], 0
	v_mfma_f32_16x16x32_bf16 v[118:121], v[22:25], v[82:85], v[34:37]
	v_mfma_f32_16x16x32_bf16 v[38:41], v[30:33], v[82:85], v[38:41]
	v_mfma_f32_16x16x32_bf16 v[42:45], v[22:25], v[98:101], v[42:45]
	v_mfma_f32_16x16x32_bf16 v[46:49], v[30:33], v[98:101], v[46:49]
	v_mfma_f32_16x16x32_bf16 v[50:53], v[22:25], v[94:97], v[50:53]
	v_mfma_f32_16x16x32_bf16 v[54:57], v[30:33], v[94:97], v[54:57]
	s_waitcnt lgkmcnt(0)
	v_mfma_f32_16x16x32_bf16 v[58:61], v[22:25], v[78:81], v[58:61]
	v_mfma_f32_16x16x32_bf16 v[62:65], v[30:33], v[78:81], v[62:65]
	s_setprio 0
	s_setprio 1
	v_mfma_f32_16x16x32_bf16 v[66:69], v[2:5], v[70:73], 0
	v_mfma_f32_16x16x32_bf16 v[70:73], v[10:13], v[70:73], 0
	v_mfma_f32_16x16x32_bf16 v[66:69], v[6:9], v[82:85], v[66:69]
	v_mfma_f32_16x16x32_bf16 v[70:73], v[14:17], v[82:85], v[70:73]
	v_mfma_f32_16x16x32_bf16 v[82:85], v[2:5], v[86:89], 0
	v_mfma_f32_16x16x32_bf16 v[86:89], v[10:13], v[86:89], 0
	v_mfma_f32_16x16x32_bf16 v[82:85], v[6:9], v[98:101], v[82:85]
	v_mfma_f32_16x16x32_bf16 v[86:89], v[14:17], v[98:101], v[86:89]
	v_mfma_f32_16x16x32_bf16 v[98:101], v[2:5], v[90:93], 0
	v_mfma_f32_16x16x32_bf16 v[90:93], v[10:13], v[90:93], 0
	v_mfma_f32_16x16x32_bf16 v[134:137], v[14:17], v[94:97], v[90:93]
	v_mfma_f32_16x16x32_bf16 v[90:93], v[2:5], v[74:77], 0
	v_mfma_f32_16x16x32_bf16 v[74:77], v[10:13], v[74:77], 0
	v_mfma_f32_16x16x32_bf16 v[130:133], v[6:9], v[94:97], v[98:101]
	v_mfma_f32_16x16x32_bf16 v[138:141], v[6:9], v[78:81], v[90:93]
	v_mfma_f32_16x16x32_bf16 v[142:145], v[14:17], v[78:81], v[74:77]
	s_setprio 0
	s_barrier
	ds_read_b128 v[106:109], v182 offset:16384
	ds_read_b128 v[110:113], v182 offset:17408
	ds_read_b128 v[98:101], v182 offset:18432
	ds_read_b128 v[102:105], v182 offset:19456
	ds_read_b128 v[90:93], v182 offset:20480
	ds_read_b128 v[94:97], v182 offset:21504
	ds_read_b128 v[74:77], v182 offset:22528
	ds_read_b128 v[78:81], v182 offset:23552
	s_mov_b32 m0, s23
	s_nop 0
	global_load_lds_dwordx4 v1, s[34:35]
	s_mov_b32 m0, s41
	s_nop 0
	global_load_lds_dwordx4 v172, s[34:35]
	s_add_u32 s34, s26, 0x80100
	s_addc_u32 s35, s27, 0
	s_mov_b32 m0, s42
	s_nop 0
	global_load_lds_dwordx4 v1, s[34:35]
	s_and_b64 vcc, exec, s[28:29]
	s_mov_b32 m0, s43
	s_nop 0
	global_load_lds_dwordx4 v172, s[34:35]
	s_mov_b32 m0, s36
	s_nop 0
	global_load_lds_dwordx4 v173, s[30:31]
	s_mov_b32 m0, s44
	s_nop 0
	global_load_lds_dwordx4 v174, s[30:31]
	s_cbranch_vccz .LBB0_618
	s_waitcnt vmcnt(24)
	s_cbranch_execnz .LBB0_610

; #define PG8_STAGEAS(bufoff, gbase, h) PG8_STAGE2(bufoff, gbase, voffA[h][0], voffA[h][1])
; #define PG8_LDA(dst, b, h) do { _Pragma("unroll") for (int m = 0; m < 4; ++m) _Pragma("unroll") for (int k = 0; k < 2; ++k) dst[m][k] = *(const LAS bf16x8*)(lds + PG8_SA(b, h) + aoff + m * 2048 + k * 1024); } while (0)
; #define PG8_LDB(dst, b, h) do { _Pragma("unroll") for (int n = 0; n < 2; ++n) _Pragma("unroll") for (int k = 0; k < 2; ++k) dst[n][k] = *(const LAS bf16x8*)(lds + PG8_SB(b, h) + boff + n * 2048 + k * 1024); } while (0)
; #define PG8_WAIT_K() do { if constexpr (HM) PG8_WAIT_V(6); else PG8_WAIT_V(8); } while (0)
; #define PG8_WAIT_K0() do { if (EST > 0 && t == 0 && ui > 0) asm volatile("s_waitcnt vmcnt(%0)" :: "n"((HM ? 6 : 8) + EST) : "memory"); else PG8_WAIT_K(); } while (0)
; #define PG8_WAIT_L(n) asm volatile("s_waitcnt lgkmcnt(" #n ")" ::: "memory")
; #define PG8_BAR __builtin_amdgcn_s_barrier()
; #define PG8_SCHED __builtin_amdgcn_sched_barrier(0)
;     ...
;             PG8_WAIT_K0(); PG8_WAIT_L(0); PG8_BAR; if constexpr (!HM) { PG8_MMA(1, 0, At, B0); PG8_MMA(1, 1, At, B1); } PG8_BAR; PG8_SCHED;
;             PG8_LDB(B0, 1, 0); PG8_LDB(B1, 1, 1); PG8_SCHED; PG8_LDA(At, 1, 0); if constexpr (!HM) PG8_STAGEAS(PG8_SA(0, 1), a2, 1);
;             PG8_WAIT_K(); PG8_WAIT_L(0); PG8_BAR; PG8_MMA(0, 0, At, B0); PG8_MMA(0, 1, At, B1); PG8_BAR; PG8_SCHED;
.LBB0_610:
	s_add_u32 s28, s24, 0x180
	s_waitcnt lgkmcnt(0)
	s_addc_u32 s29, s25, 0
	s_add_u32 s34, s26, 0x180
	s_addc_u32 s35, s27, 0
	s_barrier
	s_setprio 1
	s_waitcnt lgkmcnt(7)
	v_mfma_f32_16x16x32_bf16 v[114:117], v[18:21], v[106:109], 0
	s_waitcnt lgkmcnt(6)
	v_mfma_f32_16x16x32_bf16 v[148:151], v[22:25], v[110:113], v[114:117]
	v_mfma_f32_16x16x32_bf16 v[114:117], v[26:29], v[106:109], 0
	v_mfma_f32_16x16x32_bf16 v[152:155], v[30:33], v[110:113], v[114:117]
	s_waitcnt lgkmcnt(5)
	v_mfma_f32_16x16x32_bf16 v[114:117], v[18:21], v[98:101], 0
	s_waitcnt lgkmcnt(4)
	v_mfma_f32_16x16x32_bf16 v[162:165], v[22:25], v[102:105], v[114:117]
	v_mfma_f32_16x16x32_bf16 v[114:117], v[26:29], v[98:101], 0
	v_mfma_f32_16x16x32_bf16 v[166:169], v[30:33], v[102:105], v[114:117]
	s_waitcnt lgkmcnt(3)
	v_mfma_f32_16x16x32_bf16 v[114:117], v[18:21], v[90:93], 0
	s_waitcnt lgkmcnt(1)
	v_mfma_f32_16x16x32_bf16 v[18:21], v[18:21], v[74:77], 0
	v_mfma_f32_16x16x32_bf16 v[184:187], v[22:25], v[94:97], v[114:117]
	s_waitcnt lgkmcnt(0)
	v_mfma_f32_16x16x32_bf16 v[18:21], v[22:25], v[78:81], v[18:21]
	v_mfma_f32_16x16x32_bf16 v[22:25], v[26:29], v[74:77], 0
	v_mfma_f32_16x16x32_bf16 v[114:117], v[26:29], v[90:93], 0
	v_mfma_f32_16x16x32_bf16 v[22:25], v[30:33], v[78:81], v[22:25]
	v_mfma_f32_16x16x32_bf16 v[188:191], v[30:33], v[94:97], v[114:117]
	s_setprio 0
	s_setprio 1
	v_mfma_f32_16x16x32_bf16 v[26:29], v[2:5], v[106:109], 0
	v_mfma_f32_16x16x32_bf16 v[192:195], v[6:9], v[110:113], v[26:29]
	v_mfma_f32_16x16x32_bf16 v[26:29], v[10:13], v[106:109], 0
	v_mfma_f32_16x16x32_bf16 v[196:199], v[14:17], v[110:113], v[26:29]
	v_mfma_f32_16x16x32_bf16 v[26:29], v[2:5], v[98:101], 0
	v_mfma_f32_16x16x32_bf16 v[200:203], v[6:9], v[102:105], v[26:29]
	v_mfma_f32_16x16x32_bf16 v[26:29], v[10:13], v[98:101], 0
	v_mfma_f32_16x16x32_bf16 v[204:207], v[14:17], v[102:105], v[26:29]
	v_mfma_f32_16x16x32_bf16 v[26:29], v[2:5], v[90:93], 0
	v_mfma_f32_16x16x32_bf16 v[2:5], v[2:5], v[74:77], 0
	v_mfma_f32_16x16x32_bf16 v[208:211], v[6:9], v[94:97], v[26:29]
	v_mfma_f32_16x16x32_bf16 v[26:29], v[10:13], v[90:93], 0
	v_mfma_f32_16x16x32_bf16 v[2:5], v[6:9], v[78:81], v[2:5]
	v_mfma_f32_16x16x32_bf16 v[6:9], v[10:13], v[74:77], 0
	v_mfma_f32_16x16x32_bf16 v[212:215], v[14:17], v[94:97], v[26:29]
	v_mfma_f32_16x16x32_bf16 v[216:219], v[14:17], v[78:81], v[6:9]
	s_setprio 0
	s_barrier
	v_add_u32_e32 v146, 0x18000, v179
	v_add_u32_e32 v147, 0x1c000, v179
	s_nop 1
	ds_read_b128 v[6:9], v146
	ds_read_b128 v[10:13], v146 offset:1024
	ds_read_b128 v[220:223], v146 offset:2048
	ds_read_b128 v[224:227], v146 offset:3072
	ds_read_b128 v[228:231], v147
	ds_read_b128 v[232:235], v147 offset:1024
	ds_read_b128 v[236:239], v147 offset:2048
	ds_read_b128 v[240:243], v147 offset:3072
	ds_read_b128 v[14:17], v182 offset:32768
	ds_read_b128 v[26:29], v182 offset:33792
	ds_read_b128 v[30:33], v182 offset:34816
	ds_read_b128 v[98:101], v182 offset:35840
	ds_read_b128 v[244:247], v182 offset:36864
	ds_read_b128 v[248:251], v182 offset:37888
	ds_read_b128 v[156:159], v182 offset:38912
	ds_read_b128 v[34:37], v182 offset:39936
	s_mov_b32 m0, s45
	s_nop 0
	global_load_lds_dwordx4 v175, s[30:31]
	s_mov_b32 m0, s46
	s_nop 0
	global_load_lds_dwordx4 v176, s[30:31]
	s_waitcnt vmcnt(8)
	s_waitcnt lgkmcnt(0)
	s_barrier
	s_setprio 1
	s_waitcnt lgkmcnt(7)
	v_mfma_f32_16x16x32_bf16 v[38:41], v[220:223], v[14:17], v[38:41]
	s_waitcnt lgkmcnt(6)
	v_mfma_f32_16x16x32_bf16 v[122:125], v[224:227], v[26:29], v[38:41]
	s_waitcnt lgkmcnt(5)
	v_mfma_f32_16x16x32_bf16 v[38:41], v[6:9], v[30:33], v[42:45]
	s_waitcnt lgkmcnt(4)
	v_mfma_f32_16x16x32_bf16 v[110:113], v[10:13], v[98:101], v[38:41]
	v_mfma_f32_16x16x32_bf16 v[38:41], v[220:223], v[30:33], v[46:49]
	v_mfma_f32_16x16x32_bf16 v[106:109], v[224:227], v[98:101], v[38:41]
	s_waitcnt lgkmcnt(3)
	v_mfma_f32_16x16x32_bf16 v[38:41], v[6:9], v[244:247], v[50:53]
	s_waitcnt lgkmcnt(2)
	v_mfma_f32_16x16x32_bf16 v[94:97], v[10:13], v[248:251], v[38:41]
	v_mfma_f32_16x16x32_bf16 v[38:41], v[220:223], v[244:247], v[54:57]
	v_mfma_f32_16x16x32_bf16 v[90:93], v[224:227], v[248:251], v[38:41]
	s_waitcnt lgkmcnt(1)
	v_mfma_f32_16x16x32_bf16 v[38:41], v[6:9], v[156:159], v[58:61]
	v_mfma_f32_16x16x32_bf16 v[74:77], v[6:9], v[14:17], v[118:121]
	s_waitcnt lgkmcnt(0)
	v_mfma_f32_16x16x32_bf16 v[78:81], v[10:13], v[34:37], v[38:41]
	v_mfma_f32_16x16x32_bf16 v[38:41], v[220:223], v[156:159], v[62:65]
	v_mfma_f32_16x16x32_bf16 v[126:129], v[10:13], v[26:29], v[74:77]
	v_mfma_f32_16x16x32_bf16 v[74:77], v[224:227], v[34:37], v[38:41]
	s_setprio 0
	s_setprio 1
	v_mfma_f32_16x16x32_bf16 v[38:41], v[228:231], v[14:17], v[66:69]
	v_mfma_f32_16x16x32_bf16 v[14:17], v[236:239], v[14:17], v[70:73]
	v_mfma_f32_16x16x32_bf16 v[114:117], v[240:243], v[26:29], v[14:17]
	v_mfma_f32_16x16x32_bf16 v[14:17], v[228:231], v[30:33], v[82:85]
	v_mfma_f32_16x16x32_bf16 v[102:105], v[232:235], v[98:101], v[14:17]
	v_mfma_f32_16x16x32_bf16 v[14:17], v[236:239], v[30:33], v[86:89]
	v_mfma_f32_16x16x32_bf16 v[98:101], v[240:243], v[98:101], v[14:17]
	v_mfma_f32_16x16x32_bf16 v[14:17], v[228:231], v[244:247], v[130:133]
	v_mfma_f32_16x16x32_bf16 v[86:89], v[232:235], v[248:251], v[14:17]
	v_mfma_f32_16x16x32_bf16 v[14:17], v[236:239], v[244:247], v[134:137]
	v_mfma_f32_16x16x32_bf16 v[82:85], v[240:243], v[248:251], v[14:17]
	v_mfma_f32_16x16x32_bf16 v[14:17], v[228:231], v[156:159], v[138:141]
	v_mfma_f32_16x16x32_bf16 v[70:73], v[232:235], v[34:37], v[14:17]
	v_mfma_f32_16x16x32_bf16 v[14:17], v[236:239], v[156:159], v[142:145]
	v_mfma_f32_16x16x32_bf16 v[118:121], v[232:235], v[26:29], v[38:41]
	v_mfma_f32_16x16x32_bf16 v[66:69], v[240:243], v[34:37], v[14:17]
	s_setprio 0
	s_barrier
; #define LAS __attribute__((address_space(3)))
; #define PG8_STAGEB(bufoff, gbase) PG8_STAGE2(bufoff, gbase, voffB[0], voffB[1])
; #define PG8_STAGEA(bufoff, gbase, h) PG8_STAGE2(bufoff, gbase, voffA[h][0], voffA[h][1])
; #define PG8_STAGEAS(bufoff, gbase, h) PG8_STAGE2(bufoff, gbase, voffA[h][0], voffA[h][1])
; #define PG8_LDA(dst, b, h) do { _Pragma("unroll") for (int m = 0; m < 4; ++m) _Pragma("unroll") for (int k = 0; k < 2; ++k) dst[m][k] = *(const LAS bf16x8*)(lds + PG8_SA(b, h) + aoff + m * 2048 + k * 1024); } while (0)
; #define PG8_LDB(dst, b, h) do { _Pragma("unroll") for (int n = 0; n < 2; ++n) _Pragma("unroll") for (int k = 0; k < 2; ++k) dst[n][k] = *(const LAS bf16x8*)(lds + PG8_SB(b, h) + boff + n * 2048 + k * 1024); } while (0)
; #define PG8_WAIT_K() do { if constexpr (HM) PG8_WAIT_V(6); else PG8_WAIT_V(8); } while (0)
; #define PG8_WAIT_K0() do { if (EST > 0 && t == 0 && ui > 0) asm volatile("s_waitcnt vmcnt(%0)" :: "n"((HM ? 6 : 8) + EST) : "memory"); else PG8_WAIT_K(); } while (0)
; #define PG8_WAIT_L(n) asm volatile("s_waitcnt lgkmcnt(" #n ")" ::: "memory")
; #define PG8_BAR __builtin_amdgcn_s_barrier()
; #define PG8_SCHED __builtin_amdgcn_sched_barrier(0)
;     ...
;             const char* a1 = cA + (size_t)(t + 1) * kstep;
;             const char* a2 = last ? nA : cA + (size_t)(t + 2) * kstep; const char* b2 = last ? nB : cB + (size_t)(t + 2) * kstep;
;             const char* a3 = a2 + kstep; const char* b3 = b2 + kstep;
;             PG8_LDB(B0, 0, 0); PG8_LDB(B1, 0, 1); PG8_SCHED; PG8_LDA(At, 0, 0); if constexpr (!HM) PG8_STAGEA(PG8_SA(1, 1), a1, 1);
;             if constexpr (Sched::kGather) { if (last && has_next) { const u32x4 tn = *(const LAS u32x4*)(S.aux + tid * 16); voffA[0][0] = tn.x; voffA[0][1] = tn.y; voffA[1][0] = tn.z; voffA[1][1] = tn.w; } }
;             PG8_WAIT_K0(); PG8_WAIT_L(0); PG8_BAR; PG8_MMA(0, 0, At, B0); PG8_MMA(0, 1, At, B1); PG8_BAR; PG8_SCHED;
;     ...
;             if constexpr (!HM) PG8_LDA(At, 1, 1);
;             PG8_STAGEB(PG8_SB(1, 0), b3); PG8_STAGEB(PG8_SB(1, 1), b3 + hstepB); PG8_STAGEAS(PG8_SA(1, 0), a3, 0);
;             PG8_WAIT_K(); PG8_WAIT_L(0); PG8_BAR; if constexpr (!HM) { PG8_MMA(1, 0, At, B0); PG8_MMA(1, 1, At, B1); } PG8_BAR; PG8_SCHED;
	ds_read_b128 v[34:37], v182 offset:49152
	ds_read_b128 v[38:41], v182 offset:50176
	ds_read_b128 v[130:133], v182 offset:51200
	ds_read_b128 v[134:137], v182 offset:52224
	ds_read_b128 v[138:141], v182 offset:53248
	ds_read_b128 v[142:145], v182 offset:54272
	ds_read_b128 v[156:159], v182 offset:55296
	ds_read_b128 v[244:247], v182 offset:56320
	s_mov_b32 m0, s47
	s_nop 0
	global_load_lds_dwordx4 v1, s[34:35]
	s_add_u32 s30, s26, 0x80180
	s_mov_b32 m0, s48
	s_nop 0
	global_load_lds_dwordx4 v172, s[34:35]
	s_addc_u32 s31, s27, 0
	s_mov_b32 m0, s51
	s_nop 0
	global_load_lds_dwordx4 v1, s[30:31]
	s_mov_b32 m0, s52
	s_nop 0
	global_load_lds_dwordx4 v172, s[30:31]
	s_mov_b32 m0, s49
	s_nop 0
	global_load_lds_dwordx4 v173, s[28:29]
	s_mov_b32 m0, s50
	s_nop 0
	global_load_lds_dwordx4 v174, s[28:29]
	s_waitcnt vmcnt(8)
	s_waitcnt lgkmcnt(0)
	s_barrier
	s_setprio 1
	s_waitcnt lgkmcnt(7)
	v_mfma_f32_16x16x32_bf16 v[14:17], v[6:9], v[34:37], v[148:151]
	s_waitcnt lgkmcnt(6)
	v_mfma_f32_16x16x32_bf16 v[62:65], v[10:13], v[38:41], v[14:17]
	v_mfma_f32_16x16x32_bf16 v[14:17], v[220:223], v[34:37], v[152:155]
	v_mfma_f32_16x16x32_bf16 v[58:61], v[224:227], v[38:41], v[14:17]
	s_waitcnt lgkmcnt(5)
	v_mfma_f32_16x16x32_bf16 v[14:17], v[6:9], v[130:133], v[162:165]
	s_waitcnt lgkmcnt(4)
	v_mfma_f32_16x16x32_bf16 v[46:49], v[10:13], v[134:137], v[14:17]
	v_mfma_f32_16x16x32_bf16 v[14:17], v[220:223], v[130:133], v[166:169]
	v_mfma_f32_16x16x32_bf16 v[42:45], v[224:227], v[134:137], v[14:17]
	s_waitcnt lgkmcnt(3)
	v_mfma_f32_16x16x32_bf16 v[14:17], v[6:9], v[138:141], v[184:187]
	s_waitcnt lgkmcnt(2)
	v_mfma_f32_16x16x32_bf16 v[30:33], v[10:13], v[142:145], v[14:17]
	v_mfma_f32_16x16x32_bf16 v[14:17], v[220:223], v[138:141], v[188:191]
	s_waitcnt lgkmcnt(1)
	v_mfma_f32_16x16x32_bf16 v[6:9], v[6:9], v[156:159], v[18:21]
	v_mfma_f32_16x16x32_bf16 v[26:29], v[224:227], v[142:145], v[14:17]
	s_waitcnt lgkmcnt(0)
	v_mfma_f32_16x16x32_bf16 v[14:17], v[10:13], v[244:247], v[6:9]
	v_mfma_f32_16x16x32_bf16 v[6:9], v[220:223], v[156:159], v[22:25]
	v_mfma_f32_16x16x32_bf16 v[10:13], v[224:227], v[244:247], v[6:9]
	s_setprio 0
	s_setprio 1
	v_mfma_f32_16x16x32_bf16 v[6:9], v[228:231], v[34:37], v[192:195]
	v_mfma_f32_16x16x32_bf16 v[54:57], v[232:235], v[38:41], v[6:9]
	v_mfma_f32_16x16x32_bf16 v[6:9], v[236:239], v[34:37], v[196:199]
	v_mfma_f32_16x16x32_bf16 v[50:53], v[240:243], v[38:41], v[6:9]
	v_mfma_f32_16x16x32_bf16 v[6:9], v[228:231], v[130:133], v[200:203]
	v_mfma_f32_16x16x32_bf16 v[38:41], v[232:235], v[134:137], v[6:9]
	v_mfma_f32_16x16x32_bf16 v[6:9], v[236:239], v[130:133], v[204:207]
	v_mfma_f32_16x16x32_bf16 v[34:37], v[240:243], v[134:137], v[6:9]
	v_mfma_f32_16x16x32_bf16 v[6:9], v[228:231], v[138:141], v[208:211]
	v_mfma_f32_16x16x32_bf16 v[22:25], v[232:235], v[142:145], v[6:9]
	v_mfma_f32_16x16x32_bf16 v[6:9], v[236:239], v[138:141], v[212:215]
	v_mfma_f32_16x16x32_bf16 v[2:5], v[228:231], v[156:159], v[2:5]
	v_mfma_f32_16x16x32_bf16 v[18:21], v[240:243], v[142:145], v[6:9]
	v_mfma_f32_16x16x32_bf16 v[6:9], v[232:235], v[244:247], v[2:5]
	v_mfma_f32_16x16x32_bf16 v[2:5], v[236:239], v[156:159], v[216:219]
	v_mfma_f32_16x16x32_bf16 v[2:5], v[240:243], v[244:247], v[2:5]
	s_setprio 0
	s_barrier
	s_add_u32 s17, s24, 0x200
	s_addc_u32 s19, s25, 0
	s_add_u32 s57, s26, 0x200
	s_addc_u32 s58, s27, 0
	s_mov_b32 s59, 0
.LBB0_611:
	ds_read_b128 v[130:133], v180
	ds_read_b128 v[134:137], v180 offset:1024
	ds_read_b128 v[138:141], v180 offset:2048
	ds_read_b128 v[142:145], v180 offset:3072
	ds_read_b128 v[148:151], v181
	ds_read_b128 v[152:155], v181 offset:1024
	ds_read_b128 v[156:159], v181 offset:2048
	ds_read_b128 v[162:165], v181 offset:3072
	s_cmp_eq_u32 s59, 28
	s_cselect_b32 s34, s0, s17
	s_cselect_b32 s35, s1, s19
	s_cselect_b32 s26, s20, s57
	s_cselect_b32 s27, s21, s58
	s_add_u32 s24, s34, 0x80
	s_addc_u32 s25, s35, 0
	ds_read_b128 v[166:169], v182
	ds_read_b128 v[184:187], v182 offset:1024
	ds_read_b128 v[188:191], v182 offset:2048
	ds_read_b128 v[192:195], v182 offset:3072
	ds_read_b128 v[196:199], v182 offset:4096
	ds_read_b128 v[200:203], v182 offset:5120
	ds_read_b128 v[204:207], v182 offset:6144
	ds_read_b128 v[208:211], v182 offset:7168
	s_mov_b32 m0, s53
	s_nop 0
	global_load_lds_dwordx4 v175, s[28:29]
	s_add_u32 s30, s26, 0x80
	s_mov_b32 m0, s54
	s_nop 0
	global_load_lds_dwordx4 v176, s[28:29]
	s_waitcnt vmcnt(8)
	s_waitcnt lgkmcnt(0)
	s_addc_u32 s31, s27, 0
	s_barrier
; #define PG8_STAGEB(bufoff, gbase) PG8_STAGE2(bufoff, gbase, voffB[0], voffB[1])
; #define PG8_STAGEAS(bufoff, gbase, h) PG8_STAGE2(bufoff, gbase, voffA[h][0], voffA[h][1])
; #define PG8_LDA(dst, b, h) do { _Pragma("unroll") for (int m = 0; m < 4; ++m) _Pragma("unroll") for (int k = 0; k < 2; ++k) dst[m][k] = *(const LAS bf16x8*)(lds + PG8_SA(b, h) + aoff + m * 2048 + k * 1024); } while (0)
; #define PG8_WAIT_K0() do { if (EST > 0 && t == 0 && ui > 0) asm volatile("s_waitcnt vmcnt(%0)" :: "n"((HM ? 6 : 8) + EST) : "memory"); else PG8_WAIT_K(); } while (0)
; #define PG8_WAIT_L(n) asm volatile("s_waitcnt lgkmcnt(" #n ")" ::: "memory")
; #define PG8_BAR __builtin_amdgcn_s_barrier()
; #define PG8_SCHED __builtin_amdgcn_sched_barrier(0)
;     ...
;             PG8_WAIT_K0(); PG8_WAIT_L(0); PG8_BAR; PG8_MMA(0, 0, At, B0); PG8_MMA(0, 1, At, B1); PG8_BAR; PG8_SCHED;
;             if constexpr (!HM) PG8_LDA(At, 0, 1);
;             PG8_STAGEB(PG8_SB(0, 0), b2); PG8_STAGEB(PG8_SB(0, 1), b2 + hstepB); PG8_STAGEAS(PG8_SA(0, 0), a2, 0);
;             PG8_WAIT_K0(); PG8_WAIT_L(0); PG8_BAR; if constexpr (!HM) { PG8_MMA(1, 0, At, B0); PG8_MMA(1, 1, At, B1); } PG8_BAR; PG8_SCHED;
	s_setprio 1
	s_waitcnt lgkmcnt(7)
	v_mfma_f32_16x16x32_bf16 v[126:129], v[130:133], v[166:169], v[126:129]
	v_mfma_f32_16x16x32_bf16 v[122:125], v[138:141], v[166:169], v[122:125]
	s_waitcnt lgkmcnt(5)
	v_mfma_f32_16x16x32_bf16 v[110:113], v[130:133], v[188:191], v[110:113]
	v_mfma_f32_16x16x32_bf16 v[106:109], v[138:141], v[188:191], v[106:109]
	s_waitcnt lgkmcnt(3)
	v_mfma_f32_16x16x32_bf16 v[94:97], v[130:133], v[196:199], v[94:97]
	v_mfma_f32_16x16x32_bf16 v[90:93], v[138:141], v[196:199], v[90:93]
	s_waitcnt lgkmcnt(1)
	v_mfma_f32_16x16x32_bf16 v[78:81], v[130:133], v[204:207], v[78:81]
	v_mfma_f32_16x16x32_bf16 v[74:77], v[138:141], v[204:207], v[74:77]
	v_mfma_f32_16x16x32_bf16 v[126:129], v[134:137], v[184:187], v[126:129]
	v_mfma_f32_16x16x32_bf16 v[122:125], v[142:145], v[184:187], v[122:125]
	v_mfma_f32_16x16x32_bf16 v[110:113], v[134:137], v[192:195], v[110:113]
	v_mfma_f32_16x16x32_bf16 v[106:109], v[142:145], v[192:195], v[106:109]
	v_mfma_f32_16x16x32_bf16 v[94:97], v[134:137], v[200:203], v[94:97]
	v_mfma_f32_16x16x32_bf16 v[90:93], v[142:145], v[200:203], v[90:93]
	s_waitcnt lgkmcnt(0)
	v_mfma_f32_16x16x32_bf16 v[78:81], v[134:137], v[208:211], v[78:81]
	v_mfma_f32_16x16x32_bf16 v[74:77], v[142:145], v[208:211], v[74:77]
	s_setprio 0
	s_setprio 1
	v_mfma_f32_16x16x32_bf16 v[118:121], v[148:151], v[166:169], v[118:121]
	v_mfma_f32_16x16x32_bf16 v[114:117], v[156:159], v[166:169], v[114:117]
	v_mfma_f32_16x16x32_bf16 v[102:105], v[148:151], v[188:191], v[102:105]
	v_mfma_f32_16x16x32_bf16 v[98:101], v[156:159], v[188:191], v[98:101]
	v_mfma_f32_16x16x32_bf16 v[86:89], v[148:151], v[196:199], v[86:89]
	v_mfma_f32_16x16x32_bf16 v[82:85], v[156:159], v[196:199], v[82:85]
	v_mfma_f32_16x16x32_bf16 v[70:73], v[148:151], v[204:207], v[70:73]
	v_mfma_f32_16x16x32_bf16 v[66:69], v[156:159], v[204:207], v[66:69]
	v_mfma_f32_16x16x32_bf16 v[118:121], v[152:155], v[184:187], v[118:121]
	v_mfma_f32_16x16x32_bf16 v[114:117], v[162:165], v[184:187], v[114:117]
	v_mfma_f32_16x16x32_bf16 v[102:105], v[152:155], v[192:195], v[102:105]
	v_mfma_f32_16x16x32_bf16 v[98:101], v[162:165], v[192:195], v[98:101]
	v_mfma_f32_16x16x32_bf16 v[86:89], v[152:155], v[200:203], v[86:89]
	v_mfma_f32_16x16x32_bf16 v[82:85], v[162:165], v[200:203], v[82:85]
	v_mfma_f32_16x16x32_bf16 v[70:73], v[152:155], v[208:211], v[70:73]
	v_mfma_f32_16x16x32_bf16 v[66:69], v[162:165], v[208:211], v[66:69]
	s_setprio 0
	s_barrier
	ds_read_b128 v[166:169], v182 offset:16384
	ds_read_b128 v[184:187], v182 offset:17408
	ds_read_b128 v[188:191], v182 offset:18432
	ds_read_b128 v[192:195], v182 offset:19456
	ds_read_b128 v[196:199], v182 offset:20480
	ds_read_b128 v[200:203], v182 offset:21504
	ds_read_b128 v[204:207], v182 offset:22528
	ds_read_b128 v[208:211], v182 offset:23552
	s_mov_b32 m0, s23
	s_nop 0
	global_load_lds_dwordx4 v1, s[26:27]
	s_mov_b32 m0, s41
	s_nop 0
	global_load_lds_dwordx4 v172, s[26:27]
	s_add_u32 s60, s26, 0x80000
	s_addc_u32 s61, s27, 0
	s_mov_b32 m0, s42
	s_nop 0
	global_load_lds_dwordx4 v1, s[60:61]
	s_mov_b32 m0, s43
	s_nop 0
	global_load_lds_dwordx4 v172, s[60:61]
	s_mov_b32 m0, s36
	s_nop 0
	global_load_lds_dwordx4 v173, s[34:35]
	s_mov_b32 m0, s44
	s_nop 0
	global_load_lds_dwordx4 v174, s[34:35]
	s_waitcnt vmcnt(8)
	s_waitcnt lgkmcnt(0)
	s_barrier
	s_setprio 1
	s_waitcnt lgkmcnt(7)
	v_mfma_f32_16x16x32_bf16 v[62:65], v[130:133], v[166:169], v[62:65]
	v_mfma_f32_16x16x32_bf16 v[58:61], v[138:141], v[166:169], v[58:61]
	s_waitcnt lgkmcnt(5)
	v_mfma_f32_16x16x32_bf16 v[46:49], v[130:133], v[188:191], v[46:49]
	v_mfma_f32_16x16x32_bf16 v[42:45], v[138:141], v[188:191], v[42:45]
	s_waitcnt lgkmcnt(3)
	v_mfma_f32_16x16x32_bf16 v[30:33], v[130:133], v[196:199], v[30:33]
	v_mfma_f32_16x16x32_bf16 v[26:29], v[138:141], v[196:199], v[26:29]
	s_waitcnt lgkmcnt(1)
	v_mfma_f32_16x16x32_bf16 v[14:17], v[130:133], v[204:207], v[14:17]
	v_mfma_f32_16x16x32_bf16 v[10:13], v[138:141], v[204:207], v[10:13]
	v_mfma_f32_16x16x32_bf16 v[62:65], v[134:137], v[184:187], v[62:65]
	v_mfma_f32_16x16x32_bf16 v[58:61], v[142:145], v[184:187], v[58:61]
	v_mfma_f32_16x16x32_bf16 v[46:49], v[134:137], v[192:195], v[46:49]
	v_mfma_f32_16x16x32_bf16 v[42:45], v[142:145], v[192:195], v[42:45]
	v_mfma_f32_16x16x32_bf16 v[30:33], v[134:137], v[200:203], v[30:33]
	v_mfma_f32_16x16x32_bf16 v[26:29], v[142:145], v[200:203], v[26:29]
	s_waitcnt lgkmcnt(0)
	v_mfma_f32_16x16x32_bf16 v[14:17], v[134:137], v[208:211], v[14:17]
	v_mfma_f32_16x16x32_bf16 v[10:13], v[142:145], v[208:211], v[10:13]
	s_setprio 0
	s_setprio 1
	v_mfma_f32_16x16x32_bf16 v[54:57], v[148:151], v[166:169], v[54:57]
	v_mfma_f32_16x16x32_bf16 v[50:53], v[156:159], v[166:169], v[50:53]
	v_mfma_f32_16x16x32_bf16 v[38:41], v[148:151], v[188:191], v[38:41]
	v_mfma_f32_16x16x32_bf16 v[34:37], v[156:159], v[188:191], v[34:37]
	v_mfma_f32_16x16x32_bf16 v[22:25], v[148:151], v[196:199], v[22:25]
	v_mfma_f32_16x16x32_bf16 v[18:21], v[156:159], v[196:199], v[18:21]
	v_mfma_f32_16x16x32_bf16 v[6:9], v[148:151], v[204:207], v[6:9]
	v_mfma_f32_16x16x32_bf16 v[2:5], v[156:159], v[204:207], v[2:5]
	v_mfma_f32_16x16x32_bf16 v[54:57], v[152:155], v[184:187], v[54:57]
	v_mfma_f32_16x16x32_bf16 v[50:53], v[162:165], v[184:187], v[50:53]
	v_mfma_f32_16x16x32_bf16 v[38:41], v[152:155], v[192:195], v[38:41]
	v_mfma_f32_16x16x32_bf16 v[34:37], v[162:165], v[192:195], v[34:37]
	v_mfma_f32_16x16x32_bf16 v[22:25], v[152:155], v[200:203], v[22:25]
	v_mfma_f32_16x16x32_bf16 v[18:21], v[162:165], v[200:203], v[18:21]
	v_mfma_f32_16x16x32_bf16 v[6:9], v[152:155], v[208:211], v[6:9]
	v_mfma_f32_16x16x32_bf16 v[2:5], v[162:165], v[208:211], v[2:5]
	s_setprio 0
	s_barrier
; #define PG8_STAGEB(bufoff, gbase) PG8_STAGE2(bufoff, gbase, voffB[0], voffB[1])
; #define PG8_STAGEAS(bufoff, gbase, h) PG8_STAGE2(bufoff, gbase, voffA[h][0], voffA[h][1])
; #define PG8_LDA(dst, b, h) do { _Pragma("unroll") for (int m = 0; m < 4; ++m) _Pragma("unroll") for (int k = 0; k < 2; ++k) dst[m][k] = *(const LAS bf16x8*)(lds + PG8_SA(b, h) + aoff + m * 2048 + k * 1024); } while (0)
; #define PG8_LDB(dst, b, h) do { _Pragma("unroll") for (int n = 0; n < 2; ++n) _Pragma("unroll") for (int k = 0; k < 2; ++k) dst[n][k] = *(const LAS bf16x8*)(lds + PG8_SB(b, h) + boff + n * 2048 + k * 1024); } while (0)
; #define PG8_WAIT_K() do { if constexpr (HM) PG8_WAIT_V(6); else PG8_WAIT_V(8); } while (0)
; #define PG8_WAIT_L(n) asm volatile("s_waitcnt lgkmcnt(" #n ")" ::: "memory")
; #define PG8_BAR __builtin_amdgcn_s_barrier()
; #define PG8_SCHED __builtin_amdgcn_sched_barrier(0)
;     ...
;             PG8_LDB(B0, 1, 0); PG8_LDB(B1, 1, 1); PG8_SCHED; PG8_LDA(At, 1, 0); if constexpr (!HM) PG8_STAGEAS(PG8_SA(0, 1), a2, 1);
;             PG8_WAIT_K(); PG8_WAIT_L(0); PG8_BAR; PG8_MMA(0, 0, At, B0); PG8_MMA(0, 1, At, B1); PG8_BAR; PG8_SCHED;
;             if constexpr (!HM) PG8_LDA(At, 1, 1);
;             PG8_STAGEB(PG8_SB(1, 0), b3); PG8_STAGEB(PG8_SB(1, 1), b3 + hstepB); PG8_STAGEAS(PG8_SA(1, 0), a3, 0);
;             PG8_WAIT_K(); PG8_WAIT_L(0); PG8_BAR; if constexpr (!HM) { PG8_MMA(1, 0, At, B0); PG8_MMA(1, 1, At, B1); } PG8_BAR; PG8_SCHED;
;         }
;         if (wr == 0) PG8_BAR;
	ds_read_b128 v[130:133], v146
	ds_read_b128 v[134:137], v146 offset:1024
	ds_read_b128 v[138:141], v146 offset:2048
	ds_read_b128 v[142:145], v146 offset:3072
	ds_read_b128 v[148:151], v147
	ds_read_b128 v[152:155], v147 offset:1024
	ds_read_b128 v[156:159], v147 offset:2048
	ds_read_b128 v[162:165], v147 offset:3072
	ds_read_b128 v[166:169], v182 offset:32768
	ds_read_b128 v[184:187], v182 offset:33792
	ds_read_b128 v[188:191], v182 offset:34816
	ds_read_b128 v[192:195], v182 offset:35840
	ds_read_b128 v[196:199], v182 offset:36864
	ds_read_b128 v[200:203], v182 offset:37888
	ds_read_b128 v[204:207], v182 offset:38912
	ds_read_b128 v[208:211], v182 offset:39936
	s_mov_b32 m0, s45
	s_nop 0
	global_load_lds_dwordx4 v175, s[34:35]
	s_mov_b32 m0, s46
	s_nop 0
	global_load_lds_dwordx4 v176, s[34:35]
	s_waitcnt vmcnt(8)
	s_waitcnt lgkmcnt(0)
	s_barrier
	s_setprio 1
	s_waitcnt lgkmcnt(7)
	v_mfma_f32_16x16x32_bf16 v[126:129], v[130:133], v[166:169], v[126:129]
	v_mfma_f32_16x16x32_bf16 v[122:125], v[138:141], v[166:169], v[122:125]
	s_waitcnt lgkmcnt(5)
	v_mfma_f32_16x16x32_bf16 v[110:113], v[130:133], v[188:191], v[110:113]
	v_mfma_f32_16x16x32_bf16 v[106:109], v[138:141], v[188:191], v[106:109]
	s_waitcnt lgkmcnt(3)
	v_mfma_f32_16x16x32_bf16 v[94:97], v[130:133], v[196:199], v[94:97]
	v_mfma_f32_16x16x32_bf16 v[90:93], v[138:141], v[196:199], v[90:93]
	s_waitcnt lgkmcnt(1)
	v_mfma_f32_16x16x32_bf16 v[78:81], v[130:133], v[204:207], v[78:81]
	v_mfma_f32_16x16x32_bf16 v[74:77], v[138:141], v[204:207], v[74:77]
	v_mfma_f32_16x16x32_bf16 v[126:129], v[134:137], v[184:187], v[126:129]
	v_mfma_f32_16x16x32_bf16 v[122:125], v[142:145], v[184:187], v[122:125]
	v_mfma_f32_16x16x32_bf16 v[110:113], v[134:137], v[192:195], v[110:113]
	v_mfma_f32_16x16x32_bf16 v[106:109], v[142:145], v[192:195], v[106:109]
	v_mfma_f32_16x16x32_bf16 v[94:97], v[134:137], v[200:203], v[94:97]
	v_mfma_f32_16x16x32_bf16 v[90:93], v[142:145], v[200:203], v[90:93]
	s_waitcnt lgkmcnt(0)
	v_mfma_f32_16x16x32_bf16 v[78:81], v[134:137], v[208:211], v[78:81]
	v_mfma_f32_16x16x32_bf16 v[74:77], v[142:145], v[208:211], v[74:77]
	s_setprio 0
	s_setprio 1
	v_mfma_f32_16x16x32_bf16 v[118:121], v[148:151], v[166:169], v[118:121]
	v_mfma_f32_16x16x32_bf16 v[114:117], v[156:159], v[166:169], v[114:117]
	v_mfma_f32_16x16x32_bf16 v[102:105], v[148:151], v[188:191], v[102:105]
	v_mfma_f32_16x16x32_bf16 v[98:101], v[156:159], v[188:191], v[98:101]
	v_mfma_f32_16x16x32_bf16 v[86:89], v[148:151], v[196:199], v[86:89]
	v_mfma_f32_16x16x32_bf16 v[82:85], v[156:159], v[196:199], v[82:85]
	v_mfma_f32_16x16x32_bf16 v[70:73], v[148:151], v[204:207], v[70:73]
	v_mfma_f32_16x16x32_bf16 v[66:69], v[156:159], v[204:207], v[66:69]
	v_mfma_f32_16x16x32_bf16 v[118:121], v[152:155], v[184:187], v[118:121]
	v_mfma_f32_16x16x32_bf16 v[114:117], v[162:165], v[184:187], v[114:117]
	v_mfma_f32_16x16x32_bf16 v[102:105], v[152:155], v[192:195], v[102:105]
	v_mfma_f32_16x16x32_bf16 v[98:101], v[162:165], v[192:195], v[98:101]
	v_mfma_f32_16x16x32_bf16 v[86:89], v[152:155], v[200:203], v[86:89]
	v_mfma_f32_16x16x32_bf16 v[82:85], v[162:165], v[200:203], v[82:85]
	v_mfma_f32_16x16x32_bf16 v[70:73], v[152:155], v[208:211], v[70:73]
	v_mfma_f32_16x16x32_bf16 v[66:69], v[162:165], v[208:211], v[66:69]
	s_setprio 0
	s_barrier
	ds_read_b128 v[166:169], v182 offset:49152
	ds_read_b128 v[184:187], v182 offset:50176
	ds_read_b128 v[188:191], v182 offset:51200
	ds_read_b128 v[192:195], v182 offset:52224
	ds_read_b128 v[196:199], v182 offset:53248
	ds_read_b128 v[200:203], v182 offset:54272
	ds_read_b128 v[204:207], v182 offset:55296
	ds_read_b128 v[208:211], v182 offset:56320
	s_mov_b32 m0, s47
	s_nop 0
	global_load_lds_dwordx4 v1, s[30:31]
	s_add_u32 s26, s26, 0x80080
	s_mov_b32 m0, s48
	s_nop 0
	global_load_lds_dwordx4 v172, s[30:31]
	s_addc_u32 s27, s27, 0
	s_mov_b32 m0, s51
	s_nop 0
	global_load_lds_dwordx4 v1, s[26:27]
	s_mov_b32 m0, s52
	s_nop 0
	global_load_lds_dwordx4 v172, s[26:27]
	s_mov_b32 m0, s49
	s_nop 0
	global_load_lds_dwordx4 v173, s[24:25]
	s_mov_b32 m0, s50
	s_nop 0
	global_load_lds_dwordx4 v174, s[24:25]
	s_waitcnt vmcnt(8)
	s_waitcnt lgkmcnt(0)
	s_barrier
	s_setprio 1
	s_waitcnt lgkmcnt(7)
	v_mfma_f32_16x16x32_bf16 v[62:65], v[130:133], v[166:169], v[62:65]
	v_mfma_f32_16x16x32_bf16 v[58:61], v[138:141], v[166:169], v[58:61]
	s_waitcnt lgkmcnt(5)
	v_mfma_f32_16x16x32_bf16 v[46:49], v[130:133], v[188:191], v[46:49]
	v_mfma_f32_16x16x32_bf16 v[42:45], v[138:141], v[188:191], v[42:45]
	s_waitcnt lgkmcnt(3)
	v_mfma_f32_16x16x32_bf16 v[30:33], v[130:133], v[196:199], v[30:33]
	v_mfma_f32_16x16x32_bf16 v[26:29], v[138:141], v[196:199], v[26:29]
	s_waitcnt lgkmcnt(1)
	v_mfma_f32_16x16x32_bf16 v[14:17], v[130:133], v[204:207], v[14:17]
	v_mfma_f32_16x16x32_bf16 v[10:13], v[138:141], v[204:207], v[10:13]
	v_mfma_f32_16x16x32_bf16 v[62:65], v[134:137], v[184:187], v[62:65]
	v_mfma_f32_16x16x32_bf16 v[58:61], v[142:145], v[184:187], v[58:61]
	v_mfma_f32_16x16x32_bf16 v[46:49], v[134:137], v[192:195], v[46:49]
	v_mfma_f32_16x16x32_bf16 v[42:45], v[142:145], v[192:195], v[42:45]
	v_mfma_f32_16x16x32_bf16 v[30:33], v[134:137], v[200:203], v[30:33]
	v_mfma_f32_16x16x32_bf16 v[26:29], v[142:145], v[200:203], v[26:29]
	s_waitcnt lgkmcnt(0)
	v_mfma_f32_16x16x32_bf16 v[14:17], v[134:137], v[208:211], v[14:17]
	v_mfma_f32_16x16x32_bf16 v[10:13], v[142:145], v[208:211], v[10:13]
	s_setprio 0
	s_setprio 1
	v_mfma_f32_16x16x32_bf16 v[54:57], v[148:151], v[166:169], v[54:57]
	v_mfma_f32_16x16x32_bf16 v[50:53], v[156:159], v[166:169], v[50:53]
	v_mfma_f32_16x16x32_bf16 v[38:41], v[148:151], v[188:191], v[38:41]
	v_mfma_f32_16x16x32_bf16 v[34:37], v[156:159], v[188:191], v[34:37]
	v_mfma_f32_16x16x32_bf16 v[22:25], v[148:151], v[196:199], v[22:25]
	v_mfma_f32_16x16x32_bf16 v[18:21], v[156:159], v[196:199], v[18:21]
	v_mfma_f32_16x16x32_bf16 v[6:9], v[148:151], v[204:207], v[6:9]
	v_mfma_f32_16x16x32_bf16 v[2:5], v[156:159], v[204:207], v[2:5]
	v_mfma_f32_16x16x32_bf16 v[54:57], v[152:155], v[184:187], v[54:57]
	v_mfma_f32_16x16x32_bf16 v[50:53], v[162:165], v[184:187], v[50:53]
	v_mfma_f32_16x16x32_bf16 v[38:41], v[152:155], v[192:195], v[38:41]
	v_mfma_f32_16x16x32_bf16 v[34:37], v[162:165], v[192:195], v[34:37]
	v_mfma_f32_16x16x32_bf16 v[22:25], v[152:155], v[200:203], v[22:25]
	v_mfma_f32_16x16x32_bf16 v[18:21], v[162:165], v[200:203], v[18:21]
	v_mfma_f32_16x16x32_bf16 v[6:9], v[152:155], v[208:211], v[6:9]
	v_mfma_f32_16x16x32_bf16 v[2:5], v[162:165], v[208:211], v[2:5]
	s_setprio 0
	s_barrier
	s_add_i32 s59, s59, 2
	s_add_u32 s17, s17, 0x100
	s_addc_u32 s19, s19, 0
	s_add_u32 s57, s57, 0x100
	s_addc_u32 s58, s58, 0
	s_add_u32 s28, s28, 0x100
	s_addc_u32 s29, s29, 0
	s_cmp_gt_u32 s59, 29
	s_cbranch_scc0 .LBB0_611
	s_and_b64 vcc, exec, s[14:15]
	s_cbranch_vccz .LBB0_614
	s_barrier

;     __device__ __forceinline__ const char* a_base(const Unit& u) const { return (const char*)A + (size_t)u.pm * BM * lda * 2; }
;     __device__ __forceinline__ const char* b_base(const Unit& u) const { return (const char*)Bt + (size_t)u.pn * BM * K * 2; }
; #define PG8_BAR __builtin_amdgcn_s_barrier()
;     ...
;     { int R[2], C[2];
; #pragma unroll
;       for (int i = 0; i < 2; ++i) { stage_rc(tid * 16 + i * 8192, R[i], C[i]); voffB[i] = (unsigned)(R[i] * K + C[i]) * 2u; } }
;     ...
;     const size_t kstep = (size_t)(BK * 2);
;     const size_t hstepB = (size_t)HALF * K * 2;
;     const unsigned ldsbase = (unsigned)__builtin_amdgcn_readfirstlane((int)((unsigned)(size_t)lds + (unsigned)wid * 1024u));
;     const int aoff = lds_byte(wr * 64 + fr, fq * 8), boff = lds_byte(wc * 32 + fr, fq * 8);
;     ...
;     constexpr int EST = HM ? Epi::kStoresHM : Epi::kStores;
;     ...
;     Unit cur, nxt; int ui = 0;
;     if (!S.next(0, cur)) return;
;     unsigned voffA[2][2];
;     { PG8_RC(); S.a_offs(cur, R, C, voffA); }
;     f32x4 acc[2][2][4][2];
; #pragma unroll
;     for (int a = 0; a < 2; ++a)
; #pragma unroll
;         for (int b = 0; b < 2; ++b)
; #pragma unroll
;             for (int m = 0; m < 4; ++m)
; #pragma unroll
;                 for (int n = 0; n < 2; ++n) acc[a][b][m][n] = (f32x4){0.f, 0.f, 0.f, 0.f};
;     bf16x8 At[4][2], B0[2][2], B1[2][2];
;     const char* cA = S.a_base(cur); const char* cB = S.b_base(cur);
;     const unsigned bias_lds = (unsigned)__builtin_amdgcn_readfirstlane((int)((unsigned)(size_t)lds + (unsigned)(AUX_OFF + 8192) + (unsigned)wid * 256u));
;     if constexpr (Epi::kBiasDMA) { if (lane < 16) glds16(E.bias_base(cur), E.bias_off(cur, wc, lane), bias_lds); }
;     const unsigned rowid_lds = (unsigned)__builtin_amdgcn_readfirstlane((int)((unsigned)(size_t)lds + (unsigned)AUX_OFF + (unsigned)wid * 512u));
;     if constexpr (Epi::kRowDMA) { if (lane < 32) glds16(E.row_base(cur), E.row_off(cur, wr, lane), rowid_lds); }
;     PG8_STAGEB(PG8_SB(0, 0), cB); PG8_STAGEB(PG8_SB(0, 1), cB + hstepB); PG8_STAGEA(PG8_SA(0, 0), cA, 0); if constexpr (!HM) PG8_STAGEA(PG8_SA(0, 1), cA, 1);
;     if (wr == 1) PG8_BAR;
;     if constexpr (HM) PG8_WAIT_V(0); else PG8_WAIT_V(2);
;     PG8_BAR;
;     PG8_STAGEB(PG8_SB(1, 0), cB + kstep); PG8_STAGEA(PG8_SA(1, 0), cA + kstep, 0); PG8_STAGEB(PG8_SB(1, 1), cB + hstepB + kstep);
;     PG8_WAIT_V(6); PG8_BAR;
.LBB0_677:
	s_andn2_b64 vcc, exec, s[0:1]
	s_cbranch_vccnz .LBB0_723
	v_bfe_i32 v4, v2, 27, 1
	v_lshlrev_b32_e32 v3, 4, v2
	v_lshrrev_b32_e32 v4, 22, v4
	v_add_u32_e32 v4, v3, v4
	v_and_b32_e32 v4, 0xfffffc00, v4
	v_sub_u32_e32 v4, v3, v4
	v_lshrrev_b32_e32 v5, 4, v4
	v_ashrrev_i32_e32 v1, 31, v2
	v_bitop3_b32 v4, v5, v4, 32 bitop3:0x6c
	v_lshrrev_b32_e32 v1, 26, v1
	s_waitcnt vmcnt(1)
	v_ashrrev_i32_e32 v6, 31, v4
	v_add_u32_e32 v1, v2, v1
	v_lshrrev_b32_e32 v6, 26, v6
	v_ashrrev_i32_e32 v1, 6, v1
	v_add_u32_e32 v6, v4, v6
	v_lshlrev_b32_e32 v5, 3, v1
	v_lshrrev_b32_e32 v7, 6, v6
	v_and_b32_e32 v6, 0xc0, v6
	v_and_b32_e32 v5, 0xffff0, v5
	v_lshlrev_b32_e32 v1, 5, v1
	v_sub_u32_e32 v4, v4, v6
	v_mov_b32_e32 v6, 1
	v_add_u32_e32 v5, v7, v5
	v_and_b32_e32 v1, 32, v1
	v_ashrrev_i16_sdwa v4, v6, sext(v4) dst_sel:DWORD dst_unused:UNUSED_PAD src0_sel:DWORD src1_sel:BYTE_0
	v_bfe_i32 v4, v4, 0, 16
	v_lshl_or_b32 v1, v5, 11, v1
	v_add_u32_e32 v3, 0x2000, v3
	v_add_lshl_u32 v1, v1, v4, 1
	v_ashrrev_i32_e32 v4, 31, v3
	v_lshrrev_b32_e32 v4, 22, v4
	v_add_u32_e32 v4, v3, v4
	v_ashrrev_i32_e32 v4, 10, v4
	v_mul_i32_i24_e32 v5, 0x400, v4
	v_sub_u32_e32 v3, v3, v5
	v_lshrrev_b32_e32 v5, 4, v3
	v_bitop3_b32 v3, v5, v3, 32 bitop3:0x6c
	v_ashrrev_i32_e32 v7, 31, v3
	v_lshrrev_b32_e32 v7, 26, v7
	v_add_u32_e32 v7, v3, v7
	v_lshlrev_b32_e32 v5, 3, v4
	v_lshrrev_b32_e32 v8, 6, v7
	v_and_b32_e32 v7, 0xc0, v7
	v_and_b32_e32 v5, 0xffff0, v5
	v_lshlrev_b32_e32 v4, 5, v4
	v_sub_u32_e32 v3, v3, v7
	v_add_u32_e32 v5, v8, v5
	v_and_b32_e32 v4, 32, v4
	v_ashrrev_i16_sdwa v3, v6, sext(v3) dst_sel:DWORD dst_unused:UNUSED_PAD src0_sel:DWORD src1_sel:BYTE_0
	v_bfe_i32 v3, v3, 0, 16
	v_lshl_or_b32 v4, v5, 11, v4
	v_add_lshl_u32 v200, v4, v3, 1
	v_mov_b32_e32 v3, v0
	s_load_dwordx2 s[10:11], s[96:97], 0x0
	s_waitcnt lgkmcnt(0)
	s_add_u32 s3, s94, 0x63000000
	v_ashrrev_i32_e32 v5, 31, v3
	v_lshrrev_b32_e32 v5, 26, v5
	v_lshlrev_b32_e32 v4, 4, v3
	v_add_u32_e32 v5, v3, v5
	v_bfe_i32 v3, v3, 27, 1
	v_lshrrev_b32_e32 v3, 22, v3
	v_add_u32_e32 v3, v4, v3
	v_and_b32_e32 v3, 0xfffffc00, v3
	v_sub_u32_e32 v3, v4, v3
	v_lshrrev_b32_e32 v7, 4, v3
	v_bitop3_b32 v3, v7, v3, 32 bitop3:0x6c
	v_ashrrev_i32_e32 v8, 31, v3
	v_lshrrev_b32_e32 v8, 26, v8
	v_add_u32_e32 v8, v3, v8
	v_ashrrev_i32_e32 v5, 6, v5
	v_ashrrev_i32_e32 v9, 6, v8
	v_and_b32_e32 v8, 0xc0, v8
	v_lshlrev_b32_e32 v7, 3, v5
	v_lshlrev_b32_e32 v5, 5, v5
	v_sub_u32_e32 v3, v3, v8
	v_and_b32_e32 v5, 32, v5
	v_ashrrev_i16_sdwa v3, v6, sext(v3) dst_sel:DWORD dst_unused:UNUSED_PAD src0_sel:DWORD src1_sel:BYTE_0
	v_add_u32_e32 v4, 0x2000, v4
	v_add_u32_sdwa v3, v5, sext(v3) dst_sel:DWORD dst_unused:UNUSED_PAD src0_sel:DWORD src1_sel:WORD_0
	v_ashrrev_i32_e32 v5, 31, v4
	v_lshrrev_b32_e32 v5, 22, v5
	v_add_u32_e32 v5, v4, v5
	s_addc_u32 s33, s95, 0
	v_ashrrev_i32_e32 v5, 10, v5
	s_add_u32 s40, s94, 0x3e00000
	v_mul_i32_i24_e32 v8, 0x400, v5
	s_addc_u32 s41, s95, 0
	s_lshl_b32 s1, s7, 10
	v_sub_u32_e32 v4, v4, v8
	s_ashr_i32 s27, s26, 31
	s_ashr_i32 s0, s6, 8
	s_add_i32 s42, s1, 0
	v_lshrrev_b32_e32 v8, 4, v4
	s_lshl_b64 s[8:9], s[26:27], 20
	v_and_b32_e32 v7, -16, v7
	v_bitop3_b32 v4, v8, v4, 32 bitop3:0x6c
	s_add_u32 s30, s3, s8
	v_add_u32_e32 v7, v9, v7
	v_ashrrev_i32_e32 v9, 31, v4
	s_addc_u32 s31, s33, s9
	s_ashr_i32 s25, s24, 31
	v_lshrrev_b32_e32 v9, 26, v9
	s_lshl_b64 s[8:9], s[24:25], 20
	v_add_u32_e32 v9, v4, v9
	s_add_u32 s34, s40, s8
	v_ashrrev_i32_e32 v10, 6, v9
	v_and_b32_e32 v9, 0xc0, v9
	s_addc_u32 s35, s41, s9
	s_add_i32 s43, s42, 0x10000
	s_mov_b32 m0, s43
	s_nop 0
	global_load_lds_dwordx4 v1, s[34:35]
	s_add_i32 s44, s42, 0x12000
	v_lshlrev_b32_e32 v8, 3, v5
	v_lshlrev_b32_e32 v5, 5, v5
	v_sub_u32_e32 v4, v4, v9
	s_mov_b32 m0, s44
	s_nop 0
	global_load_lds_dwordx4 v200, s[34:35]
	s_add_u32 s8, s34, 0x80000
	v_and_b32_e32 v8, -16, v8
	v_and_b32_e32 v5, 32, v5
	v_ashrrev_i16_sdwa v4, v6, sext(v4) dst_sel:DWORD dst_unused:UNUSED_PAD src0_sel:DWORD src1_sel:BYTE_0
	s_addc_u32 s9, s35, 0
	s_add_i32 s45, s42, 0x14000
	s_mov_b32 m0, s45
	s_nop 0
	global_load_lds_dwordx4 v1, s[8:9]
	v_add_u32_e32 v8, v10, v8
	v_add_u32_sdwa v4, v5, sext(v4) dst_sel:DWORD dst_unused:UNUSED_PAD src0_sel:DWORD src1_sel:WORD_0
	v_lshl_add_u32 v5, v7, 11, v3
	v_lshlrev_b32_e32 v7, 12, v7
	s_add_i32 s46, s42, 0x16000
	s_mov_b32 m0, s46
	s_nop 0
	global_load_lds_dwordx4 v200, s[8:9]
	v_lshl_add_u32 v201, v3, 1, v7
	v_lshlrev_b32_e32 v3, 12, v8
	s_mov_b32 m0, s42
	s_nop 0
	global_load_lds_dwordx4 v201, s[30:31]
	v_lshl_add_u32 v202, v4, 1, v3
	v_mov_b32_e32 v3, 0x80000
	s_add_i32 s47, s42, 0x2000
	s_mov_b32 m0, s47
	s_nop 0
	global_load_lds_dwordx4 v202, s[30:31]
	v_lshl_add_u32 v6, v8, 11, v4
	v_lshl_add_u32 v203, v5, 1, v3
	s_add_i32 s48, s42, 0x4000
	s_mov_b32 m0, s48
	s_nop 0
	global_load_lds_dwordx4 v203, s[30:31]
	v_lshl_add_u32 v204, v6, 1, v3
	s_add_i32 s49, s42, 0x6000
	s_mov_b32 m0, s49
	s_nop 0
	global_load_lds_dwordx4 v204, s[30:31]
	s_cmp_eq_u32 s0, 1
	s_mov_b32 s28, 0
	s_cselect_b64 s[12:13], -1, 0
	s_cmp_lg_u32 s0, 1
	s_cbranch_scc1 .LBB0_680
	s_barrier
.LBB0_680:
	v_bfe_u32 v4, v2, 4, 2
	s_add_u32 s14, s94, 0x67000000
	v_and_b32_e32 v3, 15, v2
	v_lshlrev_b32_e32 v5, 4, v4
	v_lshlrev_b32_e32 v2, 2, v2
	s_addc_u32 s15, s95, 0
	s_and_b32 s8, s7, 3
	v_lshl_or_b32 v205, s0, 6, v3
	v_lshl_or_b32 v3, v3, 6, v5
	s_lshl_b32 s0, s0, 13
	v_and_b32_e32 v2, 32, v2
	s_ashr_i32 s50, s2, 31
	s_ashr_i32 s51, s92, 31
	v_bitop3_b32 v5, v3, s0, v2 bitop3:0xde
	s_lshl_b32 s0, s8, 12
	v_bitop3_b32 v2, v3, s0, v2 bitop3:0xde
	s_add_u32 s0, s34, 0x80
	s_waitcnt vmcnt(2)
	s_barrier
	s_addc_u32 s1, s35, 0
	s_add_i32 s52, s42, 0x18000
	s_mov_b32 m0, s52
	s_nop 0
	global_load_lds_dwordx4 v1, s[0:1]
	s_add_i32 s53, s42, 0x1a000
	s_mov_b32 m0, s53
	s_nop 0
	global_load_lds_dwordx4 v200, s[0:1]
	s_add_u32 s0, s30, 0x80
	s_addc_u32 s1, s31, 0
	s_add_i32 s54, s42, 0x8000
	s_mov_b32 m0, s54
	s_nop 0
	global_load_lds_dwordx4 v201, s[0:1]
	s_add_i32 s55, s42, 0xa000
	s_mov_b32 m0, s55
	s_nop 0
	global_load_lds_dwordx4 v202, s[0:1]
	s_add_u32 s0, s34, 0x80080
	s_addc_u32 s1, s35, 0
	s_add_i32 s56, s42, 0x1c000
	s_add_i32 s57, s42, 0x1e000
	s_add_i32 s58, s42, 0xc000
	s_add_i32 s59, s42, 0xe000
	s_mov_b32 m0, s56
	s_nop 0
	global_load_lds_dwordx4 v1, s[0:1]
	s_cmpk_lt_u32 s6, 0x100
	s_mov_b32 m0, s57
	s_nop 0
	global_load_lds_dwordx4 v200, s[0:1]
	s_cselect_b64 s[16:17], -1, 0
	s_lshl_b32 s0, s8, 2
	s_add_u32 s0, s94, s0
	s_waitcnt vmcnt(6)
	s_addc_u32 s1, s95, 0
	v_lshlrev_b32_e32 v3, 2, v4
	s_add_u32 s60, s0, 0x6f000000
	v_add_u32_e32 v207, 0, v2
	v_mbcnt_lo_u32_b32 v2, -1, 0
	v_lshl_or_b32 v206, s8, 5, v3
	v_cmp_eq_u32_e64 s[6:7], 0, v4
	s_addc_u32 s61, s1, 0
	v_mov_b64_e32 v[252:253], 0x200
	v_mov_b64_e32 v[180:181], 0x1ff
	v_add_u32_e32 v208, 0x10000, v207
	v_add_u32_e32 v209, 0x14000, v207
	v_add_u32_e32 v210, 0, v5
	v_mbcnt_hi_u32_b32 v211, -1, v2
	s_barrier
	s_branch .LBB0_683

; #define LAS __attribute__((address_space(3)))
; #define PG8_STAGEA(bufoff, gbase, h) PG8_STAGE2(bufoff, gbase, voffA[h][0], voffA[h][1])
; #define PG8_LDA(dst, b, h) do { _Pragma("unroll") for (int m = 0; m < 4; ++m) _Pragma("unroll") for (int k = 0; k < 2; ++k) dst[m][k] = *(const LAS bf16x8*)(lds + PG8_SA(b, h) + aoff + m * 2048 + k * 1024); } while (0)
; #define PG8_LDB(dst, b, h) do { _Pragma("unroll") for (int n = 0; n < 2; ++n) _Pragma("unroll") for (int k = 0; k < 2; ++k) dst[n][k] = *(const LAS bf16x8*)(lds + PG8_SB(b, h) + boff + n * 2048 + k * 1024); } while (0)
; #define PG8_WAIT_K0() do { if (EST > 0 && t == 0 && ui > 0) asm volatile("s_waitcnt vmcnt(%0)" :: "n"((HM ? 6 : 8) + EST) : "memory"); else PG8_WAIT_K(); } while (0)
; #define PG8_WAIT_L(n) asm volatile("s_waitcnt lgkmcnt(" #n ")" ::: "memory")
; #define PG8_BAR __builtin_amdgcn_s_barrier()
; #define PG8_SCHED __builtin_amdgcn_sched_barrier(0)
;     ...
;             const char* a1 = cA + (size_t)(t + 1) * kstep;
;             const char* a2 = last ? nA : cA + (size_t)(t + 2) * kstep; const char* b2 = last ? nB : cB + (size_t)(t + 2) * kstep;
;             const char* a3 = a2 + kstep; const char* b3 = b2 + kstep;
;             PG8_LDB(B0, 0, 0); PG8_LDB(B1, 0, 1); PG8_SCHED; PG8_LDA(At, 0, 0); if constexpr (!HM) PG8_STAGEA(PG8_SA(1, 1), a1, 1);
;             if constexpr (Sched::kGather) { if (last && has_next) { const u32x4 tn = *(const LAS u32x4*)(S.aux + tid * 16); voffA[0][0] = tn.x; voffA[0][1] = tn.y; voffA[1][0] = tn.z; voffA[1][1] = tn.w; } }
;             PG8_WAIT_K0(); PG8_WAIT_L(0); PG8_BAR; PG8_MMA(0, 0, At, B0); PG8_MMA(0, 1, At, B1); PG8_BAR; PG8_SCHED;
.LBB0_691:
	ds_read_b128 v[18:21], v208
	ds_read_b128 v[22:25], v208 offset:1024
	ds_read_b128 v[26:29], v208 offset:2048
	ds_read_b128 v[30:33], v208 offset:3072
	s_waitcnt lgkmcnt(4)
	ds_read_b128 v[2:5], v209
	ds_read_b128 v[6:9], v209 offset:1024
	ds_read_b128 v[10:13], v209 offset:2048
	s_waitcnt vmcnt(0)
	ds_read_b128 v[14:17], v209 offset:3072
	s_cmp_lg_u32 s28, 0
	s_cselect_b64 s[28:29], -1, 0
	s_add_u32 s36, s30, 0x80
	s_addc_u32 s37, s31, 0
	ds_read_b128 v[74:77], v210
	ds_read_b128 v[82:85], v210 offset:1024
	ds_read_b128 v[90:93], v210 offset:2048
	ds_read_b128 v[98:101], v210 offset:3072
	ds_read_b128 v[86:89], v210 offset:4096
	ds_read_b128 v[94:97], v210 offset:5120
	ds_read_b128 v[70:73], v210 offset:6144
	ds_read_b128 v[78:81], v210 offset:7168
	s_mov_b32 m0, s58
	s_nop 0
	global_load_lds_dwordx4 v203, s[36:37]
	s_and_b64 vcc, exec, s[28:29]
	s_mov_b32 m0, s59
	s_nop 0
	global_load_lds_dwordx4 v204, s[36:37]
	s_cbranch_vccz .LBB0_720
	s_waitcnt vmcnt(40)
	s_cbranch_execnz .LBB0_694

; #define PG8_STAGEB(bufoff, gbase) PG8_STAGE2(bufoff, gbase, voffB[0], voffB[1])
; #define PG8_STAGEAS(bufoff, gbase, h) PG8_STAGE2(bufoff, gbase, voffA[h][0], voffA[h][1])
; #define PG8_LDA(dst, b, h) do { _Pragma("unroll") for (int m = 0; m < 4; ++m) _Pragma("unroll") for (int k = 0; k < 2; ++k) dst[m][k] = *(const LAS bf16x8*)(lds + PG8_SA(b, h) + aoff + m * 2048 + k * 1024); } while (0)
; #define PG8_WAIT_K0() do { if (EST > 0 && t == 0 && ui > 0) asm volatile("s_waitcnt vmcnt(%0)" :: "n"((HM ? 6 : 8) + EST) : "memory"); else PG8_WAIT_K(); } while (0)
; #define PG8_WAIT_L(n) asm volatile("s_waitcnt lgkmcnt(" #n ")" ::: "memory")
; #define PG8_BAR __builtin_amdgcn_s_barrier()
; #define PG8_SCHED __builtin_amdgcn_sched_barrier(0)
;     ...
;             PG8_WAIT_K0(); PG8_WAIT_L(0); PG8_BAR; PG8_MMA(0, 0, At, B0); PG8_MMA(0, 1, At, B1); PG8_BAR; PG8_SCHED;
;             if constexpr (!HM) PG8_LDA(At, 0, 1);
;             PG8_STAGEB(PG8_SB(0, 0), b2); PG8_STAGEB(PG8_SB(0, 1), b2 + hstepB); PG8_STAGEAS(PG8_SA(0, 0), a2, 0);
;             PG8_WAIT_K0(); PG8_WAIT_L(0); PG8_BAR; if constexpr (!HM) { PG8_MMA(1, 0, At, B0); PG8_MMA(1, 1, At, B1); } PG8_BAR; PG8_SCHED;
.LBB0_694:
	s_add_u32 s36, s30, 0x100
	s_waitcnt lgkmcnt(0)
	s_addc_u32 s37, s31, 0
	s_add_u32 s38, s34, 0x100
	s_addc_u32 s39, s35, 0
	s_barrier
	s_setprio 1
	s_waitcnt lgkmcnt(7)
	v_mfma_f32_16x16x32_bf16 v[34:37], v[18:21], v[74:77], 0
	v_mfma_f32_16x16x32_bf16 v[38:41], v[26:29], v[74:77], 0
	s_waitcnt lgkmcnt(5)
	v_mfma_f32_16x16x32_bf16 v[42:45], v[18:21], v[90:93], 0
	v_mfma_f32_16x16x32_bf16 v[46:49], v[26:29], v[90:93], 0
	s_waitcnt lgkmcnt(3)
	v_mfma_f32_16x16x32_bf16 v[50:53], v[18:21], v[86:89], 0
	v_mfma_f32_16x16x32_bf16 v[54:57], v[26:29], v[86:89], 0
	s_waitcnt lgkmcnt(1)
	v_mfma_f32_16x16x32_bf16 v[58:61], v[18:21], v[70:73], 0
	v_mfma_f32_16x16x32_bf16 v[62:65], v[26:29], v[70:73], 0
	v_mfma_f32_16x16x32_bf16 v[118:121], v[22:25], v[82:85], v[34:37]
	v_mfma_f32_16x16x32_bf16 v[38:41], v[30:33], v[82:85], v[38:41]
	v_mfma_f32_16x16x32_bf16 v[42:45], v[22:25], v[98:101], v[42:45]
	v_mfma_f32_16x16x32_bf16 v[46:49], v[30:33], v[98:101], v[46:49]
	v_mfma_f32_16x16x32_bf16 v[50:53], v[22:25], v[94:97], v[50:53]
	v_mfma_f32_16x16x32_bf16 v[54:57], v[30:33], v[94:97], v[54:57]
	s_waitcnt lgkmcnt(0)
	v_mfma_f32_16x16x32_bf16 v[58:61], v[22:25], v[78:81], v[58:61]
	v_mfma_f32_16x16x32_bf16 v[62:65], v[30:33], v[78:81], v[62:65]
	s_setprio 0
	s_setprio 1
	v_mfma_f32_16x16x32_bf16 v[66:69], v[2:5], v[74:77], 0
	v_mfma_f32_16x16x32_bf16 v[74:77], v[10:13], v[74:77], 0
	v_mfma_f32_16x16x32_bf16 v[66:69], v[6:9], v[82:85], v[66:69]
	v_mfma_f32_16x16x32_bf16 v[74:77], v[14:17], v[82:85], v[74:77]
	v_mfma_f32_16x16x32_bf16 v[82:85], v[2:5], v[90:93], 0
	v_mfma_f32_16x16x32_bf16 v[90:93], v[10:13], v[90:93], 0
	v_mfma_f32_16x16x32_bf16 v[82:85], v[6:9], v[98:101], v[82:85]
	v_mfma_f32_16x16x32_bf16 v[90:93], v[14:17], v[98:101], v[90:93]
	v_mfma_f32_16x16x32_bf16 v[98:101], v[2:5], v[86:89], 0
	v_mfma_f32_16x16x32_bf16 v[86:89], v[10:13], v[86:89], 0
	v_mfma_f32_16x16x32_bf16 v[134:137], v[14:17], v[94:97], v[86:89]
	v_mfma_f32_16x16x32_bf16 v[86:89], v[2:5], v[70:73], 0
	v_mfma_f32_16x16x32_bf16 v[70:73], v[10:13], v[70:73], 0
	v_mfma_f32_16x16x32_bf16 v[130:133], v[6:9], v[94:97], v[98:101]
	v_mfma_f32_16x16x32_bf16 v[138:141], v[6:9], v[78:81], v[86:89]
	v_mfma_f32_16x16x32_bf16 v[142:145], v[14:17], v[78:81], v[70:73]
	s_setprio 0
	s_barrier
	ds_read_b128 v[106:109], v210 offset:16384
	ds_read_b128 v[110:113], v210 offset:17408
	ds_read_b128 v[98:101], v210 offset:18432
	ds_read_b128 v[102:105], v210 offset:19456
	ds_read_b128 v[86:89], v210 offset:20480
	ds_read_b128 v[94:97], v210 offset:21504
	ds_read_b128 v[70:73], v210 offset:22528
	ds_read_b128 v[78:81], v210 offset:23552
	s_mov_b32 m0, s43
	s_nop 0
	global_load_lds_dwordx4 v1, s[38:39]
	s_mov_b32 m0, s44
	s_nop 0
	global_load_lds_dwordx4 v200, s[38:39]
	s_add_u32 s38, s34, 0x80100
	s_addc_u32 s39, s35, 0
	s_mov_b32 m0, s45
	s_nop 0
	global_load_lds_dwordx4 v1, s[38:39]
	s_and_b64 vcc, exec, s[28:29]
	s_mov_b32 m0, s46
	s_nop 0
	global_load_lds_dwordx4 v200, s[38:39]
	s_mov_b32 m0, s42
	s_nop 0
	global_load_lds_dwordx4 v201, s[36:37]
	s_mov_b32 m0, s47
	s_nop 0
	global_load_lds_dwordx4 v202, s[36:37]
	s_cbranch_vccz .LBB0_721
	s_waitcnt vmcnt(40)
	s_cbranch_execnz .LBB0_697

; #define PG8_STAGEAS(bufoff, gbase, h) PG8_STAGE2(bufoff, gbase, voffA[h][0], voffA[h][1])
; #define PG8_LDA(dst, b, h) do { _Pragma("unroll") for (int m = 0; m < 4; ++m) _Pragma("unroll") for (int k = 0; k < 2; ++k) dst[m][k] = *(const LAS bf16x8*)(lds + PG8_SA(b, h) + aoff + m * 2048 + k * 1024); } while (0)
; #define PG8_LDB(dst, b, h) do { _Pragma("unroll") for (int n = 0; n < 2; ++n) _Pragma("unroll") for (int k = 0; k < 2; ++k) dst[n][k] = *(const LAS bf16x8*)(lds + PG8_SB(b, h) + boff + n * 2048 + k * 1024); } while (0)
; #define PG8_WAIT_K() do { if constexpr (HM) PG8_WAIT_V(6); else PG8_WAIT_V(8); } while (0)
; #define PG8_WAIT_K0() do { if (EST > 0 && t == 0 && ui > 0) asm volatile("s_waitcnt vmcnt(%0)" :: "n"((HM ? 6 : 8) + EST) : "memory"); else PG8_WAIT_K(); } while (0)
; #define PG8_WAIT_L(n) asm volatile("s_waitcnt lgkmcnt(" #n ")" ::: "memory")
; #define PG8_BAR __builtin_amdgcn_s_barrier()
; #define PG8_SCHED __builtin_amdgcn_sched_barrier(0)
;     ...
;             PG8_WAIT_K0(); PG8_WAIT_L(0); PG8_BAR; if constexpr (!HM) { PG8_MMA(1, 0, At, B0); PG8_MMA(1, 1, At, B1); } PG8_BAR; PG8_SCHED;
;             PG8_LDB(B0, 1, 0); PG8_LDB(B1, 1, 1); PG8_SCHED; PG8_LDA(At, 1, 0); if constexpr (!HM) PG8_STAGEAS(PG8_SA(0, 1), a2, 1);
;             PG8_WAIT_K(); PG8_WAIT_L(0); PG8_BAR; PG8_MMA(0, 0, At, B0); PG8_MMA(0, 1, At, B1); PG8_BAR; PG8_SCHED;
.LBB0_697:
	s_add_u32 s28, s30, 0x180
	s_waitcnt lgkmcnt(0)
	s_addc_u32 s29, s31, 0
	s_add_u32 s38, s34, 0x180
	s_addc_u32 s39, s35, 0
	s_barrier
	s_setprio 1
	s_waitcnt lgkmcnt(7)
	v_mfma_f32_16x16x32_bf16 v[114:117], v[18:21], v[106:109], 0
	s_waitcnt lgkmcnt(6)
	v_mfma_f32_16x16x32_bf16 v[148:151], v[22:25], v[110:113], v[114:117]
	v_mfma_f32_16x16x32_bf16 v[114:117], v[26:29], v[106:109], 0
	v_mfma_f32_16x16x32_bf16 v[152:155], v[30:33], v[110:113], v[114:117]
	s_waitcnt lgkmcnt(5)
	v_mfma_f32_16x16x32_bf16 v[114:117], v[18:21], v[98:101], 0
	s_waitcnt lgkmcnt(4)
	v_mfma_f32_16x16x32_bf16 v[156:159], v[22:25], v[102:105], v[114:117]
	v_mfma_f32_16x16x32_bf16 v[114:117], v[26:29], v[98:101], 0
	v_mfma_f32_16x16x32_bf16 v[160:163], v[30:33], v[102:105], v[114:117]
	s_waitcnt lgkmcnt(3)
	v_mfma_f32_16x16x32_bf16 v[114:117], v[18:21], v[86:89], 0
	s_waitcnt lgkmcnt(1)
	v_mfma_f32_16x16x32_bf16 v[18:21], v[18:21], v[70:73], 0
	v_mfma_f32_16x16x32_bf16 v[164:167], v[22:25], v[94:97], v[114:117]
	s_waitcnt lgkmcnt(0)
	v_mfma_f32_16x16x32_bf16 v[18:21], v[22:25], v[78:81], v[18:21]
	v_mfma_f32_16x16x32_bf16 v[22:25], v[26:29], v[70:73], 0
	v_mfma_f32_16x16x32_bf16 v[114:117], v[26:29], v[86:89], 0
	v_mfma_f32_16x16x32_bf16 v[26:29], v[30:33], v[78:81], v[22:25]
	v_mfma_f32_16x16x32_bf16 v[168:171], v[30:33], v[94:97], v[114:117]
	s_setprio 0
	s_setprio 1
	v_mfma_f32_16x16x32_bf16 v[22:25], v[2:5], v[106:109], 0
	v_mfma_f32_16x16x32_bf16 v[172:175], v[6:9], v[110:113], v[22:25]
	v_mfma_f32_16x16x32_bf16 v[22:25], v[10:13], v[106:109], 0
	v_mfma_f32_16x16x32_bf16 v[182:185], v[14:17], v[110:113], v[22:25]
	v_mfma_f32_16x16x32_bf16 v[22:25], v[2:5], v[98:101], 0
	v_mfma_f32_16x16x32_bf16 v[186:189], v[6:9], v[102:105], v[22:25]
	v_mfma_f32_16x16x32_bf16 v[22:25], v[10:13], v[98:101], 0
	v_mfma_f32_16x16x32_bf16 v[190:193], v[14:17], v[102:105], v[22:25]
	v_mfma_f32_16x16x32_bf16 v[22:25], v[2:5], v[86:89], 0
	v_mfma_f32_16x16x32_bf16 v[2:5], v[2:5], v[70:73], 0
	v_mfma_f32_16x16x32_bf16 v[194:197], v[6:9], v[94:97], v[22:25]
	v_mfma_f32_16x16x32_bf16 v[22:25], v[10:13], v[86:89], 0
	v_mfma_f32_16x16x32_bf16 v[2:5], v[6:9], v[78:81], v[2:5]
	v_mfma_f32_16x16x32_bf16 v[6:9], v[10:13], v[70:73], 0
	v_mfma_f32_16x16x32_bf16 v[212:215], v[14:17], v[94:97], v[22:25]
	v_mfma_f32_16x16x32_bf16 v[216:219], v[14:17], v[78:81], v[6:9]
	s_setprio 0
	s_barrier
	v_add_u32_e32 v146, 0x18000, v207
	v_add_u32_e32 v147, 0x1c000, v207
	s_nop 1
	ds_read_b128 v[6:9], v146
	ds_read_b128 v[10:13], v146 offset:1024
	ds_read_b128 v[220:223], v146 offset:2048
	ds_read_b128 v[224:227], v146 offset:3072
	ds_read_b128 v[228:231], v147
	ds_read_b128 v[232:235], v147 offset:1024
	ds_read_b128 v[236:239], v147 offset:2048
	ds_read_b128 v[240:243], v147 offset:3072
	ds_read_b128 v[14:17], v210 offset:32768
	ds_read_b128 v[22:25], v210 offset:33792
	ds_read_b128 v[30:33], v210 offset:34816
	ds_read_b128 v[98:101], v210 offset:35840
	ds_read_b128 v[244:247], v210 offset:36864
	ds_read_b128 v[248:251], v210 offset:37888
	ds_read_b128 v[176:179], v210 offset:38912
	ds_read_b128 v[34:37], v210 offset:39936
	s_mov_b32 m0, s48
	s_nop 0
	global_load_lds_dwordx4 v203, s[36:37]
	s_mov_b32 m0, s49
	s_nop 0
	global_load_lds_dwordx4 v204, s[36:37]
	s_waitcnt vmcnt(8)
	s_waitcnt lgkmcnt(0)
	s_barrier
	s_setprio 1
	s_waitcnt lgkmcnt(7)
	v_mfma_f32_16x16x32_bf16 v[38:41], v[220:223], v[14:17], v[38:41]
	v_mfma_f32_16x16x32_bf16 v[70:73], v[6:9], v[14:17], v[118:121]
	s_waitcnt lgkmcnt(6)
	v_mfma_f32_16x16x32_bf16 v[118:121], v[224:227], v[22:25], v[38:41]
	s_waitcnt lgkmcnt(5)
	v_mfma_f32_16x16x32_bf16 v[38:41], v[6:9], v[30:33], v[42:45]
	s_waitcnt lgkmcnt(4)
	v_mfma_f32_16x16x32_bf16 v[110:113], v[10:13], v[98:101], v[38:41]
	v_mfma_f32_16x16x32_bf16 v[38:41], v[220:223], v[30:33], v[46:49]
	v_mfma_f32_16x16x32_bf16 v[102:105], v[224:227], v[98:101], v[38:41]
	s_waitcnt lgkmcnt(3)
	v_mfma_f32_16x16x32_bf16 v[38:41], v[6:9], v[244:247], v[50:53]
	s_waitcnt lgkmcnt(2)
	v_mfma_f32_16x16x32_bf16 v[94:97], v[10:13], v[248:251], v[38:41]
	v_mfma_f32_16x16x32_bf16 v[38:41], v[220:223], v[244:247], v[54:57]
	v_mfma_f32_16x16x32_bf16 v[86:89], v[224:227], v[248:251], v[38:41]
	s_waitcnt lgkmcnt(1)
	v_mfma_f32_16x16x32_bf16 v[38:41], v[6:9], v[176:179], v[58:61]
	s_waitcnt lgkmcnt(0)
	v_mfma_f32_16x16x32_bf16 v[78:81], v[10:13], v[34:37], v[38:41]
	v_mfma_f32_16x16x32_bf16 v[38:41], v[220:223], v[176:179], v[62:65]
	v_mfma_f32_16x16x32_bf16 v[126:129], v[10:13], v[22:25], v[70:73]
	v_mfma_f32_16x16x32_bf16 v[70:73], v[224:227], v[34:37], v[38:41]
	s_setprio 0
	s_setprio 1
	v_mfma_f32_16x16x32_bf16 v[38:41], v[228:231], v[14:17], v[66:69]
	v_mfma_f32_16x16x32_bf16 v[14:17], v[236:239], v[14:17], v[74:77]
	v_mfma_f32_16x16x32_bf16 v[114:117], v[240:243], v[22:25], v[14:17]
	v_mfma_f32_16x16x32_bf16 v[14:17], v[228:231], v[30:33], v[82:85]
	v_mfma_f32_16x16x32_bf16 v[106:109], v[232:235], v[98:101], v[14:17]
	v_mfma_f32_16x16x32_bf16 v[14:17], v[236:239], v[30:33], v[90:93]
	v_mfma_f32_16x16x32_bf16 v[98:101], v[240:243], v[98:101], v[14:17]
	v_mfma_f32_16x16x32_bf16 v[14:17], v[228:231], v[244:247], v[130:133]
	v_mfma_f32_16x16x32_bf16 v[90:93], v[232:235], v[248:251], v[14:17]
	v_mfma_f32_16x16x32_bf16 v[14:17], v[236:239], v[244:247], v[134:137]
	v_mfma_f32_16x16x32_bf16 v[82:85], v[240:243], v[248:251], v[14:17]
	v_mfma_f32_16x16x32_bf16 v[14:17], v[228:231], v[176:179], v[138:141]
	v_mfma_f32_16x16x32_bf16 v[74:77], v[232:235], v[34:37], v[14:17]
	v_mfma_f32_16x16x32_bf16 v[14:17], v[236:239], v[176:179], v[142:145]
	v_mfma_f32_16x16x32_bf16 v[122:125], v[232:235], v[22:25], v[38:41]
	v_mfma_f32_16x16x32_bf16 v[66:69], v[240:243], v[34:37], v[14:17]
	s_setprio 0
	s_barrier
; #define LAS __attribute__((address_space(3)))
; #define PG8_STAGEB(bufoff, gbase) PG8_STAGE2(bufoff, gbase, voffB[0], voffB[1])
; #define PG8_STAGEA(bufoff, gbase, h) PG8_STAGE2(bufoff, gbase, voffA[h][0], voffA[h][1])
; #define PG8_STAGEAS(bufoff, gbase, h) PG8_STAGE2(bufoff, gbase, voffA[h][0], voffA[h][1])
; #define PG8_LDA(dst, b, h) do { _Pragma("unroll") for (int m = 0; m < 4; ++m) _Pragma("unroll") for (int k = 0; k < 2; ++k) dst[m][k] = *(const LAS bf16x8*)(lds + PG8_SA(b, h) + aoff + m * 2048 + k * 1024); } while (0)
; #define PG8_LDB(dst, b, h) do { _Pragma("unroll") for (int n = 0; n < 2; ++n) _Pragma("unroll") for (int k = 0; k < 2; ++k) dst[n][k] = *(const LAS bf16x8*)(lds + PG8_SB(b, h) + boff + n * 2048 + k * 1024); } while (0)
; #define PG8_WAIT_K() do { if constexpr (HM) PG8_WAIT_V(6); else PG8_WAIT_V(8); } while (0)
; #define PG8_WAIT_K0() do { if (EST > 0 && t == 0 && ui > 0) asm volatile("s_waitcnt vmcnt(%0)" :: "n"((HM ? 6 : 8) + EST) : "memory"); else PG8_WAIT_K(); } while (0)
; #define PG8_WAIT_L(n) asm volatile("s_waitcnt lgkmcnt(" #n ")" ::: "memory")
; #define PG8_BAR __builtin_amdgcn_s_barrier()
; #define PG8_SCHED __builtin_amdgcn_sched_barrier(0)
;     ...
;             const char* a1 = cA + (size_t)(t + 1) * kstep;
;             const char* a2 = last ? nA : cA + (size_t)(t + 2) * kstep; const char* b2 = last ? nB : cB + (size_t)(t + 2) * kstep;
;             const char* a3 = a2 + kstep; const char* b3 = b2 + kstep;
;             PG8_LDB(B0, 0, 0); PG8_LDB(B1, 0, 1); PG8_SCHED; PG8_LDA(At, 0, 0); if constexpr (!HM) PG8_STAGEA(PG8_SA(1, 1), a1, 1);
;             if constexpr (Sched::kGather) { if (last && has_next) { const u32x4 tn = *(const LAS u32x4*)(S.aux + tid * 16); voffA[0][0] = tn.x; voffA[0][1] = tn.y; voffA[1][0] = tn.z; voffA[1][1] = tn.w; } }
;             PG8_WAIT_K0(); PG8_WAIT_L(0); PG8_BAR; PG8_MMA(0, 0, At, B0); PG8_MMA(0, 1, At, B1); PG8_BAR; PG8_SCHED;
;     ...
;             if constexpr (!HM) PG8_LDA(At, 1, 1);
;             PG8_STAGEB(PG8_SB(1, 0), b3); PG8_STAGEB(PG8_SB(1, 1), b3 + hstepB); PG8_STAGEAS(PG8_SA(1, 0), a3, 0);
;             PG8_WAIT_K(); PG8_WAIT_L(0); PG8_BAR; if constexpr (!HM) { PG8_MMA(1, 0, At, B0); PG8_MMA(1, 1, At, B1); } PG8_BAR; PG8_SCHED;
	ds_read_b128 v[34:37], v210 offset:49152
	ds_read_b128 v[42:45], v210 offset:50176
	ds_read_b128 v[130:133], v210 offset:51200
	ds_read_b128 v[134:137], v210 offset:52224
	ds_read_b128 v[138:141], v210 offset:53248
	ds_read_b128 v[142:145], v210 offset:54272
	ds_read_b128 v[176:179], v210 offset:55296
	ds_read_b128 v[244:247], v210 offset:56320
	s_mov_b32 m0, s52
	s_nop 0
	global_load_lds_dwordx4 v1, s[38:39]
	s_add_u32 s36, s34, 0x80180
	s_mov_b32 m0, s53
	s_nop 0
	global_load_lds_dwordx4 v200, s[38:39]
	s_addc_u32 s37, s35, 0
	s_mov_b32 m0, s56
	s_nop 0
	global_load_lds_dwordx4 v1, s[36:37]
	s_mov_b32 m0, s57
	s_nop 0
	global_load_lds_dwordx4 v200, s[36:37]
	s_mov_b32 m0, s54
	s_nop 0
	global_load_lds_dwordx4 v201, s[28:29]
	s_mov_b32 m0, s55
	s_nop 0
	global_load_lds_dwordx4 v202, s[28:29]
	s_waitcnt vmcnt(8)
	s_waitcnt lgkmcnt(0)
	s_barrier
	s_setprio 1
	s_waitcnt lgkmcnt(7)
	v_mfma_f32_16x16x32_bf16 v[14:17], v[6:9], v[34:37], v[148:151]
	s_waitcnt lgkmcnt(6)
	v_mfma_f32_16x16x32_bf16 v[62:65], v[10:13], v[42:45], v[14:17]
	v_mfma_f32_16x16x32_bf16 v[14:17], v[220:223], v[34:37], v[152:155]
	v_mfma_f32_16x16x32_bf16 v[54:57], v[224:227], v[42:45], v[14:17]
	s_waitcnt lgkmcnt(5)
	v_mfma_f32_16x16x32_bf16 v[14:17], v[6:9], v[130:133], v[156:159]
	s_waitcnt lgkmcnt(4)
	v_mfma_f32_16x16x32_bf16 v[46:49], v[10:13], v[134:137], v[14:17]
	v_mfma_f32_16x16x32_bf16 v[14:17], v[220:223], v[130:133], v[160:163]
	v_mfma_f32_16x16x32_bf16 v[38:41], v[224:227], v[134:137], v[14:17]
	s_waitcnt lgkmcnt(3)
	v_mfma_f32_16x16x32_bf16 v[14:17], v[6:9], v[138:141], v[164:167]
	s_waitcnt lgkmcnt(2)
	v_mfma_f32_16x16x32_bf16 v[30:33], v[10:13], v[142:145], v[14:17]
	v_mfma_f32_16x16x32_bf16 v[14:17], v[220:223], v[138:141], v[168:171]
	s_waitcnt lgkmcnt(1)
	v_mfma_f32_16x16x32_bf16 v[6:9], v[6:9], v[176:179], v[18:21]
	v_mfma_f32_16x16x32_bf16 v[22:25], v[224:227], v[142:145], v[14:17]
	s_waitcnt lgkmcnt(0)
	v_mfma_f32_16x16x32_bf16 v[14:17], v[10:13], v[244:247], v[6:9]
	v_mfma_f32_16x16x32_bf16 v[6:9], v[220:223], v[176:179], v[26:29]
	v_mfma_f32_16x16x32_bf16 v[6:9], v[224:227], v[244:247], v[6:9]
	s_setprio 0
	s_setprio 1
	v_mfma_f32_16x16x32_bf16 v[10:13], v[228:231], v[34:37], v[172:175]
	v_mfma_f32_16x16x32_bf16 v[58:61], v[232:235], v[42:45], v[10:13]
	v_mfma_f32_16x16x32_bf16 v[10:13], v[236:239], v[34:37], v[182:185]
	v_mfma_f32_16x16x32_bf16 v[50:53], v[240:243], v[42:45], v[10:13]
	v_mfma_f32_16x16x32_bf16 v[10:13], v[228:231], v[130:133], v[186:189]
	v_mfma_f32_16x16x32_bf16 v[42:45], v[232:235], v[134:137], v[10:13]
	v_mfma_f32_16x16x32_bf16 v[10:13], v[236:239], v[130:133], v[190:193]
	v_mfma_f32_16x16x32_bf16 v[34:37], v[240:243], v[134:137], v[10:13]
	v_mfma_f32_16x16x32_bf16 v[10:13], v[228:231], v[138:141], v[194:197]
	v_mfma_f32_16x16x32_bf16 v[26:29], v[232:235], v[142:145], v[10:13]
	v_mfma_f32_16x16x32_bf16 v[10:13], v[236:239], v[138:141], v[212:215]
	v_mfma_f32_16x16x32_bf16 v[2:5], v[228:231], v[176:179], v[2:5]
	v_mfma_f32_16x16x32_bf16 v[18:21], v[240:243], v[142:145], v[10:13]
	v_mfma_f32_16x16x32_bf16 v[10:13], v[232:235], v[244:247], v[2:5]
	v_mfma_f32_16x16x32_bf16 v[2:5], v[236:239], v[176:179], v[216:219]
	v_mfma_f32_16x16x32_bf16 v[2:5], v[240:243], v[244:247], v[2:5]
	s_setprio 0
	s_barrier
	s_add_u32 s19, s30, 0x200
	s_addc_u32 s21, s31, 0
	s_add_u32 s25, s34, 0x200
	s_addc_u32 s27, s35, 0
	s_mov_b32 s63, 0
.LBB0_698:
	ds_read_b128 v[130:133], v208
	ds_read_b128 v[134:137], v208 offset:1024
	ds_read_b128 v[138:141], v208 offset:2048
	ds_read_b128 v[142:145], v208 offset:3072
	ds_read_b128 v[148:151], v209
	ds_read_b128 v[152:155], v209 offset:1024
	ds_read_b128 v[156:159], v209 offset:2048
	ds_read_b128 v[160:163], v209 offset:3072
	s_cmp_eq_u32 s63, 28
	s_cselect_b32 s38, s0, s19
	s_cselect_b32 s39, s1, s21
	s_cselect_b32 s34, s22, s25
	s_cselect_b32 s35, s23, s27
	s_add_u32 s30, s38, 0x80
	s_addc_u32 s31, s39, 0
	ds_read_b128 v[164:167], v210
	ds_read_b128 v[168:171], v210 offset:1024
	ds_read_b128 v[172:175], v210 offset:2048
	ds_read_b128 v[176:179], v210 offset:3072
	ds_read_b128 v[182:185], v210 offset:4096
	ds_read_b128 v[186:189], v210 offset:5120
	ds_read_b128 v[190:193], v210 offset:6144
	ds_read_b128 v[194:197], v210 offset:7168
	s_mov_b32 m0, s58
	s_nop 0
	global_load_lds_dwordx4 v203, s[28:29]
	s_add_u32 s36, s34, 0x80
	s_mov_b32 m0, s59
	s_nop 0
	global_load_lds_dwordx4 v204, s[28:29]
	s_waitcnt vmcnt(8)
	s_waitcnt lgkmcnt(0)
	s_addc_u32 s37, s35, 0
	s_barrier
; #define PG8_STAGEB(bufoff, gbase) PG8_STAGE2(bufoff, gbase, voffB[0], voffB[1])
; #define PG8_STAGEAS(bufoff, gbase, h) PG8_STAGE2(bufoff, gbase, voffA[h][0], voffA[h][1])
; #define PG8_LDA(dst, b, h) do { _Pragma("unroll") for (int m = 0; m < 4; ++m) _Pragma("unroll") for (int k = 0; k < 2; ++k) dst[m][k] = *(const LAS bf16x8*)(lds + PG8_SA(b, h) + aoff + m * 2048 + k * 1024); } while (0)
; #define PG8_WAIT_K0() do { if (EST > 0 && t == 0 && ui > 0) asm volatile("s_waitcnt vmcnt(%0)" :: "n"((HM ? 6 : 8) + EST) : "memory"); else PG8_WAIT_K(); } while (0)
; #define PG8_WAIT_L(n) asm volatile("s_waitcnt lgkmcnt(" #n ")" ::: "memory")
; #define PG8_BAR __builtin_amdgcn_s_barrier()
; #define PG8_SCHED __builtin_amdgcn_sched_barrier(0)
;     ...
;             PG8_WAIT_K0(); PG8_WAIT_L(0); PG8_BAR; PG8_MMA(0, 0, At, B0); PG8_MMA(0, 1, At, B1); PG8_BAR; PG8_SCHED;
;             if constexpr (!HM) PG8_LDA(At, 0, 1);
;             PG8_STAGEB(PG8_SB(0, 0), b2); PG8_STAGEB(PG8_SB(0, 1), b2 + hstepB); PG8_STAGEAS(PG8_SA(0, 0), a2, 0);
;             PG8_WAIT_K0(); PG8_WAIT_L(0); PG8_BAR; if constexpr (!HM) { PG8_MMA(1, 0, At, B0); PG8_MMA(1, 1, At, B1); } PG8_BAR; PG8_SCHED;
	s_setprio 1
	s_waitcnt lgkmcnt(7)
	v_mfma_f32_16x16x32_bf16 v[126:129], v[130:133], v[164:167], v[126:129]
	v_mfma_f32_16x16x32_bf16 v[118:121], v[138:141], v[164:167], v[118:121]
	s_waitcnt lgkmcnt(5)
	v_mfma_f32_16x16x32_bf16 v[110:113], v[130:133], v[172:175], v[110:113]
	v_mfma_f32_16x16x32_bf16 v[102:105], v[138:141], v[172:175], v[102:105]
	s_waitcnt lgkmcnt(3)
	v_mfma_f32_16x16x32_bf16 v[94:97], v[130:133], v[182:185], v[94:97]
	v_mfma_f32_16x16x32_bf16 v[86:89], v[138:141], v[182:185], v[86:89]
	s_waitcnt lgkmcnt(1)
	v_mfma_f32_16x16x32_bf16 v[78:81], v[130:133], v[190:193], v[78:81]
	v_mfma_f32_16x16x32_bf16 v[70:73], v[138:141], v[190:193], v[70:73]
	v_mfma_f32_16x16x32_bf16 v[126:129], v[134:137], v[168:171], v[126:129]
	v_mfma_f32_16x16x32_bf16 v[118:121], v[142:145], v[168:171], v[118:121]
	v_mfma_f32_16x16x32_bf16 v[110:113], v[134:137], v[176:179], v[110:113]
	v_mfma_f32_16x16x32_bf16 v[102:105], v[142:145], v[176:179], v[102:105]
	v_mfma_f32_16x16x32_bf16 v[94:97], v[134:137], v[186:189], v[94:97]
	v_mfma_f32_16x16x32_bf16 v[86:89], v[142:145], v[186:189], v[86:89]
	s_waitcnt lgkmcnt(0)
	v_mfma_f32_16x16x32_bf16 v[78:81], v[134:137], v[194:197], v[78:81]
	v_mfma_f32_16x16x32_bf16 v[70:73], v[142:145], v[194:197], v[70:73]
	s_setprio 0
	s_setprio 1
	v_mfma_f32_16x16x32_bf16 v[122:125], v[148:151], v[164:167], v[122:125]
	v_mfma_f32_16x16x32_bf16 v[114:117], v[156:159], v[164:167], v[114:117]
	v_mfma_f32_16x16x32_bf16 v[106:109], v[148:151], v[172:175], v[106:109]
	v_mfma_f32_16x16x32_bf16 v[98:101], v[156:159], v[172:175], v[98:101]
	v_mfma_f32_16x16x32_bf16 v[90:93], v[148:151], v[182:185], v[90:93]
	v_mfma_f32_16x16x32_bf16 v[82:85], v[156:159], v[182:185], v[82:85]
	v_mfma_f32_16x16x32_bf16 v[74:77], v[148:151], v[190:193], v[74:77]
	v_mfma_f32_16x16x32_bf16 v[66:69], v[156:159], v[190:193], v[66:69]
	v_mfma_f32_16x16x32_bf16 v[122:125], v[152:155], v[168:171], v[122:125]
	v_mfma_f32_16x16x32_bf16 v[114:117], v[160:163], v[168:171], v[114:117]
	v_mfma_f32_16x16x32_bf16 v[106:109], v[152:155], v[176:179], v[106:109]
	v_mfma_f32_16x16x32_bf16 v[98:101], v[160:163], v[176:179], v[98:101]
	v_mfma_f32_16x16x32_bf16 v[90:93], v[152:155], v[186:189], v[90:93]
	v_mfma_f32_16x16x32_bf16 v[82:85], v[160:163], v[186:189], v[82:85]
	v_mfma_f32_16x16x32_bf16 v[74:77], v[152:155], v[194:197], v[74:77]
	v_mfma_f32_16x16x32_bf16 v[66:69], v[160:163], v[194:197], v[66:69]
	s_setprio 0
	s_barrier
	ds_read_b128 v[164:167], v210 offset:16384
	ds_read_b128 v[168:171], v210 offset:17408
	ds_read_b128 v[172:175], v210 offset:18432
	ds_read_b128 v[176:179], v210 offset:19456
	ds_read_b128 v[182:185], v210 offset:20480
	ds_read_b128 v[186:189], v210 offset:21504
	ds_read_b128 v[190:193], v210 offset:22528
	ds_read_b128 v[194:197], v210 offset:23552
	s_mov_b32 m0, s43
	s_nop 0
	global_load_lds_dwordx4 v1, s[34:35]
	s_mov_b32 m0, s44
	s_nop 0
	global_load_lds_dwordx4 v200, s[34:35]
	s_add_u32 s64, s34, 0x80000
	s_addc_u32 s65, s35, 0
	s_mov_b32 m0, s45
	s_nop 0
	global_load_lds_dwordx4 v1, s[64:65]
	s_mov_b32 m0, s46
	s_nop 0
	global_load_lds_dwordx4 v200, s[64:65]
	s_mov_b32 m0, s42
	s_nop 0
	global_load_lds_dwordx4 v201, s[38:39]
	s_mov_b32 m0, s47
	s_nop 0
	global_load_lds_dwordx4 v202, s[38:39]
	s_waitcnt vmcnt(8)
	s_waitcnt lgkmcnt(0)
	s_barrier
	s_setprio 1
	s_waitcnt lgkmcnt(7)
	v_mfma_f32_16x16x32_bf16 v[62:65], v[130:133], v[164:167], v[62:65]
	v_mfma_f32_16x16x32_bf16 v[54:57], v[138:141], v[164:167], v[54:57]
	s_waitcnt lgkmcnt(5)
	v_mfma_f32_16x16x32_bf16 v[46:49], v[130:133], v[172:175], v[46:49]
	v_mfma_f32_16x16x32_bf16 v[38:41], v[138:141], v[172:175], v[38:41]
	s_waitcnt lgkmcnt(3)
	v_mfma_f32_16x16x32_bf16 v[30:33], v[130:133], v[182:185], v[30:33]
	v_mfma_f32_16x16x32_bf16 v[22:25], v[138:141], v[182:185], v[22:25]
	s_waitcnt lgkmcnt(1)
	v_mfma_f32_16x16x32_bf16 v[14:17], v[130:133], v[190:193], v[14:17]
	v_mfma_f32_16x16x32_bf16 v[6:9], v[138:141], v[190:193], v[6:9]
	v_mfma_f32_16x16x32_bf16 v[62:65], v[134:137], v[168:171], v[62:65]
	v_mfma_f32_16x16x32_bf16 v[54:57], v[142:145], v[168:171], v[54:57]
	v_mfma_f32_16x16x32_bf16 v[46:49], v[134:137], v[176:179], v[46:49]
	v_mfma_f32_16x16x32_bf16 v[38:41], v[142:145], v[176:179], v[38:41]
	v_mfma_f32_16x16x32_bf16 v[30:33], v[134:137], v[186:189], v[30:33]
	v_mfma_f32_16x16x32_bf16 v[22:25], v[142:145], v[186:189], v[22:25]
	s_waitcnt lgkmcnt(0)
	v_mfma_f32_16x16x32_bf16 v[14:17], v[134:137], v[194:197], v[14:17]
	v_mfma_f32_16x16x32_bf16 v[6:9], v[142:145], v[194:197], v[6:9]
	s_setprio 0
	s_setprio 1
	v_mfma_f32_16x16x32_bf16 v[58:61], v[148:151], v[164:167], v[58:61]
	v_mfma_f32_16x16x32_bf16 v[50:53], v[156:159], v[164:167], v[50:53]
	v_mfma_f32_16x16x32_bf16 v[42:45], v[148:151], v[172:175], v[42:45]
	v_mfma_f32_16x16x32_bf16 v[34:37], v[156:159], v[172:175], v[34:37]
	v_mfma_f32_16x16x32_bf16 v[26:29], v[148:151], v[182:185], v[26:29]
	v_mfma_f32_16x16x32_bf16 v[18:21], v[156:159], v[182:185], v[18:21]
	v_mfma_f32_16x16x32_bf16 v[10:13], v[148:151], v[190:193], v[10:13]
	v_mfma_f32_16x16x32_bf16 v[2:5], v[156:159], v[190:193], v[2:5]
	v_mfma_f32_16x16x32_bf16 v[58:61], v[152:155], v[168:171], v[58:61]
	v_mfma_f32_16x16x32_bf16 v[50:53], v[160:163], v[168:171], v[50:53]
	v_mfma_f32_16x16x32_bf16 v[42:45], v[152:155], v[176:179], v[42:45]
	v_mfma_f32_16x16x32_bf16 v[34:37], v[160:163], v[176:179], v[34:37]
	v_mfma_f32_16x16x32_bf16 v[26:29], v[152:155], v[186:189], v[26:29]
	v_mfma_f32_16x16x32_bf16 v[18:21], v[160:163], v[186:189], v[18:21]
	v_mfma_f32_16x16x32_bf16 v[10:13], v[152:155], v[194:197], v[10:13]
	v_mfma_f32_16x16x32_bf16 v[2:5], v[160:163], v[194:197], v[2:5]
	s_setprio 0
	s_barrier
; #define PG8_STAGEB(bufoff, gbase) PG8_STAGE2(bufoff, gbase, voffB[0], voffB[1])
; #define PG8_STAGEAS(bufoff, gbase, h) PG8_STAGE2(bufoff, gbase, voffA[h][0], voffA[h][1])
; #define PG8_LDA(dst, b, h) do { _Pragma("unroll") for (int m = 0; m < 4; ++m) _Pragma("unroll") for (int k = 0; k < 2; ++k) dst[m][k] = *(const LAS bf16x8*)(lds + PG8_SA(b, h) + aoff + m * 2048 + k * 1024); } while (0)
; #define PG8_LDB(dst, b, h) do { _Pragma("unroll") for (int n = 0; n < 2; ++n) _Pragma("unroll") for (int k = 0; k < 2; ++k) dst[n][k] = *(const LAS bf16x8*)(lds + PG8_SB(b, h) + boff + n * 2048 + k * 1024); } while (0)
; #define PG8_WAIT_K() do { if constexpr (HM) PG8_WAIT_V(6); else PG8_WAIT_V(8); } while (0)
; #define PG8_WAIT_L(n) asm volatile("s_waitcnt lgkmcnt(" #n ")" ::: "memory")
; #define PG8_BAR __builtin_amdgcn_s_barrier()
; #define PG8_SCHED __builtin_amdgcn_sched_barrier(0)
;     ...
;             PG8_LDB(B0, 1, 0); PG8_LDB(B1, 1, 1); PG8_SCHED; PG8_LDA(At, 1, 0); if constexpr (!HM) PG8_STAGEAS(PG8_SA(0, 1), a2, 1);
;             PG8_WAIT_K(); PG8_WAIT_L(0); PG8_BAR; PG8_MMA(0, 0, At, B0); PG8_MMA(0, 1, At, B1); PG8_BAR; PG8_SCHED;
;             if constexpr (!HM) PG8_LDA(At, 1, 1);
;             PG8_STAGEB(PG8_SB(1, 0), b3); PG8_STAGEB(PG8_SB(1, 1), b3 + hstepB); PG8_STAGEAS(PG8_SA(1, 0), a3, 0);
;             PG8_WAIT_K(); PG8_WAIT_L(0); PG8_BAR; if constexpr (!HM) { PG8_MMA(1, 0, At, B0); PG8_MMA(1, 1, At, B1); } PG8_BAR; PG8_SCHED;
;         }
;         if (wr == 0) PG8_BAR;
	ds_read_b128 v[130:133], v146
	ds_read_b128 v[134:137], v146 offset:1024
	ds_read_b128 v[138:141], v146 offset:2048
	ds_read_b128 v[142:145], v146 offset:3072
	ds_read_b128 v[148:151], v147
	ds_read_b128 v[152:155], v147 offset:1024
	ds_read_b128 v[156:159], v147 offset:2048
	ds_read_b128 v[160:163], v147 offset:3072
	ds_read_b128 v[164:167], v210 offset:32768
	ds_read_b128 v[168:171], v210 offset:33792
	ds_read_b128 v[172:175], v210 offset:34816
	ds_read_b128 v[176:179], v210 offset:35840
	ds_read_b128 v[182:185], v210 offset:36864
	ds_read_b128 v[186:189], v210 offset:37888
	ds_read_b128 v[190:193], v210 offset:38912
	ds_read_b128 v[194:197], v210 offset:39936
	s_mov_b32 m0, s48
	s_nop 0
	global_load_lds_dwordx4 v203, s[38:39]
	s_mov_b32 m0, s49
	s_nop 0
	global_load_lds_dwordx4 v204, s[38:39]
	s_waitcnt vmcnt(8)
	s_waitcnt lgkmcnt(0)
	s_barrier
	s_setprio 1
	s_waitcnt lgkmcnt(7)
	v_mfma_f32_16x16x32_bf16 v[126:129], v[130:133], v[164:167], v[126:129]
	v_mfma_f32_16x16x32_bf16 v[118:121], v[138:141], v[164:167], v[118:121]
	s_waitcnt lgkmcnt(5)
	v_mfma_f32_16x16x32_bf16 v[110:113], v[130:133], v[172:175], v[110:113]
	v_mfma_f32_16x16x32_bf16 v[102:105], v[138:141], v[172:175], v[102:105]
	s_waitcnt lgkmcnt(3)
	v_mfma_f32_16x16x32_bf16 v[94:97], v[130:133], v[182:185], v[94:97]
	v_mfma_f32_16x16x32_bf16 v[86:89], v[138:141], v[182:185], v[86:89]
	s_waitcnt lgkmcnt(1)
	v_mfma_f32_16x16x32_bf16 v[78:81], v[130:133], v[190:193], v[78:81]
	v_mfma_f32_16x16x32_bf16 v[70:73], v[138:141], v[190:193], v[70:73]
	v_mfma_f32_16x16x32_bf16 v[126:129], v[134:137], v[168:171], v[126:129]
	v_mfma_f32_16x16x32_bf16 v[118:121], v[142:145], v[168:171], v[118:121]
	v_mfma_f32_16x16x32_bf16 v[110:113], v[134:137], v[176:179], v[110:113]
	v_mfma_f32_16x16x32_bf16 v[102:105], v[142:145], v[176:179], v[102:105]
	v_mfma_f32_16x16x32_bf16 v[94:97], v[134:137], v[186:189], v[94:97]
	v_mfma_f32_16x16x32_bf16 v[86:89], v[142:145], v[186:189], v[86:89]
	s_waitcnt lgkmcnt(0)
	v_mfma_f32_16x16x32_bf16 v[78:81], v[134:137], v[194:197], v[78:81]
	v_mfma_f32_16x16x32_bf16 v[70:73], v[142:145], v[194:197], v[70:73]
	s_setprio 0
	s_setprio 1
	v_mfma_f32_16x16x32_bf16 v[122:125], v[148:151], v[164:167], v[122:125]
	v_mfma_f32_16x16x32_bf16 v[114:117], v[156:159], v[164:167], v[114:117]
	v_mfma_f32_16x16x32_bf16 v[106:109], v[148:151], v[172:175], v[106:109]
	v_mfma_f32_16x16x32_bf16 v[98:101], v[156:159], v[172:175], v[98:101]
	v_mfma_f32_16x16x32_bf16 v[90:93], v[148:151], v[182:185], v[90:93]
	v_mfma_f32_16x16x32_bf16 v[82:85], v[156:159], v[182:185], v[82:85]
	v_mfma_f32_16x16x32_bf16 v[74:77], v[148:151], v[190:193], v[74:77]
	v_mfma_f32_16x16x32_bf16 v[66:69], v[156:159], v[190:193], v[66:69]
	v_mfma_f32_16x16x32_bf16 v[122:125], v[152:155], v[168:171], v[122:125]
	v_mfma_f32_16x16x32_bf16 v[114:117], v[160:163], v[168:171], v[114:117]
	v_mfma_f32_16x16x32_bf16 v[106:109], v[152:155], v[176:179], v[106:109]
	v_mfma_f32_16x16x32_bf16 v[98:101], v[160:163], v[176:179], v[98:101]
	v_mfma_f32_16x16x32_bf16 v[90:93], v[152:155], v[186:189], v[90:93]
	v_mfma_f32_16x16x32_bf16 v[82:85], v[160:163], v[186:189], v[82:85]
	v_mfma_f32_16x16x32_bf16 v[74:77], v[152:155], v[194:197], v[74:77]
	v_mfma_f32_16x16x32_bf16 v[66:69], v[160:163], v[194:197], v[66:69]
	s_setprio 0
	s_barrier
	ds_read_b128 v[164:167], v210 offset:49152
	ds_read_b128 v[168:171], v210 offset:50176
	ds_read_b128 v[172:175], v210 offset:51200
	ds_read_b128 v[176:179], v210 offset:52224
	ds_read_b128 v[182:185], v210 offset:53248
	ds_read_b128 v[186:189], v210 offset:54272
	ds_read_b128 v[190:193], v210 offset:55296
	ds_read_b128 v[194:197], v210 offset:56320
	s_mov_b32 m0, s52
	s_nop 0
	global_load_lds_dwordx4 v1, s[36:37]
	s_add_u32 s34, s34, 0x80080
	s_mov_b32 m0, s53
	s_nop 0
	global_load_lds_dwordx4 v200, s[36:37]
	s_addc_u32 s35, s35, 0
	s_mov_b32 m0, s56
	s_nop 0
	global_load_lds_dwordx4 v1, s[34:35]
	s_mov_b32 m0, s57
	s_nop 0
	global_load_lds_dwordx4 v200, s[34:35]
	s_mov_b32 m0, s54
	s_nop 0
	global_load_lds_dwordx4 v201, s[30:31]
	s_mov_b32 m0, s55
	s_nop 0
	global_load_lds_dwordx4 v202, s[30:31]
	s_waitcnt vmcnt(8)
	s_waitcnt lgkmcnt(0)
	s_barrier
	s_setprio 1
	s_waitcnt lgkmcnt(7)
	v_mfma_f32_16x16x32_bf16 v[62:65], v[130:133], v[164:167], v[62:65]
	v_mfma_f32_16x16x32_bf16 v[54:57], v[138:141], v[164:167], v[54:57]
	s_waitcnt lgkmcnt(5)
	v_mfma_f32_16x16x32_bf16 v[46:49], v[130:133], v[172:175], v[46:49]
	v_mfma_f32_16x16x32_bf16 v[38:41], v[138:141], v[172:175], v[38:41]
	s_waitcnt lgkmcnt(3)
	v_mfma_f32_16x16x32_bf16 v[30:33], v[130:133], v[182:185], v[30:33]
	v_mfma_f32_16x16x32_bf16 v[22:25], v[138:141], v[182:185], v[22:25]
	s_waitcnt lgkmcnt(1)
	v_mfma_f32_16x16x32_bf16 v[14:17], v[130:133], v[190:193], v[14:17]
	v_mfma_f32_16x16x32_bf16 v[6:9], v[138:141], v[190:193], v[6:9]
	v_mfma_f32_16x16x32_bf16 v[62:65], v[134:137], v[168:171], v[62:65]
	v_mfma_f32_16x16x32_bf16 v[54:57], v[142:145], v[168:171], v[54:57]
	v_mfma_f32_16x16x32_bf16 v[46:49], v[134:137], v[176:179], v[46:49]
	v_mfma_f32_16x16x32_bf16 v[38:41], v[142:145], v[176:179], v[38:41]
	v_mfma_f32_16x16x32_bf16 v[30:33], v[134:137], v[186:189], v[30:33]
	v_mfma_f32_16x16x32_bf16 v[22:25], v[142:145], v[186:189], v[22:25]
	s_waitcnt lgkmcnt(0)
	v_mfma_f32_16x16x32_bf16 v[14:17], v[134:137], v[194:197], v[14:17]
	v_mfma_f32_16x16x32_bf16 v[6:9], v[142:145], v[194:197], v[6:9]
	s_setprio 0
	s_setprio 1
	v_mfma_f32_16x16x32_bf16 v[58:61], v[148:151], v[164:167], v[58:61]
	v_mfma_f32_16x16x32_bf16 v[50:53], v[156:159], v[164:167], v[50:53]
	v_mfma_f32_16x16x32_bf16 v[42:45], v[148:151], v[172:175], v[42:45]
	v_mfma_f32_16x16x32_bf16 v[34:37], v[156:159], v[172:175], v[34:37]
	v_mfma_f32_16x16x32_bf16 v[26:29], v[148:151], v[182:185], v[26:29]
	v_mfma_f32_16x16x32_bf16 v[18:21], v[156:159], v[182:185], v[18:21]
	v_mfma_f32_16x16x32_bf16 v[10:13], v[148:151], v[190:193], v[10:13]
	v_mfma_f32_16x16x32_bf16 v[2:5], v[156:159], v[190:193], v[2:5]
	v_mfma_f32_16x16x32_bf16 v[58:61], v[152:155], v[168:171], v[58:61]
	v_mfma_f32_16x16x32_bf16 v[50:53], v[160:163], v[168:171], v[50:53]
	v_mfma_f32_16x16x32_bf16 v[42:45], v[152:155], v[176:179], v[42:45]
	v_mfma_f32_16x16x32_bf16 v[34:37], v[160:163], v[176:179], v[34:37]
	v_mfma_f32_16x16x32_bf16 v[26:29], v[152:155], v[186:189], v[26:29]
	v_mfma_f32_16x16x32_bf16 v[18:21], v[160:163], v[186:189], v[18:21]
	v_mfma_f32_16x16x32_bf16 v[10:13], v[152:155], v[194:197], v[10:13]
	v_mfma_f32_16x16x32_bf16 v[2:5], v[160:163], v[194:197], v[2:5]
	s_setprio 0
	s_barrier
	s_add_i32 s63, s63, 2
	s_add_u32 s19, s19, 0x100
	s_addc_u32 s21, s21, 0
	s_add_u32 s25, s25, 0x100
	s_addc_u32 s27, s27, 0
	s_add_u32 s28, s28, 0x100
	s_addc_u32 s29, s29, 0
	s_cmp_gt_u32 s63, 29
	s_cbranch_scc0 .LBB0_698
	s_and_b64 vcc, exec, s[16:17]
	s_cbranch_vccz .LBB0_701
	s_barrier

; #define LAS __attribute__((address_space(3)))
; #define RW_STAGE(p_) do { const char* src_ = (const char*)(rw + (size_t)(512 * kq + 64 * (p_) + 32 * ts) * NE); const unsigned dst_ = rwl_u + (unsigned)(((p_) & 1) * 32768); \
;         _Pragma("unroll") for (int j = 0; j < 4; ++j) pg8::glds16(src_, (unsigned)(lane * 16 + j * 1024), dst_ + (unsigned)(j * 1024)); } while (0)
; #define RT_LOAD(sc_, X) do { const int kb_ = 512 * kq + 64 * ((sc_) >> 1) + 32 * kh + 16 * ((sc_) & 1); \
;             _Pragma("unroll") for (int q = 0; q < 4; ++q) X[q] = *(const f32x4*)(X1 + (size_t)tok * D + kb_ + 4 * q); } while (0)
; __device__ __forceinline__ void router_tile(Frame& F, const Args& a, int tile) {
;     ...
;     if (tid < 32) cntl[tid] = 0;
;     float ssum = 0.f;
; #pragma unroll
;     for (int j = 0; j < 8; ++j) { const f32x4 v = *(const f32x4*)(SS + (size_t)tok * 32 + 4 * j); ssum += (v[0] + v[1]) + (v[2] + v[3]); }
;     const float rstd = 1.0f / sqrtf(ssum * (1.f / D) + EPS);
;     f32x16 acc;
; #pragma unroll
;     for (int r = 0; r < 16; ++r) acc[r] = 0.f;
;     LAS float* rwl = (LAS float*)(F.lds + 49152); LAS float* g2l = (LAS float*)(F.lds + 114688);
;     { const f32x4 gv = *(const f32x4*)(g2 + 4 * tid); *(LAS f32x4*)(g2l + 4 * tid) = gv; }
;     const unsigned rwl_u = (unsigned)__builtin_amdgcn_readfirstlane((int)((unsigned)(size_t)rwl + (unsigned)(kq * 8192 + ts * 4096)));
;     ...
;     RW_STAGE(0);
;     asm volatile("s_waitcnt vmcnt(0)" ::: "memory");
;     {
;         f32x4 xc[4]; float avp[16];
; #pragma unroll
;         for (int q = 0; q < 16; ++q) avp[q] = 0.f;
;     ...
;         RT_LOAD(0, xc);
.LBB0_781:
	s_and_saveexec_b64 s[0:1], s[6:7]
	ds_write_b32 v100, v53 offset:40960
	s_or_b64 exec, exec, s[0:1]
	global_load_dwordx4 v[2:5], v[70:71], off
	s_lshl_b32 s39, s38, 6
	v_or_b32_e32 v50, s39, v99
	v_ashrrev_i32_e32 v51, 31, v50
	s_waitcnt vmcnt(2)
	v_lshlrev_b64 v[6:7], 7, v[50:51]
	v_lshl_add_u64 v[38:39], s[14:15], 0, v[6:7]
	global_load_dwordx4 v[6:9], v[38:39], off
	global_load_dwordx4 v[10:13], v[38:39], off offset:16
	global_load_dwordx4 v[14:17], v[38:39], off offset:32
	global_load_dwordx4 v[18:21], v[38:39], off offset:48
	global_load_dwordx4 v[22:25], v[38:39], off offset:64
	global_load_dwordx4 v[26:29], v[38:39], off offset:80
	global_load_dwordx4 v[30:33], v[38:39], off offset:96
	global_load_dwordx4 v[34:37], v[38:39], off offset:112
	v_readfirstlane_b32 s34, v110
	s_add_i32 s0, s34, 0x400
	s_add_i32 s1, s34, 0x800
	v_lshlrev_b64 v[38:39], 13, v[50:51]
	s_add_i32 s35, s34, 0xc00
	v_lshl_add_u64 v[76:77], s[12:13], 0, v[38:39]
	v_lshl_add_u64 v[54:55], v[72:73], 2, v[76:77]
	s_waitcnt vmcnt(8)
	ds_write_b128 v101, v[2:5]
	s_mov_b32 m0, s34
	s_nop 0
	global_load_lds_dwordx4 v102, s[22:23]
	s_waitcnt vmcnt(7)
	v_add_f32_e32 v2, v6, v7
	s_mov_b32 m0, s0
	s_nop 0
	global_load_lds_dwordx4 v103, s[22:23]
	s_mov_b32 m0, s1
	s_nop 0
	global_load_lds_dwordx4 v104, s[22:23]
	s_waitcnt vmcnt(5)
	v_add_f32_e32 v7, v16, v17
	s_mov_b32 m0, s35
	s_nop 0
	global_load_lds_dwordx4 v105, s[22:23]
	s_waitcnt vmcnt(0)
	s_waitcnt vmcnt(0)
	v_add_f32_e32 v16, v34, v35
	v_add_f32_e32 v17, v36, v37
	global_load_dwordx4 v[46:49], v[54:55], off offset:48
	global_load_dwordx4 v[42:45], v[54:55], off offset:32
	global_load_dwordx4 v[38:41], v[54:55], off offset:16
	global_load_dwordx4 v[34:37], v[54:55], off
	v_add_f32_e32 v3, v8, v9
	v_add_f32_e32 v4, v10, v11
	v_add_f32_e32 v5, v12, v13
	v_add_f32_e32 v2, v2, v3
	v_add_f32_e32 v6, v14, v15
	v_add_f32_e32 v3, v4, v5
	v_add_f32_e32 v2, 0, v2
	v_add_f32_e32 v8, v18, v19
	v_add_f32_e32 v9, v20, v21
	v_add_f32_e32 v4, v6, v7
	v_add_f32_e32 v2, v2, v3
	v_add_f32_e32 v10, v22, v23
	v_add_f32_e32 v11, v24, v25
	v_add_f32_e32 v5, v8, v9
	v_add_f32_e32 v2, v2, v4
	v_add_f32_e32 v12, v26, v27
	v_add_f32_e32 v13, v28, v29
	v_add_f32_e32 v6, v10, v11
	v_add_f32_e32 v2, v2, v5
	v_add_f32_e32 v14, v30, v31
	v_add_f32_e32 v15, v32, v33
	v_add_f32_e32 v7, v12, v13
	v_add_f32_e32 v2, v2, v6
	v_add_f32_e32 v8, v14, v15
	v_add_f32_e32 v2, v2, v7
	v_add_f32_e32 v9, v16, v17
	v_add_f32_e32 v2, v2, v8
	v_add_f32_e32 v2, v2, v9
	v_fmamk_f32 v2, v2, 0x3a000000, v108
	v_mul_f32_e32 v3, 0x4f800000, v2
	v_cmp_gt_f32_e32 vcc, s21, v2
	v_mov_b32_e32 v18, 0
	s_mov_b32 s36, 0
	v_cndmask_b32_e32 v2, v2, v3, vcc
	v_sqrt_f32_e32 v3, v2
	v_mov_b32_e32 v19, v18
	v_mov_b32_e32 v20, v18
	v_mov_b32_e32 v21, v18
	v_add_u32_e32 v4, -1, v3
	v_fma_f32 v5, -v4, v3, v2
	v_cmp_ge_f32_e64 s[0:1], 0, v5
	v_add_u32_e32 v5, 1, v3
	v_mov_b32_e32 v22, v18
	v_cndmask_b32_e64 v4, v3, v4, s[0:1]
	v_fma_f32 v3, -v5, v3, v2
	v_cmp_lt_f32_e64 s[0:1], 0, v3
	v_mov_b32_e32 v23, v18
	v_mov_b32_e32 v24, v18
	v_cndmask_b32_e64 v3, v4, v5, s[0:1]
	v_mul_f32_e32 v4, 0x37800000, v3
	v_cndmask_b32_e32 v3, v3, v4, vcc
	v_cmp_class_f32_e32 vcc, v2, v109
	v_mov_b32_e32 v25, v18
	v_mov_b32_e32 v26, v18
	v_cndmask_b32_e32 v2, v3, v2, vcc
	v_div_scale_f32 v3, s[0:1], v2, v2, 1.0
	v_rcp_f32_e32 v4, v3
	v_mov_b32_e32 v27, v18
	v_mov_b32_e32 v28, v18
	v_mov_b32_e32 v29, v18
	v_fma_f32 v5, -v3, v4, 1.0
	v_fmac_f32_e32 v4, v5, v4
	v_div_scale_f32 v5, vcc, 1.0, v2, 1.0
	v_mul_f32_e32 v6, v5, v4
	v_fma_f32 v7, -v3, v6, v5
	v_fmac_f32_e32 v6, v7, v4
	v_fma_f32 v3, -v3, v6, v5
	v_div_fmas_f32 v3, v3, v4, v6
	v_div_fixup_f32 v78, v3, v2, 1.0
	v_lshlrev_b64 v[2:3], 11, v[50:51]
	v_lshl_add_u64 v[80:81], s[16:17], 0, v[2:3]
	v_mov_b32_e32 v79, v78
	v_mov_b32_e32 v30, v18
	v_mov_b32_e32 v31, v18
	v_mov_b32_e32 v32, v18
	v_mov_b32_e32 v33, v18
	v_mov_b32_e32 v2, v18
	v_mov_b32_e32 v3, v18
	v_mov_b32_e32 v4, v18
	v_mov_b32_e32 v5, v18
	v_mov_b32_e32 v6, v18
	v_mov_b32_e32 v7, v18
	v_mov_b32_e32 v8, v18
	v_mov_b32_e32 v9, v18
	v_mov_b32_e32 v10, v18
	v_mov_b32_e32 v11, v18
	v_mov_b32_e32 v12, v18
	v_mov_b32_e32 v13, v18
	v_mov_b32_e32 v14, v18
	v_mov_b32_e32 v15, v18
	v_mov_b32_e32 v16, v18
	v_mov_b32_e32 v17, v18
	s_branch .LBB0_785

; #define RW_STAGE(p_) do { const char* src_ = (const char*)(rw + (size_t)(512 * kq + 64 * (p_) + 32 * ts) * NE); const unsigned dst_ = rwl_u + (unsigned)(((p_) & 1) * 32768); \
;         _Pragma("unroll") for (int j = 0; j < 4; ++j) pg8::glds16(src_, (unsigned)(lane * 16 + j * 1024), dst_ + (unsigned)(j * 1024)); } while (0)
; __device__ __forceinline__ void router_tile(Frame& F, const Args& a, int tile) {
;     ...
;         for (int sc = 0; sc < 16; ++sc) {
;             if ((sc & 1) == 0) {
;                 asm volatile("s_waitcnt lgkmcnt(0)" ::: "memory"); __builtin_amdgcn_s_barrier(); asm volatile("" ::: "memory");
;                 if (sc < 14) RW_STAGE((sc >> 1) + 1); }
.LBB0_785:
	s_bitcmp1_b32 s36, 0
	s_cselect_b64 s[0:1], -1, 0
	s_and_b64 vcc, exec, s[0:1]
	s_cbranch_vccnz .LBB0_788
	s_waitcnt lgkmcnt(0)
	s_barrier
	s_cmp_gt_u32 s36, 13
	s_cbranch_scc1 .LBB0_788
	s_lshr_b32 s35, s36, 1
	s_add_i32 s35, s35, 1
	s_lshl_b32 s37, s35, 6
	s_add_i32 s40, s37, s20
	s_ashr_i32 s41, s40, 31
	s_lshl_b64 s[40:41], s[40:41], 7
	s_add_u32 s40, s10, s40
	s_addc_u32 s41, s11, s41
	s_lshl_b32 s35, s35, 15
	s_and_b32 s35, s35, 0x8000
	s_add_i32 s35, s35, s34
	s_mov_b32 m0, s35
	s_nop 0
	global_load_lds_dwordx4 v102, s[40:41]
	s_add_i32 s37, s35, 0x400
	s_mov_b32 m0, s37
	s_nop 0
	global_load_lds_dwordx4 v103, s[40:41]
	s_add_i32 s37, s35, 0x800
	s_mov_b32 m0, s37
	s_nop 0
	global_load_lds_dwordx4 v104, s[40:41]
	s_addk_i32 s35, 0xc00
	s_mov_b32 m0, s35
	s_nop 0
	global_load_lds_dwordx4 v105, s[40:41]

;     __device__ __forceinline__ const char* a_base(const Unit& u) const { return (const char*)A + (size_t)u.pm * BM * lda * 2; }
;     __device__ __forceinline__ const char* b_base(const Unit& u) const { return (const char*)Bt + (size_t)u.pn * BM * K * 2; }
;     __device__ __forceinline__ const char* b_base(const Unit& u) const { return (const char*)Bt + ((size_t)u.e * NB + (size_t)u.pn * BM) * K * 2; }
; #define PG8_RC() int R[2], C[2]; { int t_ = threadIdx.x; asm volatile("" : "+v"(t_)); _Pragma("unroll") for (int i = 0; i < 2; ++i) stage_rc(t_ * 16 + i * 8192, R[i], C[i]); }
;     __device__ __forceinline__ const char* bias_base(const pg8::Unit& u) const { return (const char*)(bgu + (size_t)u.e * 4096 + u.pn * 128); }
;     __device__ __forceinline__ unsigned bias_off(const pg8::Unit&, int wc, int lane) const { return (unsigned)(((lane >> 3) & 1) * 2048 + wc * 32 + (lane & 7) * 4) * 4u; }
;     __device__ __forceinline__ const char* bias_base(const pg8::Unit& u) const { return (const char*)(bdn + (size_t)u.e * D + u.pn * 256); }
;     __device__ __forceinline__ void a_offs(const Unit& u, const int (&R)[2], const int (&C)[2], unsigned (&off)[2][2]) const {
;         if constexpr (GATHER) {
;             const int ce = __builtin_amdgcn_readfirstlane(cnt[u.e]);
; #pragma unroll
;             for (int h = 0; h < 2; ++h)
; #pragma unroll
;                 for (int i = 0; i < 2; ++i) { const int g = u.mt * BM + u.hx * HALF + h * HALF + R[i]; const int tok = rowtok[u.e * T + (g < ce ? g : 0)] >> 2; off[h][i] = (unsigned)(tok * lda + C[i]) * 2u; }
;     ...
;     if (!S.next(0, cur)) return;
;     unsigned voffA[2][2];
;     { PG8_RC(); S.a_offs(cur, R, C, voffA); }
;     f32x4 acc[2][2][4][2];
; #pragma unroll
;     for (int a = 0; a < 2; ++a)
; #pragma unroll
;         for (int b = 0; b < 2; ++b)
; #pragma unroll
;             for (int m = 0; m < 4; ++m)
; #pragma unroll
;                 for (int n = 0; n < 2; ++n) acc[a][b][m][n] = (f32x4){0.f, 0.f, 0.f, 0.f};
;     bf16x8 At[4][2], B0[2][2], B1[2][2];
;     const char* cA = S.a_base(cur); const char* cB = S.b_base(cur);
;     const unsigned bias_lds = (unsigned)__builtin_amdgcn_readfirstlane((int)((unsigned)(size_t)lds + (unsigned)(AUX_OFF + 8192) + (unsigned)wid * 256u));
;     if constexpr (Epi::kBiasDMA) { if (lane < 16) glds16(E.bias_base(cur), E.bias_off(cur, wc, lane), bias_lds); }
.LBB0_1110:
	s_add_u32 s0, s94, 0x34600000
	s_addc_u32 s1, s95, 0
	s_add_u32 s33, s94, 0x4600000
	s_addc_u32 s60, s95, 0
	s_add_u32 s4, s94, 0x6f500000
	s_addc_u32 s5, s95, 0
	s_add_u32 s30, s94, 0x34600080
	s_addc_u32 s31, s95, 0
	s_ashr_i32 s61, s2, 31
	s_add_u32 s24, s94, 0x34600100
	s_addc_u32 s25, s95, 0
	s_add_u32 s26, s94, 0x34600180
	s_addc_u32 s27, s95, 0
	s_add_u32 s28, s94, 0x6f700000
	s_addc_u32 s29, s95, 0
	s_andn2_b64 vcc, exec, s[6:7]
	s_cbranch_vccnz .LBB0_1150
	v_mov_b32_e32 v3, v0
	s_lshl_b32 s6, s34, 2
	v_ashrrev_i32_e32 v1, 31, v3
	v_lshrrev_b32_e32 v1, 26, v1
	v_lshlrev_b32_e32 v4, 4, v3
	v_add_u32_e32 v1, v3, v1
	v_bfe_i32 v3, v3, 27, 1
	v_lshrrev_b32_e32 v3, 22, v3
	v_add_u32_e32 v3, v4, v3
	v_and_b32_e32 v3, 0xfffffc00, v3
	v_sub_u32_e32 v3, v4, v3
	v_add_u32_e32 v4, 0x2000, v4
	s_waitcnt vmcnt(1)
	v_ashrrev_i32_e32 v7, 31, v4
	v_lshrrev_b32_e32 v7, 22, v7
	s_add_i32 s6, s6, 0
	v_add_u32_e32 v7, v4, v7
	s_add_i32 s6, s6, 0x23100
	v_lshrrev_b32_e32 v5, 4, v3
	v_ashrrev_i32_e32 v7, 10, v7
	v_mov_b32_e32 v9, s6
	v_bitop3_b32 v5, v5, v3, 32 bitop3:0x6c
	v_mul_i32_i24_e32 v8, 0x400, v7
	ds_read_b32 v10, v9
	v_ashrrev_i32_e32 v6, 31, v5
	v_sub_u32_e32 v4, v4, v8
	v_ashrrev_i32_e32 v1, 6, v1
	v_lshrrev_b32_e32 v6, 26, v6
	v_lshrrev_b32_e32 v8, 4, v4
	v_lshlrev_b32_e32 v3, 3, v1
	v_add_u32_e32 v6, v5, v6
	v_bitop3_b32 v8, v8, v4, 32 bitop3:0x6c
	v_and_b32_e32 v3, -16, v3
	v_ashrrev_i32_e32 v6, 6, v6
	v_ashrrev_i32_e32 v9, 31, v8
	v_lshrrev_b32_e32 v9, 26, v9
	s_waitcnt lgkmcnt(0)
	v_readfirstlane_b32 s6, v10
	v_add3_u32 v3, v3, s10, v6
	v_lshlrev_b32_e32 v4, 3, v7
	v_add_u32_e32 v9, v8, v9
	v_cmp_gt_i32_e32 vcc, s6, v3
	v_and_b32_e32 v4, -16, v4
	v_ashrrev_i32_e32 v9, 6, v9
	s_lshl_b32 s7, s34, 14
	v_cndmask_b32_e32 v10, 0, v3, vcc
	v_add_u32_e32 v10, s7, v10
	v_add3_u32 v4, v4, s10, v9
	v_ashrrev_i32_e32 v11, 31, v10
	v_cmp_gt_i32_e32 vcc, s6, v4
	s_waitcnt vmcnt(0)
	v_lshl_add_u64 v[14:15], v[10:11], 2, s[4:5]
	v_add_u32_e32 v3, 0x80, v3
	v_cndmask_b32_e32 v10, 0, v4, vcc
	v_add_u32_e32 v10, s7, v10
	v_cmp_gt_i32_e32 vcc, s6, v3
	v_ashrrev_i32_e32 v11, 31, v10
	v_lshl_add_u64 v[16:17], v[10:11], 2, s[4:5]
	v_cndmask_b32_e32 v3, 0, v3, vcc
	v_add_u32_e32 v10, s7, v3
	v_add_u32_e32 v3, 0x80, v4
	v_cmp_gt_i32_e32 vcc, s6, v3
	v_ashrrev_i32_e32 v11, 31, v10
	v_lshl_add_u64 v[18:19], v[10:11], 2, s[4:5]
	v_cndmask_b32_e32 v3, 0, v3, vcc
	v_add_u32_e32 v10, s7, v3
	v_ashrrev_i32_e32 v11, 31, v10
	v_lshl_add_u64 v[20:21], v[10:11], 2, s[4:5]
	global_load_dword v13, v[14:15], off
	global_load_dword v12, v[16:17], off
	global_load_dword v11, v[18:19], off
	global_load_dword v10, v[20:21], off
	s_lshl_b32 s6, s12, 8
	v_and_b32_e32 v3, 63, v2
	s_add_i32 s6, s6, 0
	s_and_b32 s13, s12, 3
	s_ashr_i32 s35, s34, 31
	s_add_i32 s65, s6, 0x22000
	v_cmp_gt_u32_e64 s[6:7], 16, v3
	v_lshlrev_b32_e32 v4, 10, v3
	v_lshlrev_b32_e32 v3, 4, v3
	s_and_saveexec_b64 s[10:11], s[6:7]
	s_cbranch_execz .LBB0_1113
	s_lshl_b64 s[14:15], s[34:35], 14
	s_add_u32 s16, s22, s14
	s_addc_u32 s17, s23, s15
	s_lshl_b32 s14, s46, 7
	s_ashr_i32 s15, s14, 31
	s_lshl_b64 s[14:15], s[14:15], 2
	s_add_u32 s14, s16, s14
	s_addc_u32 s15, s17, s15
	v_and_b32_e32 v14, 0x2000, v4
	s_lshl_b32 s16, s13, 7
	v_and_b32_e32 v15, 0x70, v3
	v_or3_b32 v14, s16, v14, v15
	s_mov_b32 m0, s65
	s_nop 0
	global_load_lds_dwordx4 v14, s[14:15]
;     __device__ __forceinline__ const char* a_base(const Unit& u) const { return (const char*)A + (size_t)u.pm * BM * lda * 2; }
;     __device__ __forceinline__ const char* b_base(const Unit& u) const { return (const char*)Bt + (size_t)u.pn * BM * K * 2; }
; #define PG8_BAR __builtin_amdgcn_s_barrier()
;     ...
;     { int R[2], C[2];
; #pragma unroll
;       for (int i = 0; i < 2; ++i) { stage_rc(tid * 16 + i * 8192, R[i], C[i]); voffB[i] = (unsigned)(R[i] * K + C[i]) * 2u; } }
;     ...
;     const size_t kstep = (size_t)(BK * 2);
;     const size_t hstepB = (size_t)HALF * K * 2;
;     const unsigned ldsbase = (unsigned)__builtin_amdgcn_readfirstlane((int)((unsigned)(size_t)lds + (unsigned)wid * 1024u));
;     const int aoff = lds_byte(wr * 64 + fr, fq * 8), boff = lds_byte(wc * 32 + fr, fq * 8);
;     ...
;     constexpr int EST = HM ? Epi::kStoresHM : Epi::kStores;
;     ...
;     Unit cur, nxt; int ui = 0;
;     if (!S.next(0, cur)) return;
;     unsigned voffA[2][2];
;     { PG8_RC(); S.a_offs(cur, R, C, voffA); }
;     f32x4 acc[2][2][4][2];
; #pragma unroll
;     for (int a = 0; a < 2; ++a)
; #pragma unroll
;         for (int b = 0; b < 2; ++b)
; #pragma unroll
;             for (int m = 0; m < 4; ++m)
; #pragma unroll
;                 for (int n = 0; n < 2; ++n) acc[a][b][m][n] = (f32x4){0.f, 0.f, 0.f, 0.f};
;     bf16x8 At[4][2], B0[2][2], B1[2][2];
;     const char* cA = S.a_base(cur); const char* cB = S.b_base(cur);
;     const unsigned bias_lds = (unsigned)__builtin_amdgcn_readfirstlane((int)((unsigned)(size_t)lds + (unsigned)(AUX_OFF + 8192) + (unsigned)wid * 256u));
;     if constexpr (Epi::kBiasDMA) { if (lane < 16) glds16(E.bias_base(cur), E.bias_off(cur, wc, lane), bias_lds); }
;     const unsigned rowid_lds = (unsigned)__builtin_amdgcn_readfirstlane((int)((unsigned)(size_t)lds + (unsigned)AUX_OFF + (unsigned)wid * 512u));
;     if constexpr (Epi::kRowDMA) { if (lane < 32) glds16(E.row_base(cur), E.row_off(cur, wr, lane), rowid_lds); }
;     PG8_STAGEB(PG8_SB(0, 0), cB); PG8_STAGEB(PG8_SB(0, 1), cB + hstepB); PG8_STAGEA(PG8_SA(0, 0), cA, 0); if constexpr (!HM) PG8_STAGEA(PG8_SA(0, 1), cA, 1);
;     if (wr == 1) PG8_BAR;
;     if constexpr (HM) PG8_WAIT_V(0); else PG8_WAIT_V(2);
;     PG8_BAR;
;     PG8_STAGEB(PG8_SB(1, 0), cB + kstep); PG8_STAGEA(PG8_SA(1, 0), cA + kstep, 0); PG8_STAGEB(PG8_SB(1, 1), cB + hstepB + kstep);
;     PG8_WAIT_V(6); PG8_BAR;
.LBB0_1113:
	s_or_b64 exec, exec, s[10:11]
	v_lshlrev_b32_e32 v1, 5, v1
	v_and_b32_e32 v14, 32, v1
	v_lshlrev_b32_e32 v1, 6, v6
	v_lshlrev_b32_e32 v6, 5, v7
	v_lshlrev_b32_e32 v7, 6, v9
	v_sub_u32_e32 v5, v5, v1
	v_mov_b32_e32 v1, 1
	v_sub_u32_e32 v7, v8, v7
	v_and_b32_e32 v6, 32, v6
	v_ashrrev_i16_sdwa v7, v1, sext(v7) dst_sel:DWORD dst_unused:UNUSED_PAD src0_sel:DWORD src1_sel:BYTE_0
	s_waitcnt vmcnt(2)
	v_lshlrev_b32_e32 v8, 8, v12
	s_waitcnt vmcnt(0)
	v_lshlrev_b32_e32 v10, 8, v10
	v_add_u32_sdwa v6, v6, sext(v7) dst_sel:DWORD dst_unused:UNUSED_PAD src0_sel:DWORD src1_sel:WORD_0
	v_and_b32_e32 v8, 0x7ffffc00, v8
	v_and_b32_e32 v10, 0x7ffffc00, v10
	v_add_lshl_u32 v51, v6, v8, 1
	v_add_lshl_u32 v53, v6, v10, 1
	v_bfe_i32 v6, v2, 27, 1
	v_lshlrev_b32_e32 v216, 4, v2
	v_lshrrev_b32_e32 v6, 22, v6
	v_add_u32_e32 v6, v216, v6
	v_ashrrev_i16_sdwa v5, v1, sext(v5) dst_sel:DWORD dst_unused:UNUSED_PAD src0_sel:DWORD src1_sel:BYTE_0
	v_lshlrev_b32_e32 v7, 8, v13
	v_and_b32_e32 v6, 0xfffffc00, v6
	v_add_u32_sdwa v5, v14, sext(v5) dst_sel:DWORD dst_unused:UNUSED_PAD src0_sel:DWORD src1_sel:WORD_0
	v_and_b32_e32 v7, 0x7ffffc00, v7
	v_lshlrev_b32_e32 v9, 8, v11
	v_sub_u32_e32 v6, v216, v6
	v_and_b32_e32 v9, 0x7ffffc00, v9
	v_add_lshl_u32 v50, v5, v7, 1
	v_lshrrev_b32_e32 v7, 4, v6
	v_add_lshl_u32 v52, v5, v9, 1
	v_ashrrev_i32_e32 v5, 31, v2
	v_bitop3_b32 v6, v7, v6, 32 bitop3:0x6c
	v_lshrrev_b32_e32 v5, 26, v5
	v_ashrrev_i32_e32 v8, 31, v6
	v_add_u32_e32 v5, v2, v5
	v_lshrrev_b32_e32 v8, 26, v8
	v_ashrrev_i32_e32 v5, 6, v5
	v_add_u32_e32 v8, v6, v8
	v_lshlrev_b32_e32 v7, 3, v5
	v_lshrrev_b32_e32 v9, 6, v8
	v_and_b32_e32 v8, 0xc0, v8
	v_and_b32_e32 v7, 0x1ffff0, v7
	v_lshlrev_b32_e32 v5, 5, v5
	v_sub_u32_e32 v6, v6, v8
	v_add_u32_e32 v7, v9, v7
	v_and_b32_e32 v5, 32, v5
	v_ashrrev_i16_sdwa v6, v1, sext(v6) dst_sel:DWORD dst_unused:UNUSED_PAD src0_sel:DWORD src1_sel:BYTE_0
	v_bfe_i32 v6, v6, 0, 16
	v_lshl_or_b32 v5, v7, 10, v5
	v_add_lshl_u32 v217, v5, v6, 1
	v_add_u32_e32 v5, 0x2000, v216
	v_ashrrev_i32_e32 v6, 31, v5
	v_lshrrev_b32_e32 v6, 22, v6
	v_add_u32_e32 v6, v5, v6
	v_ashrrev_i32_e32 v6, 10, v6
	v_mul_i32_i24_e32 v7, 0x400, v6
	v_sub_u32_e32 v5, v5, v7
	v_lshrrev_b32_e32 v7, 4, v5
	s_ashr_i32 s47, s46, 31
	v_bitop3_b32 v5, v7, v5, 32 bitop3:0x6c
	s_lshl_b64 s[10:11], s[46:47], 19
	s_lshl_b64 s[14:15], s[34:35], 23
	v_ashrrev_i32_e32 v8, 31, v5
	s_add_u32 s14, s33, s14
	v_lshrrev_b32_e32 v8, 26, v8
	s_addc_u32 s15, s60, s15
	v_add_u32_e32 v8, v5, v8
	s_add_u32 s48, s14, s10
	v_lshlrev_b32_e32 v7, 3, v6
	v_lshrrev_b32_e32 v9, 6, v8
	v_and_b32_e32 v8, 0xc0, v8
	s_addc_u32 s49, s15, s11
	v_and_b32_e32 v7, 0x1ffff0, v7
	v_lshlrev_b32_e32 v6, 5, v6
	v_sub_u32_e32 v5, v5, v8
	s_lshl_b32 s11, s12, 10
	v_add_u32_e32 v7, v9, v7
	v_and_b32_e32 v6, 32, v6
	v_ashrrev_i16_sdwa v5, v1, sext(v5) dst_sel:DWORD dst_unused:UNUSED_PAD src0_sel:DWORD src1_sel:BYTE_0
	s_add_i32 s35, s11, 0
	v_bfe_i32 v5, v5, 0, 16
	v_lshl_or_b32 v6, v7, 10, v6
	s_ashr_i32 s10, s9, 8
	s_add_i32 s47, s35, 0x10000
	s_mov_b32 m0, s47
	s_nop 0
	global_load_lds_dwordx4 v217, s[48:49]
	s_add_i32 s66, s35, 0x12000
	v_add_lshl_u32 v218, v6, v5, 1
	s_mov_b32 m0, s66
	s_nop 0
	global_load_lds_dwordx4 v218, s[48:49]
	s_add_u32 s14, s48, 0x40000
	s_addc_u32 s15, s49, 0
	s_add_i32 s67, s35, 0x14000
	s_mov_b32 m0, s67
	s_nop 0
	global_load_lds_dwordx4 v217, s[14:15]
	s_add_i32 s68, s35, 0x16000
	s_mov_b32 m0, s68
	s_nop 0
	global_load_lds_dwordx4 v218, s[14:15]
	s_add_i32 s69, s35, 0x2000
	s_mov_b32 m0, s35
	s_nop 0
	global_load_lds_dwordx4 v50, s[0:1]
	s_add_i32 s70, s35, 0x4000
	s_mov_b32 m0, s69
	s_nop 0
	global_load_lds_dwordx4 v51, s[0:1]
	s_add_i32 s71, s35, 0x6000
	s_mov_b32 m0, s70
	s_nop 0
	global_load_lds_dwordx4 v52, s[0:1]
	s_cmp_eq_u32 s10, 1
	s_mov_b32 m0, s71
	s_nop 0
	global_load_lds_dwordx4 v53, s[0:1]
	s_cselect_b64 s[36:37], -1, 0
	s_cmp_lg_u32 s10, 1
	s_cbranch_scc1 .LBB0_1115
	s_barrier
.LBB0_1115:
	v_lshrrev_b32_e32 v6, 1, v2
	v_and_b32_e32 v6, 24, v6
	v_and_b32_e32 v5, 15, v2
	v_lshlrev_b32_e32 v7, 1, v6
	v_lshlrev_b32_e32 v2, 2, v2
	v_lshl_or_b32 v219, s10, 6, v5
	v_lshl_or_b32 v5, v5, 6, v7
	s_lshl_b32 s10, s10, 13
	v_and_b32_e32 v2, 32, v2
	v_bitop3_b32 v7, v5, s10, v2 bitop3:0xde
	s_lshl_b32 s10, s13, 12
	v_bitop3_b32 v2, v5, s10, v2 bitop3:0xde
	s_add_u32 s10, s48, 0x80
	s_waitcnt vmcnt(2)
	s_barrier
	s_addc_u32 s11, s49, 0
	s_add_i32 s72, s35, 0x18000
	s_mov_b32 m0, s72
	s_nop 0
	global_load_lds_dwordx4 v217, s[10:11]
	s_add_i32 s73, s35, 0x1a000
	s_mov_b32 m0, s73
	s_nop 0
	global_load_lds_dwordx4 v218, s[10:11]
	s_add_i32 s74, s35, 0x8000
	s_mov_b32 m0, s74
	s_nop 0
	global_load_lds_dwordx4 v50, s[30:31]
	s_add_i32 s75, s35, 0xa000
	s_mov_b32 m0, s75
	s_nop 0
	global_load_lds_dwordx4 v51, s[30:31]
	s_add_u32 s10, s48, 0x40080
	s_addc_u32 s11, s49, 0
	s_add_i32 s76, s35, 0x1c000
	s_mov_b32 m0, s76
	s_nop 0
	global_load_lds_dwordx4 v217, s[10:11]
	s_add_i32 s77, s35, 0x1e000
	s_add_i32 s78, s35, 0xc000
	s_add_i32 s79, s35, 0xe000
	s_mov_b32 m0, s77
	s_nop 0
	global_load_lds_dwordx4 v218, s[10:11]
	s_cmpk_lt_u32 s9, 0x100
	s_waitcnt vmcnt(6)
	s_cselect_b64 s[38:39], -1, 0
	v_and_b32_e32 v4, 0x2000, v4
	s_lshl_b32 s9, s13, 7
	v_and_b32_e32 v3, 0x70, v3
	s_mov_b32 s12, 0
	v_or3_b32 v221, s9, v4, v3
	s_ashr_i32 s9, s8, 31
	v_lshl_add_u32 v220, v6, 2, s65
	v_lshl_or_b32 v222, s13, 5, v6
	v_mov_b64_e32 v[214:215], s[8:9]
	v_add_u32_e32 v223, 0, v2
	s_mov_b32 s13, s12
	s_mov_b32 s14, s12
	s_mov_b32 s15, s12
	s_mov_b32 s80, 0xc0e00000
	v_add_u32_e32 v224, 0, v7
	v_mov_b32_e32 v225, 0x40e00000
	s_mov_b32 s16, s12
	s_barrier
	s_branch .LBB0_1118

; #define LAS __attribute__((address_space(3)))
; #define PG8_STAGEA(bufoff, gbase, h) PG8_STAGE2(bufoff, gbase, voffA[h][0], voffA[h][1])
; #define PG8_LDA(dst, b, h) do { _Pragma("unroll") for (int m = 0; m < 4; ++m) _Pragma("unroll") for (int k = 0; k < 2; ++k) dst[m][k] = *(const LAS bf16x8*)(lds + PG8_SA(b, h) + aoff + m * 2048 + k * 1024); } while (0)
; #define PG8_LDB(dst, b, h) do { _Pragma("unroll") for (int n = 0; n < 2; ++n) _Pragma("unroll") for (int k = 0; k < 2; ++k) dst[n][k] = *(const LAS bf16x8*)(lds + PG8_SB(b, h) + boff + n * 2048 + k * 1024); } while (0)
; #define PG8_WAIT_K0() do { if (EST > 0 && t == 0 && ui > 0) asm volatile("s_waitcnt vmcnt(%0)" :: "n"((HM ? 6 : 8) + EST) : "memory"); else PG8_WAIT_K(); } while (0)
; #define PG8_WAIT_L(n) asm volatile("s_waitcnt lgkmcnt(" #n ")" ::: "memory")
; #define PG8_BAR __builtin_amdgcn_s_barrier()
; #define PG8_SCHED __builtin_amdgcn_sched_barrier(0)
;     ...
;             const char* a1 = cA + (size_t)(t + 1) * kstep;
;             const char* a2 = last ? nA : cA + (size_t)(t + 2) * kstep; const char* b2 = last ? nB : cB + (size_t)(t + 2) * kstep;
;             const char* a3 = a2 + kstep; const char* b3 = b2 + kstep;
;             PG8_LDB(B0, 0, 0); PG8_LDB(B1, 0, 1); PG8_SCHED; PG8_LDA(At, 0, 0); if constexpr (!HM) PG8_STAGEA(PG8_SA(1, 1), a1, 1);
;             if constexpr (Sched::kGather) { if (last && has_next) { const u32x4 tn = *(const LAS u32x4*)(S.aux + tid * 16); voffA[0][0] = tn.x; voffA[0][1] = tn.y; voffA[1][0] = tn.z; voffA[1][1] = tn.w; } }
;             PG8_WAIT_K0(); PG8_WAIT_L(0); PG8_BAR; PG8_MMA(0, 0, At, B0); PG8_MMA(0, 1, At, B1); PG8_BAR; PG8_SCHED;
.LBB0_1128:
	v_add_u32_e32 v230, 0x14000, v223
	v_add_u32_e32 v231, 0x10000, v223
	ds_read_b128 v[182:185], v230 offset:3072
	ds_read_b128 v[2:5], v230 offset:2048
	ds_read_b128 v[186:189], v230 offset:1024
	ds_read_b128 v[8:11], v230
	ds_read_b128 v[64:67], v231 offset:3072
	ds_read_b128 v[14:17], v231 offset:2048
	ds_read_b128 v[56:59], v231 offset:1024
	ds_read_b128 v[20:23], v231
	s_cmp_lg_u32 s16, 0
	s_cselect_b64 s[16:17], -1, 0
	ds_read_b128 v[44:47], v224
	ds_read_b128 v[76:79], v224 offset:1024
	ds_read_b128 v[38:41], v224 offset:2048
	ds_read_b128 v[72:75], v224 offset:3072
	ds_read_b128 v[32:35], v224 offset:4096
	ds_read_b128 v[68:71], v224 offset:5120
	ds_read_b128 v[26:29], v224 offset:6144
	ds_read_b128 v[60:63], v224 offset:7168
	s_mov_b32 m0, s78
	s_nop 0
	global_load_lds_dwordx4 v52, s[30:31]
	s_and_b64 vcc, exec, s[16:17]
	s_mov_b32 m0, s79
	s_nop 0
	global_load_lds_dwordx4 v53, s[30:31]
	s_cbranch_vccz .LBB0_1147
	s_waitcnt vmcnt(16)
	s_cbranch_execnz .LBB0_1131

; #define PG8_STAGEB(bufoff, gbase) PG8_STAGE2(bufoff, gbase, voffB[0], voffB[1])
; #define PG8_STAGEAS(bufoff, gbase, h) PG8_STAGE2(bufoff, gbase, voffA[h][0], voffA[h][1])
; #define PG8_LDA(dst, b, h) do { _Pragma("unroll") for (int m = 0; m < 4; ++m) _Pragma("unroll") for (int k = 0; k < 2; ++k) dst[m][k] = *(const LAS bf16x8*)(lds + PG8_SA(b, h) + aoff + m * 2048 + k * 1024); } while (0)
; #define PG8_WAIT_K0() do { if (EST > 0 && t == 0 && ui > 0) asm volatile("s_waitcnt vmcnt(%0)" :: "n"((HM ? 6 : 8) + EST) : "memory"); else PG8_WAIT_K(); } while (0)
; #define PG8_WAIT_L(n) asm volatile("s_waitcnt lgkmcnt(" #n ")" ::: "memory")
; #define PG8_BAR __builtin_amdgcn_s_barrier()
; #define PG8_SCHED __builtin_amdgcn_sched_barrier(0)
;     ...
;             PG8_WAIT_K0(); PG8_WAIT_L(0); PG8_BAR; PG8_MMA(0, 0, At, B0); PG8_MMA(0, 1, At, B1); PG8_BAR; PG8_SCHED;
;             if constexpr (!HM) PG8_LDA(At, 0, 1);
;             PG8_STAGEB(PG8_SB(0, 0), b2); PG8_STAGEB(PG8_SB(0, 1), b2 + hstepB); PG8_STAGEAS(PG8_SA(0, 0), a2, 0);
;             PG8_WAIT_K0(); PG8_WAIT_L(0); PG8_BAR; if constexpr (!HM) { PG8_MMA(1, 0, At, B0); PG8_MMA(1, 1, At, B1); } PG8_BAR; PG8_SCHED;
.LBB0_1131:
	s_waitcnt lgkmcnt(0)
	s_add_u32 s18, s48, 0x100
	s_addc_u32 s19, s49, 0
	s_barrier
	s_setprio 1
	v_mov_b64_e32 v[100:101], s[14:15]
	v_mov_b64_e32 v[172:173], s[14:15]
	v_mov_b64_e32 v[168:169], s[14:15]
	v_mov_b64_e32 v[156:157], s[14:15]
	v_mov_b64_e32 v[152:153], s[14:15]
	v_mov_b64_e32 v[144:145], s[14:15]
	v_mov_b64_e32 v[136:137], s[14:15]
	v_mov_b64_e32 v[120:121], s[14:15]
	v_mov_b64_e32 v[112:113], s[14:15]
	s_waitcnt lgkmcnt(9)
	v_mov_b32_e32 v24, v56
	v_mov_b32_e32 v25, v57
	v_mov_b64_e32 v[98:99], s[12:13]
	v_mov_b64_e32 v[170:171], s[12:13]
	v_mov_b32_e32 v18, v64
	v_mov_b32_e32 v19, v65
	v_mov_b64_e32 v[166:167], s[12:13]
	v_mov_b64_e32 v[154:155], s[12:13]
	v_mov_b64_e32 v[150:151], s[12:13]
	v_mov_b64_e32 v[142:143], s[12:13]
	v_mov_b64_e32 v[134:135], s[12:13]
	v_mov_b64_e32 v[118:119], s[12:13]
	v_mov_b64_e32 v[110:111], s[12:13]
	s_waitcnt lgkmcnt(6)
	v_mov_b32_e32 v48, v76
	v_mov_b32_e32 v49, v77
	s_nop 1
	v_mfma_scale_f32_16x16x128_f8f6f4 v[170:173], v[20:25], v[44:49], v[170:173], v58, v78 op_sel_hi:[0,0,0] cbsz:2 blgp:2
	s_nop 1
	v_mfma_scale_f32_16x16x128_f8f6f4 v[166:169], v[14:19], v[44:49], v[166:169], v66, v78 op_sel_hi:[0,0,0] cbsz:2 blgp:2
	s_waitcnt lgkmcnt(4)
	v_mov_b32_e32 v42, v72
	v_mov_b32_e32 v43, v73
	s_nop 1
	v_mfma_scale_f32_16x16x128_f8f6f4 v[154:157], v[20:25], v[38:43], v[154:157], v58, v74 op_sel_hi:[0,0,0] cbsz:2 blgp:2
	s_nop 1
	v_mfma_scale_f32_16x16x128_f8f6f4 v[150:153], v[14:19], v[38:43], v[150:153], v66, v74 op_sel_hi:[0,0,0] cbsz:2 blgp:2
	s_waitcnt lgkmcnt(2)
	v_mov_b32_e32 v36, v68
	v_mov_b32_e32 v37, v69
	s_nop 1
	v_mfma_scale_f32_16x16x128_f8f6f4 v[142:145], v[20:25], v[32:37], v[142:145], v58, v70 op_sel_hi:[0,0,0] cbsz:2 blgp:2
	s_nop 1
	v_mfma_scale_f32_16x16x128_f8f6f4 v[134:137], v[14:19], v[32:37], v[134:137], v66, v70 op_sel_hi:[0,0,0] cbsz:2 blgp:2
	s_waitcnt lgkmcnt(0)
	v_mov_b32_e32 v30, v60
	v_mov_b32_e32 v31, v61
	s_nop 1
	v_mfma_scale_f32_16x16x128_f8f6f4 v[118:121], v[20:25], v[26:31], v[118:121], v58, v62 op_sel_hi:[0,0,0] cbsz:2 blgp:2
	s_nop 1
	v_mfma_scale_f32_16x16x128_f8f6f4 v[110:113], v[14:19], v[26:31], v[110:113], v66, v62 op_sel_hi:[0,0,0] cbsz:2 blgp:2
	s_setprio 0
	s_setprio 1
	v_mov_b64_e32 v[180:181], s[14:15]
	v_mov_b64_e32 v[176:177], s[14:15]
	v_mov_b64_e32 v[164:165], s[14:15]
	v_mov_b64_e32 v[160:161], s[14:15]
	v_mov_b64_e32 v[148:149], s[14:15]
	v_mov_b64_e32 v[140:141], s[14:15]
	v_mov_b64_e32 v[128:129], s[14:15]
	v_mov_b32_e32 v12, v186
	v_mov_b32_e32 v13, v187
	v_mov_b64_e32 v[178:179], s[12:13]
	v_mov_b32_e32 v6, v182
	v_mov_b32_e32 v7, v183
	v_mov_b64_e32 v[174:175], s[12:13]
	v_mov_b64_e32 v[162:163], s[12:13]
	v_mov_b64_e32 v[158:159], s[12:13]
	v_mov_b64_e32 v[146:147], s[12:13]
	v_mov_b64_e32 v[138:139], s[12:13]
	v_mov_b64_e32 v[126:127], s[12:13]
	s_nop 1
	v_mfma_scale_f32_16x16x128_f8f6f4 v[178:181], v[8:13], v[44:49], v[178:181], v188, v78 op_sel_hi:[0,0,0] cbsz:2 blgp:2
	s_nop 1
	v_mfma_scale_f32_16x16x128_f8f6f4 v[174:177], v[2:7], v[44:49], v[174:177], v184, v78 op_sel_hi:[0,0,0] cbsz:2 blgp:2
	s_nop 1
	v_mfma_scale_f32_16x16x128_f8f6f4 v[162:165], v[8:13], v[38:43], v[162:165], v188, v74 op_sel_hi:[0,0,0] cbsz:2 blgp:2
	s_nop 1
	v_mfma_scale_f32_16x16x128_f8f6f4 v[158:161], v[2:7], v[38:43], v[158:161], v184, v74 op_sel_hi:[0,0,0] cbsz:2 blgp:2
	s_nop 1
	v_mfma_scale_f32_16x16x128_f8f6f4 v[146:149], v[8:13], v[32:37], v[146:149], v188, v70 op_sel_hi:[0,0,0] cbsz:2 blgp:2
	s_nop 1
	v_mfma_scale_f32_16x16x128_f8f6f4 v[138:141], v[2:7], v[32:37], v[138:141], v184, v70 op_sel_hi:[0,0,0] cbsz:2 blgp:2
	s_nop 1
	v_mfma_scale_f32_16x16x128_f8f6f4 v[126:129], v[8:13], v[26:31], v[126:129], v188, v62 op_sel_hi:[0,0,0] cbsz:2 blgp:2
	s_nop 1
	v_mfma_scale_f32_16x16x128_f8f6f4 v[98:101], v[2:7], v[26:31], v[98:101], v184, v62 op_sel_hi:[0,0,0] cbsz:2 blgp:2
	s_setprio 0
	s_barrier
	ds_read_b128 v[44:47], v224 offset:16384
	ds_read_b128 v[80:83], v224 offset:17408
	ds_read_b128 v[38:41], v224 offset:18432
	ds_read_b128 v[72:75], v224 offset:19456
	ds_read_b128 v[32:35], v224 offset:20480
	ds_read_b128 v[194:197], v224 offset:21504
	ds_read_b128 v[26:29], v224 offset:22528
	ds_read_b128 v[190:193], v224 offset:23552
	s_mov_b32 m0, s47
	s_nop 0
	global_load_lds_dwordx4 v217, s[18:19]
	s_mov_b32 m0, s66
	s_nop 0
	global_load_lds_dwordx4 v218, s[18:19]
	s_add_u32 s18, s48, 0x40100
	s_addc_u32 s19, s49, 0
	s_mov_b32 m0, s67
	s_nop 0
	global_load_lds_dwordx4 v217, s[18:19]
	s_and_b64 vcc, exec, s[16:17]
	s_mov_b32 m0, s68
	s_nop 0
	global_load_lds_dwordx4 v218, s[18:19]
	s_mov_b32 m0, s35
	s_nop 0
	global_load_lds_dwordx4 v50, s[24:25]
	s_mov_b32 m0, s69
	s_nop 0
	global_load_lds_dwordx4 v51, s[24:25]
	s_cbranch_vccz .LBB0_1148
	s_waitcnt vmcnt(16)
	s_cbranch_execnz .LBB0_1134

; #define PG8_STAGEAS(bufoff, gbase, h) PG8_STAGE2(bufoff, gbase, voffA[h][0], voffA[h][1])
; #define PG8_LDA(dst, b, h) do { _Pragma("unroll") for (int m = 0; m < 4; ++m) _Pragma("unroll") for (int k = 0; k < 2; ++k) dst[m][k] = *(const LAS bf16x8*)(lds + PG8_SA(b, h) + aoff + m * 2048 + k * 1024); } while (0)
; #define PG8_LDB(dst, b, h) do { _Pragma("unroll") for (int n = 0; n < 2; ++n) _Pragma("unroll") for (int k = 0; k < 2; ++k) dst[n][k] = *(const LAS bf16x8*)(lds + PG8_SB(b, h) + boff + n * 2048 + k * 1024); } while (0)
; #define PG8_WAIT_K() do { if constexpr (HM) PG8_WAIT_V(6); else PG8_WAIT_V(8); } while (0)
; #define PG8_WAIT_K0() do { if (EST > 0 && t == 0 && ui > 0) asm volatile("s_waitcnt vmcnt(%0)" :: "n"((HM ? 6 : 8) + EST) : "memory"); else PG8_WAIT_K(); } while (0)
; #define PG8_WAIT_L(n) asm volatile("s_waitcnt lgkmcnt(" #n ")" ::: "memory")
; #define PG8_BAR __builtin_amdgcn_s_barrier()
; #define PG8_SCHED __builtin_amdgcn_sched_barrier(0)
;     ...
;             PG8_WAIT_K0(); PG8_WAIT_L(0); PG8_BAR; if constexpr (!HM) { PG8_MMA(1, 0, At, B0); PG8_MMA(1, 1, At, B1); } PG8_BAR; PG8_SCHED;
;             PG8_LDB(B0, 1, 0); PG8_LDB(B1, 1, 1); PG8_SCHED; PG8_LDA(At, 1, 0); if constexpr (!HM) PG8_STAGEAS(PG8_SA(0, 1), a2, 1);
;             PG8_WAIT_K(); PG8_WAIT_L(0); PG8_BAR; PG8_MMA(0, 0, At, B0); PG8_MMA(0, 1, At, B1); PG8_BAR; PG8_SCHED;
.LBB0_1134:
	s_waitcnt lgkmcnt(0)
	s_add_u32 s50, s48, 0x180
	s_addc_u32 s51, s49, 0
	s_barrier
	s_setprio 1
	s_mov_b32 s16, 0
	s_mov_b32 s18, s16
	s_mov_b32 s19, s16
	s_waitcnt lgkmcnt(6)
	v_mov_b32_e32 v48, v80
	v_mov_b32_e32 v49, v81
	s_mov_b32 s17, s16
	v_mov_b64_e32 v[116:117], s[18:19]
	v_mov_b64_e32 v[108:109], s[18:19]
	s_waitcnt lgkmcnt(4)
	v_mov_b32_e32 v42, v72
	v_mov_b32_e32 v43, v73
	v_mov_b64_e32 v[96:97], s[18:19]
	v_mov_b64_e32 v[88:89], s[18:19]
	v_mov_b64_e32 v[80:81], s[18:19]
	v_mov_b64_e32 v[72:73], s[18:19]
	v_mov_b64_e32 v[64:65], s[18:19]
	v_mov_b64_e32 v[114:115], s[16:17]
	v_mov_b64_e32 v[106:107], s[16:17]
	v_mov_b64_e32 v[94:95], s[16:17]
	v_mov_b64_e32 v[86:87], s[16:17]
	v_mov_b64_e32 v[78:79], s[16:17]
	v_mov_b64_e32 v[70:71], s[16:17]
	v_mov_b64_e32 v[62:63], s[16:17]
	v_mov_b64_e32 v[56:57], s[18:19]
	s_nop 1
	v_mfma_scale_f32_16x16x128_f8f6f4 v[114:117], v[20:25], v[44:49], v[114:117], v58, v82 op_sel_hi:[0,0,0] cbsz:2 blgp:2
	s_nop 1
	v_mfma_scale_f32_16x16x128_f8f6f4 v[106:109], v[14:19], v[44:49], v[106:109], v66, v82 op_sel_hi:[0,0,0] cbsz:2 blgp:2
	s_nop 1
	v_mfma_scale_f32_16x16x128_f8f6f4 v[94:97], v[20:25], v[38:43], v[94:97], v58, v74 op_sel_hi:[0,0,0] cbsz:2 blgp:2
	s_nop 1
	v_mfma_scale_f32_16x16x128_f8f6f4 v[86:89], v[14:19], v[38:43], v[86:89], v66, v74 op_sel_hi:[0,0,0] cbsz:2 blgp:2
	s_waitcnt lgkmcnt(2)
	v_mov_b32_e32 v36, v194
	v_mov_b32_e32 v37, v195
	s_nop 1
	v_mfma_scale_f32_16x16x128_f8f6f4 v[78:81], v[20:25], v[32:37], v[78:81], v58, v196 op_sel_hi:[0,0,0] cbsz:2 blgp:2
	s_nop 1
	v_mfma_scale_f32_16x16x128_f8f6f4 v[70:73], v[14:19], v[32:37], v[70:73], v66, v196 op_sel_hi:[0,0,0] cbsz:2 blgp:2
	s_waitcnt lgkmcnt(0)
	v_mov_b32_e32 v30, v190
	v_mov_b32_e32 v31, v191
	s_nop 1
	v_mfma_scale_f32_16x16x128_f8f6f4 v[62:65], v[20:25], v[26:31], v[62:65], v58, v192 op_sel_hi:[0,0,0] cbsz:2 blgp:2
	v_mov_b64_e32 v[60:61], s[18:19]
	v_mov_b64_e32 v[54:55], s[16:17]
	v_mov_b64_e32 v[58:59], s[16:17]
	s_nop 1
	v_mfma_scale_f32_16x16x128_f8f6f4 v[58:61], v[14:19], v[26:31], v[58:61], v66, v192 op_sel_hi:[0,0,0] cbsz:2 blgp:2
	s_setprio 0
	s_setprio 1
	v_mov_b64_e32 v[132:133], s[18:19]
	v_mov_b64_e32 v[124:125], s[18:19]
	v_mov_b64_e32 v[104:105], s[18:19]
	v_mov_b64_e32 v[92:93], s[18:19]
	v_mov_b64_e32 v[130:131], s[16:17]
	v_mov_b64_e32 v[122:123], s[16:17]
	v_mov_b64_e32 v[102:103], s[16:17]
	v_mov_b64_e32 v[90:91], s[16:17]
	s_nop 1
	v_mfma_scale_f32_16x16x128_f8f6f4 v[130:133], v[8:13], v[44:49], v[130:133], v188, v82 op_sel_hi:[0,0,0] cbsz:2 blgp:2
	s_nop 1
	v_mfma_scale_f32_16x16x128_f8f6f4 v[122:125], v[2:7], v[44:49], v[122:125], v184, v82 op_sel_hi:[0,0,0] cbsz:2 blgp:2
	s_nop 1
	v_mfma_scale_f32_16x16x128_f8f6f4 v[102:105], v[8:13], v[38:43], v[102:105], v188, v74 op_sel_hi:[0,0,0] cbsz:2 blgp:2
	s_nop 1
	v_mfma_scale_f32_16x16x128_f8f6f4 v[90:93], v[2:7], v[38:43], v[90:93], v184, v74 op_sel_hi:[0,0,0] cbsz:2 blgp:2
	v_mov_b64_e32 v[84:85], s[18:19]
	v_mov_b64_e32 v[76:77], s[18:19]
	v_mov_b64_e32 v[68:69], s[18:19]
	v_mov_b64_e32 v[82:83], s[16:17]
	v_mov_b64_e32 v[74:75], s[16:17]
	v_mov_b64_e32 v[66:67], s[16:17]
	s_nop 1
	v_mfma_scale_f32_16x16x128_f8f6f4 v[82:85], v[8:13], v[32:37], v[82:85], v188, v196 op_sel_hi:[0,0,0] cbsz:2 blgp:2
	s_nop 1
	v_mfma_scale_f32_16x16x128_f8f6f4 v[74:77], v[2:7], v[32:37], v[74:77], v184, v196 op_sel_hi:[0,0,0] cbsz:2 blgp:2
	s_nop 1
	v_mfma_scale_f32_16x16x128_f8f6f4 v[66:69], v[8:13], v[26:31], v[66:69], v188, v192 op_sel_hi:[0,0,0] cbsz:2 blgp:2
	s_nop 1
	v_mfma_scale_f32_16x16x128_f8f6f4 v[54:57], v[2:7], v[26:31], v[54:57], v184, v192 op_sel_hi:[0,0,0] cbsz:2 blgp:2
	s_setprio 0
	s_barrier
	v_add_u32_e32 v232, 0x18000, v223
	v_add_u32_e32 v233, 0x1c000, v223
	ds_read_b128 v[20:23], v232
	ds_read_b128 v[38:41], v232 offset:1024
	ds_read_b128 v[14:17], v232 offset:2048
	ds_read_b128 v[34:37], v232 offset:3072
	ds_read_b128 v[8:11], v233
	ds_read_b128 v[30:33], v233 offset:1024
	ds_read_b128 v[2:5], v233 offset:2048
	ds_read_b128 v[26:29], v233 offset:3072
	ds_read_b128 v[42:45], v224 offset:32768
	ds_read_b128 v[46:49], v224 offset:33792
	ds_read_b128 v[182:185], v224 offset:34816
	ds_read_b128 v[198:201], v224 offset:35840
	ds_read_b128 v[188:191], v224 offset:36864
	ds_read_b128 v[202:205], v224 offset:37888
	ds_read_b128 v[194:197], v224 offset:38912
	ds_read_b128 v[206:209], v224 offset:39936
	s_mov_b32 m0, s70
	s_nop 0
	global_load_lds_dwordx4 v52, s[24:25]
	s_mov_b32 m0, s71
	s_nop 0
	global_load_lds_dwordx4 v53, s[24:25]
	s_waitcnt vmcnt(8)
	s_waitcnt lgkmcnt(0)
	s_barrier
; #define PG8_STAGEB(bufoff, gbase) PG8_STAGE2(bufoff, gbase, voffB[0], voffB[1])
; #define PG8_STAGEAS(bufoff, gbase, h) PG8_STAGE2(bufoff, gbase, voffA[h][0], voffA[h][1])
; #define PG8_LDA(dst, b, h) do { _Pragma("unroll") for (int m = 0; m < 4; ++m) _Pragma("unroll") for (int k = 0; k < 2; ++k) dst[m][k] = *(const LAS bf16x8*)(lds + PG8_SA(b, h) + aoff + m * 2048 + k * 1024); } while (0)
; #define PG8_WAIT_K() do { if constexpr (HM) PG8_WAIT_V(6); else PG8_WAIT_V(8); } while (0)
; #define PG8_WAIT_L(n) asm volatile("s_waitcnt lgkmcnt(" #n ")" ::: "memory")
; #define PG8_BAR __builtin_amdgcn_s_barrier()
; #define PG8_SCHED __builtin_amdgcn_sched_barrier(0)
;     ...
;             PG8_WAIT_K(); PG8_WAIT_L(0); PG8_BAR; PG8_MMA(0, 0, At, B0); PG8_MMA(0, 1, At, B1); PG8_BAR; PG8_SCHED;
;             if constexpr (!HM) PG8_LDA(At, 1, 1);
;             PG8_STAGEB(PG8_SB(1, 0), b3); PG8_STAGEB(PG8_SB(1, 1), b3 + hstepB); PG8_STAGEAS(PG8_SA(1, 0), a3, 0);
;             PG8_WAIT_K(); PG8_WAIT_L(0); PG8_BAR; if constexpr (!HM) { PG8_MMA(1, 0, At, B0); PG8_MMA(1, 1, At, B1); } PG8_BAR; PG8_SCHED;
	s_setprio 1
	s_waitcnt lgkmcnt(14)
	v_mov_b32_e32 v24, v38
	v_mov_b32_e32 v25, v39
	s_waitcnt lgkmcnt(6)
	s_nop 1
	v_mfma_scale_f32_16x16x128_f8f6f4 v[170:173], v[20:25], v[42:47], v[170:173], v40, v48 op_sel_hi:[0,0,0] cbsz:2 blgp:2
	v_mov_b32_e32 v18, v34
	v_mov_b32_e32 v19, v35
	s_nop 1
	v_mfma_scale_f32_16x16x128_f8f6f4 v[166:169], v[14:19], v[42:47], v[166:169], v36, v48 op_sel_hi:[0,0,0] cbsz:2 blgp:2
	s_waitcnt lgkmcnt(4)
	v_mov_b32_e32 v186, v198
	v_mov_b32_e32 v187, v199
	s_nop 1
	v_mfma_scale_f32_16x16x128_f8f6f4 v[154:157], v[20:25], v[182:187], v[154:157], v40, v200 op_sel_hi:[0,0,0] cbsz:2 blgp:2
	s_nop 1
	v_mfma_scale_f32_16x16x128_f8f6f4 v[150:153], v[14:19], v[182:187], v[150:153], v36, v200 op_sel_hi:[0,0,0] cbsz:2 blgp:2
	s_waitcnt lgkmcnt(2)
	v_mov_b32_e32 v192, v202
	v_mov_b32_e32 v193, v203
	s_nop 1
	v_mfma_scale_f32_16x16x128_f8f6f4 v[142:145], v[20:25], v[188:193], v[142:145], v40, v204 op_sel_hi:[0,0,0] cbsz:2 blgp:2
	s_nop 1
	v_mfma_scale_f32_16x16x128_f8f6f4 v[134:137], v[14:19], v[188:193], v[134:137], v36, v204 op_sel_hi:[0,0,0] cbsz:2 blgp:2
	s_waitcnt lgkmcnt(0)
	v_mov_b32_e32 v198, v206
	v_mov_b32_e32 v199, v207
	s_nop 1
	v_mfma_scale_f32_16x16x128_f8f6f4 v[118:121], v[20:25], v[194:199], v[118:121], v40, v208 op_sel_hi:[0,0,0] cbsz:2 blgp:2
	s_nop 1
	v_mfma_scale_f32_16x16x128_f8f6f4 v[110:113], v[14:19], v[194:199], v[110:113], v36, v208 op_sel_hi:[0,0,0] cbsz:2 blgp:2
	s_setprio 0
	s_setprio 1
	v_mov_b32_e32 v12, v30
	v_mov_b32_e32 v13, v31
	s_nop 1
	v_mfma_scale_f32_16x16x128_f8f6f4 v[178:181], v[8:13], v[42:47], v[178:181], v32, v48 op_sel_hi:[0,0,0] cbsz:2 blgp:2
	v_mov_b32_e32 v6, v26
	v_mov_b32_e32 v7, v27
	s_nop 1
	v_mfma_scale_f32_16x16x128_f8f6f4 v[174:177], v[2:7], v[42:47], v[174:177], v28, v48 op_sel_hi:[0,0,0] cbsz:2 blgp:2
	s_nop 1
	v_mfma_scale_f32_16x16x128_f8f6f4 v[162:165], v[8:13], v[182:187], v[162:165], v32, v200 op_sel_hi:[0,0,0] cbsz:2 blgp:2
	s_nop 1
	v_mfma_scale_f32_16x16x128_f8f6f4 v[158:161], v[2:7], v[182:187], v[158:161], v28, v200 op_sel_hi:[0,0,0] cbsz:2 blgp:2
	s_nop 1
	v_mfma_scale_f32_16x16x128_f8f6f4 v[146:149], v[8:13], v[188:193], v[146:149], v32, v204 op_sel_hi:[0,0,0] cbsz:2 blgp:2
	s_nop 1
	v_mfma_scale_f32_16x16x128_f8f6f4 v[138:141], v[2:7], v[188:193], v[138:141], v28, v204 op_sel_hi:[0,0,0] cbsz:2 blgp:2
	s_nop 1
	v_mfma_scale_f32_16x16x128_f8f6f4 v[126:129], v[8:13], v[194:199], v[126:129], v32, v208 op_sel_hi:[0,0,0] cbsz:2 blgp:2
	s_nop 1
	v_mfma_scale_f32_16x16x128_f8f6f4 v[98:101], v[2:7], v[194:199], v[98:101], v28, v208 op_sel_hi:[0,0,0] cbsz:2 blgp:2
	s_setprio 0
	s_barrier
	ds_read_b128 v[42:45], v224 offset:49152
	ds_read_b128 v[46:49], v224 offset:50176
	ds_read_b128 v[182:185], v224 offset:51200
	ds_read_b128 v[198:201], v224 offset:52224
	ds_read_b128 v[188:191], v224 offset:53248
	ds_read_b128 v[202:205], v224 offset:54272
	ds_read_b128 v[194:197], v224 offset:55296
	ds_read_b128 v[206:209], v224 offset:56320
	s_mov_b32 m0, s72
	s_nop 0
	global_load_lds_dwordx4 v217, s[50:51]
	s_add_u32 s18, s48, 0x40180
	s_mov_b32 m0, s73
	s_nop 0
	global_load_lds_dwordx4 v218, s[50:51]
	s_addc_u32 s19, s49, 0
	s_mov_b32 m0, s76
	s_nop 0
	global_load_lds_dwordx4 v217, s[18:19]
	s_mov_b32 m0, s77
	s_nop 0
	global_load_lds_dwordx4 v218, s[18:19]
	s_mov_b32 m0, s74
	s_nop 0
	global_load_lds_dwordx4 v50, s[26:27]
	s_mov_b32 m0, s75
	s_nop 0
	global_load_lds_dwordx4 v51, s[26:27]
	s_waitcnt vmcnt(8)
	s_waitcnt lgkmcnt(0)
	s_barrier
	s_setprio 1
	s_waitcnt lgkmcnt(6)
	s_nop 1
	v_mfma_scale_f32_16x16x128_f8f6f4 v[114:117], v[20:25], v[42:47], v[114:117], v40, v48 op_sel_hi:[0,0,0] cbsz:2 blgp:2
	s_nop 1
	v_mfma_scale_f32_16x16x128_f8f6f4 v[106:109], v[14:19], v[42:47], v[106:109], v36, v48 op_sel_hi:[0,0,0] cbsz:2 blgp:2
	s_waitcnt lgkmcnt(4)
	v_mov_b32_e32 v186, v198
	v_mov_b32_e32 v187, v199
	s_nop 1
	v_mfma_scale_f32_16x16x128_f8f6f4 v[94:97], v[20:25], v[182:187], v[94:97], v40, v200 op_sel_hi:[0,0,0] cbsz:2 blgp:2
	s_nop 1
	v_mfma_scale_f32_16x16x128_f8f6f4 v[86:89], v[14:19], v[182:187], v[86:89], v36, v200 op_sel_hi:[0,0,0] cbsz:2 blgp:2
	s_waitcnt lgkmcnt(2)
	v_mov_b32_e32 v192, v202
	v_mov_b32_e32 v193, v203
	s_nop 1
	v_mfma_scale_f32_16x16x128_f8f6f4 v[78:81], v[20:25], v[188:193], v[78:81], v40, v204 op_sel_hi:[0,0,0] cbsz:2 blgp:2
	s_nop 1
	v_mfma_scale_f32_16x16x128_f8f6f4 v[70:73], v[14:19], v[188:193], v[70:73], v36, v204 op_sel_hi:[0,0,0] cbsz:2 blgp:2
	s_waitcnt lgkmcnt(0)
	v_mov_b32_e32 v198, v206
	v_mov_b32_e32 v199, v207
	s_nop 1
	v_mfma_scale_f32_16x16x128_f8f6f4 v[62:65], v[20:25], v[194:199], v[62:65], v40, v208 op_sel_hi:[0,0,0] cbsz:2 blgp:2
	s_nop 1
	v_mfma_scale_f32_16x16x128_f8f6f4 v[58:61], v[14:19], v[194:199], v[58:61], v36, v208 op_sel_hi:[0,0,0] cbsz:2 blgp:2
	s_setprio 0
	s_setprio 1
	s_nop 1
	v_mfma_scale_f32_16x16x128_f8f6f4 v[130:133], v[8:13], v[42:47], v[130:133], v32, v48 op_sel_hi:[0,0,0] cbsz:2 blgp:2
	s_nop 1
	v_mfma_scale_f32_16x16x128_f8f6f4 v[122:125], v[2:7], v[42:47], v[122:125], v28, v48 op_sel_hi:[0,0,0] cbsz:2 blgp:2
	s_nop 1
	v_mfma_scale_f32_16x16x128_f8f6f4 v[102:105], v[8:13], v[182:187], v[102:105], v32, v200 op_sel_hi:[0,0,0] cbsz:2 blgp:2
	s_nop 1
	v_mfma_scale_f32_16x16x128_f8f6f4 v[90:93], v[2:7], v[182:187], v[90:93], v28, v200 op_sel_hi:[0,0,0] cbsz:2 blgp:2
	s_nop 1
	v_mfma_scale_f32_16x16x128_f8f6f4 v[82:85], v[8:13], v[188:193], v[82:85], v32, v204 op_sel_hi:[0,0,0] cbsz:2 blgp:2
	s_nop 1
	v_mfma_scale_f32_16x16x128_f8f6f4 v[74:77], v[2:7], v[188:193], v[74:77], v28, v204 op_sel_hi:[0,0,0] cbsz:2 blgp:2
	s_nop 1
	v_mfma_scale_f32_16x16x128_f8f6f4 v[66:69], v[8:13], v[194:199], v[66:69], v32, v208 op_sel_hi:[0,0,0] cbsz:2 blgp:2
	s_nop 1
	v_mfma_scale_f32_16x16x128_f8f6f4 v[54:57], v[2:7], v[194:199], v[54:57], v28, v208 op_sel_hi:[0,0,0] cbsz:2 blgp:2
	s_setprio 0
	s_barrier
	s_mov_b64 s[18:19], 0x200
	s_xor_b64 s[50:51], s[10:11], -1
	s_branch .LBB0_1136
; #define LAS __attribute__((address_space(3)))
; #define PG8_STAGEB(bufoff, gbase) PG8_STAGE2(bufoff, gbase, voffB[0], voffB[1])
; #define PG8_STAGEA(bufoff, gbase, h) PG8_STAGE2(bufoff, gbase, voffA[h][0], voffA[h][1])
; #define PG8_STAGEAS(bufoff, gbase, h) PG8_STAGE2(bufoff, gbase, voffA[h][0], voffA[h][1])
; #define PG8_LDA(dst, b, h) do { _Pragma("unroll") for (int m = 0; m < 4; ++m) _Pragma("unroll") for (int k = 0; k < 2; ++k) dst[m][k] = *(const LAS bf16x8*)(lds + PG8_SA(b, h) + aoff + m * 2048 + k * 1024); } while (0)
; #define PG8_LDB(dst, b, h) do { _Pragma("unroll") for (int n = 0; n < 2; ++n) _Pragma("unroll") for (int k = 0; k < 2; ++k) dst[n][k] = *(const LAS bf16x8*)(lds + PG8_SB(b, h) + boff + n * 2048 + k * 1024); } while (0)
; #define PG8_WAIT_K0() do { if (EST > 0 && t == 0 && ui > 0) asm volatile("s_waitcnt vmcnt(%0)" :: "n"((HM ? 6 : 8) + EST) : "memory"); else PG8_WAIT_K(); } while (0)
; #define PG8_WAIT_L(n) asm volatile("s_waitcnt lgkmcnt(" #n ")" ::: "memory")
; #define PG8_BAR __builtin_amdgcn_s_barrier()
; #define PG8_SCHED __builtin_amdgcn_sched_barrier(0)
;     ...
;             const char* a2 = last ? nA : cA + (size_t)(t + 2) * kstep; const char* b2 = last ? nB : cB + (size_t)(t + 2) * kstep;
;             const char* a3 = a2 + kstep; const char* b3 = b2 + kstep;
;             PG8_LDB(B0, 0, 0); PG8_LDB(B1, 0, 1); PG8_SCHED; PG8_LDA(At, 0, 0); if constexpr (!HM) PG8_STAGEA(PG8_SA(1, 1), a1, 1);
;             if constexpr (Sched::kGather) { if (last && has_next) { const u32x4 tn = *(const LAS u32x4*)(S.aux + tid * 16); voffA[0][0] = tn.x; voffA[0][1] = tn.y; voffA[1][0] = tn.z; voffA[1][1] = tn.w; } }
;             PG8_WAIT_K0(); PG8_WAIT_L(0); PG8_BAR; PG8_MMA(0, 0, At, B0); PG8_MMA(0, 1, At, B1); PG8_BAR; PG8_SCHED;
;             if constexpr (!HM) PG8_LDA(At, 0, 1);
;             PG8_STAGEB(PG8_SB(0, 0), b2); PG8_STAGEB(PG8_SB(0, 1), b2 + hstepB); PG8_STAGEAS(PG8_SA(0, 0), a2, 0);
;             PG8_WAIT_K0(); PG8_WAIT_L(0); PG8_BAR; if constexpr (!HM) { PG8_MMA(1, 0, At, B0); PG8_MMA(1, 1, At, B1); } PG8_BAR; PG8_SCHED;
.LBB0_1135:
	s_and_b64 s[52:53], s[54:55], exec
	s_cselect_b32 s41, 0, s18
	s_cselect_b32 s17, 0, s19
	s_add_u32 s58, s0, s41
	s_addc_u32 s59, s1, s17
	s_add_u32 s17, s48, s18
	s_addc_u32 s41, s49, s19
	s_add_u32 s52, s58, 0x80
	s_addc_u32 s53, s59, 0
	s_waitcnt vmcnt(8)
	s_and_b64 s[54:55], s[54:55], exec
	s_waitcnt lgkmcnt(0)
	s_cselect_b32 s54, s44, s17
	s_cselect_b32 s55, s45, s41
	s_add_u32 s56, s54, 0x80
	s_addc_u32 s57, s55, 0
	s_barrier
	s_setprio 1
	s_waitcnt lgkmcnt(6)
	v_mov_b32_e32 v48, v210
	v_mov_b32_e32 v49, v211
	v_mov_b32_e32 v24, v194
	v_mov_b32_e32 v25, v195
	s_nop 1
	v_mfma_scale_f32_16x16x128_f8f6f4 v[170:173], v[20:25], v[44:49], v[170:173], v196, v212 op_sel_hi:[0,0,0] cbsz:2 blgp:2
	v_mov_b32_e32 v18, v190
	v_mov_b32_e32 v19, v191
	s_nop 1
	v_mfma_scale_f32_16x16x128_f8f6f4 v[166:169], v[14:19], v[44:49], v[166:169], v192, v212 op_sel_hi:[0,0,0] cbsz:2 blgp:2
	s_waitcnt lgkmcnt(4)
	v_mov_b32_e32 v42, v206
	v_mov_b32_e32 v43, v207
	s_nop 1
	v_mfma_scale_f32_16x16x128_f8f6f4 v[154:157], v[20:25], v[38:43], v[154:157], v196, v208 op_sel_hi:[0,0,0] cbsz:2 blgp:2
	s_nop 1
	v_mfma_scale_f32_16x16x128_f8f6f4 v[150:153], v[14:19], v[38:43], v[150:153], v192, v208 op_sel_hi:[0,0,0] cbsz:2 blgp:2
	s_waitcnt lgkmcnt(2)
	v_mov_b32_e32 v36, v202
	v_mov_b32_e32 v37, v203
	s_nop 1
	v_mfma_scale_f32_16x16x128_f8f6f4 v[142:145], v[20:25], v[32:37], v[142:145], v196, v204 op_sel_hi:[0,0,0] cbsz:2 blgp:2
	s_nop 1
	v_mfma_scale_f32_16x16x128_f8f6f4 v[134:137], v[14:19], v[32:37], v[134:137], v192, v204 op_sel_hi:[0,0,0] cbsz:2 blgp:2
	s_waitcnt lgkmcnt(0)
	v_mov_b32_e32 v30, v198
	v_mov_b32_e32 v31, v199
	s_nop 1
	v_mfma_scale_f32_16x16x128_f8f6f4 v[118:121], v[20:25], v[26:31], v[118:121], v196, v200 op_sel_hi:[0,0,0] cbsz:2 blgp:2
	s_nop 1
	v_mfma_scale_f32_16x16x128_f8f6f4 v[110:113], v[14:19], v[26:31], v[110:113], v192, v200 op_sel_hi:[0,0,0] cbsz:2 blgp:2
	s_setprio 0
	s_setprio 1
	v_mov_b32_e32 v12, v182
	v_mov_b32_e32 v13, v183
	s_nop 1
	v_mfma_scale_f32_16x16x128_f8f6f4 v[178:181], v[8:13], v[44:49], v[178:181], v184, v212 op_sel_hi:[0,0,0] cbsz:2 blgp:2
	v_mov_b32_e32 v6, v186
	v_mov_b32_e32 v7, v187
	s_nop 1
	v_mfma_scale_f32_16x16x128_f8f6f4 v[174:177], v[2:7], v[44:49], v[174:177], v188, v212 op_sel_hi:[0,0,0] cbsz:2 blgp:2
	s_nop 1
	v_mfma_scale_f32_16x16x128_f8f6f4 v[162:165], v[8:13], v[38:43], v[162:165], v184, v208 op_sel_hi:[0,0,0] cbsz:2 blgp:2
	s_nop 1
	v_mfma_scale_f32_16x16x128_f8f6f4 v[158:161], v[2:7], v[38:43], v[158:161], v188, v208 op_sel_hi:[0,0,0] cbsz:2 blgp:2
	s_nop 1
	v_mfma_scale_f32_16x16x128_f8f6f4 v[146:149], v[8:13], v[32:37], v[146:149], v184, v204 op_sel_hi:[0,0,0] cbsz:2 blgp:2
	s_nop 1
	v_mfma_scale_f32_16x16x128_f8f6f4 v[138:141], v[2:7], v[32:37], v[138:141], v188, v204 op_sel_hi:[0,0,0] cbsz:2 blgp:2
	s_nop 1
	v_mfma_scale_f32_16x16x128_f8f6f4 v[126:129], v[8:13], v[26:31], v[126:129], v184, v200 op_sel_hi:[0,0,0] cbsz:2 blgp:2
	s_nop 1
	v_mfma_scale_f32_16x16x128_f8f6f4 v[98:101], v[2:7], v[26:31], v[98:101], v188, v200 op_sel_hi:[0,0,0] cbsz:2 blgp:2
	s_setprio 0
	s_barrier
	ds_read_b128 v[26:29], v224 offset:16384
	ds_read_b128 v[198:201], v224 offset:17408
	ds_read_b128 v[32:35], v224 offset:18432
	ds_read_b128 v[202:205], v224 offset:19456
	ds_read_b128 v[38:41], v224 offset:20480
	ds_read_b128 v[206:209], v224 offset:21504
	ds_read_b128 v[44:47], v224 offset:22528
	ds_read_b128 v[210:213], v224 offset:23552
	s_mov_b32 m0, s47
	s_nop 0
	global_load_lds_dwordx4 v217, s[54:55]
	s_add_u32 s86, s54, 0x40000
	s_mov_b32 m0, s66
	s_nop 0
	global_load_lds_dwordx4 v218, s[54:55]
	s_addc_u32 s87, s55, 0
	s_mov_b32 m0, s67
	s_nop 0
	global_load_lds_dwordx4 v217, s[86:87]
	s_mov_b32 m0, s68
	s_nop 0
	global_load_lds_dwordx4 v218, s[86:87]
	s_mov_b32 m0, s35
	s_nop 0
	global_load_lds_dwordx4 v50, s[58:59]
	s_mov_b32 m0, s69
	s_nop 0
	global_load_lds_dwordx4 v51, s[58:59]
	s_waitcnt vmcnt(8)
	s_waitcnt lgkmcnt(0)
	s_barrier
	s_setprio 1
	s_waitcnt lgkmcnt(6)
	v_mov_b32_e32 v30, v198
	v_mov_b32_e32 v31, v199
	s_nop 1
	v_mfma_scale_f32_16x16x128_f8f6f4 v[114:117], v[20:25], v[26:31], v[114:117], v196, v200 op_sel_hi:[0,0,0] cbsz:2 blgp:2
	s_nop 1
	v_mfma_scale_f32_16x16x128_f8f6f4 v[106:109], v[14:19], v[26:31], v[106:109], v192, v200 op_sel_hi:[0,0,0] cbsz:2 blgp:2
	s_waitcnt lgkmcnt(4)
	v_mov_b32_e32 v36, v202
	v_mov_b32_e32 v37, v203
	s_nop 1
	v_mfma_scale_f32_16x16x128_f8f6f4 v[94:97], v[20:25], v[32:37], v[94:97], v196, v204 op_sel_hi:[0,0,0] cbsz:2 blgp:2
	s_nop 1
	v_mfma_scale_f32_16x16x128_f8f6f4 v[86:89], v[14:19], v[32:37], v[86:89], v192, v204 op_sel_hi:[0,0,0] cbsz:2 blgp:2
	s_waitcnt lgkmcnt(2)
	v_mov_b32_e32 v42, v206
	v_mov_b32_e32 v43, v207
	s_nop 1
	v_mfma_scale_f32_16x16x128_f8f6f4 v[78:81], v[20:25], v[38:43], v[78:81], v196, v208 op_sel_hi:[0,0,0] cbsz:2 blgp:2
	s_nop 1
	v_mfma_scale_f32_16x16x128_f8f6f4 v[70:73], v[14:19], v[38:43], v[70:73], v192, v208 op_sel_hi:[0,0,0] cbsz:2 blgp:2
	s_waitcnt lgkmcnt(0)
	v_mov_b32_e32 v48, v210
	v_mov_b32_e32 v49, v211
	s_nop 1
	v_mfma_scale_f32_16x16x128_f8f6f4 v[62:65], v[20:25], v[44:49], v[62:65], v196, v212 op_sel_hi:[0,0,0] cbsz:2 blgp:2
	s_nop 1
	v_mfma_scale_f32_16x16x128_f8f6f4 v[58:61], v[14:19], v[44:49], v[58:61], v192, v212 op_sel_hi:[0,0,0] cbsz:2 blgp:2
	s_setprio 0
	s_setprio 1
	s_nop 1
	v_mfma_scale_f32_16x16x128_f8f6f4 v[130:133], v[8:13], v[26:31], v[130:133], v184, v200 op_sel_hi:[0,0,0] cbsz:2 blgp:2
	s_nop 1
	v_mfma_scale_f32_16x16x128_f8f6f4 v[122:125], v[2:7], v[26:31], v[122:125], v188, v200 op_sel_hi:[0,0,0] cbsz:2 blgp:2
	s_nop 1
	v_mfma_scale_f32_16x16x128_f8f6f4 v[102:105], v[8:13], v[32:37], v[102:105], v184, v204 op_sel_hi:[0,0,0] cbsz:2 blgp:2
	s_nop 1
	v_mfma_scale_f32_16x16x128_f8f6f4 v[90:93], v[2:7], v[32:37], v[90:93], v188, v204 op_sel_hi:[0,0,0] cbsz:2 blgp:2
	s_nop 1
	v_mfma_scale_f32_16x16x128_f8f6f4 v[82:85], v[8:13], v[38:43], v[82:85], v184, v208 op_sel_hi:[0,0,0] cbsz:2 blgp:2
	s_nop 1
	v_mfma_scale_f32_16x16x128_f8f6f4 v[74:77], v[2:7], v[38:43], v[74:77], v188, v208 op_sel_hi:[0,0,0] cbsz:2 blgp:2
	s_nop 1
	v_mfma_scale_f32_16x16x128_f8f6f4 v[66:69], v[8:13], v[44:49], v[66:69], v184, v212 op_sel_hi:[0,0,0] cbsz:2 blgp:2
	s_nop 1
	v_mfma_scale_f32_16x16x128_f8f6f4 v[54:57], v[2:7], v[44:49], v[54:57], v188, v212 op_sel_hi:[0,0,0] cbsz:2 blgp:2
	s_setprio 0
	s_barrier
; #define PG8_STAGEB(bufoff, gbase) PG8_STAGE2(bufoff, gbase, voffB[0], voffB[1])
; #define PG8_STAGEAS(bufoff, gbase, h) PG8_STAGE2(bufoff, gbase, voffA[h][0], voffA[h][1])
; #define PG8_LDA(dst, b, h) do { _Pragma("unroll") for (int m = 0; m < 4; ++m) _Pragma("unroll") for (int k = 0; k < 2; ++k) dst[m][k] = *(const LAS bf16x8*)(lds + PG8_SA(b, h) + aoff + m * 2048 + k * 1024); } while (0)
; #define PG8_LDB(dst, b, h) do { _Pragma("unroll") for (int n = 0; n < 2; ++n) _Pragma("unroll") for (int k = 0; k < 2; ++k) dst[n][k] = *(const LAS bf16x8*)(lds + PG8_SB(b, h) + boff + n * 2048 + k * 1024); } while (0)
; #define PG8_WAIT_K() do { if constexpr (HM) PG8_WAIT_V(6); else PG8_WAIT_V(8); } while (0)
; #define PG8_WAIT_L(n) asm volatile("s_waitcnt lgkmcnt(" #n ")" ::: "memory")
; #define PG8_BAR __builtin_amdgcn_s_barrier()
; #define PG8_SCHED __builtin_amdgcn_sched_barrier(0)
;     ...
;             PG8_LDB(B0, 1, 0); PG8_LDB(B1, 1, 1); PG8_SCHED; PG8_LDA(At, 1, 0); if constexpr (!HM) PG8_STAGEAS(PG8_SA(0, 1), a2, 1);
;             PG8_WAIT_K(); PG8_WAIT_L(0); PG8_BAR; PG8_MMA(0, 0, At, B0); PG8_MMA(0, 1, At, B1); PG8_BAR; PG8_SCHED;
;             if constexpr (!HM) PG8_LDA(At, 1, 1);
;             PG8_STAGEB(PG8_SB(1, 0), b3); PG8_STAGEB(PG8_SB(1, 1), b3 + hstepB); PG8_STAGEAS(PG8_SA(1, 0), a3, 0);
;             PG8_WAIT_K(); PG8_WAIT_L(0); PG8_BAR; if constexpr (!HM) { PG8_MMA(1, 0, At, B0); PG8_MMA(1, 1, At, B1); } PG8_BAR; PG8_SCHED;
	ds_read_b128 v[20:23], v232
	ds_read_b128 v[38:41], v232 offset:1024
	ds_read_b128 v[14:17], v232 offset:2048
	ds_read_b128 v[34:37], v232 offset:3072
	ds_read_b128 v[8:11], v233
	ds_read_b128 v[30:33], v233 offset:1024
	ds_read_b128 v[2:5], v233 offset:2048
	ds_read_b128 v[26:29], v233 offset:3072
	ds_read_b128 v[42:45], v224 offset:32768
	ds_read_b128 v[46:49], v224 offset:33792
	ds_read_b128 v[182:185], v224 offset:34816
	ds_read_b128 v[198:201], v224 offset:35840
	ds_read_b128 v[188:191], v224 offset:36864
	ds_read_b128 v[202:205], v224 offset:37888
	ds_read_b128 v[194:197], v224 offset:38912
	ds_read_b128 v[206:209], v224 offset:39936
	s_mov_b32 m0, s70
	s_nop 0
	global_load_lds_dwordx4 v52, s[58:59]
	s_mov_b32 m0, s71
	s_nop 0
	global_load_lds_dwordx4 v53, s[58:59]
	s_waitcnt vmcnt(8)
	s_waitcnt lgkmcnt(0)
	s_barrier
	s_setprio 1
	s_waitcnt lgkmcnt(14)
	v_mov_b32_e32 v24, v38
	v_mov_b32_e32 v25, v39
	s_waitcnt lgkmcnt(6)
	s_nop 1
	v_mfma_scale_f32_16x16x128_f8f6f4 v[170:173], v[20:25], v[42:47], v[170:173], v40, v48 op_sel_hi:[0,0,0] cbsz:2 blgp:2
	v_mov_b32_e32 v18, v34
	v_mov_b32_e32 v19, v35
	s_nop 1
	v_mfma_scale_f32_16x16x128_f8f6f4 v[166:169], v[14:19], v[42:47], v[166:169], v36, v48 op_sel_hi:[0,0,0] cbsz:2 blgp:2
	s_waitcnt lgkmcnt(4)
	v_mov_b32_e32 v186, v198
	v_mov_b32_e32 v187, v199
	s_nop 1
	v_mfma_scale_f32_16x16x128_f8f6f4 v[154:157], v[20:25], v[182:187], v[154:157], v40, v200 op_sel_hi:[0,0,0] cbsz:2 blgp:2
	s_nop 1
	v_mfma_scale_f32_16x16x128_f8f6f4 v[150:153], v[14:19], v[182:187], v[150:153], v36, v200 op_sel_hi:[0,0,0] cbsz:2 blgp:2
	s_waitcnt lgkmcnt(2)
	v_mov_b32_e32 v192, v202
	v_mov_b32_e32 v193, v203
	s_nop 1
	v_mfma_scale_f32_16x16x128_f8f6f4 v[142:145], v[20:25], v[188:193], v[142:145], v40, v204 op_sel_hi:[0,0,0] cbsz:2 blgp:2
	s_nop 1
	v_mfma_scale_f32_16x16x128_f8f6f4 v[134:137], v[14:19], v[188:193], v[134:137], v36, v204 op_sel_hi:[0,0,0] cbsz:2 blgp:2
	s_waitcnt lgkmcnt(0)
	v_mov_b32_e32 v198, v206
	v_mov_b32_e32 v199, v207
	s_nop 1
	v_mfma_scale_f32_16x16x128_f8f6f4 v[118:121], v[20:25], v[194:199], v[118:121], v40, v208 op_sel_hi:[0,0,0] cbsz:2 blgp:2
	s_nop 1
	v_mfma_scale_f32_16x16x128_f8f6f4 v[110:113], v[14:19], v[194:199], v[110:113], v36, v208 op_sel_hi:[0,0,0] cbsz:2 blgp:2
	s_setprio 0
	s_setprio 1
	v_mov_b32_e32 v12, v30
	v_mov_b32_e32 v13, v31
	s_nop 1
	v_mfma_scale_f32_16x16x128_f8f6f4 v[178:181], v[8:13], v[42:47], v[178:181], v32, v48 op_sel_hi:[0,0,0] cbsz:2 blgp:2
	v_mov_b32_e32 v6, v26
	v_mov_b32_e32 v7, v27
	s_nop 1
	v_mfma_scale_f32_16x16x128_f8f6f4 v[174:177], v[2:7], v[42:47], v[174:177], v28, v48 op_sel_hi:[0,0,0] cbsz:2 blgp:2
	s_nop 1
	v_mfma_scale_f32_16x16x128_f8f6f4 v[162:165], v[8:13], v[182:187], v[162:165], v32, v200 op_sel_hi:[0,0,0] cbsz:2 blgp:2
	s_nop 1
	v_mfma_scale_f32_16x16x128_f8f6f4 v[158:161], v[2:7], v[182:187], v[158:161], v28, v200 op_sel_hi:[0,0,0] cbsz:2 blgp:2
	s_nop 1
	v_mfma_scale_f32_16x16x128_f8f6f4 v[146:149], v[8:13], v[188:193], v[146:149], v32, v204 op_sel_hi:[0,0,0] cbsz:2 blgp:2
	s_nop 1
	v_mfma_scale_f32_16x16x128_f8f6f4 v[138:141], v[2:7], v[188:193], v[138:141], v28, v204 op_sel_hi:[0,0,0] cbsz:2 blgp:2
	s_nop 1
	v_mfma_scale_f32_16x16x128_f8f6f4 v[126:129], v[8:13], v[194:199], v[126:129], v32, v208 op_sel_hi:[0,0,0] cbsz:2 blgp:2
	s_nop 1
	v_mfma_scale_f32_16x16x128_f8f6f4 v[98:101], v[2:7], v[194:199], v[98:101], v28, v208 op_sel_hi:[0,0,0] cbsz:2 blgp:2
	s_setprio 0
	s_barrier
	ds_read_b128 v[42:45], v224 offset:49152
	ds_read_b128 v[46:49], v224 offset:50176
	ds_read_b128 v[182:185], v224 offset:51200
	ds_read_b128 v[198:201], v224 offset:52224
	ds_read_b128 v[188:191], v224 offset:53248
	ds_read_b128 v[202:205], v224 offset:54272
	ds_read_b128 v[194:197], v224 offset:55296
	ds_read_b128 v[206:209], v224 offset:56320
	s_mov_b32 m0, s72
	s_nop 0
	global_load_lds_dwordx4 v217, s[56:57]
	s_add_u32 s54, s54, 0x40080
	s_mov_b32 m0, s73
	s_nop 0
	global_load_lds_dwordx4 v218, s[56:57]
	s_addc_u32 s55, s55, 0
	s_mov_b32 m0, s76
	s_nop 0
	global_load_lds_dwordx4 v217, s[54:55]
	s_mov_b32 m0, s77
	s_nop 0
	global_load_lds_dwordx4 v218, s[54:55]
	s_mov_b32 m0, s74
	s_nop 0
	global_load_lds_dwordx4 v50, s[52:53]
	s_mov_b32 m0, s75
	s_nop 0
	global_load_lds_dwordx4 v51, s[52:53]
	s_waitcnt vmcnt(8)
	s_waitcnt lgkmcnt(0)
	s_barrier
	s_setprio 1
	s_waitcnt lgkmcnt(6)
	s_nop 1
	v_mfma_scale_f32_16x16x128_f8f6f4 v[114:117], v[20:25], v[42:47], v[114:117], v40, v48 op_sel_hi:[0,0,0] cbsz:2 blgp:2
	s_nop 1
	v_mfma_scale_f32_16x16x128_f8f6f4 v[106:109], v[14:19], v[42:47], v[106:109], v36, v48 op_sel_hi:[0,0,0] cbsz:2 blgp:2
	s_waitcnt lgkmcnt(4)
	v_mov_b32_e32 v186, v198
	v_mov_b32_e32 v187, v199
	s_nop 1
	v_mfma_scale_f32_16x16x128_f8f6f4 v[94:97], v[20:25], v[182:187], v[94:97], v40, v200 op_sel_hi:[0,0,0] cbsz:2 blgp:2
	s_nop 1
	v_mfma_scale_f32_16x16x128_f8f6f4 v[86:89], v[14:19], v[182:187], v[86:89], v36, v200 op_sel_hi:[0,0,0] cbsz:2 blgp:2
	s_waitcnt lgkmcnt(2)
	v_mov_b32_e32 v192, v202
	v_mov_b32_e32 v193, v203
	s_nop 1
	v_mfma_scale_f32_16x16x128_f8f6f4 v[78:81], v[20:25], v[188:193], v[78:81], v40, v204 op_sel_hi:[0,0,0] cbsz:2 blgp:2
	s_nop 1
	v_mfma_scale_f32_16x16x128_f8f6f4 v[70:73], v[14:19], v[188:193], v[70:73], v36, v204 op_sel_hi:[0,0,0] cbsz:2 blgp:2
	s_waitcnt lgkmcnt(0)
	v_mov_b32_e32 v198, v206
	v_mov_b32_e32 v199, v207
	s_nop 1
	v_mfma_scale_f32_16x16x128_f8f6f4 v[62:65], v[20:25], v[194:199], v[62:65], v40, v208 op_sel_hi:[0,0,0] cbsz:2 blgp:2
	s_nop 1
	v_mfma_scale_f32_16x16x128_f8f6f4 v[58:61], v[14:19], v[194:199], v[58:61], v36, v208 op_sel_hi:[0,0,0] cbsz:2 blgp:2
	s_setprio 0
	s_setprio 1
	s_nop 1
	v_mfma_scale_f32_16x16x128_f8f6f4 v[130:133], v[8:13], v[42:47], v[130:133], v32, v48 op_sel_hi:[0,0,0] cbsz:2 blgp:2
	s_nop 1
	v_mfma_scale_f32_16x16x128_f8f6f4 v[122:125], v[2:7], v[42:47], v[122:125], v28, v48 op_sel_hi:[0,0,0] cbsz:2 blgp:2
	s_nop 1
	v_mfma_scale_f32_16x16x128_f8f6f4 v[102:105], v[8:13], v[182:187], v[102:105], v32, v200 op_sel_hi:[0,0,0] cbsz:2 blgp:2
	s_nop 1
	v_mfma_scale_f32_16x16x128_f8f6f4 v[90:93], v[2:7], v[182:187], v[90:93], v28, v200 op_sel_hi:[0,0,0] cbsz:2 blgp:2
	s_nop 1
	v_mfma_scale_f32_16x16x128_f8f6f4 v[82:85], v[8:13], v[188:193], v[82:85], v32, v204 op_sel_hi:[0,0,0] cbsz:2 blgp:2
	s_nop 1
	v_mfma_scale_f32_16x16x128_f8f6f4 v[74:77], v[2:7], v[188:193], v[74:77], v28, v204 op_sel_hi:[0,0,0] cbsz:2 blgp:2
	s_nop 1
	v_mfma_scale_f32_16x16x128_f8f6f4 v[66:69], v[8:13], v[194:199], v[66:69], v32, v208 op_sel_hi:[0,0,0] cbsz:2 blgp:2
	s_nop 1
	v_mfma_scale_f32_16x16x128_f8f6f4 v[54:57], v[2:7], v[194:199], v[54:57], v28, v208 op_sel_hi:[0,0,0] cbsz:2 blgp:2
	s_setprio 0
	s_barrier
	s_add_i32 s16, s16, 2
	s_add_u32 s18, s18, 0x100
	s_addc_u32 s19, s19, 0
	s_cmp_gt_u32 s16, 13
	s_cbranch_scc1 .LBB0_1140

; #define LAS __attribute__((address_space(3)))
; #define PG8_STAGEA(bufoff, gbase, h) PG8_STAGE2(bufoff, gbase, voffA[h][0], voffA[h][1])
; #define PG8_LDA(dst, b, h) do { _Pragma("unroll") for (int m = 0; m < 4; ++m) _Pragma("unroll") for (int k = 0; k < 2; ++k) dst[m][k] = *(const LAS bf16x8*)(lds + PG8_SA(b, h) + aoff + m * 2048 + k * 1024); } while (0)
; #define PG8_LDB(dst, b, h) do { _Pragma("unroll") for (int n = 0; n < 2; ++n) _Pragma("unroll") for (int k = 0; k < 2; ++k) dst[n][k] = *(const LAS bf16x8*)(lds + PG8_SB(b, h) + boff + n * 2048 + k * 1024); } while (0)
; #define PG8_SCHED __builtin_amdgcn_sched_barrier(0)
;     ...
;             const char* a1 = cA + (size_t)(t + 1) * kstep;
;             const char* a2 = last ? nA : cA + (size_t)(t + 2) * kstep; const char* b2 = last ? nB : cB + (size_t)(t + 2) * kstep;
;             const char* a3 = a2 + kstep; const char* b3 = b2 + kstep;
;             PG8_LDB(B0, 0, 0); PG8_LDB(B1, 0, 1); PG8_SCHED; PG8_LDA(At, 0, 0); if constexpr (!HM) PG8_STAGEA(PG8_SA(1, 1), a1, 1);
;             if constexpr (Sched::kGather) { if (last && has_next) { const u32x4 tn = *(const LAS u32x4*)(S.aux + tid * 16); voffA[0][0] = tn.x; voffA[0][1] = tn.y; voffA[1][0] = tn.z; voffA[1][1] = tn.w; } }
.LBB0_1138:
	ds_read_b128 v[20:23], v231
	ds_read_b128 v[194:197], v231 offset:1024
	ds_read_b128 v[14:17], v231 offset:2048
	ds_read_b128 v[190:193], v231 offset:3072
	ds_read_b128 v[8:11], v230
	ds_read_b128 v[182:185], v230 offset:1024
	ds_read_b128 v[2:5], v230 offset:2048
	ds_read_b128 v[186:189], v230 offset:3072
	s_cmp_eq_u32 s16, 12
	s_cselect_b64 s[54:55], -1, 0
	s_add_u32 s17, s0, s18
	s_addc_u32 s41, s1, s19
	s_add_u32 s52, s17, 0xffffff80
	s_addc_u32 s53, s41, -1
	ds_read_b128 v[44:47], v224
	ds_read_b128 v[210:213], v224 offset:1024
	ds_read_b128 v[38:41], v224 offset:2048
	ds_read_b128 v[206:209], v224 offset:3072
	ds_read_b128 v[32:35], v224 offset:4096
	ds_read_b128 v[202:205], v224 offset:5120
	ds_read_b128 v[26:29], v224 offset:6144
	ds_read_b128 v[198:201], v224 offset:7168
	s_mov_b32 m0, s78
	s_nop 0
	global_load_lds_dwordx4 v52, s[52:53]
	s_and_b64 s[56:57], s[10:11], s[54:55]
	s_mov_b32 m0, s79
	s_nop 0
	global_load_lds_dwordx4 v53, s[52:53]
	s_andn2_b64 vcc, exec, s[56:57]
	s_cbranch_vccnz .LBB0_1135
	ds_read_b128 v[50:53], v6
	s_branch .LBB0_1135

; #define LAS __attribute__((address_space(3)))
; __device__ __forceinline__ unsigned pk4_fp8(float a, float b, float c, float d) { int w = 0; w = __builtin_amdgcn_cvt_pk_fp8_f32(a, b, w, false); w = __builtin_amdgcn_cvt_pk_fp8_f32(c, d, w, true); return (unsigned)w; }
;     ...
;         if constexpr (FP8 >= 1) asm volatile("s_nop 15\n\ts_nop 15" ::: "memory");
;     __device__ __forceinline__ void operator()(const AccT& acc, const pg8::Unit& u, int wr, int wc, int fr, int fq, const LAS float* bl, int nai) const {
;         const int row0 = u.pm * 256 + u.hx * 128 + wr * 64 + fr, a0 = u.pn * 128 + wc * 32 + 8 * fq;
;         unsigned char* act = (unsigned char*)(ws + WS_ACT);
;         const f32x4 bg0 = *(const LAS f32x4*)(bl + 8 * fq), bg1 = *(const LAS f32x4*)(bl + 8 * fq + 4), bu0 = *(const LAS f32x4*)(bl + 32 + 8 * fq), bu1 = *(const LAS f32x4*)(bl + 32 + 8 * fq + 4);
; #pragma unroll
;         for (int ai = 0; ai < 2; ++ai) if (ai < nai)
; #pragma unroll
;             for (int m = 0; m < 4; ++m) { const size_t ro = (size_t)(row0 + ai * 128 + m * 16) * DFF + a0; float o[8];
; #pragma unroll
;                 for (int n = 0; n < 2; ++n) {
;                     f32x4 g4 = acc[ai][0][m][n] + (n ? bg1 : bg0), u4 = acc[ai][1][m][n] + (n ? bu1 : bu0);
; #pragma unroll
;                     for (int j = 0; j < 4; ++j) { g4[j] = fminf(g4[j], 7.0f); u4[j] = __builtin_amdgcn_fmed3f(u4[j], -7.0f, 7.0f); }
;                     const f32x4 t4 = g4 * (-1.702f * 1.4426950408889634f);
;                     f32x4 e4;
; #pragma unroll
;                     for (int j = 0; j < 4; ++j) e4[j] = __builtin_amdgcn_exp2f(t4[j]);
;                     e4 = e4 + 1.0f;
;                     f32x4 r4;
; #pragma unroll
;                     for (int j = 0; j < 4; ++j) r4[j] = __builtin_amdgcn_rcpf(e4[j]);
;                     const f32x4 o4 = (u4 * A8_SCALE + A8_SCALE) * (g4 * r4);
; #pragma unroll
;                     for (int j = 0; j < 4; ++j) o[4 * n + j] = o4[j]; }
;                 u32x2 w; w.x = pk4_fp8(o[0], o[1], o[2], o[3]); w.y = pk4_fp8(o[4], o[5], o[6], o[7]);
;                 *(u32x2*)(act + ro) = w; }
.LBB0_1142:
	s_nop 15
	s_nop 15
	ds_read_b128 v[14:17], v220
	ds_read_b128 v[6:9], v220 offset:16
	ds_read_b128 v[10:13], v220 offset:128
	ds_read_b128 v[2:5], v220 offset:144
	v_lshl_or_b32 v18, s46, 7, v222
	s_waitcnt lgkmcnt(3)
	v_pk_add_f32 v[22:23], v[172:173], v[16:17]
	v_pk_add_f32 v[24:25], v[170:171], v[14:15]
	v_min_f32_e32 v22, 0x40e00000, v22
	v_min_f32_e32 v24, 0x40e00000, v24
	v_min_f32_e32 v25, 0x40e00000, v25
	v_min_f32_e32 v23, 0x40e00000, v23
	v_mul_f32_e32 v21, 0xc01d265f, v24
	v_mul_f32_e32 v31, 0xc01d265f, v22
	v_exp_f32_e32 v30, v21
	v_mul_f32_e32 v21, 0xc01d265f, v25
	v_exp_f32_e32 v32, v31
	v_mul_f32_e32 v31, 0xc01d265f, v23
	v_exp_f32_e32 v33, v31
	v_exp_f32_e32 v31, v21
	s_waitcnt lgkmcnt(1)
	v_pk_add_f32 v[28:29], v[178:179], v[10:11]
	v_pk_add_f32 v[26:27], v[180:181], v[12:13]
	v_med3_f32 v21, v28, s80, v225
	v_pk_add_f32 v[30:31], v[30:31], 1.0 op_sel_hi:[1,0]
	v_med3_f32 v34, v29, s80, v225
	v_rcp_f32_e32 v30, v30
	v_rcp_f32_e32 v31, v31
	v_pk_add_f32 v[28:29], v[32:33], 1.0 op_sel_hi:[1,0]
	v_fma_f32 v21, v21, 4.0, 4.0
	v_rcp_f32_e32 v28, v28
	v_rcp_f32_e32 v29, v29
	v_pk_mul_f32 v[24:25], v[24:25], v[30:31]
	v_med3_f32 v26, v26, s80, v225
	v_mul_f32_e32 v21, v21, v24
	v_fma_f32 v24, v34, 4.0, 4.0
	v_med3_f32 v27, v27, s80, v225
	v_pk_mul_f32 v[22:23], v[22:23], v[28:29]
	v_mul_f32_e32 v34, v24, v25
	v_fma_f32 v24, v26, 4.0, 4.0
	v_mul_f32_e32 v35, v24, v22
	v_fma_f32 v22, v27, 4.0, 4.0
	v_mul_f32_e32 v36, v22, v23
	v_pk_add_f32 v[22:23], v[168:169], v[8:9]
	v_pk_add_f32 v[24:25], v[166:167], v[6:7]
	v_min_f32_e32 v22, 0x40e00000, v22
	v_min_f32_e32 v24, 0x40e00000, v24
	v_min_f32_e32 v25, 0x40e00000, v25
	v_min_f32_e32 v23, 0x40e00000, v23
	v_mul_f32_e32 v30, 0xc01d265f, v24
	v_mul_f32_e32 v31, 0xc01d265f, v25
	v_mul_f32_e32 v32, 0xc01d265f, v22
	v_mul_f32_e32 v33, 0xc01d265f, v23
	v_exp_f32_e32 v30, v30
	v_exp_f32_e32 v32, v32
	v_exp_f32_e32 v33, v33
	v_exp_f32_e32 v31, v31
	s_waitcnt lgkmcnt(0)
	v_pk_add_f32 v[28:29], v[174:175], v[2:3]
	v_pk_add_f32 v[26:27], v[176:177], v[4:5]
	v_med3_f32 v37, v28, s80, v225
	v_med3_f32 v38, v29, s80, v225
	v_pk_add_f32 v[28:29], v[32:33], 1.0 op_sel_hi:[1,0]
	v_pk_add_f32 v[30:31], v[30:31], 1.0 op_sel_hi:[1,0]
	v_rcp_f32_e32 v28, v28
	v_rcp_f32_e32 v30, v30
	v_rcp_f32_e32 v29, v29
	v_rcp_f32_e32 v31, v31
	v_med3_f32 v26, v26, s80, v225
	v_med3_f32 v27, v27, s80, v225
	v_pk_mul_f32 v[22:23], v[22:23], v[28:29]
	v_pk_mul_f32 v[24:25], v[24:25], v[30:31]
	v_fma_f32 v28, v37, 4.0, 4.0
	v_mul_f32_e32 v28, v28, v24
	v_fma_f32 v24, v38, 4.0, 4.0
	v_mul_f32_e32 v29, v24, v25
	v_fma_f32 v24, v26, 4.0, 4.0
	v_mul_f32_e32 v22, v24, v22
	v_mov_b32_e32 v24, 0
	v_mov_b32_e32 v25, 0
	v_cvt_pk_fp8_f32 v24, v21, v34
	v_cvt_pk_fp8_f32 v25, v28, v29
	v_fma_f32 v21, v27, 4.0, 4.0
	v_mul_f32_e32 v21, v21, v23
	v_lshl_add_u32 v20, s84, 8, v219
	v_cvt_pk_fp8_f32 v24, v35, v36 op_sel:[0,0,1]
	v_cvt_pk_fp8_f32 v25, v22, v21 op_sel:[0,0,1]
	v_ashrrev_i32_e32 v19, 31, v18
	v_ashrrev_i32_e32 v21, 31, v20
	v_lshl_add_u64 v[18:19], s[28:29], 0, v[18:19]
	v_lshlrev_b64 v[22:23], 11, v[20:21]
	v_lshl_add_u64 v[22:23], v[18:19], 0, v[22:23]
	v_pk_add_f32 v[26:27], v[154:155], v[14:15]
	global_store_dwordx2 v[22:23], v[24:25], off
	v_pk_add_f32 v[24:25], v[156:157], v[16:17]
	v_min_f32_e32 v26, 0x40e00000, v26
	v_min_f32_e32 v27, 0x40e00000, v27
	v_min_f32_e32 v24, 0x40e00000, v24
	v_mul_f32_e32 v21, 0xc01d265f, v26
	v_min_f32_e32 v25, 0x40e00000, v25
	v_exp_f32_e32 v32, v21
	v_mul_f32_e32 v21, 0xc01d265f, v27
	v_mul_f32_e32 v23, 0xc01d265f, v24
	v_exp_f32_e32 v34, v23
	v_mul_f32_e32 v23, 0xc01d265f, v25
	v_exp_f32_e32 v33, v21
	v_exp_f32_e32 v35, v23
	v_pk_add_f32 v[30:31], v[162:163], v[10:11]
	v_pk_add_f32 v[28:29], v[164:165], v[12:13]
	v_pk_add_f32 v[32:33], v[32:33], 1.0 op_sel_hi:[1,0]
	v_med3_f32 v21, v30, s80, v225
	v_med3_f32 v23, v31, s80, v225
	v_pk_add_f32 v[30:31], v[34:35], 1.0 op_sel_hi:[1,0]
	v_rcp_f32_e32 v32, v32
	v_rcp_f32_e32 v33, v33
	v_rcp_f32_e32 v30, v30
	v_rcp_f32_e32 v31, v31
	v_med3_f32 v28, v28, s80, v225
	v_pk_mul_f32 v[26:27], v[26:27], v[32:33]
	v_fma_f32 v21, v21, 4.0, 4.0
	v_med3_f32 v29, v29, s80, v225
	v_pk_mul_f32 v[24:25], v[24:25], v[30:31]
	v_mul_f32_e32 v21, v21, v26
	v_fma_f32 v26, v28, 4.0, 4.0
	v_fma_f32 v23, v23, 4.0, 4.0
	v_mul_f32_e32 v36, v26, v24
	v_fma_f32 v24, v29, 4.0, 4.0
	v_mul_f32_e32 v23, v23, v27
	v_mul_f32_e32 v37, v24, v25
	v_pk_add_f32 v[24:25], v[152:153], v[8:9]
	v_pk_add_f32 v[26:27], v[150:151], v[6:7]
	v_min_f32_e32 v24, 0x40e00000, v24
	v_min_f32_e32 v26, 0x40e00000, v26
	v_min_f32_e32 v27, 0x40e00000, v27
	v_min_f32_e32 v25, 0x40e00000, v25
	v_mul_f32_e32 v32, 0xc01d265f, v26
	v_mul_f32_e32 v33, 0xc01d265f, v27
	v_mul_f32_e32 v34, 0xc01d265f, v24
	v_mul_f32_e32 v35, 0xc01d265f, v25
	v_exp_f32_e32 v32, v32
	v_exp_f32_e32 v34, v34
	v_exp_f32_e32 v35, v35
	v_exp_f32_e32 v33, v33
	v_pk_add_f32 v[30:31], v[158:159], v[2:3]
	v_pk_add_f32 v[28:29], v[160:161], v[4:5]
	v_med3_f32 v38, v30, s80, v225
	v_med3_f32 v39, v31, s80, v225
	v_pk_add_f32 v[30:31], v[34:35], 1.0 op_sel_hi:[1,0]
	v_pk_add_f32 v[32:33], v[32:33], 1.0 op_sel_hi:[1,0]
	v_rcp_f32_e32 v30, v30
	v_rcp_f32_e32 v32, v32
	v_rcp_f32_e32 v31, v31
	v_rcp_f32_e32 v33, v33
	v_med3_f32 v28, v28, s80, v225
	v_med3_f32 v29, v29, s80, v225
	v_pk_mul_f32 v[24:25], v[24:25], v[30:31]
	v_pk_mul_f32 v[26:27], v[26:27], v[32:33]
	v_fma_f32 v30, v38, 4.0, 4.0
	v_mul_f32_e32 v30, v30, v26
	v_fma_f32 v26, v39, 4.0, 4.0
	v_mul_f32_e32 v31, v26, v27
	v_fma_f32 v26, v28, 4.0, 4.0
	v_mul_f32_e32 v24, v26, v24
	v_mov_b32_e32 v26, 0
	v_mov_b32_e32 v27, 0
	v_cvt_pk_fp8_f32 v26, v21, v23
; __device__ __forceinline__ unsigned pk4_fp8(float a, float b, float c, float d) { int w = 0; w = __builtin_amdgcn_cvt_pk_fp8_f32(a, b, w, false); w = __builtin_amdgcn_cvt_pk_fp8_f32(c, d, w, true); return (unsigned)w; }
;     __device__ __forceinline__ void operator()(const AccT& acc, const pg8::Unit& u, int wr, int wc, int fr, int fq, const LAS float* bl, int nai) const {
;     ...
;             for (int m = 0; m < 4; ++m) { const size_t ro = (size_t)(row0 + ai * 128 + m * 16) * DFF + a0; float o[8];
; #pragma unroll
;                 for (int n = 0; n < 2; ++n) {
;                     f32x4 g4 = acc[ai][0][m][n] + (n ? bg1 : bg0), u4 = acc[ai][1][m][n] + (n ? bu1 : bu0);
; #pragma unroll
;                     for (int j = 0; j < 4; ++j) { g4[j] = fminf(g4[j], 7.0f); u4[j] = __builtin_amdgcn_fmed3f(u4[j], -7.0f, 7.0f); }
;                     const f32x4 t4 = g4 * (-1.702f * 1.4426950408889634f);
;                     f32x4 e4;
; #pragma unroll
;                     for (int j = 0; j < 4; ++j) e4[j] = __builtin_amdgcn_exp2f(t4[j]);
;                     e4 = e4 + 1.0f;
;                     f32x4 r4;
; #pragma unroll
;                     for (int j = 0; j < 4; ++j) r4[j] = __builtin_amdgcn_rcpf(e4[j]);
;                     const f32x4 o4 = (u4 * A8_SCALE + A8_SCALE) * (g4 * r4);
; #pragma unroll
;                     for (int j = 0; j < 4; ++j) o[4 * n + j] = o4[j]; }
;                 u32x2 w; w.x = pk4_fp8(o[0], o[1], o[2], o[3]); w.y = pk4_fp8(o[4], o[5], o[6], o[7]);
;                 *(u32x2*)(act + ro) = w; }
	v_cvt_pk_fp8_f32 v27, v30, v31
	v_fma_f32 v21, v29, 4.0, 4.0
	v_mul_f32_e32 v21, v21, v25
	v_or_b32_e32 v22, 16, v20
	v_cvt_pk_fp8_f32 v26, v36, v37 op_sel:[0,0,1]
	v_cvt_pk_fp8_f32 v27, v24, v21 op_sel:[0,0,1]
	v_ashrrev_i32_e32 v23, 31, v22
	v_lshlrev_b64 v[22:23], 11, v[22:23]
	v_lshl_add_u64 v[22:23], v[18:19], 0, v[22:23]
	global_store_dwordx2 v[22:23], v[26:27], off
	v_pk_add_f32 v[26:27], v[142:143], v[14:15]
	v_pk_add_f32 v[24:25], v[144:145], v[16:17]
	v_min_f32_e32 v26, 0x40e00000, v26
	v_min_f32_e32 v27, 0x40e00000, v27
	v_min_f32_e32 v24, 0x40e00000, v24
	v_mul_f32_e32 v21, 0xc01d265f, v26
	v_min_f32_e32 v25, 0x40e00000, v25
	v_exp_f32_e32 v32, v21
	v_mul_f32_e32 v21, 0xc01d265f, v27
	v_mul_f32_e32 v23, 0xc01d265f, v24
	v_exp_f32_e32 v34, v23
	v_mul_f32_e32 v23, 0xc01d265f, v25
	v_exp_f32_e32 v33, v21
	v_exp_f32_e32 v35, v23
	v_pk_add_f32 v[30:31], v[146:147], v[10:11]
	v_pk_add_f32 v[28:29], v[148:149], v[12:13]
	v_pk_add_f32 v[32:33], v[32:33], 1.0 op_sel_hi:[1,0]
	v_med3_f32 v21, v30, s80, v225
	v_med3_f32 v23, v31, s80, v225
	v_pk_add_f32 v[30:31], v[34:35], 1.0 op_sel_hi:[1,0]
	v_rcp_f32_e32 v32, v32
	v_rcp_f32_e32 v33, v33
	v_rcp_f32_e32 v30, v30
	v_rcp_f32_e32 v31, v31
	v_med3_f32 v28, v28, s80, v225
	v_pk_mul_f32 v[26:27], v[26:27], v[32:33]
	v_fma_f32 v21, v21, 4.0, 4.0
	v_med3_f32 v29, v29, s80, v225
	v_pk_mul_f32 v[24:25], v[24:25], v[30:31]
	v_mul_f32_e32 v21, v21, v26
	v_fma_f32 v26, v28, 4.0, 4.0
	v_fma_f32 v23, v23, 4.0, 4.0
	v_mul_f32_e32 v36, v26, v24
	v_fma_f32 v24, v29, 4.0, 4.0
	v_mul_f32_e32 v23, v23, v27
	v_mul_f32_e32 v37, v24, v25
	v_pk_add_f32 v[24:25], v[136:137], v[8:9]
	v_pk_add_f32 v[26:27], v[134:135], v[6:7]
	v_min_f32_e32 v24, 0x40e00000, v24
	v_min_f32_e32 v26, 0x40e00000, v26
	v_min_f32_e32 v27, 0x40e00000, v27
	v_min_f32_e32 v25, 0x40e00000, v25
	v_mul_f32_e32 v32, 0xc01d265f, v26
	v_mul_f32_e32 v33, 0xc01d265f, v27
	v_mul_f32_e32 v34, 0xc01d265f, v24
	v_mul_f32_e32 v35, 0xc01d265f, v25
	v_exp_f32_e32 v32, v32
	v_exp_f32_e32 v34, v34
	v_exp_f32_e32 v35, v35
	v_exp_f32_e32 v33, v33
	v_pk_add_f32 v[30:31], v[138:139], v[2:3]
	v_pk_add_f32 v[28:29], v[140:141], v[4:5]
	v_med3_f32 v38, v30, s80, v225
	v_med3_f32 v39, v31, s80, v225
	v_pk_add_f32 v[30:31], v[34:35], 1.0 op_sel_hi:[1,0]
	v_pk_add_f32 v[32:33], v[32:33], 1.0 op_sel_hi:[1,0]
	v_rcp_f32_e32 v30, v30
	v_rcp_f32_e32 v32, v32
	v_rcp_f32_e32 v31, v31
	v_rcp_f32_e32 v33, v33
	v_med3_f32 v28, v28, s80, v225
	v_med3_f32 v29, v29, s80, v225
	v_pk_mul_f32 v[24:25], v[24:25], v[30:31]
	v_pk_mul_f32 v[26:27], v[26:27], v[32:33]
	v_fma_f32 v30, v38, 4.0, 4.0
	v_mul_f32_e32 v30, v30, v26
	v_fma_f32 v26, v39, 4.0, 4.0
	v_mul_f32_e32 v31, v26, v27
	v_fma_f32 v26, v28, 4.0, 4.0
	v_mul_f32_e32 v24, v26, v24
	v_mov_b32_e32 v26, 0
	v_mov_b32_e32 v27, 0
	v_cvt_pk_fp8_f32 v26, v21, v23
	v_cvt_pk_fp8_f32 v27, v30, v31
	v_fma_f32 v21, v29, 4.0, 4.0
	v_mul_f32_e32 v21, v21, v25
	v_or_b32_e32 v22, 32, v20
	v_cvt_pk_fp8_f32 v26, v36, v37 op_sel:[0,0,1]
	v_cvt_pk_fp8_f32 v27, v24, v21 op_sel:[0,0,1]
	v_ashrrev_i32_e32 v23, 31, v22
	v_lshlrev_b64 v[22:23], 11, v[22:23]
	v_lshl_add_u64 v[22:23], v[18:19], 0, v[22:23]
	global_store_dwordx2 v[22:23], v[26:27], off
	v_pk_add_f32 v[26:27], v[118:119], v[14:15]
	v_pk_add_f32 v[24:25], v[120:121], v[16:17]
	v_min_f32_e32 v26, 0x40e00000, v26
	v_min_f32_e32 v27, 0x40e00000, v27
	v_min_f32_e32 v24, 0x40e00000, v24
	v_mul_f32_e32 v21, 0xc01d265f, v26
	v_min_f32_e32 v25, 0x40e00000, v25
	v_exp_f32_e32 v32, v21
	v_mul_f32_e32 v21, 0xc01d265f, v27
	v_mul_f32_e32 v23, 0xc01d265f, v24
	v_exp_f32_e32 v34, v23
	v_mul_f32_e32 v23, 0xc01d265f, v25
	v_exp_f32_e32 v33, v21
	v_exp_f32_e32 v35, v23
	v_pk_add_f32 v[30:31], v[126:127], v[10:11]
	v_pk_add_f32 v[28:29], v[128:129], v[12:13]
	v_pk_add_f32 v[32:33], v[32:33], 1.0 op_sel_hi:[1,0]
	v_med3_f32 v21, v30, s80, v225
	v_med3_f32 v23, v31, s80, v225
	v_pk_add_f32 v[30:31], v[34:35], 1.0 op_sel_hi:[1,0]
	v_rcp_f32_e32 v32, v32
	v_rcp_f32_e32 v33, v33
	v_rcp_f32_e32 v30, v30
	v_rcp_f32_e32 v31, v31
	v_med3_f32 v28, v28, s80, v225
	v_pk_mul_f32 v[26:27], v[26:27], v[32:33]
	v_fma_f32 v21, v21, 4.0, 4.0
	v_med3_f32 v29, v29, s80, v225
	v_pk_mul_f32 v[24:25], v[24:25], v[30:31]
	v_mul_f32_e32 v21, v21, v26
	v_fma_f32 v26, v28, 4.0, 4.0
	v_fma_f32 v23, v23, 4.0, 4.0
	v_mul_f32_e32 v36, v26, v24
	v_fma_f32 v24, v29, 4.0, 4.0
	v_mul_f32_e32 v23, v23, v27
	v_mul_f32_e32 v37, v24, v25
	v_pk_add_f32 v[24:25], v[112:113], v[8:9]
	v_pk_add_f32 v[26:27], v[110:111], v[6:7]
	v_min_f32_e32 v24, 0x40e00000, v24
	v_min_f32_e32 v26, 0x40e00000, v26
	v_min_f32_e32 v27, 0x40e00000, v27
	v_min_f32_e32 v25, 0x40e00000, v25
	v_mul_f32_e32 v32, 0xc01d265f, v26
	v_mul_f32_e32 v33, 0xc01d265f, v27
	v_mul_f32_e32 v34, 0xc01d265f, v24
	v_mul_f32_e32 v35, 0xc01d265f, v25
	v_exp_f32_e32 v32, v32
	v_exp_f32_e32 v34, v34
	v_exp_f32_e32 v35, v35
	v_exp_f32_e32 v33, v33
	v_pk_add_f32 v[30:31], v[98:99], v[2:3]
	v_pk_add_f32 v[28:29], v[100:101], v[4:5]
	v_med3_f32 v38, v30, s80, v225
	v_med3_f32 v39, v31, s80, v225
	v_pk_add_f32 v[30:31], v[34:35], 1.0 op_sel_hi:[1,0]
	v_pk_add_f32 v[32:33], v[32:33], 1.0 op_sel_hi:[1,0]
	v_rcp_f32_e32 v30, v30
	v_rcp_f32_e32 v32, v32
	v_rcp_f32_e32 v31, v31
	v_rcp_f32_e32 v33, v33
	v_med3_f32 v28, v28, s80, v225
	v_med3_f32 v29, v29, s80, v225
	v_pk_mul_f32 v[24:25], v[24:25], v[30:31]
	v_pk_mul_f32 v[26:27], v[26:27], v[32:33]
	v_fma_f32 v30, v38, 4.0, 4.0
	v_mul_f32_e32 v30, v30, v26
	v_fma_f32 v26, v39, 4.0, 4.0
	v_mul_f32_e32 v31, v26, v27
	v_fma_f32 v26, v28, 4.0, 4.0
	v_mul_f32_e32 v24, v26, v24
	v_mov_b32_e32 v26, 0
	v_mov_b32_e32 v27, 0
	v_cvt_pk_fp8_f32 v26, v21, v23
; __device__ __forceinline__ unsigned pk4_fp8(float a, float b, float c, float d) { int w = 0; w = __builtin_amdgcn_cvt_pk_fp8_f32(a, b, w, false); w = __builtin_amdgcn_cvt_pk_fp8_f32(c, d, w, true); return (unsigned)w; }
;     __device__ __forceinline__ void operator()(const AccT& acc, const pg8::Unit& u, int wr, int wc, int fr, int fq, const LAS float* bl, int nai) const {
;     ...
;             for (int m = 0; m < 4; ++m) { const size_t ro = (size_t)(row0 + ai * 128 + m * 16) * DFF + a0; float o[8];
; #pragma unroll
;                 for (int n = 0; n < 2; ++n) {
;                     f32x4 g4 = acc[ai][0][m][n] + (n ? bg1 : bg0), u4 = acc[ai][1][m][n] + (n ? bu1 : bu0);
; #pragma unroll
;                     for (int j = 0; j < 4; ++j) { g4[j] = fminf(g4[j], 7.0f); u4[j] = __builtin_amdgcn_fmed3f(u4[j], -7.0f, 7.0f); }
;                     const f32x4 t4 = g4 * (-1.702f * 1.4426950408889634f);
;                     f32x4 e4;
; #pragma unroll
;                     for (int j = 0; j < 4; ++j) e4[j] = __builtin_amdgcn_exp2f(t4[j]);
;                     e4 = e4 + 1.0f;
;                     f32x4 r4;
; #pragma unroll
;                     for (int j = 0; j < 4; ++j) r4[j] = __builtin_amdgcn_rcpf(e4[j]);
;                     const f32x4 o4 = (u4 * A8_SCALE + A8_SCALE) * (g4 * r4);
; #pragma unroll
;                     for (int j = 0; j < 4; ++j) o[4 * n + j] = o4[j]; }
;                 u32x2 w; w.x = pk4_fp8(o[0], o[1], o[2], o[3]); w.y = pk4_fp8(o[4], o[5], o[6], o[7]);
;                 *(u32x2*)(act + ro) = w; }
	v_cvt_pk_fp8_f32 v27, v30, v31
	v_fma_f32 v21, v29, 4.0, 4.0
	v_mul_f32_e32 v21, v21, v25
	v_or_b32_e32 v22, 48, v20
	v_cvt_pk_fp8_f32 v26, v36, v37 op_sel:[0,0,1]
	v_cvt_pk_fp8_f32 v27, v24, v21 op_sel:[0,0,1]
	v_ashrrev_i32_e32 v23, 31, v22
	v_lshlrev_b64 v[22:23], 11, v[22:23]
	v_lshl_add_u64 v[22:23], v[18:19], 0, v[22:23]
	global_store_dwordx2 v[22:23], v[26:27], off
	v_pk_add_f32 v[26:27], v[114:115], v[14:15]
	v_pk_add_f32 v[24:25], v[116:117], v[16:17]
	v_min_f32_e32 v26, 0x40e00000, v26
	v_min_f32_e32 v27, 0x40e00000, v27
	v_min_f32_e32 v24, 0x40e00000, v24
	v_mul_f32_e32 v21, 0xc01d265f, v26
	v_min_f32_e32 v25, 0x40e00000, v25
	v_exp_f32_e32 v32, v21
	v_mul_f32_e32 v21, 0xc01d265f, v27
	v_mul_f32_e32 v23, 0xc01d265f, v24
	v_exp_f32_e32 v34, v23
	v_mul_f32_e32 v23, 0xc01d265f, v25
	v_exp_f32_e32 v33, v21
	v_exp_f32_e32 v35, v23
	v_pk_add_f32 v[30:31], v[130:131], v[10:11]
	v_pk_add_f32 v[28:29], v[132:133], v[12:13]
	v_pk_add_f32 v[32:33], v[32:33], 1.0 op_sel_hi:[1,0]
	v_med3_f32 v21, v30, s80, v225
	v_med3_f32 v23, v31, s80, v225
	v_pk_add_f32 v[30:31], v[34:35], 1.0 op_sel_hi:[1,0]
	v_rcp_f32_e32 v32, v32
	v_rcp_f32_e32 v33, v33
	v_rcp_f32_e32 v30, v30
	v_rcp_f32_e32 v31, v31
	v_med3_f32 v28, v28, s80, v225
	v_pk_mul_f32 v[26:27], v[26:27], v[32:33]
	v_fma_f32 v21, v21, 4.0, 4.0
	v_med3_f32 v29, v29, s80, v225
	v_pk_mul_f32 v[24:25], v[24:25], v[30:31]
	v_mul_f32_e32 v21, v21, v26
	v_fma_f32 v26, v28, 4.0, 4.0
	v_fma_f32 v23, v23, 4.0, 4.0
	v_mul_f32_e32 v36, v26, v24
	v_fma_f32 v24, v29, 4.0, 4.0
	v_mul_f32_e32 v23, v23, v27
	v_mul_f32_e32 v37, v24, v25
	v_pk_add_f32 v[24:25], v[108:109], v[8:9]
	v_pk_add_f32 v[26:27], v[106:107], v[6:7]
	v_min_f32_e32 v24, 0x40e00000, v24
	v_min_f32_e32 v26, 0x40e00000, v26
	v_min_f32_e32 v27, 0x40e00000, v27
	v_min_f32_e32 v25, 0x40e00000, v25
	v_mul_f32_e32 v32, 0xc01d265f, v26
	v_mul_f32_e32 v33, 0xc01d265f, v27
	v_mul_f32_e32 v34, 0xc01d265f, v24
	v_mul_f32_e32 v35, 0xc01d265f, v25
	v_exp_f32_e32 v32, v32
	v_exp_f32_e32 v34, v34
	v_exp_f32_e32 v35, v35
	v_exp_f32_e32 v33, v33
	v_pk_add_f32 v[30:31], v[122:123], v[2:3]
	v_pk_add_f32 v[28:29], v[124:125], v[4:5]
	v_med3_f32 v38, v30, s80, v225
	v_med3_f32 v39, v31, s80, v225
	v_pk_add_f32 v[30:31], v[34:35], 1.0 op_sel_hi:[1,0]
	v_pk_add_f32 v[32:33], v[32:33], 1.0 op_sel_hi:[1,0]
	v_rcp_f32_e32 v30, v30
	v_rcp_f32_e32 v32, v32
	v_rcp_f32_e32 v31, v31
	v_rcp_f32_e32 v33, v33
	v_med3_f32 v28, v28, s80, v225
	v_med3_f32 v29, v29, s80, v225
	v_pk_mul_f32 v[24:25], v[24:25], v[30:31]
	v_pk_mul_f32 v[26:27], v[26:27], v[32:33]
	v_fma_f32 v30, v38, 4.0, 4.0
	v_mul_f32_e32 v30, v30, v26
	v_fma_f32 v26, v39, 4.0, 4.0
	v_mul_f32_e32 v31, v26, v27
	v_fma_f32 v26, v28, 4.0, 4.0
	v_mul_f32_e32 v24, v26, v24
	v_mov_b32_e32 v26, 0
	v_mov_b32_e32 v27, 0
	v_cvt_pk_fp8_f32 v26, v21, v23
	v_cvt_pk_fp8_f32 v27, v30, v31
	v_fma_f32 v21, v29, 4.0, 4.0
	v_mul_f32_e32 v21, v21, v25
	v_add_u32_e32 v22, 0x80, v20
	v_cvt_pk_fp8_f32 v26, v36, v37 op_sel:[0,0,1]
	v_cvt_pk_fp8_f32 v27, v24, v21 op_sel:[0,0,1]
	v_ashrrev_i32_e32 v23, 31, v22
	v_lshlrev_b64 v[22:23], 11, v[22:23]
	v_lshl_add_u64 v[22:23], v[18:19], 0, v[22:23]
	global_store_dwordx2 v[22:23], v[26:27], off
	v_pk_add_f32 v[26:27], v[94:95], v[14:15]
	v_pk_add_f32 v[24:25], v[96:97], v[16:17]
	v_min_f32_e32 v26, 0x40e00000, v26
	v_min_f32_e32 v27, 0x40e00000, v27
	v_min_f32_e32 v24, 0x40e00000, v24
	v_mul_f32_e32 v21, 0xc01d265f, v26
	v_min_f32_e32 v25, 0x40e00000, v25
	v_exp_f32_e32 v32, v21
	v_mul_f32_e32 v21, 0xc01d265f, v27
	v_mul_f32_e32 v23, 0xc01d265f, v24
	v_exp_f32_e32 v34, v23
	v_mul_f32_e32 v23, 0xc01d265f, v25
	v_exp_f32_e32 v33, v21
	v_exp_f32_e32 v35, v23
	v_pk_add_f32 v[30:31], v[102:103], v[10:11]
	v_pk_add_f32 v[28:29], v[104:105], v[12:13]
	v_pk_add_f32 v[32:33], v[32:33], 1.0 op_sel_hi:[1,0]
	v_med3_f32 v21, v30, s80, v225
	v_med3_f32 v23, v31, s80, v225
	v_pk_add_f32 v[30:31], v[34:35], 1.0 op_sel_hi:[1,0]
	v_rcp_f32_e32 v32, v32
	v_rcp_f32_e32 v33, v33
	v_rcp_f32_e32 v30, v30
	v_rcp_f32_e32 v31, v31
	v_med3_f32 v28, v28, s80, v225
	v_pk_mul_f32 v[26:27], v[26:27], v[32:33]
	v_fma_f32 v21, v21, 4.0, 4.0
	v_med3_f32 v29, v29, s80, v225
	v_pk_mul_f32 v[24:25], v[24:25], v[30:31]
	v_mul_f32_e32 v21, v21, v26
	v_fma_f32 v26, v28, 4.0, 4.0
	v_fma_f32 v23, v23, 4.0, 4.0
	v_mul_f32_e32 v36, v26, v24
	v_fma_f32 v24, v29, 4.0, 4.0
	v_mul_f32_e32 v23, v23, v27
	v_mul_f32_e32 v37, v24, v25
	v_pk_add_f32 v[24:25], v[88:89], v[8:9]
	v_pk_add_f32 v[26:27], v[86:87], v[6:7]
	v_min_f32_e32 v24, 0x40e00000, v24
	v_min_f32_e32 v26, 0x40e00000, v26
	v_min_f32_e32 v27, 0x40e00000, v27
	v_min_f32_e32 v25, 0x40e00000, v25
	v_mul_f32_e32 v32, 0xc01d265f, v26
	v_mul_f32_e32 v33, 0xc01d265f, v27
	v_mul_f32_e32 v34, 0xc01d265f, v24
	v_mul_f32_e32 v35, 0xc01d265f, v25
	v_exp_f32_e32 v32, v32
	v_exp_f32_e32 v34, v34
	v_exp_f32_e32 v35, v35
	v_exp_f32_e32 v33, v33
	v_pk_add_f32 v[30:31], v[90:91], v[2:3]
	v_pk_add_f32 v[28:29], v[92:93], v[4:5]
	v_med3_f32 v38, v30, s80, v225
	v_med3_f32 v39, v31, s80, v225
	v_pk_add_f32 v[30:31], v[34:35], 1.0 op_sel_hi:[1,0]
	v_pk_add_f32 v[32:33], v[32:33], 1.0 op_sel_hi:[1,0]
	v_rcp_f32_e32 v30, v30
	v_rcp_f32_e32 v32, v32
	v_rcp_f32_e32 v31, v31
	v_rcp_f32_e32 v33, v33
	v_med3_f32 v28, v28, s80, v225
	v_med3_f32 v29, v29, s80, v225
	v_pk_mul_f32 v[24:25], v[24:25], v[30:31]
	v_pk_mul_f32 v[26:27], v[26:27], v[32:33]
	v_fma_f32 v30, v38, 4.0, 4.0
	v_mul_f32_e32 v30, v30, v26
	v_fma_f32 v26, v39, 4.0, 4.0
	v_mul_f32_e32 v31, v26, v27
	v_fma_f32 v26, v28, 4.0, 4.0
	v_mul_f32_e32 v24, v26, v24
	v_mov_b32_e32 v26, 0
	v_mov_b32_e32 v27, 0
	v_cvt_pk_fp8_f32 v26, v21, v23
; __device__ __forceinline__ unsigned pk4_fp8(float a, float b, float c, float d) { int w = 0; w = __builtin_amdgcn_cvt_pk_fp8_f32(a, b, w, false); w = __builtin_amdgcn_cvt_pk_fp8_f32(c, d, w, true); return (unsigned)w; }
;     __device__ __forceinline__ const char* bias_base(const pg8::Unit& u) const { return (const char*)(bgu + (size_t)u.e * 4096 + u.pn * 128); }
;     __device__ __forceinline__ unsigned bias_off(const pg8::Unit&, int wc, int lane) const { return (unsigned)(((lane >> 3) & 1) * 2048 + wc * 32 + (lane & 7) * 4) * 4u; }
;     ...
;         if (!has_next) break;
;         if constexpr (RSYNC) xcd_barrier(*rbar);
; #pragma unroll
;         for (int a = 0; a < 2; ++a)
; #pragma unroll
;             for (int b = 0; b < 2; ++b)
; #pragma unroll
;                 for (int m = 0; m < 4; ++m)
; #pragma unroll
;                     for (int n = 0; n < 2; ++n) acc[a][b][m][n] = (f32x4){0.f, 0.f, 0.f, 0.f};
;         cur = nxt; cA = nA; cB = nB; ++ui;
;         if constexpr (Epi::kBiasDMA) { if (lane < 16) glds16(E.bias_base(cur), E.bias_off(cur, wc, lane), bias_lds); }
;     __device__ __forceinline__ void operator()(const AccT& acc, const pg8::Unit& u, int wr, int wc, int fr, int fq, const LAS float* bl, int nai) const {
;     ...
;             for (int m = 0; m < 4; ++m) { const size_t ro = (size_t)(row0 + ai * 128 + m * 16) * DFF + a0; float o[8];
; #pragma unroll
;                 for (int n = 0; n < 2; ++n) {
;                     f32x4 g4 = acc[ai][0][m][n] + (n ? bg1 : bg0), u4 = acc[ai][1][m][n] + (n ? bu1 : bu0);
; #pragma unroll
;                     for (int j = 0; j < 4; ++j) { g4[j] = fminf(g4[j], 7.0f); u4[j] = __builtin_amdgcn_fmed3f(u4[j], -7.0f, 7.0f); }
;                     const f32x4 t4 = g4 * (-1.702f * 1.4426950408889634f);
;                     f32x4 e4;
; #pragma unroll
;                     for (int j = 0; j < 4; ++j) e4[j] = __builtin_amdgcn_exp2f(t4[j]);
;                     e4 = e4 + 1.0f;
;                     f32x4 r4;
; #pragma unroll
;                     for (int j = 0; j < 4; ++j) r4[j] = __builtin_amdgcn_rcpf(e4[j]);
;                     const f32x4 o4 = (u4 * A8_SCALE + A8_SCALE) * (g4 * r4);
; #pragma unroll
;                     for (int j = 0; j < 4; ++j) o[4 * n + j] = o4[j]; }
;                 u32x2 w; w.x = pk4_fp8(o[0], o[1], o[2], o[3]); w.y = pk4_fp8(o[4], o[5], o[6], o[7]);
;                 *(u32x2*)(act + ro) = w; }
	v_cvt_pk_fp8_f32 v27, v30, v31
	v_fma_f32 v21, v29, 4.0, 4.0
	v_mul_f32_e32 v21, v21, v25
	v_add_u32_e32 v22, 0x90, v20
	v_cvt_pk_fp8_f32 v26, v36, v37 op_sel:[0,0,1]
	v_cvt_pk_fp8_f32 v27, v24, v21 op_sel:[0,0,1]
	v_ashrrev_i32_e32 v23, 31, v22
	v_lshlrev_b64 v[22:23], 11, v[22:23]
	v_lshl_add_u64 v[22:23], v[18:19], 0, v[22:23]
	global_store_dwordx2 v[22:23], v[26:27], off
	v_pk_add_f32 v[26:27], v[78:79], v[14:15]
	v_pk_add_f32 v[24:25], v[80:81], v[16:17]
	v_min_f32_e32 v26, 0x40e00000, v26
	v_min_f32_e32 v27, 0x40e00000, v27
	v_min_f32_e32 v24, 0x40e00000, v24
	v_mul_f32_e32 v21, 0xc01d265f, v26
	v_min_f32_e32 v25, 0x40e00000, v25
	v_exp_f32_e32 v32, v21
	v_mul_f32_e32 v21, 0xc01d265f, v27
	v_mul_f32_e32 v23, 0xc01d265f, v24
	v_exp_f32_e32 v34, v23
	v_mul_f32_e32 v23, 0xc01d265f, v25
	v_exp_f32_e32 v33, v21
	v_exp_f32_e32 v35, v23
	v_pk_add_f32 v[30:31], v[82:83], v[10:11]
	v_pk_add_f32 v[28:29], v[84:85], v[12:13]
	v_pk_add_f32 v[32:33], v[32:33], 1.0 op_sel_hi:[1,0]
	v_med3_f32 v21, v30, s80, v225
	v_med3_f32 v23, v31, s80, v225
	v_pk_add_f32 v[30:31], v[34:35], 1.0 op_sel_hi:[1,0]
	v_rcp_f32_e32 v32, v32
	v_rcp_f32_e32 v33, v33
	v_rcp_f32_e32 v30, v30
	v_rcp_f32_e32 v31, v31
	v_med3_f32 v28, v28, s80, v225
	v_pk_mul_f32 v[26:27], v[26:27], v[32:33]
	v_fma_f32 v21, v21, 4.0, 4.0
	v_med3_f32 v29, v29, s80, v225
	v_pk_mul_f32 v[24:25], v[24:25], v[30:31]
	v_mul_f32_e32 v21, v21, v26
	v_fma_f32 v26, v28, 4.0, 4.0
	v_fma_f32 v23, v23, 4.0, 4.0
	v_mul_f32_e32 v36, v26, v24
	v_fma_f32 v24, v29, 4.0, 4.0
	v_mul_f32_e32 v23, v23, v27
	v_mul_f32_e32 v37, v24, v25
	v_pk_add_f32 v[24:25], v[72:73], v[8:9]
	v_pk_add_f32 v[26:27], v[70:71], v[6:7]
	v_min_f32_e32 v24, 0x40e00000, v24
	v_min_f32_e32 v26, 0x40e00000, v26
	v_min_f32_e32 v27, 0x40e00000, v27
	v_min_f32_e32 v25, 0x40e00000, v25
	v_mul_f32_e32 v32, 0xc01d265f, v26
	v_mul_f32_e32 v33, 0xc01d265f, v27
	v_mul_f32_e32 v34, 0xc01d265f, v24
	v_mul_f32_e32 v35, 0xc01d265f, v25
	v_exp_f32_e32 v32, v32
	v_exp_f32_e32 v34, v34
	v_exp_f32_e32 v35, v35
	v_exp_f32_e32 v33, v33
	v_pk_add_f32 v[30:31], v[74:75], v[2:3]
	v_pk_add_f32 v[28:29], v[76:77], v[4:5]
	v_med3_f32 v38, v30, s80, v225
	v_med3_f32 v39, v31, s80, v225
	v_pk_add_f32 v[30:31], v[34:35], 1.0 op_sel_hi:[1,0]
	v_pk_add_f32 v[32:33], v[32:33], 1.0 op_sel_hi:[1,0]
	v_rcp_f32_e32 v30, v30
	v_rcp_f32_e32 v32, v32
	v_rcp_f32_e32 v31, v31
	v_rcp_f32_e32 v33, v33
	v_med3_f32 v28, v28, s80, v225
	v_med3_f32 v29, v29, s80, v225
	v_pk_mul_f32 v[24:25], v[24:25], v[30:31]
	v_pk_mul_f32 v[26:27], v[26:27], v[32:33]
	v_fma_f32 v30, v38, 4.0, 4.0
	v_mul_f32_e32 v30, v30, v26
	v_fma_f32 v26, v39, 4.0, 4.0
	v_mul_f32_e32 v31, v26, v27
	v_fma_f32 v26, v28, 4.0, 4.0
	v_mul_f32_e32 v24, v26, v24
	v_mov_b32_e32 v26, 0
	v_mov_b32_e32 v27, 0
	v_cvt_pk_fp8_f32 v26, v21, v23
	v_cvt_pk_fp8_f32 v27, v30, v31
	v_fma_f32 v21, v29, 4.0, 4.0
	v_mul_f32_e32 v21, v21, v25
	v_add_u32_e32 v22, 0xa0, v20
	v_cvt_pk_fp8_f32 v26, v36, v37 op_sel:[0,0,1]
	v_cvt_pk_fp8_f32 v27, v24, v21 op_sel:[0,0,1]
	v_ashrrev_i32_e32 v23, 31, v22
	v_lshlrev_b64 v[22:23], 11, v[22:23]
	v_pk_add_f32 v[16:17], v[64:65], v[16:17]
	v_pk_add_f32 v[14:15], v[62:63], v[14:15]
	v_lshl_add_u64 v[22:23], v[18:19], 0, v[22:23]
	v_min_f32_e32 v14, 0x40e00000, v14
	v_min_f32_e32 v16, 0x40e00000, v16
	global_store_dwordx2 v[22:23], v[26:27], off
	v_min_f32_e32 v15, 0x40e00000, v15
	v_min_f32_e32 v17, 0x40e00000, v17
	v_mul_f32_e32 v21, 0xc01d265f, v14
	v_mul_f32_e32 v23, 0xc01d265f, v16
	v_exp_f32_e32 v22, v21
	v_mul_f32_e32 v21, 0xc01d265f, v15
	v_exp_f32_e32 v24, v23
	v_mul_f32_e32 v23, 0xc01d265f, v17
	v_exp_f32_e32 v25, v23
	v_exp_f32_e32 v23, v21
	v_pk_add_f32 v[10:11], v[66:67], v[10:11]
	v_pk_add_f32 v[12:13], v[68:69], v[12:13]
	v_med3_f32 v21, v10, s80, v225
	v_pk_add_f32 v[22:23], v[22:23], 1.0 op_sel_hi:[1,0]
	v_med3_f32 v26, v11, s80, v225
	v_rcp_f32_e32 v22, v22
	v_rcp_f32_e32 v23, v23
	v_pk_add_f32 v[10:11], v[24:25], 1.0 op_sel_hi:[1,0]
	v_med3_f32 v24, v12, s80, v225
	v_rcp_f32_e32 v10, v10
	v_rcp_f32_e32 v11, v11
	v_med3_f32 v25, v13, s80, v225
	v_pk_mul_f32 v[12:13], v[14:15], v[22:23]
	v_fma_f32 v14, v21, 4.0, 4.0
	v_mul_f32_e32 v14, v14, v12
	v_fma_f32 v12, v26, 4.0, 4.0
	v_pk_mul_f32 v[10:11], v[16:17], v[10:11]
	v_mul_f32_e32 v15, v12, v13
	v_fma_f32 v12, v24, 4.0, 4.0
	v_pk_add_f32 v[6:7], v[58:59], v[6:7]
	v_mul_f32_e32 v16, v12, v10
	v_fma_f32 v10, v25, 4.0, 4.0
	v_min_f32_e32 v6, 0x40e00000, v6
	v_min_f32_e32 v7, 0x40e00000, v7
	v_mul_f32_e32 v17, v10, v11
	v_pk_add_f32 v[8:9], v[60:61], v[8:9]
	v_mul_f32_e32 v10, 0xc01d265f, v6
	v_mul_f32_e32 v11, 0xc01d265f, v7
	v_min_f32_e32 v8, 0x40e00000, v8
	v_min_f32_e32 v9, 0x40e00000, v9
	v_exp_f32_e32 v10, v10
	v_exp_f32_e32 v11, v11
	v_mul_f32_e32 v12, 0xc01d265f, v8
	v_mul_f32_e32 v13, 0xc01d265f, v9
	v_exp_f32_e32 v12, v12
	v_exp_f32_e32 v13, v13
	v_pk_add_f32 v[10:11], v[10:11], 1.0 op_sel_hi:[1,0]
	v_pk_add_f32 v[2:3], v[54:55], v[2:3]
	v_rcp_f32_e32 v10, v10
	v_rcp_f32_e32 v11, v11
	v_med3_f32 v21, v2, s80, v225
	v_med3_f32 v22, v3, s80, v225
	v_pk_add_f32 v[2:3], v[12:13], 1.0 op_sel_hi:[1,0]
	v_pk_add_f32 v[4:5], v[56:57], v[4:5]
	v_rcp_f32_e32 v2, v2
	v_rcp_f32_e32 v3, v3
	v_med3_f32 v12, v4, s80, v225
	v_med3_f32 v13, v5, s80, v225
	v_pk_mul_f32 v[4:5], v[6:7], v[10:11]
	v_fma_f32 v6, v21, 4.0, 4.0
	v_mul_f32_e32 v6, v6, v4
	v_fma_f32 v4, v22, 4.0, 4.0
	v_pk_mul_f32 v[2:3], v[8:9], v[2:3]
	v_mul_f32_e32 v7, v4, v5
	v_fma_f32 v4, v12, 4.0, 4.0
	v_mul_f32_e32 v2, v4, v2
	v_mov_b32_e32 v4, 0
	v_mov_b32_e32 v5, 0
	v_cvt_pk_fp8_f32 v4, v14, v15
	v_cvt_pk_fp8_f32 v5, v6, v7
	v_fma_f32 v6, v13, 4.0, 4.0
	v_mul_f32_e32 v3, v6, v3
	v_add_u32_e32 v20, 0xb0, v20
	v_cvt_pk_fp8_f32 v4, v16, v17 op_sel:[0,0,1]
	v_cvt_pk_fp8_f32 v5, v2, v3 op_sel:[0,0,1]
	v_ashrrev_i32_e32 v21, 31, v20
	v_lshlrev_b64 v[2:3], 11, v[20:21]
	v_lshl_add_u64 v[2:3], v[18:19], 0, v[2:3]
	s_and_b64 vcc, exec, s[8:9]
	s_mov_b64 s[8:9], -1
	global_store_dwordx2 v[2:3], v[4:5], off
	s_cbranch_vccnz .LBB0_1117
	s_and_saveexec_b64 s[8:9], s[6:7]
	s_cbranch_execz .LBB0_1145
	s_ashr_i32 s41, s40, 31
	s_lshl_b64 s[10:11], s[40:41], 14
	s_add_u32 s16, s22, s10
	s_addc_u32 s17, s23, s11
	s_lshl_b32 s10, s42, 7
	s_ashr_i32 s11, s10, 31
	s_lshl_b64 s[10:11], s[10:11], 2
	s_add_u32 s10, s16, s10
	s_addc_u32 s11, s17, s11
	s_mov_b32 m0, s65
	s_nop 0
	global_load_lds_dwordx4 v221, s[10:11]

;     __device__ __forceinline__ const char* bias_base(const pg8::Unit& u) const { return (const char*)(bgu + (size_t)u.e * 4096 + u.pn * 128); }
;     __device__ __forceinline__ unsigned bias_off(const pg8::Unit&, int wc, int lane) const { return (unsigned)(((lane >> 3) & 1) * 2048 + wc * 32 + (lane & 7) * 4) * 4u; }
;     __device__ __forceinline__ const char* bias_base(const pg8::Unit& u) const { return (const char*)(bdn + (size_t)u.e * D + u.pn * 256); }
;     __device__ __forceinline__ unsigned bias_off(const pg8::Unit&, int wc, int lane) const { return (unsigned)(wc * 64 + lane * 4) * 4u; }
;     __device__ __forceinline__ void a_offs(const Unit& u, const int (&R)[2], const int (&C)[2], unsigned (&off)[2][2]) const {
;         if constexpr (GATHER) {
;             const int ce = __builtin_amdgcn_readfirstlane(cnt[u.e]);
; #pragma unroll
;             for (int h = 0; h < 2; ++h)
; #pragma unroll
;                 for (int i = 0; i < 2; ++i) { const int g = u.mt * BM + u.hx * HALF + h * HALF + R[i]; const int tok = rowtok[u.e * T + (g < ce ? g : 0)] >> 2; off[h][i] = (unsigned)(tok * lda + C[i]) * 2u; }
;     ...
;     const unsigned bias_lds = (unsigned)__builtin_amdgcn_readfirstlane((int)((unsigned)(size_t)lds + (unsigned)(AUX_OFF + 8192) + (unsigned)wid * 256u));
;     if constexpr (Epi::kBiasDMA) { if (lane < 16) glds16(E.bias_base(cur), E.bias_off(cur, wc, lane), bias_lds); }
.LBB0_1158:
	s_andn2_b64 vcc, exec, s[6:7]
	s_cbranch_vccnz .LBB0_1200
	v_mov_b32_e32 v3, v0
	s_lshl_b32 s6, s16, 2
	v_ashrrev_i32_e32 v1, 31, v3
	v_lshrrev_b32_e32 v1, 26, v1
	v_lshlrev_b32_e32 v4, 4, v3
	v_add_u32_e32 v1, v3, v1
	v_bfe_i32 v3, v3, 27, 1
	v_lshrrev_b32_e32 v3, 22, v3
	v_add_u32_e32 v3, v4, v3
	v_and_b32_e32 v3, 0xfffffc00, v3
	v_sub_u32_e32 v3, v4, v3
	v_add_u32_e32 v4, 0x2000, v4
	s_waitcnt vmcnt(1)
	v_ashrrev_i32_e32 v7, 31, v4
	v_lshrrev_b32_e32 v7, 22, v7
	s_add_i32 s6, s6, 0
	v_add_u32_e32 v7, v4, v7
	s_add_i32 s6, s6, 0x23100
	v_lshrrev_b32_e32 v5, 4, v3
	v_ashrrev_i32_e32 v7, 10, v7
	v_mov_b32_e32 v9, s6
	v_bitop3_b32 v5, v5, v3, 32 bitop3:0x6c
	v_mul_i32_i24_e32 v8, 0x400, v7
	ds_read_b32 v10, v9
	v_ashrrev_i32_e32 v6, 31, v5
	v_sub_u32_e32 v4, v4, v8
	v_ashrrev_i32_e32 v1, 6, v1
	v_lshrrev_b32_e32 v6, 26, v6
	v_lshrrev_b32_e32 v8, 4, v4
	v_lshlrev_b32_e32 v3, 3, v1
	v_add_u32_e32 v6, v5, v6
	v_bitop3_b32 v8, v8, v4, 32 bitop3:0x6c
	v_and_b32_e32 v3, -16, v3
	v_ashrrev_i32_e32 v6, 6, v6
	v_ashrrev_i32_e32 v9, 31, v8
	v_lshrrev_b32_e32 v9, 26, v9
	s_waitcnt lgkmcnt(0)
	v_readfirstlane_b32 s6, v10
	v_add3_u32 v3, v3, s10, v6
	v_lshlrev_b32_e32 v4, 3, v7
	v_add_u32_e32 v9, v8, v9
	v_cmp_gt_i32_e32 vcc, s6, v3
	v_and_b32_e32 v4, -16, v4
	v_ashrrev_i32_e32 v9, 6, v9
	s_lshl_b32 s7, s16, 14
	v_cndmask_b32_e32 v3, 0, v3, vcc
	v_add_u32_e32 v10, s7, v3
	v_add3_u32 v3, v4, s10, v9
	v_cmp_gt_i32_e32 vcc, s6, v3
	v_ashrrev_i32_e32 v11, 31, v10
	v_lshl_add_u64 v[12:13], v[10:11], 2, s[4:5]
	v_cndmask_b32_e32 v3, 0, v3, vcc
	v_add_u32_e32 v10, s7, v3
	v_ashrrev_i32_e32 v11, 31, v10
	s_waitcnt vmcnt(0)
	v_lshl_add_u64 v[14:15], v[10:11], 2, s[4:5]
	global_load_dword v11, v[12:13], off
	global_load_dword v10, v[14:15], off
	s_lshl_b32 s6, s14, 8
	v_and_b32_e32 v3, 63, v2
	s_add_i32 s59, s6, 0
	s_and_b32 s13, s14, 3
	s_ashr_i32 s17, s16, 31
	s_add_i32 s59, s59, 0x22000
	v_cmp_gt_u32_e64 s[6:7], 16, v3
	v_lshlrev_b32_e32 v4, 10, v3
	v_lshlrev_b32_e32 v3, 4, v3
	s_and_saveexec_b64 s[10:11], s[6:7]
	s_cbranch_execz .LBB0_1161
	s_lshl_b64 s[18:19], s[16:17], 14
	s_add_u32 s12, s22, s18
	s_addc_u32 s15, s23, s19
	s_lshl_b32 s18, s44, 7
	s_ashr_i32 s19, s18, 31
	s_lshl_b64 s[18:19], s[18:19], 2
	s_add_u32 s18, s12, s18
	s_addc_u32 s19, s15, s19
	v_and_b32_e32 v12, 0x2000, v4
	s_lshl_b32 s12, s13, 7
	v_and_b32_e32 v13, 0x70, v3
	v_or3_b32 v12, s12, v12, v13
	s_mov_b32 m0, s59
	s_nop 0
	global_load_lds_dwordx4 v12, s[18:19]
;     __device__ __forceinline__ const char* a_base(const Unit& u) const { return (const char*)A + (size_t)u.pm * BM * lda * 2; }
;     __device__ __forceinline__ const char* b_base(const Unit& u) const { return (const char*)Bt + (size_t)u.pn * BM * K * 2; }
;     __device__ __forceinline__ const char* b_base(const Unit& u) const { return (const char*)Bt + ((size_t)u.e * NB + (size_t)u.pn * BM) * K * 2; }
; #define PG8_RC() int R[2], C[2]; { int t_ = threadIdx.x; asm volatile("" : "+v"(t_)); _Pragma("unroll") for (int i = 0; i < 2; ++i) stage_rc(t_ * 16 + i * 8192, R[i], C[i]); }
; #define PG8_STAGEB(bufoff, gbase) PG8_STAGE2(bufoff, gbase, voffB[0], voffB[1])
; #define PG8_STAGEA(bufoff, gbase, h) PG8_STAGE2(bufoff, gbase, voffA[h][0], voffA[h][1])
; #define PG8_WAIT_V(n) asm volatile("s_waitcnt vmcnt(" #n ")" ::: "memory")
; #define PG8_BAR __builtin_amdgcn_s_barrier()
;     ...
;     { PG8_RC(); S.a_offs(cur, R, C, voffA); }
;     f32x4 acc[2][2][4][2];
; #pragma unroll
;     for (int a = 0; a < 2; ++a)
; #pragma unroll
;         for (int b = 0; b < 2; ++b)
; #pragma unroll
;             for (int m = 0; m < 4; ++m)
; #pragma unroll
;                 for (int n = 0; n < 2; ++n) acc[a][b][m][n] = (f32x4){0.f, 0.f, 0.f, 0.f};
;     bf16x8 At[4][2], B0[2][2], B1[2][2];
;     const char* cA = S.a_base(cur); const char* cB = S.b_base(cur);
;     const unsigned bias_lds = (unsigned)__builtin_amdgcn_readfirstlane((int)((unsigned)(size_t)lds + (unsigned)(AUX_OFF + 8192) + (unsigned)wid * 256u));
;     if constexpr (Epi::kBiasDMA) { if (lane < 16) glds16(E.bias_base(cur), E.bias_off(cur, wc, lane), bias_lds); }
;     const unsigned rowid_lds = (unsigned)__builtin_amdgcn_readfirstlane((int)((unsigned)(size_t)lds + (unsigned)AUX_OFF + (unsigned)wid * 512u));
;     if constexpr (Epi::kRowDMA) { if (lane < 32) glds16(E.row_base(cur), E.row_off(cur, wr, lane), rowid_lds); }
;     PG8_STAGEB(PG8_SB(0, 0), cB); PG8_STAGEB(PG8_SB(0, 1), cB + hstepB); PG8_STAGEA(PG8_SA(0, 0), cA, 0); if constexpr (!HM) PG8_STAGEA(PG8_SA(0, 1), cA, 1);
;     if (wr == 1) PG8_BAR;
;     if constexpr (HM) PG8_WAIT_V(0); else PG8_WAIT_V(2);
;     PG8_BAR;
;     PG8_STAGEB(PG8_SB(1, 0), cB + kstep); PG8_STAGEA(PG8_SA(1, 0), cA + kstep, 0); PG8_STAGEB(PG8_SB(1, 1), cB + hstepB + kstep);
;     PG8_WAIT_V(6); PG8_BAR;
.LBB0_1161:
	s_or_b64 exec, exec, s[10:11]
	v_lshlrev_b32_e32 v1, 5, v1
	v_and_b32_e32 v12, 32, v1
	v_lshlrev_b32_e32 v1, 6, v6
	v_lshlrev_b32_e32 v6, 5, v7
	v_lshlrev_b32_e32 v7, 6, v9
	v_sub_u32_e32 v5, v5, v1
	v_mov_b32_e32 v1, 1
	v_sub_u32_e32 v7, v8, v7
	v_and_b32_e32 v6, 32, v6
	v_ashrrev_i16_sdwa v7, v1, sext(v7) dst_sel:DWORD dst_unused:UNUSED_PAD src0_sel:DWORD src1_sel:BYTE_0
	s_mov_b32 s10, 0x7ffffc00
	s_waitcnt vmcnt(0)
	v_lshlrev_b32_e32 v9, 8, v10
	v_bfe_i32 v7, v7, 0, 16
	v_and_or_b32 v6, v9, s10, v6
	v_add_lshl_u32 v51, v6, v7, 1
	v_bfe_i32 v6, v2, 27, 1
	v_lshlrev_b32_e32 v152, 4, v2
	v_lshrrev_b32_e32 v6, 22, v6
	v_add_u32_e32 v6, v152, v6
	v_and_b32_e32 v6, 0xfffffc00, v6
	v_ashrrev_i16_sdwa v5, v1, sext(v5) dst_sel:DWORD dst_unused:UNUSED_PAD src0_sel:DWORD src1_sel:BYTE_0
	v_lshlrev_b32_e32 v8, 8, v11
	v_sub_u32_e32 v6, v152, v6
	v_bfe_i32 v5, v5, 0, 16
	v_and_or_b32 v8, v8, s10, v12
	v_lshrrev_b32_e32 v7, 4, v6
	v_add_lshl_u32 v50, v8, v5, 1
	v_ashrrev_i32_e32 v5, 31, v2
	v_bitop3_b32 v6, v7, v6, 32 bitop3:0x6c
	v_lshrrev_b32_e32 v5, 26, v5
	v_ashrrev_i32_e32 v8, 31, v6
	v_add_u32_e32 v5, v2, v5
	v_lshrrev_b32_e32 v8, 26, v8
	v_ashrrev_i32_e32 v5, 6, v5
	v_add_u32_e32 v8, v6, v8
	v_lshlrev_b32_e32 v7, 3, v5
	v_lshrrev_b32_e32 v9, 6, v8
	v_and_b32_e32 v8, 0xc0, v8
	v_and_b32_e32 v7, 0x1ffff0, v7
	v_lshlrev_b32_e32 v5, 5, v5
	v_sub_u32_e32 v6, v6, v8
	v_add_u32_e32 v7, v9, v7
	v_and_b32_e32 v5, 32, v5
	v_ashrrev_i16_sdwa v6, v1, sext(v6) dst_sel:DWORD dst_unused:UNUSED_PAD src0_sel:DWORD src1_sel:BYTE_0
	v_bfe_i32 v6, v6, 0, 16
	v_lshl_or_b32 v5, v7, 10, v5
	v_add_lshl_u32 v153, v5, v6, 1
	v_add_u32_e32 v5, 0x2000, v152
	v_ashrrev_i32_e32 v6, 31, v5
	v_lshrrev_b32_e32 v6, 22, v6
	v_add_u32_e32 v6, v5, v6
	v_ashrrev_i32_e32 v6, 10, v6
	v_mul_i32_i24_e32 v7, 0x400, v6
	v_sub_u32_e32 v5, v5, v7
	v_lshrrev_b32_e32 v7, 4, v5
	s_ashr_i32 s45, s44, 31
	v_bitop3_b32 v5, v7, v5, 32 bitop3:0x6c
	s_lshl_b64 s[10:11], s[44:45], 19
	s_lshl_b64 s[18:19], s[16:17], 23
	v_ashrrev_i32_e32 v8, 31, v5
	s_add_u32 s12, s33, s18
	v_lshrrev_b32_e32 v8, 26, v8
	s_addc_u32 s15, s60, s19
	v_add_u32_e32 v8, v5, v8
	s_add_u32 s46, s12, s10
	v_lshlrev_b32_e32 v7, 3, v6
	v_lshrrev_b32_e32 v9, 6, v8
	v_and_b32_e32 v8, 0xc0, v8
	s_addc_u32 s47, s15, s11
	v_and_b32_e32 v7, 0x1ffff0, v7
	v_lshlrev_b32_e32 v6, 5, v6
	v_sub_u32_e32 v5, v5, v8
	s_lshl_b32 s17, s14, 10
	v_add_u32_e32 v7, v9, v7
	v_and_b32_e32 v6, 32, v6
	v_ashrrev_i16_sdwa v5, v1, sext(v5) dst_sel:DWORD dst_unused:UNUSED_PAD src0_sel:DWORD src1_sel:BYTE_0
	s_add_i32 s17, s17, 0
	v_bfe_i32 v5, v5, 0, 16
	v_lshl_or_b32 v6, v7, 10, v6
	s_ashr_i32 s10, s9, 8
	s_add_i32 s45, s17, 0x10000
	s_mov_b32 m0, s45
	s_nop 0
	global_load_lds_dwordx4 v153, s[46:47]
	s_add_i32 s62, s17, 0x12000
	v_add_lshl_u32 v154, v6, v5, 1
	s_mov_b32 m0, s62
	s_nop 0
	global_load_lds_dwordx4 v154, s[46:47]
	s_add_u32 s14, s46, 0x40000
	s_addc_u32 s15, s47, 0
	s_add_i32 s63, s17, 0x14000
	s_mov_b32 m0, s63
	s_nop 0
	global_load_lds_dwordx4 v153, s[14:15]
	s_add_i32 s64, s17, 0x16000
	s_mov_b32 m0, s64
	s_nop 0
	global_load_lds_dwordx4 v154, s[14:15]
	s_add_i32 s65, s17, 0x2000
	s_mov_b32 m0, s17
	s_nop 0
	global_load_lds_dwordx4 v50, s[0:1]
	s_cmp_eq_u32 s10, 1
	s_mov_b32 m0, s65
	s_nop 0
	global_load_lds_dwordx4 v51, s[0:1]
	s_cselect_b64 s[18:19], -1, 0
	s_cmp_lg_u32 s10, 1
	s_cbranch_scc1 .LBB0_1163
	s_barrier
.LBB0_1163:
	v_lshrrev_b32_e32 v6, 1, v2
	v_and_b32_e32 v6, 24, v6
	v_and_b32_e32 v5, 15, v2
	v_lshlrev_b32_e32 v7, 1, v6
	v_lshlrev_b32_e32 v2, 2, v2
	v_lshl_or_b32 v155, s10, 6, v5
	v_lshl_or_b32 v5, v5, 6, v7
	s_lshl_b32 s10, s10, 13
	v_and_b32_e32 v2, 32, v2
	v_bitop3_b32 v7, v5, s10, v2 bitop3:0xde
	s_lshl_b32 s10, s13, 12
	s_add_u32 s34, s94, 0x34600200
	s_addc_u32 s35, s95, 0
	s_add_u32 s36, s94, 0x34600280
	s_addc_u32 s37, s95, 0
	v_bitop3_b32 v2, v5, s10, v2 bitop3:0xde
	s_add_u32 s10, s46, 0x80
	s_waitcnt vmcnt(0)
	s_barrier
	s_addc_u32 s11, s47, 0
	s_add_i32 s66, s17, 0x18000
	s_mov_b32 m0, s66
	s_nop 0
	global_load_lds_dwordx4 v153, s[10:11]
	s_add_i32 s67, s17, 0x1a000
	s_mov_b32 m0, s67
	s_nop 0
	global_load_lds_dwordx4 v154, s[10:11]
	s_add_i32 s68, s17, 0x8000
	s_mov_b32 m0, s68
	s_nop 0
	global_load_lds_dwordx4 v50, s[30:31]
	s_add_i32 s69, s17, 0xa000
	s_mov_b32 m0, s69
	s_nop 0
	global_load_lds_dwordx4 v51, s[30:31]
	s_add_u32 s10, s46, 0x40080
	s_addc_u32 s11, s47, 0
	s_add_i32 s70, s17, 0x1c000
	s_mov_b32 m0, s70
	s_nop 0
	global_load_lds_dwordx4 v153, s[10:11]
	s_add_i32 s71, s17, 0x1e000
	s_mov_b32 m0, s71
	s_nop 0
	global_load_lds_dwordx4 v154, s[10:11]
	s_cmpk_lt_u32 s9, 0x100
	s_waitcnt vmcnt(6)
	s_cselect_b64 s[30:31], -1, 0
	v_and_b32_e32 v4, 0x2000, v4
	s_lshl_b32 s9, s13, 7
	v_and_b32_e32 v3, 0x70, v3
	s_mov_b32 s12, 0
	v_or3_b32 v157, s9, v4, v3
	s_ashr_i32 s9, s8, 31
	v_lshl_add_u32 v156, v6, 2, s59
	v_lshl_or_b32 v158, s13, 5, v6
	v_mov_b64_e32 v[150:151], s[8:9]
	s_add_i32 s72, 0, 0x23180
	s_mov_b32 s13, s12
	s_mov_b32 s14, s12
	s_mov_b32 s15, s12
	s_mov_b32 s73, 0xc0e00000
	v_add_u32_e32 v159, 0, v2
	v_add_u32_e32 v160, 0, v7
	v_mov_b32_e32 v161, 0x40e00000
	s_mov_b32 s48, s12
	s_barrier
	s_branch .LBB0_1166

; #define LAS __attribute__((address_space(3)))
; #define PG8_STAGEB(bufoff, gbase) PG8_STAGE2(bufoff, gbase, voffB[0], voffB[1])
; #define PG8_STAGEA(bufoff, gbase, h) PG8_STAGE2(bufoff, gbase, voffA[h][0], voffA[h][1])
; #define PG8_STAGEAS(bufoff, gbase, h) PG8_STAGE2(bufoff, gbase, voffA[h][0], voffA[h][1])
; #define PG8_LDA(dst, b, h) do { _Pragma("unroll") for (int m = 0; m < 4; ++m) _Pragma("unroll") for (int k = 0; k < 2; ++k) dst[m][k] = *(const LAS bf16x8*)(lds + PG8_SA(b, h) + aoff + m * 2048 + k * 1024); } while (0)
; #define PG8_LDB(dst, b, h) do { _Pragma("unroll") for (int n = 0; n < 2; ++n) _Pragma("unroll") for (int k = 0; k < 2; ++k) dst[n][k] = *(const LAS bf16x8*)(lds + PG8_SB(b, h) + boff + n * 2048 + k * 1024); } while (0)
; #define PG8_WAIT_K0() do { if (EST > 0 && t == 0 && ui > 0) asm volatile("s_waitcnt vmcnt(%0)" :: "n"((HM ? 6 : 8) + EST) : "memory"); else PG8_WAIT_K(); } while (0)
; #define PG8_WAIT_L(n) asm volatile("s_waitcnt lgkmcnt(" #n ")" ::: "memory")
; #define PG8_BAR __builtin_amdgcn_s_barrier()
; #define PG8_SCHED __builtin_amdgcn_sched_barrier(0)
;     ...
;             PG8_LDB(B0, 0, 0); PG8_LDB(B1, 0, 1); PG8_SCHED; PG8_LDA(At, 0, 0); if constexpr (!HM) PG8_STAGEA(PG8_SA(1, 1), a1, 1);
;             if constexpr (Sched::kGather) { if (last && has_next) { const u32x4 tn = *(const LAS u32x4*)(S.aux + tid * 16); voffA[0][0] = tn.x; voffA[0][1] = tn.y; voffA[1][0] = tn.z; voffA[1][1] = tn.w; } }
;             PG8_WAIT_K0(); PG8_WAIT_L(0); PG8_BAR; PG8_MMA(0, 0, At, B0); PG8_MMA(0, 1, At, B1); PG8_BAR; PG8_SCHED;
;             if constexpr (!HM) PG8_LDA(At, 0, 1);
;             PG8_STAGEB(PG8_SB(0, 0), b2); PG8_STAGEB(PG8_SB(0, 1), b2 + hstepB); PG8_STAGEAS(PG8_SA(0, 0), a2, 0);
;             PG8_WAIT_K0(); PG8_WAIT_L(0); PG8_BAR; if constexpr (!HM) { PG8_MMA(1, 0, At, B0); PG8_MMA(1, 1, At, B1); } PG8_BAR; PG8_SCHED;
.LBB0_1181:
	s_waitcnt lgkmcnt(0)
	s_add_u32 s50, s46, 0x100
	s_addc_u32 s51, s47, 0
	s_barrier
	s_setprio 1
	s_waitcnt lgkmcnt(6)
	v_mov_b32_e32 v36, v80
	v_mov_b32_e32 v37, v81
	v_mov_b64_e32 v[108:109], s[14:15]
	v_mov_b32_e32 v42, v92
	v_mov_b32_e32 v43, v93
	v_mov_b64_e32 v[104:105], s[14:15]
	s_waitcnt lgkmcnt(4)
	v_mov_b32_e32 v30, v72
	v_mov_b32_e32 v31, v73
	v_mov_b64_e32 v[92:93], s[14:15]
	v_mov_b64_e32 v[88:89], s[14:15]
	s_waitcnt lgkmcnt(2)
	v_mov_b32_e32 v24, v64
	v_mov_b32_e32 v25, v65
	v_mov_b64_e32 v[80:81], s[14:15]
	v_mov_b64_e32 v[72:73], s[14:15]
	v_mov_b64_e32 v[64:65], s[14:15]
	v_mov_b64_e32 v[106:107], s[12:13]
	v_mov_b64_e32 v[102:103], s[12:13]
	v_mov_b64_e32 v[90:91], s[12:13]
	v_mov_b64_e32 v[86:87], s[12:13]
	v_mov_b64_e32 v[78:79], s[12:13]
	v_mov_b64_e32 v[70:71], s[12:13]
	v_mov_b64_e32 v[62:63], s[12:13]
	v_mov_b32_e32 v48, v56
	v_mov_b32_e32 v49, v57
	v_mov_b64_e32 v[56:57], s[14:15]
	s_nop 1
	v_mfma_scale_f32_16x16x128_f8f6f4 v[106:109], v[44:49], v[32:37], v[106:109], v58, v82 op_sel_hi:[0,0,0] cbsz:2 blgp:2
	s_nop 1
	v_mfma_scale_f32_16x16x128_f8f6f4 v[102:105], v[38:43], v[32:37], v[102:105], v94, v82 op_sel_hi:[0,0,0] cbsz:2 blgp:2
	s_nop 1
	v_mfma_scale_f32_16x16x128_f8f6f4 v[90:93], v[44:49], v[26:31], v[90:93], v58, v74 op_sel_hi:[0,0,0] cbsz:2 blgp:2
	s_nop 1
	v_mfma_scale_f32_16x16x128_f8f6f4 v[86:89], v[38:43], v[26:31], v[86:89], v94, v74 op_sel_hi:[0,0,0] cbsz:2 blgp:2
	s_nop 1
	v_mfma_scale_f32_16x16x128_f8f6f4 v[78:81], v[44:49], v[20:25], v[78:81], v58, v66 op_sel_hi:[0,0,0] cbsz:2 blgp:2
	s_nop 1
	v_mfma_scale_f32_16x16x128_f8f6f4 v[70:73], v[38:43], v[20:25], v[70:73], v94, v66 op_sel_hi:[0,0,0] cbsz:2 blgp:2
	s_waitcnt lgkmcnt(0)
	v_mov_b32_e32 v18, v126
	v_mov_b32_e32 v19, v127
	s_nop 1
	v_mfma_scale_f32_16x16x128_f8f6f4 v[62:65], v[44:49], v[14:19], v[62:65], v58, v128 op_sel_hi:[0,0,0] cbsz:2 blgp:2
	v_mov_b64_e32 v[60:61], s[14:15]
	v_mov_b64_e32 v[54:55], s[12:13]
	v_mov_b64_e32 v[58:59], s[12:13]
	s_nop 1
	v_mfma_scale_f32_16x16x128_f8f6f4 v[58:61], v[38:43], v[14:19], v[58:61], v94, v128 op_sel_hi:[0,0,0] cbsz:2 blgp:2
	s_setprio 0
	s_setprio 1
	v_mov_b64_e32 v[116:117], s[14:15]
	v_mov_b64_e32 v[112:113], s[14:15]
	v_mov_b64_e32 v[100:101], s[14:15]
	v_mov_b64_e32 v[96:97], s[14:15]
	v_mov_b64_e32 v[114:115], s[12:13]
	v_mov_b64_e32 v[110:111], s[12:13]
	v_mov_b64_e32 v[98:99], s[12:13]
	v_mov_b64_e32 v[94:95], s[12:13]
	v_mov_b32_e32 v12, v122
	v_mov_b32_e32 v13, v123
	s_nop 1
	v_mfma_scale_f32_16x16x128_f8f6f4 v[114:117], v[8:13], v[32:37], v[114:117], v124, v82 op_sel_hi:[0,0,0] cbsz:2 blgp:2
	v_mov_b32_e32 v6, v118
	v_mov_b32_e32 v7, v119
	s_nop 1
	v_mfma_scale_f32_16x16x128_f8f6f4 v[110:113], v[2:7], v[32:37], v[110:113], v120, v82 op_sel_hi:[0,0,0] cbsz:2 blgp:2
	s_nop 1
	v_mfma_scale_f32_16x16x128_f8f6f4 v[98:101], v[8:13], v[26:31], v[98:101], v124, v74 op_sel_hi:[0,0,0] cbsz:2 blgp:2
	s_nop 1
	v_mfma_scale_f32_16x16x128_f8f6f4 v[94:97], v[2:7], v[26:31], v[94:97], v120, v74 op_sel_hi:[0,0,0] cbsz:2 blgp:2
	v_mov_b64_e32 v[84:85], s[14:15]
	v_mov_b64_e32 v[76:77], s[14:15]
	v_mov_b64_e32 v[82:83], s[12:13]
	v_mov_b64_e32 v[74:75], s[12:13]
	s_nop 1
	v_mfma_scale_f32_16x16x128_f8f6f4 v[82:85], v[8:13], v[20:25], v[82:85], v124, v66 op_sel_hi:[0,0,0] cbsz:2 blgp:2
	s_nop 1
	v_mfma_scale_f32_16x16x128_f8f6f4 v[74:77], v[2:7], v[20:25], v[74:77], v120, v66 op_sel_hi:[0,0,0] cbsz:2 blgp:2
	v_mov_b64_e32 v[68:69], s[14:15]
	v_mov_b64_e32 v[66:67], s[12:13]
	s_nop 1
	v_mfma_scale_f32_16x16x128_f8f6f4 v[66:69], v[8:13], v[14:19], v[66:69], v124, v128 op_sel_hi:[0,0,0] cbsz:2 blgp:2
	s_nop 1
	v_mfma_scale_f32_16x16x128_f8f6f4 v[54:57], v[2:7], v[14:19], v[54:57], v120, v128 op_sel_hi:[0,0,0] cbsz:2 blgp:2
	s_setprio 0
	s_barrier
	s_mov_b32 m0, s45
	s_nop 0
	global_load_lds_dwordx4 v153, s[50:51]
	s_mov_b32 m0, s62
	s_nop 0
	global_load_lds_dwordx4 v154, s[50:51]
	s_add_u32 s50, s46, 0x40100
	s_addc_u32 s51, s47, 0
	s_mov_b32 m0, s63
	s_nop 0
	global_load_lds_dwordx4 v153, s[50:51]
	s_and_b64 vcc, exec, s[48:49]
	s_mov_b32 m0, s64
	s_nop 0
	global_load_lds_dwordx4 v154, s[50:51]
	s_mov_b32 m0, s17
	s_nop 0
	global_load_lds_dwordx4 v50, s[24:25]
	s_mov_b32 m0, s65
	s_nop 0
	global_load_lds_dwordx4 v51, s[24:25]
	s_cbranch_vccz .LBB0_1198
	s_waitcnt vmcnt(10)
	s_cbranch_execnz .LBB0_1184

; #define LAS __attribute__((address_space(3)))
; #define PG8_STAGEB(bufoff, gbase) PG8_STAGE2(bufoff, gbase, voffB[0], voffB[1])
;     ...
;                 if (t == 2 && has_next) {
;                     if constexpr (HM) asm volatile("s_waitcnt vmcnt(12)" : "+v"(gtok0), "+v"(gtok1), "+v"(gtok2), "+v"(gtok3) :: "memory");
;                     else asm volatile("s_waitcnt vmcnt(16)" : "+v"(gtok0), "+v"(gtok1), "+v"(gtok2), "+v"(gtok3) :: "memory");
;                     PG8_RC(); *(LAS u32x4*)(S.aux + tid * 16) = (u32x4){(unsigned)(((int)gtok0 >> 2) * S.lda + C[0]) * 2u, (unsigned)(((int)gtok1 >> 2) * S.lda + C[1]) * 2u, (unsigned)(((int)gtok2 >> 2) * S.lda + C[0]) * 2u, (unsigned)(((int)gtok3 >> 2) * S.lda + C[1]) * 2u};
;                 }
;             }
;             const char* a1 = cA + (size_t)(t + 1) * kstep;
;             const char* a2 = last ? nA : cA + (size_t)(t + 2) * kstep; const char* b2 = last ? nB : cB + (size_t)(t + 2) * kstep;
;             const char* a3 = a2 + kstep; const char* b3 = b2 + kstep;
;             PG8_LDB(B0, 0, 0); PG8_LDB(B1, 0, 1); PG8_SCHED; PG8_LDA(At, 0, 0); if constexpr (!HM) PG8_STAGEA(PG8_SA(1, 1), a1, 1);
;             if constexpr (Sched::kGather) { if (last && has_next) { const u32x4 tn = *(const LAS u32x4*)(S.aux + tid * 16); voffA[0][0] = tn.x; voffA[0][1] = tn.y; voffA[1][0] = tn.z; voffA[1][1] = tn.w; } }
;             PG8_WAIT_K0(); PG8_WAIT_L(0); PG8_BAR; PG8_MMA(0, 0, At, B0); PG8_MMA(0, 1, At, B1); PG8_BAR; PG8_SCHED;
;             if constexpr (!HM) PG8_LDA(At, 0, 1);
;             PG8_STAGEB(PG8_SB(0, 0), b2); PG8_STAGEB(PG8_SB(0, 1), b2 + hstepB); PG8_STAGEAS(PG8_SA(0, 0), a2, 0);
;             PG8_WAIT_K0(); PG8_WAIT_L(0); PG8_BAR; if constexpr (!HM) { PG8_MMA(1, 0, At, B0); PG8_MMA(1, 1, At, B1); } PG8_BAR; PG8_SCHED;
;             PG8_LDB(B0, 1, 0); PG8_LDB(B1, 1, 1); PG8_SCHED; PG8_LDA(At, 1, 0); if constexpr (!HM) PG8_STAGEAS(PG8_SA(0, 1), a2, 1);
;             PG8_WAIT_K(); PG8_WAIT_L(0); PG8_BAR; PG8_MMA(0, 0, At, B0); PG8_MMA(0, 1, At, B1); PG8_BAR; PG8_SCHED;
;             if constexpr (!HM) PG8_LDA(At, 1, 1);
;             PG8_STAGEB(PG8_SB(1, 0), b3); PG8_STAGEB(PG8_SB(1, 1), b3 + hstepB); PG8_STAGEAS(PG8_SA(1, 0), a3, 0);
;             PG8_WAIT_K(); PG8_WAIT_L(0); PG8_BAR; if constexpr (!HM) { PG8_MMA(1, 0, At, B0); PG8_MMA(1, 1, At, B1); } PG8_BAR; PG8_SCHED;
.LBB0_1184:
	s_waitcnt lgkmcnt(0)
	s_add_u32 s48, s46, 0x180
	s_addc_u32 s49, s47, 0
	s_barrier
	s_barrier
	v_add_u32_e32 v164, 0x18000, v159
	v_add_u32_e32 v165, 0x1c000, v159
	ds_read_b128 v[2:5], v164
	ds_read_b128 v[118:121], v164 offset:1024
	ds_read_b128 v[8:11], v164 offset:2048
	ds_read_b128 v[122:125], v164 offset:3072
	ds_read_b128 v[14:17], v165
	ds_read_b128 v[126:129], v165 offset:1024
	ds_read_b128 v[20:23], v165 offset:2048
	ds_read_b128 v[132:135], v165 offset:3072
	ds_read_b128 v[26:29], v160 offset:32768
	ds_read_b128 v[136:139], v160 offset:33792
	ds_read_b128 v[32:35], v160 offset:34816
	ds_read_b128 v[140:143], v160 offset:35840
	ds_read_b128 v[38:41], v160 offset:36864
	ds_read_b128 v[144:147], v160 offset:37888
	ds_read_b128 v[44:47], v160 offset:38912
	ds_read_b128 v[166:169], v160 offset:39936
	s_waitcnt vmcnt(6)
	s_waitcnt lgkmcnt(0)
	s_barrier
	s_setprio 1
	s_waitcnt lgkmcnt(6)
	v_mov_b32_e32 v30, v136
	v_mov_b32_e32 v31, v137
	v_mov_b32_e32 v6, v118
	v_mov_b32_e32 v7, v119
	s_nop 1
	v_mfma_scale_f32_16x16x128_f8f6f4 v[106:109], v[2:7], v[26:31], v[106:109], v120, v138 op_sel_hi:[0,0,0] cbsz:2 blgp:2
	v_mov_b32_e32 v12, v122
	v_mov_b32_e32 v13, v123
	s_nop 1
	v_mfma_scale_f32_16x16x128_f8f6f4 v[102:105], v[8:13], v[26:31], v[102:105], v124, v138 op_sel_hi:[0,0,0] cbsz:2 blgp:2
	s_waitcnt lgkmcnt(4)
	v_mov_b32_e32 v36, v140
	v_mov_b32_e32 v37, v141
	s_nop 1
	v_mfma_scale_f32_16x16x128_f8f6f4 v[90:93], v[2:7], v[32:37], v[90:93], v120, v142 op_sel_hi:[0,0,0] cbsz:2 blgp:2
	s_nop 1
	v_mfma_scale_f32_16x16x128_f8f6f4 v[86:89], v[8:13], v[32:37], v[86:89], v124, v142 op_sel_hi:[0,0,0] cbsz:2 blgp:2
	s_waitcnt lgkmcnt(2)
	v_mov_b32_e32 v42, v144
	v_mov_b32_e32 v43, v145
	s_nop 1
	v_mfma_scale_f32_16x16x128_f8f6f4 v[78:81], v[2:7], v[38:43], v[78:81], v120, v146 op_sel_hi:[0,0,0] cbsz:2 blgp:2
	s_nop 1
	v_mfma_scale_f32_16x16x128_f8f6f4 v[70:73], v[8:13], v[38:43], v[70:73], v124, v146 op_sel_hi:[0,0,0] cbsz:2 blgp:2
	s_waitcnt lgkmcnt(0)
	v_mov_b32_e32 v48, v166
	v_mov_b32_e32 v49, v167
	s_nop 1
	v_mfma_scale_f32_16x16x128_f8f6f4 v[62:65], v[2:7], v[44:49], v[62:65], v120, v168 op_sel_hi:[0,0,0] cbsz:2 blgp:2
	s_nop 1
	v_mfma_scale_f32_16x16x128_f8f6f4 v[58:61], v[8:13], v[44:49], v[58:61], v124, v168 op_sel_hi:[0,0,0] cbsz:2 blgp:2
	s_setprio 0
	s_setprio 1
	v_mov_b32_e32 v18, v126
	v_mov_b32_e32 v19, v127
	s_nop 1
	v_mfma_scale_f32_16x16x128_f8f6f4 v[114:117], v[14:19], v[26:31], v[114:117], v128, v138 op_sel_hi:[0,0,0] cbsz:2 blgp:2
	v_mov_b32_e32 v24, v132
	v_mov_b32_e32 v25, v133
	s_nop 1
	v_mfma_scale_f32_16x16x128_f8f6f4 v[110:113], v[20:25], v[26:31], v[110:113], v134, v138 op_sel_hi:[0,0,0] cbsz:2 blgp:2
	s_nop 1
	v_mfma_scale_f32_16x16x128_f8f6f4 v[98:101], v[14:19], v[32:37], v[98:101], v128, v142 op_sel_hi:[0,0,0] cbsz:2 blgp:2
	s_nop 1
	v_mfma_scale_f32_16x16x128_f8f6f4 v[94:97], v[20:25], v[32:37], v[94:97], v134, v142 op_sel_hi:[0,0,0] cbsz:2 blgp:2
	s_nop 1
	v_mfma_scale_f32_16x16x128_f8f6f4 v[82:85], v[14:19], v[38:43], v[82:85], v128, v146 op_sel_hi:[0,0,0] cbsz:2 blgp:2
	s_nop 1
	v_mfma_scale_f32_16x16x128_f8f6f4 v[74:77], v[20:25], v[38:43], v[74:77], v134, v146 op_sel_hi:[0,0,0] cbsz:2 blgp:2
	s_nop 1
	v_mfma_scale_f32_16x16x128_f8f6f4 v[66:69], v[14:19], v[44:49], v[66:69], v128, v168 op_sel_hi:[0,0,0] cbsz:2 blgp:2
	s_nop 1
	v_mfma_scale_f32_16x16x128_f8f6f4 v[54:57], v[20:25], v[44:49], v[54:57], v134, v168 op_sel_hi:[0,0,0] cbsz:2 blgp:2
	s_setprio 0
	s_barrier
	s_mov_b32 m0, s66
	s_nop 0
	global_load_lds_dwordx4 v153, s[48:49]
	s_mov_b32 m0, s67
	s_nop 0
	global_load_lds_dwordx4 v154, s[48:49]
	s_add_u32 s48, s46, 0x40180
	s_addc_u32 s49, s47, 0
	s_mov_b32 m0, s70
	s_nop 0
	global_load_lds_dwordx4 v153, s[48:49]
	s_mov_b32 m0, s71
	s_nop 0
	global_load_lds_dwordx4 v154, s[48:49]
	s_mov_b32 m0, s68
	s_nop 0
	global_load_lds_dwordx4 v50, s[26:27]
	s_mov_b32 m0, s69
	s_nop 0
	global_load_lds_dwordx4 v51, s[26:27]
	s_waitcnt vmcnt(6)
	s_waitcnt lgkmcnt(0)
	s_barrier
	s_barrier
	v_add_u32_e32 v2, 0, v152
	s_and_b64 vcc, exec, s[8:9]
	v_add_u32_e32 v166, 0x20000, v2
	s_cbranch_vccnz .LBB0_1186
	v_mov_b32_e32 v2, v0
	s_waitcnt vmcnt(12)
	s_nop 0
	v_ashrrev_i32_e32 v4, 31, v2
	v_lshrrev_b32_e32 v4, 26, v4
	v_lshlrev_b32_e32 v3, 4, v2
	v_add_u32_e32 v4, v2, v4
	v_bfe_i32 v2, v2, 27, 1
	v_lshrrev_b32_e32 v2, 22, v2
	v_add_u32_e32 v2, v3, v2
	v_and_b32_e32 v2, 0xfffffc00, v2
	v_sub_u32_e32 v2, v3, v2
	v_lshrrev_b32_e32 v5, 4, v2
	v_bitop3_b32 v5, v5, v2, 32 bitop3:0x6c
	v_ashrrev_i32_e32 v2, 31, v2
	v_lshrrev_b32_e32 v2, 26, v2
	v_add_u32_e32 v2, v5, v2
	v_and_b32_e32 v2, 0xc0, v2
	v_lshrrev_b32_e32 v4, 1, v4
	v_sub_u32_e32 v2, v5, v2
	v_and_b32_e32 v4, 32, v4
	v_ashrrev_i16_sdwa v2, v1, sext(v2) dst_sel:DWORD dst_unused:UNUSED_PAD src0_sel:DWORD src1_sel:BYTE_0
	v_add_u32_sdwa v4, v4, sext(v2) dst_sel:DWORD dst_unused:UNUSED_PAD src0_sel:DWORD src1_sel:WORD_0
	v_add_u32_e32 v2, 0x2000, v3
	v_ashrrev_i32_e32 v3, 31, v2
	v_lshrrev_b32_e32 v3, 22, v3
	v_add_u32_e32 v3, v2, v3
	v_ashrrev_i32_e32 v3, 10, v3
	v_mul_i32_i24_e32 v5, 0x400, v3
	v_sub_u32_e32 v2, v2, v5
	v_lshrrev_b32_e32 v5, 4, v2
	v_bitop3_b32 v5, v5, v2, 32 bitop3:0x6c
	v_ashrrev_i32_e32 v2, 31, v2
	v_lshrrev_b32_e32 v2, 26, v2
	v_add_u32_e32 v2, v5, v2
	v_and_b32_e32 v2, 0xc0, v2
	v_lshlrev_b32_e32 v3, 5, v3
	v_sub_u32_e32 v2, v5, v2
	v_and_b32_e32 v3, 32, v3
	v_ashrrev_i16_sdwa v2, v1, sext(v2) dst_sel:DWORD dst_unused:UNUSED_PAD src0_sel:DWORD src1_sel:BYTE_0
	v_add_u32_sdwa v5, v3, sext(v2) dst_sel:DWORD dst_unused:UNUSED_PAD src0_sel:DWORD src1_sel:WORD_0
	v_lshlrev_b32_e32 v2, 8, v131
	v_lshlrev_b32_e32 v6, 8, v53
	v_and_b32_e32 v2, 0x7ffffc00, v2
	v_and_b32_e32 v6, 0x7ffffc00, v6
	v_add_lshl_u32 v2, v4, v2, 1
	v_lshlrev_b32_e32 v3, 8, v130
	v_add_lshl_u32 v4, v4, v6, 1
	v_lshlrev_b32_e32 v6, 8, v52
	v_and_b32_e32 v3, 0x7ffffc00, v3
	v_and_b32_e32 v6, 0x7ffffc00, v6
	v_add_lshl_u32 v3, v5, v3, 1
	v_add_lshl_u32 v5, v5, v6, 1
	ds_write_b128 v166, v[2:5]
; #define LAS __attribute__((address_space(3)))
; #define PG8_STAGEB(bufoff, gbase) PG8_STAGE2(bufoff, gbase, voffB[0], voffB[1])
; #define PG8_STAGEA(bufoff, gbase, h) PG8_STAGE2(bufoff, gbase, voffA[h][0], voffA[h][1])
; #define PG8_STAGEAS(bufoff, gbase, h) PG8_STAGE2(bufoff, gbase, voffA[h][0], voffA[h][1])
; #define PG8_LDA(dst, b, h) do { _Pragma("unroll") for (int m = 0; m < 4; ++m) _Pragma("unroll") for (int k = 0; k < 2; ++k) dst[m][k] = *(const LAS bf16x8*)(lds + PG8_SA(b, h) + aoff + m * 2048 + k * 1024); } while (0)
; #define PG8_LDB(dst, b, h) do { _Pragma("unroll") for (int n = 0; n < 2; ++n) _Pragma("unroll") for (int k = 0; k < 2; ++k) dst[n][k] = *(const LAS bf16x8*)(lds + PG8_SB(b, h) + boff + n * 2048 + k * 1024); } while (0)
; #define PG8_WAIT_K() do { if constexpr (HM) PG8_WAIT_V(6); else PG8_WAIT_V(8); } while (0)
; #define PG8_WAIT_K0() do { if (EST > 0 && t == 0 && ui > 0) asm volatile("s_waitcnt vmcnt(%0)" :: "n"((HM ? 6 : 8) + EST) : "memory"); else PG8_WAIT_K(); } while (0)
; #define PG8_BAR __builtin_amdgcn_s_barrier()
;     ...
;             PG8_LDB(B0, 0, 0); PG8_LDB(B1, 0, 1); PG8_SCHED; PG8_LDA(At, 0, 0); if constexpr (!HM) PG8_STAGEA(PG8_SA(1, 1), a1, 1);
;             if constexpr (Sched::kGather) { if (last && has_next) { const u32x4 tn = *(const LAS u32x4*)(S.aux + tid * 16); voffA[0][0] = tn.x; voffA[0][1] = tn.y; voffA[1][0] = tn.z; voffA[1][1] = tn.w; } }
;             PG8_WAIT_K0(); PG8_WAIT_L(0); PG8_BAR; PG8_MMA(0, 0, At, B0); PG8_MMA(0, 1, At, B1); PG8_BAR; PG8_SCHED;
;             if constexpr (!HM) PG8_LDA(At, 0, 1);
;             PG8_STAGEB(PG8_SB(0, 0), b2); PG8_STAGEB(PG8_SB(0, 1), b2 + hstepB); PG8_STAGEAS(PG8_SA(0, 0), a2, 0);
;             PG8_WAIT_K0(); PG8_WAIT_L(0); PG8_BAR; if constexpr (!HM) { PG8_MMA(1, 0, At, B0); PG8_MMA(1, 1, At, B1); } PG8_BAR; PG8_SCHED;
;             PG8_LDB(B0, 1, 0); PG8_LDB(B1, 1, 1); PG8_SCHED; PG8_LDA(At, 1, 0); if constexpr (!HM) PG8_STAGEAS(PG8_SA(0, 1), a2, 1);
;             PG8_WAIT_K(); PG8_WAIT_L(0); PG8_BAR; PG8_MMA(0, 0, At, B0); PG8_MMA(0, 1, At, B1); PG8_BAR; PG8_SCHED;
;             if constexpr (!HM) PG8_LDA(At, 1, 1);
;             PG8_STAGEB(PG8_SB(1, 0), b3); PG8_STAGEB(PG8_SB(1, 1), b3 + hstepB); PG8_STAGEAS(PG8_SA(1, 0), a3, 0);
;             PG8_WAIT_K(); PG8_WAIT_L(0); PG8_BAR; if constexpr (!HM) { PG8_MMA(1, 0, At, B0); PG8_MMA(1, 1, At, B1); } PG8_BAR; PG8_SCHED;
.LBB0_1186:
	ds_read_b128 v[2:5], v163
	ds_read_b128 v[118:121], v163 offset:1024
	ds_read_b128 v[8:11], v163 offset:2048
	ds_read_b128 v[122:125], v163 offset:3072
	ds_read_b128 v[14:17], v162
	ds_read_b128 v[126:129], v162 offset:1024
	ds_read_b128 v[20:23], v162 offset:2048
	ds_read_b128 v[130:133], v162 offset:3072
	s_add_u32 s50, s46, 0x200
	s_addc_u32 s51, s47, 0
	ds_read_b128 v[26:29], v160
	ds_read_b128 v[134:137], v160 offset:1024
	ds_read_b128 v[32:35], v160 offset:2048
	ds_read_b128 v[138:141], v160 offset:3072
	ds_read_b128 v[38:41], v160 offset:4096
	ds_read_b128 v[142:145], v160 offset:5120
	ds_read_b128 v[44:47], v160 offset:6144
	ds_read_b128 v[146:149], v160 offset:7168
	s_waitcnt vmcnt(6)
	s_waitcnt lgkmcnt(0)
	s_add_u32 s48, s46, 0x280
	s_addc_u32 s49, s47, 0
	s_barrier
	s_setprio 1
	s_waitcnt lgkmcnt(6)
	v_mov_b32_e32 v30, v134
	v_mov_b32_e32 v31, v135
	v_mov_b32_e32 v6, v118
	v_mov_b32_e32 v7, v119
	s_nop 1
	v_mfma_scale_f32_16x16x128_f8f6f4 v[106:109], v[2:7], v[26:31], v[106:109], v120, v136 op_sel_hi:[0,0,0] cbsz:2 blgp:2
	v_mov_b32_e32 v12, v122
	v_mov_b32_e32 v13, v123
	s_nop 1
	v_mfma_scale_f32_16x16x128_f8f6f4 v[102:105], v[8:13], v[26:31], v[102:105], v124, v136 op_sel_hi:[0,0,0] cbsz:2 blgp:2
	s_waitcnt lgkmcnt(4)
	v_mov_b32_e32 v36, v138
	v_mov_b32_e32 v37, v139
	s_nop 1
	v_mfma_scale_f32_16x16x128_f8f6f4 v[90:93], v[2:7], v[32:37], v[90:93], v120, v140 op_sel_hi:[0,0,0] cbsz:2 blgp:2
	s_nop 1
	v_mfma_scale_f32_16x16x128_f8f6f4 v[86:89], v[8:13], v[32:37], v[86:89], v124, v140 op_sel_hi:[0,0,0] cbsz:2 blgp:2
	s_waitcnt lgkmcnt(2)
	v_mov_b32_e32 v42, v142
	v_mov_b32_e32 v43, v143
	s_nop 1
	v_mfma_scale_f32_16x16x128_f8f6f4 v[78:81], v[2:7], v[38:43], v[78:81], v120, v144 op_sel_hi:[0,0,0] cbsz:2 blgp:2
	s_nop 1
	v_mfma_scale_f32_16x16x128_f8f6f4 v[70:73], v[8:13], v[38:43], v[70:73], v124, v144 op_sel_hi:[0,0,0] cbsz:2 blgp:2
	s_waitcnt lgkmcnt(0)
	v_mov_b32_e32 v48, v146
	v_mov_b32_e32 v49, v147
	s_nop 1
	v_mfma_scale_f32_16x16x128_f8f6f4 v[62:65], v[2:7], v[44:49], v[62:65], v120, v148 op_sel_hi:[0,0,0] cbsz:2 blgp:2
	s_nop 1
	v_mfma_scale_f32_16x16x128_f8f6f4 v[58:61], v[8:13], v[44:49], v[58:61], v124, v148 op_sel_hi:[0,0,0] cbsz:2 blgp:2
	s_setprio 0
	s_setprio 1
	v_mov_b32_e32 v18, v126
	v_mov_b32_e32 v19, v127
	s_nop 1
	v_mfma_scale_f32_16x16x128_f8f6f4 v[114:117], v[14:19], v[26:31], v[114:117], v128, v136 op_sel_hi:[0,0,0] cbsz:2 blgp:2
	v_mov_b32_e32 v24, v130
	v_mov_b32_e32 v25, v131
	s_nop 1
	v_mfma_scale_f32_16x16x128_f8f6f4 v[110:113], v[20:25], v[26:31], v[110:113], v132, v136 op_sel_hi:[0,0,0] cbsz:2 blgp:2
	s_nop 1
	v_mfma_scale_f32_16x16x128_f8f6f4 v[98:101], v[14:19], v[32:37], v[98:101], v128, v140 op_sel_hi:[0,0,0] cbsz:2 blgp:2
	s_nop 1
	v_mfma_scale_f32_16x16x128_f8f6f4 v[94:97], v[20:25], v[32:37], v[94:97], v132, v140 op_sel_hi:[0,0,0] cbsz:2 blgp:2
	s_nop 1
	v_mfma_scale_f32_16x16x128_f8f6f4 v[82:85], v[14:19], v[38:43], v[82:85], v128, v144 op_sel_hi:[0,0,0] cbsz:2 blgp:2
	s_nop 1
	v_mfma_scale_f32_16x16x128_f8f6f4 v[74:77], v[20:25], v[38:43], v[74:77], v132, v144 op_sel_hi:[0,0,0] cbsz:2 blgp:2
	s_nop 1
	v_mfma_scale_f32_16x16x128_f8f6f4 v[66:69], v[14:19], v[44:49], v[66:69], v128, v148 op_sel_hi:[0,0,0] cbsz:2 blgp:2
	s_nop 1
	v_mfma_scale_f32_16x16x128_f8f6f4 v[54:57], v[20:25], v[44:49], v[54:57], v132, v148 op_sel_hi:[0,0,0] cbsz:2 blgp:2
	s_setprio 0
	s_barrier
	s_mov_b32 m0, s45
	s_nop 0
	global_load_lds_dwordx4 v153, s[50:51]
	s_mov_b32 m0, s62
	s_nop 0
	global_load_lds_dwordx4 v154, s[50:51]
	s_add_u32 s50, s46, 0x40200
	s_addc_u32 s51, s47, 0
	s_mov_b32 m0, s63
	s_nop 0
	global_load_lds_dwordx4 v153, s[50:51]
	s_mov_b32 m0, s64
	s_nop 0
	global_load_lds_dwordx4 v154, s[50:51]
	s_mov_b32 m0, s17
	s_nop 0
	global_load_lds_dwordx4 v50, s[34:35]
	s_mov_b32 m0, s65
	s_nop 0
	global_load_lds_dwordx4 v51, s[34:35]
	s_waitcnt vmcnt(6)
	s_waitcnt lgkmcnt(0)
	s_barrier
	s_barrier
	ds_read_b128 v[2:5], v164
	ds_read_b128 v[118:121], v164 offset:1024
	ds_read_b128 v[8:11], v164 offset:2048
	ds_read_b128 v[122:125], v164 offset:3072
	ds_read_b128 v[14:17], v165
	ds_read_b128 v[126:129], v165 offset:1024
	ds_read_b128 v[20:23], v165 offset:2048
	ds_read_b128 v[130:133], v165 offset:3072
	ds_read_b128 v[26:29], v160 offset:32768
	ds_read_b128 v[134:137], v160 offset:33792
	ds_read_b128 v[32:35], v160 offset:34816
	ds_read_b128 v[138:141], v160 offset:35840
	ds_read_b128 v[38:41], v160 offset:36864
	ds_read_b128 v[142:145], v160 offset:37888
	ds_read_b128 v[44:47], v160 offset:38912
	ds_read_b128 v[146:149], v160 offset:39936
	s_waitcnt vmcnt(6)
	s_waitcnt lgkmcnt(0)
	s_barrier
; #define LAS __attribute__((address_space(3)))
; #define PG8_STAGEB(bufoff, gbase) PG8_STAGE2(bufoff, gbase, voffB[0], voffB[1])
; #define PG8_STAGEA(bufoff, gbase, h) PG8_STAGE2(bufoff, gbase, voffA[h][0], voffA[h][1])
; #define PG8_STAGEAS(bufoff, gbase, h) PG8_STAGE2(bufoff, gbase, voffA[h][0], voffA[h][1])
; #define PG8_LDA(dst, b, h) do { _Pragma("unroll") for (int m = 0; m < 4; ++m) _Pragma("unroll") for (int k = 0; k < 2; ++k) dst[m][k] = *(const LAS bf16x8*)(lds + PG8_SA(b, h) + aoff + m * 2048 + k * 1024); } while (0)
; #define PG8_LDB(dst, b, h) do { _Pragma("unroll") for (int n = 0; n < 2; ++n) _Pragma("unroll") for (int k = 0; k < 2; ++k) dst[n][k] = *(const LAS bf16x8*)(lds + PG8_SB(b, h) + boff + n * 2048 + k * 1024); } while (0)
; #define PG8_WAIT_K() do { if constexpr (HM) PG8_WAIT_V(6); else PG8_WAIT_V(8); } while (0)
; #define PG8_WAIT_K0() do { if (EST > 0 && t == 0 && ui > 0) asm volatile("s_waitcnt vmcnt(%0)" :: "n"((HM ? 6 : 8) + EST) : "memory"); else PG8_WAIT_K(); } while (0)
; #define PG8_BAR __builtin_amdgcn_s_barrier()
;     ...
;             PG8_LDB(B0, 0, 0); PG8_LDB(B1, 0, 1); PG8_SCHED; PG8_LDA(At, 0, 0); if constexpr (!HM) PG8_STAGEA(PG8_SA(1, 1), a1, 1);
;             if constexpr (Sched::kGather) { if (last && has_next) { const u32x4 tn = *(const LAS u32x4*)(S.aux + tid * 16); voffA[0][0] = tn.x; voffA[0][1] = tn.y; voffA[1][0] = tn.z; voffA[1][1] = tn.w; } }
;             PG8_WAIT_K0(); PG8_WAIT_L(0); PG8_BAR; PG8_MMA(0, 0, At, B0); PG8_MMA(0, 1, At, B1); PG8_BAR; PG8_SCHED;
;             if constexpr (!HM) PG8_LDA(At, 0, 1);
;             PG8_STAGEB(PG8_SB(0, 0), b2); PG8_STAGEB(PG8_SB(0, 1), b2 + hstepB); PG8_STAGEAS(PG8_SA(0, 0), a2, 0);
;             PG8_WAIT_K0(); PG8_WAIT_L(0); PG8_BAR; if constexpr (!HM) { PG8_MMA(1, 0, At, B0); PG8_MMA(1, 1, At, B1); } PG8_BAR; PG8_SCHED;
;             PG8_LDB(B0, 1, 0); PG8_LDB(B1, 1, 1); PG8_SCHED; PG8_LDA(At, 1, 0); if constexpr (!HM) PG8_STAGEAS(PG8_SA(0, 1), a2, 1);
;             PG8_WAIT_K(); PG8_WAIT_L(0); PG8_BAR; PG8_MMA(0, 0, At, B0); PG8_MMA(0, 1, At, B1); PG8_BAR; PG8_SCHED;
;             if constexpr (!HM) PG8_LDA(At, 1, 1);
;             PG8_STAGEB(PG8_SB(1, 0), b3); PG8_STAGEB(PG8_SB(1, 1), b3 + hstepB); PG8_STAGEAS(PG8_SA(1, 0), a3, 0);
;             PG8_WAIT_K(); PG8_WAIT_L(0); PG8_BAR; if constexpr (!HM) { PG8_MMA(1, 0, At, B0); PG8_MMA(1, 1, At, B1); } PG8_BAR; PG8_SCHED;
	s_setprio 1
	s_waitcnt lgkmcnt(6)
	v_mov_b32_e32 v30, v134
	v_mov_b32_e32 v31, v135
	v_mov_b32_e32 v6, v118
	v_mov_b32_e32 v7, v119
	s_nop 1
	v_mfma_scale_f32_16x16x128_f8f6f4 v[106:109], v[2:7], v[26:31], v[106:109], v120, v136 op_sel_hi:[0,0,0] cbsz:2 blgp:2
	v_mov_b32_e32 v12, v122
	v_mov_b32_e32 v13, v123
	s_nop 1
	v_mfma_scale_f32_16x16x128_f8f6f4 v[102:105], v[8:13], v[26:31], v[102:105], v124, v136 op_sel_hi:[0,0,0] cbsz:2 blgp:2
	s_waitcnt lgkmcnt(4)
	v_mov_b32_e32 v36, v138
	v_mov_b32_e32 v37, v139
	s_nop 1
	v_mfma_scale_f32_16x16x128_f8f6f4 v[90:93], v[2:7], v[32:37], v[90:93], v120, v140 op_sel_hi:[0,0,0] cbsz:2 blgp:2
	s_nop 1
	v_mfma_scale_f32_16x16x128_f8f6f4 v[86:89], v[8:13], v[32:37], v[86:89], v124, v140 op_sel_hi:[0,0,0] cbsz:2 blgp:2
	s_waitcnt lgkmcnt(2)
	v_mov_b32_e32 v42, v142
	v_mov_b32_e32 v43, v143
	s_nop 1
	v_mfma_scale_f32_16x16x128_f8f6f4 v[78:81], v[2:7], v[38:43], v[78:81], v120, v144 op_sel_hi:[0,0,0] cbsz:2 blgp:2
	s_nop 1
	v_mfma_scale_f32_16x16x128_f8f6f4 v[70:73], v[8:13], v[38:43], v[70:73], v124, v144 op_sel_hi:[0,0,0] cbsz:2 blgp:2
	s_waitcnt lgkmcnt(0)
	v_mov_b32_e32 v48, v146
	v_mov_b32_e32 v49, v147
	s_nop 1
	v_mfma_scale_f32_16x16x128_f8f6f4 v[62:65], v[2:7], v[44:49], v[62:65], v120, v148 op_sel_hi:[0,0,0] cbsz:2 blgp:2
	s_nop 1
	v_mfma_scale_f32_16x16x128_f8f6f4 v[58:61], v[8:13], v[44:49], v[58:61], v124, v148 op_sel_hi:[0,0,0] cbsz:2 blgp:2
	s_setprio 0
	s_setprio 1
	v_mov_b32_e32 v18, v126
	v_mov_b32_e32 v19, v127
	s_nop 1
	v_mfma_scale_f32_16x16x128_f8f6f4 v[114:117], v[14:19], v[26:31], v[114:117], v128, v136 op_sel_hi:[0,0,0] cbsz:2 blgp:2
	v_mov_b32_e32 v24, v130
	v_mov_b32_e32 v25, v131
	s_nop 1
	v_mfma_scale_f32_16x16x128_f8f6f4 v[110:113], v[20:25], v[26:31], v[110:113], v132, v136 op_sel_hi:[0,0,0] cbsz:2 blgp:2
	s_nop 1
	v_mfma_scale_f32_16x16x128_f8f6f4 v[98:101], v[14:19], v[32:37], v[98:101], v128, v140 op_sel_hi:[0,0,0] cbsz:2 blgp:2
	s_nop 1
	v_mfma_scale_f32_16x16x128_f8f6f4 v[94:97], v[20:25], v[32:37], v[94:97], v132, v140 op_sel_hi:[0,0,0] cbsz:2 blgp:2
	s_nop 1
	v_mfma_scale_f32_16x16x128_f8f6f4 v[82:85], v[14:19], v[38:43], v[82:85], v128, v144 op_sel_hi:[0,0,0] cbsz:2 blgp:2
	s_nop 1
	v_mfma_scale_f32_16x16x128_f8f6f4 v[74:77], v[20:25], v[38:43], v[74:77], v132, v144 op_sel_hi:[0,0,0] cbsz:2 blgp:2
	s_nop 1
	v_mfma_scale_f32_16x16x128_f8f6f4 v[66:69], v[14:19], v[44:49], v[66:69], v128, v148 op_sel_hi:[0,0,0] cbsz:2 blgp:2
	s_nop 1
	v_mfma_scale_f32_16x16x128_f8f6f4 v[54:57], v[20:25], v[44:49], v[54:57], v132, v148 op_sel_hi:[0,0,0] cbsz:2 blgp:2
	s_setprio 0
	s_barrier
	s_mov_b32 m0, s66
	s_nop 0
	global_load_lds_dwordx4 v153, s[48:49]
	s_mov_b32 m0, s67
	s_nop 0
	global_load_lds_dwordx4 v154, s[48:49]
	s_add_u32 s48, s46, 0x40280
	s_addc_u32 s49, s47, 0
	s_mov_b32 m0, s70
	s_nop 0
	global_load_lds_dwordx4 v153, s[48:49]
	s_mov_b32 m0, s71
	s_nop 0
	global_load_lds_dwordx4 v154, s[48:49]
	s_mov_b32 m0, s68
	s_nop 0
	global_load_lds_dwordx4 v50, s[36:37]
	s_mov_b32 m0, s69
	s_nop 0
	global_load_lds_dwordx4 v51, s[36:37]
	s_waitcnt vmcnt(6)
	s_waitcnt lgkmcnt(0)
	s_barrier
	s_barrier
	s_mov_b32 s39, 2
	s_mov_b64 s[48:49], 0x300
	s_branch .LBB0_1188
.LBB0_1187:
	s_and_b64 s[50:51], s[52:53], exec
	s_cselect_b32 s50, 0, s48
	s_cselect_b32 s41, 0, s49
	s_add_u32 s56, s0, s50
	s_addc_u32 s57, s1, s41
	s_add_u32 s41, s46, s48
	s_addc_u32 s54, s47, s49
	s_add_u32 s50, s56, 0x80
	s_addc_u32 s51, s57, 0
	s_waitcnt vmcnt(6)
	s_and_b64 s[52:53], s[52:53], exec
	s_waitcnt lgkmcnt(0)
	s_cselect_b32 s52, s42, s41
	s_cselect_b32 s53, s43, s54
	s_add_u32 s54, s52, 0x80
	s_addc_u32 s55, s53, 0
	s_barrier
	s_setprio 1
	s_waitcnt lgkmcnt(6)
	v_mov_b32_e32 v36, v138
	v_mov_b32_e32 v37, v139
	v_mov_b32_e32 v48, v146
	v_mov_b32_e32 v49, v147
	s_nop 1
	v_mfma_scale_f32_16x16x128_f8f6f4 v[106:109], v[44:49], v[32:37], v[106:109], v148, v140 op_sel_hi:[0,0,0] cbsz:2 blgp:2
	v_mov_b32_e32 v42, v142
	v_mov_b32_e32 v43, v143
	s_nop 1
	v_mfma_scale_f32_16x16x128_f8f6f4 v[102:105], v[38:43], v[32:37], v[102:105], v144, v140 op_sel_hi:[0,0,0] cbsz:2 blgp:2
	s_waitcnt lgkmcnt(4)
	v_mov_b32_e32 v30, v134
	v_mov_b32_e32 v31, v135
	s_nop 1
	v_mfma_scale_f32_16x16x128_f8f6f4 v[90:93], v[44:49], v[26:31], v[90:93], v148, v136 op_sel_hi:[0,0,0] cbsz:2 blgp:2
	s_nop 1
	v_mfma_scale_f32_16x16x128_f8f6f4 v[86:89], v[38:43], v[26:31], v[86:89], v144, v136 op_sel_hi:[0,0,0] cbsz:2 blgp:2
	s_waitcnt lgkmcnt(2)
	v_mov_b32_e32 v24, v130
	v_mov_b32_e32 v25, v131
	s_nop 1
	v_mfma_scale_f32_16x16x128_f8f6f4 v[78:81], v[44:49], v[20:25], v[78:81], v148, v132 op_sel_hi:[0,0,0] cbsz:2 blgp:2
	s_nop 1
	v_mfma_scale_f32_16x16x128_f8f6f4 v[70:73], v[38:43], v[20:25], v[70:73], v144, v132 op_sel_hi:[0,0,0] cbsz:2 blgp:2
	s_waitcnt lgkmcnt(0)
	v_mov_b32_e32 v18, v126
	v_mov_b32_e32 v19, v127
	s_nop 1
	v_mfma_scale_f32_16x16x128_f8f6f4 v[62:65], v[44:49], v[14:19], v[62:65], v148, v128 op_sel_hi:[0,0,0] cbsz:2 blgp:2
	s_nop 1
	v_mfma_scale_f32_16x16x128_f8f6f4 v[58:61], v[38:43], v[14:19], v[58:61], v144, v128 op_sel_hi:[0,0,0] cbsz:2 blgp:2
	s_setprio 0
	s_setprio 1
	v_mov_b32_e32 v12, v122
	v_mov_b32_e32 v13, v123
	s_nop 1
	v_mfma_scale_f32_16x16x128_f8f6f4 v[114:117], v[8:13], v[32:37], v[114:117], v124, v140 op_sel_hi:[0,0,0] cbsz:2 blgp:2
	v_mov_b32_e32 v6, v118
	v_mov_b32_e32 v7, v119
	s_nop 1
	v_mfma_scale_f32_16x16x128_f8f6f4 v[110:113], v[2:7], v[32:37], v[110:113], v120, v140 op_sel_hi:[0,0,0] cbsz:2 blgp:2
	s_nop 1
	v_mfma_scale_f32_16x16x128_f8f6f4 v[98:101], v[8:13], v[26:31], v[98:101], v124, v136 op_sel_hi:[0,0,0] cbsz:2 blgp:2
	s_nop 1
	v_mfma_scale_f32_16x16x128_f8f6f4 v[94:97], v[2:7], v[26:31], v[94:97], v120, v136 op_sel_hi:[0,0,0] cbsz:2 blgp:2
	s_nop 1
	v_mfma_scale_f32_16x16x128_f8f6f4 v[82:85], v[8:13], v[20:25], v[82:85], v124, v132 op_sel_hi:[0,0,0] cbsz:2 blgp:2
	s_nop 1
	v_mfma_scale_f32_16x16x128_f8f6f4 v[74:77], v[2:7], v[20:25], v[74:77], v120, v132 op_sel_hi:[0,0,0] cbsz:2 blgp:2
	s_nop 1
	v_mfma_scale_f32_16x16x128_f8f6f4 v[66:69], v[8:13], v[14:19], v[66:69], v124, v128 op_sel_hi:[0,0,0] cbsz:2 blgp:2
	s_nop 1
	v_mfma_scale_f32_16x16x128_f8f6f4 v[54:57], v[2:7], v[14:19], v[54:57], v120, v128 op_sel_hi:[0,0,0] cbsz:2 blgp:2
	s_setprio 0
	s_barrier
; #define LAS __attribute__((address_space(3)))
; #define PG8_STAGEB(bufoff, gbase) PG8_STAGE2(bufoff, gbase, voffB[0], voffB[1])
; #define PG8_STAGEA(bufoff, gbase, h) PG8_STAGE2(bufoff, gbase, voffA[h][0], voffA[h][1])
; #define PG8_STAGEAS(bufoff, gbase, h) PG8_STAGE2(bufoff, gbase, voffA[h][0], voffA[h][1])
; #define PG8_LDA(dst, b, h) do { _Pragma("unroll") for (int m = 0; m < 4; ++m) _Pragma("unroll") for (int k = 0; k < 2; ++k) dst[m][k] = *(const LAS bf16x8*)(lds + PG8_SA(b, h) + aoff + m * 2048 + k * 1024); } while (0)
; #define PG8_LDB(dst, b, h) do { _Pragma("unroll") for (int n = 0; n < 2; ++n) _Pragma("unroll") for (int k = 0; k < 2; ++k) dst[n][k] = *(const LAS bf16x8*)(lds + PG8_SB(b, h) + boff + n * 2048 + k * 1024); } while (0)
; #define PG8_WAIT_K() do { if constexpr (HM) PG8_WAIT_V(6); else PG8_WAIT_V(8); } while (0)
; #define PG8_WAIT_K0() do { if (EST > 0 && t == 0 && ui > 0) asm volatile("s_waitcnt vmcnt(%0)" :: "n"((HM ? 6 : 8) + EST) : "memory"); else PG8_WAIT_K(); } while (0)
;     ...
;             PG8_LDB(B0, 0, 0); PG8_LDB(B1, 0, 1); PG8_SCHED; PG8_LDA(At, 0, 0); if constexpr (!HM) PG8_STAGEA(PG8_SA(1, 1), a1, 1);
;             if constexpr (Sched::kGather) { if (last && has_next) { const u32x4 tn = *(const LAS u32x4*)(S.aux + tid * 16); voffA[0][0] = tn.x; voffA[0][1] = tn.y; voffA[1][0] = tn.z; voffA[1][1] = tn.w; } }
;             PG8_WAIT_K0(); PG8_WAIT_L(0); PG8_BAR; PG8_MMA(0, 0, At, B0); PG8_MMA(0, 1, At, B1); PG8_BAR; PG8_SCHED;
;             if constexpr (!HM) PG8_LDA(At, 0, 1);
;             PG8_STAGEB(PG8_SB(0, 0), b2); PG8_STAGEB(PG8_SB(0, 1), b2 + hstepB); PG8_STAGEAS(PG8_SA(0, 0), a2, 0);
;             PG8_WAIT_K0(); PG8_WAIT_L(0); PG8_BAR; if constexpr (!HM) { PG8_MMA(1, 0, At, B0); PG8_MMA(1, 1, At, B1); } PG8_BAR; PG8_SCHED;
;             PG8_LDB(B0, 1, 0); PG8_LDB(B1, 1, 1); PG8_SCHED; PG8_LDA(At, 1, 0); if constexpr (!HM) PG8_STAGEAS(PG8_SA(0, 1), a2, 1);
;             PG8_WAIT_K(); PG8_WAIT_L(0); PG8_BAR; PG8_MMA(0, 0, At, B0); PG8_MMA(0, 1, At, B1); PG8_BAR; PG8_SCHED;
;             if constexpr (!HM) PG8_LDA(At, 1, 1);
;             PG8_STAGEB(PG8_SB(1, 0), b3); PG8_STAGEB(PG8_SB(1, 1), b3 + hstepB); PG8_STAGEAS(PG8_SA(1, 0), a3, 0);
;             PG8_WAIT_K(); PG8_WAIT_L(0); PG8_BAR; if constexpr (!HM) { PG8_MMA(1, 0, At, B0); PG8_MMA(1, 1, At, B1); } PG8_BAR; PG8_SCHED;
;         }
	s_mov_b32 m0, s45
	s_nop 0
	global_load_lds_dwordx4 v153, s[52:53]
	s_add_u32 s78, s52, 0x40000
	s_mov_b32 m0, s62
	s_nop 0
	global_load_lds_dwordx4 v154, s[52:53]
	s_addc_u32 s79, s53, 0
	s_mov_b32 m0, s63
	s_nop 0
	global_load_lds_dwordx4 v153, s[78:79]
	s_mov_b32 m0, s64
	s_nop 0
	global_load_lds_dwordx4 v154, s[78:79]
	s_mov_b32 m0, s17
	s_nop 0
	global_load_lds_dwordx4 v50, s[56:57]
	s_mov_b32 m0, s65
	s_nop 0
	global_load_lds_dwordx4 v51, s[56:57]
	s_waitcnt vmcnt(6)
	s_waitcnt lgkmcnt(0)
	s_barrier
	s_barrier
	ds_read_b128 v[2:5], v164
	ds_read_b128 v[118:121], v164 offset:1024
	ds_read_b128 v[8:11], v164 offset:2048
	ds_read_b128 v[122:125], v164 offset:3072
	ds_read_b128 v[14:17], v165
	ds_read_b128 v[126:129], v165 offset:1024
	ds_read_b128 v[20:23], v165 offset:2048
	ds_read_b128 v[130:133], v165 offset:3072
	ds_read_b128 v[26:29], v160 offset:32768
	ds_read_b128 v[134:137], v160 offset:33792
	ds_read_b128 v[32:35], v160 offset:34816
	ds_read_b128 v[138:141], v160 offset:35840
	ds_read_b128 v[38:41], v160 offset:36864
	ds_read_b128 v[142:145], v160 offset:37888
	ds_read_b128 v[44:47], v160 offset:38912
	ds_read_b128 v[146:149], v160 offset:39936
	s_waitcnt vmcnt(6)
	s_waitcnt lgkmcnt(0)
	s_barrier
	s_setprio 1
	s_waitcnt lgkmcnt(6)
	v_mov_b32_e32 v30, v134
	v_mov_b32_e32 v31, v135
	v_mov_b32_e32 v6, v118
	v_mov_b32_e32 v7, v119
	s_nop 1
	v_mfma_scale_f32_16x16x128_f8f6f4 v[106:109], v[2:7], v[26:31], v[106:109], v120, v136 op_sel_hi:[0,0,0] cbsz:2 blgp:2
	v_mov_b32_e32 v12, v122
	v_mov_b32_e32 v13, v123
	s_nop 1
	v_mfma_scale_f32_16x16x128_f8f6f4 v[102:105], v[8:13], v[26:31], v[102:105], v124, v136 op_sel_hi:[0,0,0] cbsz:2 blgp:2
	s_waitcnt lgkmcnt(4)
	v_mov_b32_e32 v36, v138
	v_mov_b32_e32 v37, v139
	s_nop 1
	v_mfma_scale_f32_16x16x128_f8f6f4 v[90:93], v[2:7], v[32:37], v[90:93], v120, v140 op_sel_hi:[0,0,0] cbsz:2 blgp:2
	s_nop 1
	v_mfma_scale_f32_16x16x128_f8f6f4 v[86:89], v[8:13], v[32:37], v[86:89], v124, v140 op_sel_hi:[0,0,0] cbsz:2 blgp:2
	s_waitcnt lgkmcnt(2)
	v_mov_b32_e32 v42, v142
	v_mov_b32_e32 v43, v143
	s_nop 1
	v_mfma_scale_f32_16x16x128_f8f6f4 v[78:81], v[2:7], v[38:43], v[78:81], v120, v144 op_sel_hi:[0,0,0] cbsz:2 blgp:2
	s_nop 1
	v_mfma_scale_f32_16x16x128_f8f6f4 v[70:73], v[8:13], v[38:43], v[70:73], v124, v144 op_sel_hi:[0,0,0] cbsz:2 blgp:2
	s_waitcnt lgkmcnt(0)
	v_mov_b32_e32 v48, v146
	v_mov_b32_e32 v49, v147
	s_nop 1
	v_mfma_scale_f32_16x16x128_f8f6f4 v[62:65], v[2:7], v[44:49], v[62:65], v120, v148 op_sel_hi:[0,0,0] cbsz:2 blgp:2
	s_nop 1
	v_mfma_scale_f32_16x16x128_f8f6f4 v[58:61], v[8:13], v[44:49], v[58:61], v124, v148 op_sel_hi:[0,0,0] cbsz:2 blgp:2
	s_setprio 0
	s_setprio 1
	v_mov_b32_e32 v18, v126
	v_mov_b32_e32 v19, v127
	s_nop 1
	v_mfma_scale_f32_16x16x128_f8f6f4 v[114:117], v[14:19], v[26:31], v[114:117], v128, v136 op_sel_hi:[0,0,0] cbsz:2 blgp:2
	v_mov_b32_e32 v24, v130
	v_mov_b32_e32 v25, v131
	s_nop 1
	v_mfma_scale_f32_16x16x128_f8f6f4 v[110:113], v[20:25], v[26:31], v[110:113], v132, v136 op_sel_hi:[0,0,0] cbsz:2 blgp:2
	s_nop 1
	v_mfma_scale_f32_16x16x128_f8f6f4 v[98:101], v[14:19], v[32:37], v[98:101], v128, v140 op_sel_hi:[0,0,0] cbsz:2 blgp:2
	s_nop 1
	v_mfma_scale_f32_16x16x128_f8f6f4 v[94:97], v[20:25], v[32:37], v[94:97], v132, v140 op_sel_hi:[0,0,0] cbsz:2 blgp:2
	s_nop 1
	v_mfma_scale_f32_16x16x128_f8f6f4 v[82:85], v[14:19], v[38:43], v[82:85], v128, v144 op_sel_hi:[0,0,0] cbsz:2 blgp:2
	s_nop 1
	v_mfma_scale_f32_16x16x128_f8f6f4 v[74:77], v[20:25], v[38:43], v[74:77], v132, v144 op_sel_hi:[0,0,0] cbsz:2 blgp:2
	s_nop 1
	v_mfma_scale_f32_16x16x128_f8f6f4 v[66:69], v[14:19], v[44:49], v[66:69], v128, v148 op_sel_hi:[0,0,0] cbsz:2 blgp:2
	s_nop 1
	v_mfma_scale_f32_16x16x128_f8f6f4 v[54:57], v[20:25], v[44:49], v[54:57], v132, v148 op_sel_hi:[0,0,0] cbsz:2 blgp:2
	s_setprio 0
	s_barrier
	s_mov_b32 m0, s66
	s_nop 0
	global_load_lds_dwordx4 v153, s[54:55]
	s_add_u32 s52, s52, 0x40080
	s_mov_b32 m0, s67
	s_nop 0
	global_load_lds_dwordx4 v154, s[54:55]
	s_addc_u32 s53, s53, 0
	s_mov_b32 m0, s70
	s_nop 0
	global_load_lds_dwordx4 v153, s[52:53]
	s_mov_b32 m0, s71
	s_nop 0
	global_load_lds_dwordx4 v154, s[52:53]
	s_mov_b32 m0, s68
	s_nop 0
	global_load_lds_dwordx4 v50, s[50:51]
	s_mov_b32 m0, s69
	s_nop 0
	global_load_lds_dwordx4 v51, s[50:51]
	s_waitcnt vmcnt(6)
	s_waitcnt lgkmcnt(0)
	s_barrier
	s_barrier
	s_add_i32 s39, s39, 2
	s_add_u32 s48, s48, 0x100
	s_addc_u32 s49, s49, 0
	s_cmp_gt_u32 s39, 13
	s_cbranch_scc1 .LBB0_1190

; #define LAS __attribute__((address_space(3)))
; __device__ __forceinline__ unsigned pk4_fp8(float a, float b, float c, float d) { int w = 0; w = __builtin_amdgcn_cvt_pk_fp8_f32(a, b, w, false); w = __builtin_amdgcn_cvt_pk_fp8_f32(c, d, w, true); return (unsigned)w; }
;     ...
;         if constexpr (FP8 >= 1) asm volatile("s_nop 15\n\ts_nop 15" ::: "memory");
;     __device__ __forceinline__ void operator()(const AccT& acc, const pg8::Unit& u, int wr, int wc, int fr, int fq, const LAS float* bl, int nai) const {
;         const int row0 = u.pm * 256 + u.hx * 128 + wr * 64 + fr, a0 = u.pn * 128 + wc * 32 + 8 * fq;
;         unsigned char* act = (unsigned char*)(ws + WS_ACT);
;         const f32x4 bg0 = *(const LAS f32x4*)(bl + 8 * fq), bg1 = *(const LAS f32x4*)(bl + 8 * fq + 4), bu0 = *(const LAS f32x4*)(bl + 32 + 8 * fq), bu1 = *(const LAS f32x4*)(bl + 32 + 8 * fq + 4);
; #pragma unroll
;         for (int ai = 0; ai < 2; ++ai) if (ai < nai)
; #pragma unroll
;             for (int m = 0; m < 4; ++m) { const size_t ro = (size_t)(row0 + ai * 128 + m * 16) * DFF + a0; float o[8];
; #pragma unroll
;                 for (int n = 0; n < 2; ++n) {
;                     f32x4 g4 = acc[ai][0][m][n] + (n ? bg1 : bg0), u4 = acc[ai][1][m][n] + (n ? bu1 : bu0);
; #pragma unroll
;                     for (int j = 0; j < 4; ++j) { g4[j] = fminf(g4[j], 7.0f); u4[j] = __builtin_amdgcn_fmed3f(u4[j], -7.0f, 7.0f); }
;                     const f32x4 t4 = g4 * (-1.702f * 1.4426950408889634f);
;                     f32x4 e4;
; #pragma unroll
;                     for (int j = 0; j < 4; ++j) e4[j] = __builtin_amdgcn_exp2f(t4[j]);
;                     e4 = e4 + 1.0f;
;                     f32x4 r4;
; #pragma unroll
;                     for (int j = 0; j < 4; ++j) r4[j] = __builtin_amdgcn_rcpf(e4[j]);
;                     const f32x4 o4 = (u4 * A8_SCALE + A8_SCALE) * (g4 * r4);
; #pragma unroll
;                     for (int j = 0; j < 4; ++j) o[4 * n + j] = o4[j]; }
;                 u32x2 w; w.x = pk4_fp8(o[0], o[1], o[2], o[3]); w.y = pk4_fp8(o[4], o[5], o[6], o[7]);
;                 *(u32x2*)(act + ro) = w; }
.LBB0_1192:
	s_nop 15
	s_nop 15
	ds_read_b128 v[14:17], v156
	ds_read_b128 v[6:9], v156 offset:16
	ds_read_b128 v[10:13], v156 offset:128
	ds_read_b128 v[2:5], v156 offset:144
	v_lshl_or_b32 v18, s44, 7, v158
	s_waitcnt lgkmcnt(3)
	v_pk_add_f32 v[22:23], v[108:109], v[16:17]
	v_pk_add_f32 v[24:25], v[106:107], v[14:15]
	v_min_f32_e32 v22, 0x40e00000, v22
	v_min_f32_e32 v24, 0x40e00000, v24
	v_min_f32_e32 v25, 0x40e00000, v25
	v_min_f32_e32 v23, 0x40e00000, v23
	v_mul_f32_e32 v21, 0xc01d265f, v24
	v_mul_f32_e32 v31, 0xc01d265f, v22
	v_exp_f32_e32 v30, v21
	v_mul_f32_e32 v21, 0xc01d265f, v25
	v_exp_f32_e32 v32, v31
	v_mul_f32_e32 v31, 0xc01d265f, v23
	v_exp_f32_e32 v33, v31
	v_exp_f32_e32 v31, v21
	s_waitcnt lgkmcnt(1)
	v_pk_add_f32 v[28:29], v[114:115], v[10:11]
	v_pk_add_f32 v[26:27], v[116:117], v[12:13]
	v_med3_f32 v21, v28, s73, v161
	v_pk_add_f32 v[30:31], v[30:31], 1.0 op_sel_hi:[1,0]
	v_med3_f32 v34, v29, s73, v161
	v_rcp_f32_e32 v30, v30
	v_rcp_f32_e32 v31, v31
	v_pk_add_f32 v[28:29], v[32:33], 1.0 op_sel_hi:[1,0]
	v_fma_f32 v21, v21, 4.0, 4.0
	v_rcp_f32_e32 v28, v28
	v_rcp_f32_e32 v29, v29
	v_pk_mul_f32 v[24:25], v[24:25], v[30:31]
	v_med3_f32 v26, v26, s73, v161
	v_mul_f32_e32 v21, v21, v24
	v_fma_f32 v24, v34, 4.0, 4.0
	v_med3_f32 v27, v27, s73, v161
	v_pk_mul_f32 v[22:23], v[22:23], v[28:29]
	v_mul_f32_e32 v34, v24, v25
	v_fma_f32 v24, v26, 4.0, 4.0
	v_mul_f32_e32 v35, v24, v22
	v_fma_f32 v22, v27, 4.0, 4.0
	v_mul_f32_e32 v36, v22, v23
	v_pk_add_f32 v[22:23], v[104:105], v[8:9]
	v_pk_add_f32 v[24:25], v[102:103], v[6:7]
	v_min_f32_e32 v22, 0x40e00000, v22
	v_min_f32_e32 v24, 0x40e00000, v24
	v_min_f32_e32 v25, 0x40e00000, v25
	v_min_f32_e32 v23, 0x40e00000, v23
	v_mul_f32_e32 v30, 0xc01d265f, v24
	v_mul_f32_e32 v31, 0xc01d265f, v25
	v_mul_f32_e32 v32, 0xc01d265f, v22
	v_mul_f32_e32 v33, 0xc01d265f, v23
	v_exp_f32_e32 v30, v30
	v_exp_f32_e32 v32, v32
	v_exp_f32_e32 v33, v33
	v_exp_f32_e32 v31, v31
	s_waitcnt lgkmcnt(0)
	v_pk_add_f32 v[28:29], v[110:111], v[2:3]
	v_pk_add_f32 v[26:27], v[112:113], v[4:5]
	v_med3_f32 v37, v28, s73, v161
	v_med3_f32 v38, v29, s73, v161
	v_pk_add_f32 v[28:29], v[32:33], 1.0 op_sel_hi:[1,0]
	v_pk_add_f32 v[30:31], v[30:31], 1.0 op_sel_hi:[1,0]
	v_rcp_f32_e32 v28, v28
	v_rcp_f32_e32 v30, v30
	v_rcp_f32_e32 v29, v29
	v_rcp_f32_e32 v31, v31
	v_med3_f32 v26, v26, s73, v161
	v_med3_f32 v27, v27, s73, v161
	v_pk_mul_f32 v[22:23], v[22:23], v[28:29]
	v_pk_mul_f32 v[24:25], v[24:25], v[30:31]
	v_fma_f32 v28, v37, 4.0, 4.0
	v_mul_f32_e32 v28, v28, v24
	v_fma_f32 v24, v38, 4.0, 4.0
	v_mul_f32_e32 v29, v24, v25
	v_fma_f32 v24, v26, 4.0, 4.0
	v_mul_f32_e32 v22, v24, v22
	v_mov_b32_e32 v24, 0
	v_mov_b32_e32 v25, 0
	v_cvt_pk_fp8_f32 v24, v21, v34
	v_cvt_pk_fp8_f32 v25, v28, v29
	v_fma_f32 v21, v27, 4.0, 4.0
	v_mul_f32_e32 v21, v21, v23
	v_lshl_add_u32 v20, s77, 8, v155
	v_cvt_pk_fp8_f32 v24, v35, v36 op_sel:[0,0,1]
	v_cvt_pk_fp8_f32 v25, v22, v21 op_sel:[0,0,1]
	v_ashrrev_i32_e32 v19, 31, v18
	v_ashrrev_i32_e32 v21, 31, v20
	v_lshl_add_u64 v[18:19], s[28:29], 0, v[18:19]
	v_lshlrev_b64 v[22:23], 11, v[20:21]
	v_lshl_add_u64 v[22:23], v[18:19], 0, v[22:23]
	v_pk_add_f32 v[26:27], v[90:91], v[14:15]
	global_store_dwordx2 v[22:23], v[24:25], off
	v_pk_add_f32 v[24:25], v[92:93], v[16:17]
	v_min_f32_e32 v26, 0x40e00000, v26
	v_min_f32_e32 v27, 0x40e00000, v27
	v_min_f32_e32 v24, 0x40e00000, v24
	v_mul_f32_e32 v21, 0xc01d265f, v26
	v_min_f32_e32 v25, 0x40e00000, v25
	v_exp_f32_e32 v32, v21
	v_mul_f32_e32 v21, 0xc01d265f, v27
	v_mul_f32_e32 v23, 0xc01d265f, v24
	v_exp_f32_e32 v34, v23
	v_mul_f32_e32 v23, 0xc01d265f, v25
	v_exp_f32_e32 v33, v21
	v_exp_f32_e32 v35, v23
	v_pk_add_f32 v[30:31], v[98:99], v[10:11]
	v_pk_add_f32 v[28:29], v[100:101], v[12:13]
	v_pk_add_f32 v[32:33], v[32:33], 1.0 op_sel_hi:[1,0]
	v_med3_f32 v21, v30, s73, v161
	v_med3_f32 v23, v31, s73, v161
	v_pk_add_f32 v[30:31], v[34:35], 1.0 op_sel_hi:[1,0]
	v_rcp_f32_e32 v32, v32
	v_rcp_f32_e32 v33, v33
	v_rcp_f32_e32 v30, v30
	v_rcp_f32_e32 v31, v31
	v_med3_f32 v28, v28, s73, v161
	v_pk_mul_f32 v[26:27], v[26:27], v[32:33]
	v_fma_f32 v21, v21, 4.0, 4.0
	v_med3_f32 v29, v29, s73, v161
	v_pk_mul_f32 v[24:25], v[24:25], v[30:31]
	v_mul_f32_e32 v21, v21, v26
	v_fma_f32 v26, v28, 4.0, 4.0
	v_fma_f32 v23, v23, 4.0, 4.0
	v_mul_f32_e32 v36, v26, v24
	v_fma_f32 v24, v29, 4.0, 4.0
	v_mul_f32_e32 v23, v23, v27
	v_mul_f32_e32 v37, v24, v25
	v_pk_add_f32 v[24:25], v[88:89], v[8:9]
	v_pk_add_f32 v[26:27], v[86:87], v[6:7]
	v_min_f32_e32 v24, 0x40e00000, v24
	v_min_f32_e32 v26, 0x40e00000, v26
	v_min_f32_e32 v27, 0x40e00000, v27
	v_min_f32_e32 v25, 0x40e00000, v25
	v_mul_f32_e32 v32, 0xc01d265f, v26
	v_mul_f32_e32 v33, 0xc01d265f, v27
	v_mul_f32_e32 v34, 0xc01d265f, v24
	v_mul_f32_e32 v35, 0xc01d265f, v25
	v_exp_f32_e32 v32, v32
	v_exp_f32_e32 v34, v34
	v_exp_f32_e32 v35, v35
	v_exp_f32_e32 v33, v33
	v_pk_add_f32 v[30:31], v[94:95], v[2:3]
	v_pk_add_f32 v[28:29], v[96:97], v[4:5]
	v_med3_f32 v38, v30, s73, v161
	v_med3_f32 v39, v31, s73, v161
	v_pk_add_f32 v[30:31], v[34:35], 1.0 op_sel_hi:[1,0]
	v_pk_add_f32 v[32:33], v[32:33], 1.0 op_sel_hi:[1,0]
	v_rcp_f32_e32 v30, v30
	v_rcp_f32_e32 v32, v32
	v_rcp_f32_e32 v31, v31
	v_rcp_f32_e32 v33, v33
	v_med3_f32 v28, v28, s73, v161
	v_med3_f32 v29, v29, s73, v161
	v_pk_mul_f32 v[24:25], v[24:25], v[30:31]
	v_pk_mul_f32 v[26:27], v[26:27], v[32:33]
	v_fma_f32 v30, v38, 4.0, 4.0
	v_mul_f32_e32 v30, v30, v26
	v_fma_f32 v26, v39, 4.0, 4.0
	v_mul_f32_e32 v31, v26, v27
	v_fma_f32 v26, v28, 4.0, 4.0
	v_mul_f32_e32 v24, v26, v24
	v_mov_b32_e32 v26, 0
	v_mov_b32_e32 v27, 0
	v_cvt_pk_fp8_f32 v26, v21, v23
	v_cvt_pk_fp8_f32 v27, v30, v31
; __device__ __forceinline__ unsigned pk4_fp8(float a, float b, float c, float d) { int w = 0; w = __builtin_amdgcn_cvt_pk_fp8_f32(a, b, w, false); w = __builtin_amdgcn_cvt_pk_fp8_f32(c, d, w, true); return (unsigned)w; }
;     __device__ __forceinline__ const char* bias_base(const pg8::Unit& u) const { return (const char*)(bgu + (size_t)u.e * 4096 + u.pn * 128); }
;     __device__ __forceinline__ unsigned bias_off(const pg8::Unit&, int wc, int lane) const { return (unsigned)(((lane >> 3) & 1) * 2048 + wc * 32 + (lane & 7) * 4) * 4u; }
;     ...
;         if (!has_next) break;
;         if constexpr (RSYNC) xcd_barrier(*rbar);
; #pragma unroll
;         for (int a = 0; a < 2; ++a)
; #pragma unroll
;             for (int b = 0; b < 2; ++b)
; #pragma unroll
;                 for (int m = 0; m < 4; ++m)
; #pragma unroll
;                     for (int n = 0; n < 2; ++n) acc[a][b][m][n] = (f32x4){0.f, 0.f, 0.f, 0.f};
;         cur = nxt; cA = nA; cB = nB; ++ui;
;         if constexpr (Epi::kBiasDMA) { if (lane < 16) glds16(E.bias_base(cur), E.bias_off(cur, wc, lane), bias_lds); }
;     __device__ __forceinline__ void operator()(const AccT& acc, const pg8::Unit& u, int wr, int wc, int fr, int fq, const LAS float* bl, int nai) const {
;     ...
;             for (int m = 0; m < 4; ++m) { const size_t ro = (size_t)(row0 + ai * 128 + m * 16) * DFF + a0; float o[8];
; #pragma unroll
;                 for (int n = 0; n < 2; ++n) {
;                     f32x4 g4 = acc[ai][0][m][n] + (n ? bg1 : bg0), u4 = acc[ai][1][m][n] + (n ? bu1 : bu0);
; #pragma unroll
;                     for (int j = 0; j < 4; ++j) { g4[j] = fminf(g4[j], 7.0f); u4[j] = __builtin_amdgcn_fmed3f(u4[j], -7.0f, 7.0f); }
;                     const f32x4 t4 = g4 * (-1.702f * 1.4426950408889634f);
;                     f32x4 e4;
; #pragma unroll
;                     for (int j = 0; j < 4; ++j) e4[j] = __builtin_amdgcn_exp2f(t4[j]);
;                     e4 = e4 + 1.0f;
;                     f32x4 r4;
; #pragma unroll
;                     for (int j = 0; j < 4; ++j) r4[j] = __builtin_amdgcn_rcpf(e4[j]);
;                     const f32x4 o4 = (u4 * A8_SCALE + A8_SCALE) * (g4 * r4);
; #pragma unroll
;                     for (int j = 0; j < 4; ++j) o[4 * n + j] = o4[j]; }
;                 u32x2 w; w.x = pk4_fp8(o[0], o[1], o[2], o[3]); w.y = pk4_fp8(o[4], o[5], o[6], o[7]);
;                 *(u32x2*)(act + ro) = w; }
	v_fma_f32 v21, v29, 4.0, 4.0
	v_mul_f32_e32 v21, v21, v25
	v_or_b32_e32 v22, 16, v20
	v_cvt_pk_fp8_f32 v26, v36, v37 op_sel:[0,0,1]
	v_cvt_pk_fp8_f32 v27, v24, v21 op_sel:[0,0,1]
	v_ashrrev_i32_e32 v23, 31, v22
	v_lshlrev_b64 v[22:23], 11, v[22:23]
	v_lshl_add_u64 v[22:23], v[18:19], 0, v[22:23]
	global_store_dwordx2 v[22:23], v[26:27], off
	v_pk_add_f32 v[26:27], v[78:79], v[14:15]
	v_pk_add_f32 v[24:25], v[80:81], v[16:17]
	v_min_f32_e32 v26, 0x40e00000, v26
	v_min_f32_e32 v27, 0x40e00000, v27
	v_min_f32_e32 v24, 0x40e00000, v24
	v_mul_f32_e32 v21, 0xc01d265f, v26
	v_min_f32_e32 v25, 0x40e00000, v25
	v_exp_f32_e32 v32, v21
	v_mul_f32_e32 v21, 0xc01d265f, v27
	v_mul_f32_e32 v23, 0xc01d265f, v24
	v_exp_f32_e32 v34, v23
	v_mul_f32_e32 v23, 0xc01d265f, v25
	v_exp_f32_e32 v33, v21
	v_exp_f32_e32 v35, v23
	v_pk_add_f32 v[30:31], v[82:83], v[10:11]
	v_pk_add_f32 v[28:29], v[84:85], v[12:13]
	v_pk_add_f32 v[32:33], v[32:33], 1.0 op_sel_hi:[1,0]
	v_med3_f32 v21, v30, s73, v161
	v_med3_f32 v23, v31, s73, v161
	v_pk_add_f32 v[30:31], v[34:35], 1.0 op_sel_hi:[1,0]
	v_rcp_f32_e32 v32, v32
	v_rcp_f32_e32 v33, v33
	v_rcp_f32_e32 v30, v30
	v_rcp_f32_e32 v31, v31
	v_med3_f32 v28, v28, s73, v161
	v_pk_mul_f32 v[26:27], v[26:27], v[32:33]
	v_fma_f32 v21, v21, 4.0, 4.0
	v_med3_f32 v29, v29, s73, v161
	v_pk_mul_f32 v[24:25], v[24:25], v[30:31]
	v_mul_f32_e32 v21, v21, v26
	v_fma_f32 v26, v28, 4.0, 4.0
	v_fma_f32 v23, v23, 4.0, 4.0
	v_mul_f32_e32 v36, v26, v24
	v_fma_f32 v24, v29, 4.0, 4.0
	v_mul_f32_e32 v23, v23, v27
	v_mul_f32_e32 v37, v24, v25
	v_pk_add_f32 v[24:25], v[72:73], v[8:9]
	v_pk_add_f32 v[26:27], v[70:71], v[6:7]
	v_min_f32_e32 v24, 0x40e00000, v24
	v_min_f32_e32 v26, 0x40e00000, v26
	v_min_f32_e32 v27, 0x40e00000, v27
	v_min_f32_e32 v25, 0x40e00000, v25
	v_mul_f32_e32 v32, 0xc01d265f, v26
	v_mul_f32_e32 v33, 0xc01d265f, v27
	v_mul_f32_e32 v34, 0xc01d265f, v24
	v_mul_f32_e32 v35, 0xc01d265f, v25
	v_exp_f32_e32 v32, v32
	v_exp_f32_e32 v34, v34
	v_exp_f32_e32 v35, v35
	v_exp_f32_e32 v33, v33
	v_pk_add_f32 v[30:31], v[74:75], v[2:3]
	v_pk_add_f32 v[28:29], v[76:77], v[4:5]
	v_med3_f32 v38, v30, s73, v161
	v_med3_f32 v39, v31, s73, v161
	v_pk_add_f32 v[30:31], v[34:35], 1.0 op_sel_hi:[1,0]
	v_pk_add_f32 v[32:33], v[32:33], 1.0 op_sel_hi:[1,0]
	v_rcp_f32_e32 v30, v30
	v_rcp_f32_e32 v32, v32
	v_rcp_f32_e32 v31, v31
	v_rcp_f32_e32 v33, v33
	v_med3_f32 v28, v28, s73, v161
	v_med3_f32 v29, v29, s73, v161
	v_pk_mul_f32 v[24:25], v[24:25], v[30:31]
	v_pk_mul_f32 v[26:27], v[26:27], v[32:33]
	v_fma_f32 v30, v38, 4.0, 4.0
	v_mul_f32_e32 v30, v30, v26
	v_fma_f32 v26, v39, 4.0, 4.0
	v_mul_f32_e32 v31, v26, v27
	v_fma_f32 v26, v28, 4.0, 4.0
	v_mul_f32_e32 v24, v26, v24
	v_mov_b32_e32 v26, 0
	v_mov_b32_e32 v27, 0
	v_cvt_pk_fp8_f32 v26, v21, v23
	v_cvt_pk_fp8_f32 v27, v30, v31
	v_fma_f32 v21, v29, 4.0, 4.0
	v_mul_f32_e32 v21, v21, v25
	v_or_b32_e32 v22, 32, v20
	v_cvt_pk_fp8_f32 v26, v36, v37 op_sel:[0,0,1]
	v_cvt_pk_fp8_f32 v27, v24, v21 op_sel:[0,0,1]
	v_ashrrev_i32_e32 v23, 31, v22
	v_lshlrev_b64 v[22:23], 11, v[22:23]
	v_pk_add_f32 v[16:17], v[64:65], v[16:17]
	v_pk_add_f32 v[14:15], v[62:63], v[14:15]
	v_lshl_add_u64 v[22:23], v[18:19], 0, v[22:23]
	v_min_f32_e32 v14, 0x40e00000, v14
	v_min_f32_e32 v16, 0x40e00000, v16
	global_store_dwordx2 v[22:23], v[26:27], off
	v_min_f32_e32 v15, 0x40e00000, v15
	v_min_f32_e32 v17, 0x40e00000, v17
	v_mul_f32_e32 v21, 0xc01d265f, v14
	v_mul_f32_e32 v23, 0xc01d265f, v16
	v_exp_f32_e32 v22, v21
	v_mul_f32_e32 v21, 0xc01d265f, v15
	v_exp_f32_e32 v24, v23
	v_mul_f32_e32 v23, 0xc01d265f, v17
	v_exp_f32_e32 v25, v23
	v_exp_f32_e32 v23, v21
	v_pk_add_f32 v[10:11], v[66:67], v[10:11]
	v_pk_add_f32 v[12:13], v[68:69], v[12:13]
	v_med3_f32 v21, v10, s73, v161
	v_pk_add_f32 v[22:23], v[22:23], 1.0 op_sel_hi:[1,0]
	v_med3_f32 v26, v11, s73, v161
	v_rcp_f32_e32 v22, v22
	v_rcp_f32_e32 v23, v23
	v_pk_add_f32 v[10:11], v[24:25], 1.0 op_sel_hi:[1,0]
	v_med3_f32 v24, v12, s73, v161
	v_rcp_f32_e32 v10, v10
	v_rcp_f32_e32 v11, v11
	v_med3_f32 v25, v13, s73, v161
	v_pk_mul_f32 v[12:13], v[14:15], v[22:23]
	v_fma_f32 v14, v21, 4.0, 4.0
	v_mul_f32_e32 v14, v14, v12
	v_fma_f32 v12, v26, 4.0, 4.0
	v_pk_mul_f32 v[10:11], v[16:17], v[10:11]
	v_mul_f32_e32 v15, v12, v13
	v_fma_f32 v12, v24, 4.0, 4.0
	v_pk_add_f32 v[6:7], v[58:59], v[6:7]
	v_mul_f32_e32 v16, v12, v10
	v_fma_f32 v10, v25, 4.0, 4.0
	v_min_f32_e32 v6, 0x40e00000, v6
	v_min_f32_e32 v7, 0x40e00000, v7
	v_mul_f32_e32 v17, v10, v11
	v_pk_add_f32 v[8:9], v[60:61], v[8:9]
	v_mul_f32_e32 v10, 0xc01d265f, v6
	v_mul_f32_e32 v11, 0xc01d265f, v7
	v_min_f32_e32 v8, 0x40e00000, v8
	v_min_f32_e32 v9, 0x40e00000, v9
	v_exp_f32_e32 v10, v10
	v_exp_f32_e32 v11, v11
	v_mul_f32_e32 v12, 0xc01d265f, v8
	v_mul_f32_e32 v13, 0xc01d265f, v9
	v_exp_f32_e32 v12, v12
	v_exp_f32_e32 v13, v13
	v_pk_add_f32 v[10:11], v[10:11], 1.0 op_sel_hi:[1,0]
	v_pk_add_f32 v[2:3], v[54:55], v[2:3]
	v_rcp_f32_e32 v10, v10
	v_rcp_f32_e32 v11, v11
	v_med3_f32 v21, v2, s73, v161
	v_med3_f32 v22, v3, s73, v161
	v_pk_add_f32 v[2:3], v[12:13], 1.0 op_sel_hi:[1,0]
	v_pk_add_f32 v[4:5], v[56:57], v[4:5]
	v_rcp_f32_e32 v2, v2
	v_rcp_f32_e32 v3, v3
	v_med3_f32 v12, v4, s73, v161
	v_med3_f32 v13, v5, s73, v161
	v_pk_mul_f32 v[4:5], v[6:7], v[10:11]
	v_fma_f32 v6, v21, 4.0, 4.0
	v_mul_f32_e32 v6, v6, v4
	v_fma_f32 v4, v22, 4.0, 4.0
	v_pk_mul_f32 v[2:3], v[8:9], v[2:3]
	v_mul_f32_e32 v7, v4, v5
	v_fma_f32 v4, v12, 4.0, 4.0
	v_mul_f32_e32 v2, v4, v2
	v_mov_b32_e32 v4, 0
	v_mov_b32_e32 v5, 0
	v_cvt_pk_fp8_f32 v4, v14, v15
	v_cvt_pk_fp8_f32 v5, v6, v7
	v_fma_f32 v6, v13, 4.0, 4.0
	v_mul_f32_e32 v3, v6, v3
	v_or_b32_e32 v20, 48, v20
	v_cvt_pk_fp8_f32 v4, v16, v17 op_sel:[0,0,1]
	v_cvt_pk_fp8_f32 v5, v2, v3 op_sel:[0,0,1]
	v_ashrrev_i32_e32 v21, 31, v20
	v_lshlrev_b64 v[2:3], 11, v[20:21]
	v_lshl_add_u64 v[2:3], v[18:19], 0, v[2:3]
	s_and_b64 vcc, exec, s[8:9]
	s_mov_b64 s[8:9], -1
	global_store_dwordx2 v[2:3], v[4:5], off
	s_cbranch_vccnz .LBB0_1165
	s_and_saveexec_b64 s[8:9], s[6:7]
	s_cbranch_execz .LBB0_1195
	s_ashr_i32 s39, s38, 31
	s_lshl_b64 s[10:11], s[38:39], 14
	s_add_u32 s39, s22, s10
	s_addc_u32 s41, s23, s11
	s_lshl_b32 s10, s40, 7
	s_ashr_i32 s11, s10, 31
	s_lshl_b64 s[10:11], s[10:11], 2
	s_add_u32 s10, s39, s10
	s_addc_u32 s11, s41, s11
	s_mov_b32 m0, s59
	s_nop 0
	global_load_lds_dwordx4 v157, s[10:11]

;     __device__ __forceinline__ const char* a_base(const Unit& u) const { return (const char*)A + (size_t)u.pm * BM * lda * 2; }
;     __device__ __forceinline__ const char* b_base(const Unit& u) const { return (const char*)Bt + (size_t)u.pn * BM * K * 2; }
;     __device__ __forceinline__ const char* b_base(const Unit& u) const { return (const char*)Bt + ((size_t)u.e * NB + (size_t)u.pn * BM) * K * 2; }
; #define PG8_STAGEB(bufoff, gbase) PG8_STAGE2(bufoff, gbase, voffB[0], voffB[1])
; #define PG8_STAGEA(bufoff, gbase, h) PG8_STAGE2(bufoff, gbase, voffA[h][0], voffA[h][1])
; #define PG8_BAR __builtin_amdgcn_s_barrier()
;     __device__ __forceinline__ const char* bias_base(const pg8::Unit& u) const { return (const char*)(bgu + (size_t)u.e * 4096 + u.pn * 128); }
;     __device__ __forceinline__ unsigned bias_off(const pg8::Unit&, int wc, int lane) const { return (unsigned)(((lane >> 3) & 1) * 2048 + wc * 32 + (lane & 7) * 4) * 4u; }
;     ...
;     const char* cA = S.a_base(cur); const char* cB = S.b_base(cur);
;     const unsigned bias_lds = (unsigned)__builtin_amdgcn_readfirstlane((int)((unsigned)(size_t)lds + (unsigned)(AUX_OFF + 8192) + (unsigned)wid * 256u));
;     if constexpr (Epi::kBiasDMA) { if (lane < 16) glds16(E.bias_base(cur), E.bias_off(cur, wc, lane), bias_lds); }
;     const unsigned rowid_lds = (unsigned)__builtin_amdgcn_readfirstlane((int)((unsigned)(size_t)lds + (unsigned)AUX_OFF + (unsigned)wid * 512u));
;     if constexpr (Epi::kRowDMA) { if (lane < 32) glds16(E.row_base(cur), E.row_off(cur, wr, lane), rowid_lds); }
;     PG8_STAGEB(PG8_SB(0, 0), cB); PG8_STAGEB(PG8_SB(0, 1), cB + hstepB); PG8_STAGEA(PG8_SA(0, 0), cA, 0); if constexpr (!HM) PG8_STAGEA(PG8_SA(0, 1), cA, 1);
;     if (wr == 1) PG8_BAR;
;     __device__ __forceinline__ const char* bias_base(const pg8::Unit& u) const { return (const char*)(bdn + (size_t)u.e * D + u.pn * 256); }
;     __device__ __forceinline__ unsigned bias_off(const pg8::Unit&, int wc, int lane) const { return (unsigned)(wc * 64 + lane * 4) * 4u; }
;     __device__ __forceinline__ const char* row_base(const pg8::Unit& u) const { return (const char*)((const int*)(ws + WS_ROWTOK) + (size_t)u.e * T + u.mt * 256 + u.hx * 128); }
;     __device__ __forceinline__ unsigned row_off(const pg8::Unit&, int wr, int lane) const { return (unsigned)(((lane >> 4) & 1) * 128 + wr * 64 + (lane & 15) * 4) * 4u; }
.LBB0_1271:
	s_add_u32 s23, s94, 0x6f700000
	s_addc_u32 s33, s95, 0
	s_add_u32 s44, s94, 0x24600000
	s_addc_u32 s45, s95, 0
	s_add_u32 s46, s94, 0x6f500000
	s_addc_u32 s47, s95, 0
	s_ashr_i32 s48, s2, 31
	s_add_u32 s4, s94, 0x81700000
	s_addc_u32 s5, s95, 0
	s_andn2_b64 vcc, exec, s[6:7]
	s_cbranch_vccnz .LBB0_1317
	s_lshl_b32 s6, s20, 8
	v_and_b32_e32 v4, 63, v2
	s_add_i32 s6, s6, 0
	s_and_b32 s22, s20, 3
	s_waitcnt vmcnt(1)
	v_mov_b32_e32 v6, v0
	s_ashr_i32 s17, s16, 31
	s_add_i32 s52, s6, 0x22000
	v_cmp_gt_u32_e64 s[6:7], 16, v4
	v_lshlrev_b32_e32 v3, 4, v4
	s_and_saveexec_b64 s[8:9], s[6:7]
	s_cbranch_execz .LBB0_1274
	s_lshl_b32 s18, s34, 8
	s_ashr_i32 s19, s18, 31
	s_lshl_b64 s[24:25], s[16:17], 13
	s_add_u32 s21, s14, s24
	s_addc_u32 s24, s15, s25
	s_lshl_b64 s[18:19], s[18:19], 2
	s_add_u32 s18, s21, s18
	v_lshl_or_b32 v5, s22, 8, v3
	s_addc_u32 s19, s24, s19
	s_mov_b32 m0, s52
	s_nop 0
	global_load_lds_dwordx4 v5, s[18:19]
.LBB0_1274:
	s_or_b64 exec, exec, s[8:9]
	s_lshl_b32 s8, s20, 9
	s_ashr_i32 s21, s1, 8
	s_add_i32 s8, s8, 0
	s_lshl_b32 s24, s21, 6
	s_add_i32 s53, s8, 0x20000
	v_cmp_gt_u32_e64 s[8:9], 32, v4
	v_lshlrev_b32_e32 v5, 3, v4
	v_lshlrev_b32_e32 v4, 2, v4
	s_and_saveexec_b64 s[18:19], s[8:9]
	s_cbranch_execz .LBB0_1276
	s_lshl_b64 s[26:27], s[16:17], 16
	s_add_u32 s25, s46, s26
	s_addc_u32 s28, s47, s27
	s_lshl_b32 s26, s71, 8
	s_ashr_i32 s27, s26, 31
	v_and_b32_e32 v7, 0x80, v5
	s_lshl_b64 s[26:27], s[26:27], 2
	v_add_u32_e32 v7, s24, v7
	s_add_u32 s26, s25, s26
	v_and_or_b32 v7, v4, 60, v7
	s_addc_u32 s27, s28, s27
	v_lshlrev_b32_e32 v7, 2, v7
	s_mov_b32 m0, s53
	s_nop 0
	global_load_lds_dwordx4 v7, s[26:27]
.LBB0_1276:
	s_or_b64 exec, exec, s[18:19]
	v_ashrrev_i32_e32 v8, 31, v6
	v_lshrrev_b32_e32 v8, 26, v8
	v_lshlrev_b32_e32 v7, 4, v6
	v_add_u32_e32 v8, v6, v8
	v_bfe_i32 v6, v6, 27, 1
	v_lshrrev_b32_e32 v6, 22, v6
	v_add_u32_e32 v6, v7, v6
	v_and_b32_e32 v6, 0xfffffc00, v6
	v_sub_u32_e32 v6, v7, v6
	v_lshrrev_b32_e32 v9, 4, v6
	v_bitop3_b32 v6, v9, v6, 32 bitop3:0x6c
	v_ashrrev_i32_e32 v10, 31, v6
	v_lshrrev_b32_e32 v10, 26, v10
	v_add_u32_e32 v10, v6, v10
	v_ashrrev_i32_e32 v8, 6, v8
	v_ashrrev_i32_e32 v11, 6, v10
	v_and_b32_e32 v10, 0xc0, v10
	v_lshlrev_b32_e32 v9, 3, v8
	v_lshlrev_b32_e32 v8, 5, v8
	v_sub_u32_e32 v6, v6, v10
	v_mov_b32_e32 v10, 1
	v_and_b32_e32 v8, 32, v8
	v_ashrrev_i16_sdwa v6, v10, sext(v6) dst_sel:DWORD dst_unused:UNUSED_PAD src0_sel:DWORD src1_sel:BYTE_0
	v_add_u32_e32 v7, 0x2000, v7
	v_add_u32_sdwa v6, v8, sext(v6) dst_sel:DWORD dst_unused:UNUSED_PAD src0_sel:DWORD src1_sel:WORD_0
	v_ashrrev_i32_e32 v8, 31, v7
	v_lshrrev_b32_e32 v8, 22, v8
	v_add_u32_e32 v8, v7, v8
	v_and_b32_e32 v9, -16, v9
	v_ashrrev_i32_e32 v8, 10, v8
	v_add_u32_e32 v9, v11, v9
	v_mul_i32_i24_e32 v11, 0x400, v8
	v_sub_u32_e32 v7, v7, v11
	v_lshrrev_b32_e32 v11, 4, v7
	v_bitop3_b32 v7, v11, v7, 32 bitop3:0x6c
	v_ashrrev_i32_e32 v12, 31, v7
	v_lshrrev_b32_e32 v12, 26, v12
	v_add_u32_e32 v12, v7, v12
	v_ashrrev_i32_e32 v13, 6, v12
	v_and_b32_e32 v12, 0xc0, v12
	v_lshlrev_b32_e32 v11, 3, v8
	v_lshlrev_b32_e32 v8, 5, v8
	v_sub_u32_e32 v7, v7, v12
	v_and_b32_e32 v11, -16, v11
	v_and_b32_e32 v8, 32, v8
	v_ashrrev_i16_sdwa v7, v10, sext(v7) dst_sel:DWORD dst_unused:UNUSED_PAD src0_sel:DWORD src1_sel:BYTE_0
	v_add_u32_e32 v11, v13, v11
	v_add_u32_sdwa v7, v8, sext(v7) dst_sel:DWORD dst_unused:UNUSED_PAD src0_sel:DWORD src1_sel:WORD_0
	v_lshl_add_u32 v8, v9, 10, v6
	v_lshlrev_b32_e32 v9, 11, v9
	v_lshl_add_u32 v165, v6, 1, v9
	v_lshlrev_b32_e32 v6, 11, v11
	v_lshl_add_u32 v166, v7, 1, v6
	v_mov_b32_e32 v6, 0x40000
	v_lshl_add_u32 v12, v11, 10, v7
	v_lshl_add_u32 v167, v8, 1, v6
	v_bfe_i32 v8, v2, 27, 1
	v_lshl_add_u32 v168, v12, 1, v6
	v_lshlrev_b32_e32 v6, 4, v2
	v_lshrrev_b32_e32 v8, 22, v8
	v_add_u32_e32 v8, v6, v8
	v_and_b32_e32 v8, 0xfffffc00, v8
	v_sub_u32_e32 v8, v6, v8
	v_lshrrev_b32_e32 v9, 4, v8
	v_ashrrev_i32_e32 v7, 31, v2
	v_bitop3_b32 v8, v9, v8, 32 bitop3:0x6c
	v_lshrrev_b32_e32 v7, 26, v7
	v_ashrrev_i32_e32 v11, 31, v8
	v_add_u32_e32 v7, v2, v7
	v_lshrrev_b32_e32 v11, 26, v11
	v_ashrrev_i32_e32 v7, 6, v7
	v_add_u32_e32 v11, v8, v11
	v_lshlrev_b32_e32 v9, 3, v7
	v_lshrrev_b32_e32 v12, 6, v11
	v_and_b32_e32 v11, 0xc0, v11
	v_and_b32_e32 v9, 0x1ffff0, v9
	v_lshlrev_b32_e32 v7, 5, v7
	v_sub_u32_e32 v8, v8, v11
	v_add_u32_e32 v9, v12, v9
	v_and_b32_e32 v7, 32, v7
	v_ashrrev_i16_sdwa v8, v10, sext(v8) dst_sel:DWORD dst_unused:UNUSED_PAD src0_sel:DWORD src1_sel:BYTE_0
	v_bfe_i32 v8, v8, 0, 16
	v_lshl_or_b32 v7, v9, 10, v7
	v_add_u32_e32 v6, 0x2000, v6
	v_add_lshl_u32 v169, v7, v8, 1
	v_ashrrev_i32_e32 v7, 31, v6
	v_lshrrev_b32_e32 v7, 22, v7
	v_add_u32_e32 v7, v6, v7
	v_ashrrev_i32_e32 v7, 10, v7
	v_mul_i32_i24_e32 v8, 0x400, v7
	v_sub_u32_e32 v6, v6, v8
	s_add_u32 s36, s23, s10
	v_lshrrev_b32_e32 v8, 4, v6
	s_addc_u32 s37, s33, s11
	s_ashr_i32 s35, s34, 31
	v_bitop3_b32 v6, v8, v6, 32 bitop3:0x6c
	s_lshl_b64 s[10:11], s[34:35], 19
	s_lshl_b64 s[18:19], s[16:17], 22
	v_ashrrev_i32_e32 v9, 31, v6
	s_add_u32 s17, s44, s18
	v_lshrrev_b32_e32 v9, 26, v9
	s_addc_u32 s18, s45, s19
	v_add_u32_e32 v9, v6, v9
	s_add_u32 s38, s17, s10
	v_lshlrev_b32_e32 v8, 3, v7
	v_lshrrev_b32_e32 v11, 6, v9
	v_and_b32_e32 v9, 0xc0, v9
	s_addc_u32 s39, s18, s11
	v_and_b32_e32 v8, 0x1ffff0, v8
	v_lshlrev_b32_e32 v7, 5, v7
	v_sub_u32_e32 v6, v6, v9
	s_lshl_b32 s10, s20, 10
	v_add_u32_e32 v8, v11, v8
	v_and_b32_e32 v7, 32, v7
	v_ashrrev_i16_sdwa v6, v10, sext(v6) dst_sel:DWORD dst_unused:UNUSED_PAD src0_sel:DWORD src1_sel:BYTE_0
	s_add_i32 s54, s10, 0
	v_bfe_i32 v6, v6, 0, 16
	v_lshl_or_b32 v7, v8, 10, v7
	s_add_i32 s55, s54, 0x10000
	s_mov_b32 m0, s55
	s_nop 0
	global_load_lds_dwordx4 v169, s[38:39]
	v_add_lshl_u32 v170, v7, v6, 1
	s_add_i32 s56, s54, 0x12000
	s_mov_b32 m0, s56
	s_nop 0
	global_load_lds_dwordx4 v170, s[38:39]
	s_add_u32 s10, s38, 0x40000
	s_addc_u32 s11, s39, 0
	s_add_i32 s57, s54, 0x14000
	s_mov_b32 m0, s57
	s_nop 0
	global_load_lds_dwordx4 v169, s[10:11]
	s_add_i32 s58, s54, 0x16000
	s_mov_b32 m0, s58
	s_nop 0
	global_load_lds_dwordx4 v170, s[10:11]
	s_mov_b32 m0, s54
	s_nop 0
	global_load_lds_dwordx4 v165, s[36:37]
	s_add_i32 s59, s54, 0x2000
	s_mov_b32 m0, s59
	s_nop 0
	global_load_lds_dwordx4 v166, s[36:37]
	s_add_i32 s60, s54, 0x4000
	s_mov_b32 m0, s60
	s_nop 0
	global_load_lds_dwordx4 v167, s[36:37]
	s_add_i32 s61, s54, 0x6000
	s_mov_b32 m0, s61
	s_nop 0
	global_load_lds_dwordx4 v168, s[36:37]
	s_cmp_eq_u32 s21, 1
	s_mov_b32 s17, 0
	s_cselect_b64 s[18:19], -1, 0
	s_cmp_lg_u32 s21, 1
	s_cbranch_scc1 .LBB0_1278
	s_barrier
; #define PG8_STAGEB(bufoff, gbase) PG8_STAGE2(bufoff, gbase, voffB[0], voffB[1])
; #define PG8_STAGEA(bufoff, gbase, h) PG8_STAGE2(bufoff, gbase, voffA[h][0], voffA[h][1])
; #define PG8_WAIT_V(n) asm volatile("s_waitcnt vmcnt(" #n ")" ::: "memory")
; #define PG8_BAR __builtin_amdgcn_s_barrier()
;     ...
;     if (wr == 1) PG8_BAR;
;     if constexpr (HM) PG8_WAIT_V(0); else PG8_WAIT_V(2);
;     PG8_BAR;
;     PG8_STAGEB(PG8_SB(1, 0), cB + kstep); PG8_STAGEA(PG8_SA(1, 0), cA + kstep, 0); PG8_STAGEB(PG8_SB(1, 1), cB + hstepB + kstep);
;     PG8_WAIT_V(6); PG8_BAR;
.LBB0_1278:
	v_and_b32_e32 v6, 15, v2
	v_or_b32_e32 v171, s24, v6
	v_and_b32_e32 v2, 48, v2
	v_lshlrev_b32_e32 v7, 6, v171
	s_movk_i32 s10, 0x3c0
	v_lshlrev_b32_e32 v8, 2, v171
	v_and_or_b32 v7, v7, s10, v2
	s_lshl_b32 s10, s21, 13
	v_and_b32_e32 v8, 32, v8
	v_lshlrev_b32_e32 v9, 2, v6
	v_bitop3_b32 v7, v7, s10, v8 bitop3:0xde
	v_lshl_or_b32 v8, v6, 6, v2
	s_lshl_b32 s10, s22, 12
	v_and_b32_e32 v10, 32, v9
	v_bitop3_b32 v8, v8, s10, v10 bitop3:0xde
	s_add_u32 s10, s38, 0x80
	s_waitcnt vmcnt(2)
	s_barrier
	s_addc_u32 s11, s39, 0
	s_add_i32 s62, s54, 0x18000
	s_mov_b32 m0, s62
	s_nop 0
	global_load_lds_dwordx4 v169, s[10:11]
	s_add_i32 s63, s54, 0x1a000
	s_mov_b32 m0, s63
	s_nop 0
	global_load_lds_dwordx4 v170, s[10:11]
	s_add_u32 s10, s36, 0x80
	s_addc_u32 s11, s37, 0
	s_add_i32 s64, s54, 0x8000
	s_mov_b32 m0, s64
	s_nop 0
	global_load_lds_dwordx4 v165, s[10:11]
	s_add_i32 s65, s54, 0xa000
	s_mov_b32 m0, s65
	s_nop 0
	global_load_lds_dwordx4 v166, s[10:11]
	s_add_u32 s10, s38, 0x40080
	s_addc_u32 s11, s39, 0
	s_add_i32 s66, s54, 0x1c000
	s_mov_b32 m0, s66
	s_nop 0
	global_load_lds_dwordx4 v169, s[10:11]
	s_add_i32 s67, s54, 0x1e000
	s_add_i32 s68, s54, 0xc000
	s_add_i32 s69, s54, 0xe000
	s_mov_b32 m0, s67
	s_nop 0
	global_load_lds_dwordx4 v170, s[10:11]
	s_cmpk_lt_u32 s1, 0x100
	s_cselect_b64 s[20:21], -1, 0
	s_add_i32 s1, s24, 0x80
	v_or_b32_e32 v177, s1, v6
	s_add_i32 s1, s24, 0x90
	v_or_b32_e32 v178, s1, v6
	s_add_i32 s1, s24, 0xa0
	v_lshl_add_u32 v181, s22, 8, v3
	v_and_b32_e32 v3, 0x80, v5
	s_waitcnt vmcnt(6)
	v_or_b32_e32 v179, s1, v6
	s_add_i32 s1, s24, 0xb0
	v_add_u32_e32 v3, s24, v3
	v_lshl_add_u32 v172, v2, 2, s52
	v_or_b32_e32 v180, s1, v6
	v_and_or_b32 v3, v4, 60, v3
	s_ashr_i32 s1, s0, 31
	v_lshl_or_b32 v183, s22, 6, v2
	v_add_u32_e32 v2, 0, v8
	v_add_u32_e32 v173, s53, v9
	v_or_b32_e32 v174, 16, v171
	v_or_b32_e32 v175, 32, v171
	v_or_b32_e32 v176, 48, v171
	v_lshlrev_b32_e32 v182, 2, v3
	v_mov_b64_e32 v[162:163], s[0:1]
	v_add_u32_e32 v184, 0x10000, v2
	v_add_u32_e32 v185, 0x14000, v2
	v_add_u32_e32 v186, 0, v7
	v_add_u32_e32 v187, 0x18000, v2
	v_add_u32_e32 v188, 0x1c000, v2
	s_mov_b32 s22, 0x42000000
	s_mov_b32 s35, s16
	s_barrier
	s_waitcnt vmcnt(0)
	s_branch .LBB0_1281

; #define LAS __attribute__((address_space(3)))
; #define PG8_STAGEB(bufoff, gbase) PG8_STAGE2(bufoff, gbase, voffB[0], voffB[1])
; #define PG8_STAGEA(bufoff, gbase, h) PG8_STAGE2(bufoff, gbase, voffA[h][0], voffA[h][1])
; #define PG8_STAGEAS(bufoff, gbase, h) PG8_STAGE2(bufoff, gbase, voffA[h][0], voffA[h][1])
; #define PG8_LDA(dst, b, h) do { _Pragma("unroll") for (int m = 0; m < 4; ++m) _Pragma("unroll") for (int k = 0; k < 2; ++k) dst[m][k] = *(const LAS bf16x8*)(lds + PG8_SA(b, h) + aoff + m * 2048 + k * 1024); } while (0)
; #define PG8_LDB(dst, b, h) do { _Pragma("unroll") for (int n = 0; n < 2; ++n) _Pragma("unroll") for (int k = 0; k < 2; ++k) dst[n][k] = *(const LAS bf16x8*)(lds + PG8_SB(b, h) + boff + n * 2048 + k * 1024); } while (0)
;     ...
;             const char* a1 = cA + (size_t)(t + 1) * kstep;
;             const char* a2 = last ? nA : cA + (size_t)(t + 2) * kstep; const char* b2 = last ? nB : cB + (size_t)(t + 2) * kstep;
;             const char* a3 = a2 + kstep; const char* b3 = b2 + kstep;
;             PG8_LDB(B0, 0, 0); PG8_LDB(B1, 0, 1); PG8_SCHED; PG8_LDA(At, 0, 0); if constexpr (!HM) PG8_STAGEA(PG8_SA(1, 1), a1, 1);
;             if constexpr (Sched::kGather) { if (last && has_next) { const u32x4 tn = *(const LAS u32x4*)(S.aux + tid * 16); voffA[0][0] = tn.x; voffA[0][1] = tn.y; voffA[1][0] = tn.z; voffA[1][1] = tn.w; } }
;             PG8_WAIT_K0(); PG8_WAIT_L(0); PG8_BAR; PG8_MMA(0, 0, At, B0); PG8_MMA(0, 1, At, B1); PG8_BAR; PG8_SCHED;
;             if constexpr (!HM) PG8_LDA(At, 0, 1);
;             PG8_STAGEB(PG8_SB(0, 0), b2); PG8_STAGEB(PG8_SB(0, 1), b2 + hstepB); PG8_STAGEAS(PG8_SA(0, 0), a2, 0);
;             PG8_WAIT_K0(); PG8_WAIT_L(0); PG8_BAR; if constexpr (!HM) { PG8_MMA(1, 0, At, B0); PG8_MMA(1, 1, At, B1); } PG8_BAR; PG8_SCHED;
;             PG8_LDB(B0, 1, 0); PG8_LDB(B1, 1, 1); PG8_SCHED; PG8_LDA(At, 1, 0); if constexpr (!HM) PG8_STAGEAS(PG8_SA(0, 1), a2, 1);
;             PG8_WAIT_K(); PG8_WAIT_L(0); PG8_BAR; PG8_MMA(0, 0, At, B0); PG8_MMA(0, 1, At, B1); PG8_BAR; PG8_SCHED;
;             if constexpr (!HM) PG8_LDA(At, 1, 1);
;             PG8_STAGEB(PG8_SB(1, 0), b3); PG8_STAGEB(PG8_SB(1, 1), b3 + hstepB); PG8_STAGEAS(PG8_SA(1, 0), a3, 0);
;             PG8_WAIT_K(); PG8_WAIT_L(0); PG8_BAR; if constexpr (!HM) { PG8_MMA(1, 0, At, B0); PG8_MMA(1, 1, At, B1); } PG8_BAR; PG8_SCHED;
.LBB0_1290:
	ds_read_b128 v[26:29], v184
	ds_read_b128 v[30:33], v184 offset:1024
	ds_read_b128 v[18:21], v184 offset:2048
	ds_read_b128 v[22:25], v184 offset:3072
	ds_read_b128 v[10:13], v185
	ds_read_b128 v[14:17], v185 offset:1024
	ds_read_b128 v[2:5], v185 offset:2048
	ds_read_b128 v[6:9], v185 offset:3072
	s_cmp_eq_u32 s73, 12
	s_cselect_b32 s42, s0, s25
	s_cselect_b32 s43, s1, s27
	s_cselect_b32 s40, s30, s29
	s_cselect_b32 s41, s31, s72
	s_add_u32 s38, s42, 0x80
	s_addc_u32 s39, s43, 0
	ds_read_b128 v[190:193], v186
	ds_read_b128 v[194:197], v186 offset:1024
	ds_read_b128 v[198:201], v186 offset:2048
	ds_read_b128 v[202:205], v186 offset:3072
	ds_read_b128 v[206:209], v186 offset:4096
	ds_read_b128 v[210:213], v186 offset:5120
	ds_read_b128 v[214:217], v186 offset:6144
	ds_read_b128 v[218:221], v186 offset:7168
	s_mov_b32 m0, s68
	s_nop 0
	global_load_lds_dwordx4 v167, s[36:37]
	s_mov_b32 m0, s69
	s_nop 0
	global_load_lds_dwordx4 v168, s[36:37]
	s_waitcnt vmcnt(8)
	s_waitcnt lgkmcnt(0)
	s_barrier
	s_setprio 1
	s_waitcnt lgkmcnt(6)
	v_mfma_scale_f32_16x16x128_f8f6f4 v[158:161], v[26:33], v[190:197], v[158:161], v1, v164 op_sel_hi:[0,0,0]
	v_mfma_scale_f32_16x16x128_f8f6f4 v[154:157], v[18:25], v[190:197], v[154:157], v1, v164 op_sel_hi:[0,0,0]
	s_waitcnt lgkmcnt(4)
	v_mfma_scale_f32_16x16x128_f8f6f4 v[142:145], v[26:33], v[198:205], v[142:145], v1, v164 op_sel_hi:[0,0,0]
	v_mfma_scale_f32_16x16x128_f8f6f4 v[138:141], v[18:25], v[198:205], v[138:141], v1, v164 op_sel_hi:[0,0,0]
	s_waitcnt lgkmcnt(2)
	v_mfma_scale_f32_16x16x128_f8f6f4 v[126:129], v[26:33], v[206:213], v[126:129], v1, v164 op_sel_hi:[0,0,0]
	v_mfma_scale_f32_16x16x128_f8f6f4 v[122:125], v[18:25], v[206:213], v[122:125], v1, v164 op_sel_hi:[0,0,0]
	s_waitcnt lgkmcnt(0)
	v_mfma_scale_f32_16x16x128_f8f6f4 v[110:113], v[26:33], v[214:221], v[110:113], v1, v164 op_sel_hi:[0,0,0]
	v_mfma_scale_f32_16x16x128_f8f6f4 v[106:109], v[18:25], v[214:221], v[106:109], v1, v164 op_sel_hi:[0,0,0]
	s_setprio 0
	s_setprio 1
	v_mfma_scale_f32_16x16x128_f8f6f4 v[150:153], v[10:17], v[190:197], v[150:153], v1, v164 op_sel_hi:[0,0,0]
	v_mfma_scale_f32_16x16x128_f8f6f4 v[146:149], v[2:9], v[190:197], v[146:149], v1, v164 op_sel_hi:[0,0,0]
	v_mfma_scale_f32_16x16x128_f8f6f4 v[134:137], v[10:17], v[198:205], v[134:137], v1, v164 op_sel_hi:[0,0,0]
	v_mfma_scale_f32_16x16x128_f8f6f4 v[130:133], v[2:9], v[198:205], v[130:133], v1, v164 op_sel_hi:[0,0,0]
	v_mfma_scale_f32_16x16x128_f8f6f4 v[118:121], v[10:17], v[206:213], v[118:121], v1, v164 op_sel_hi:[0,0,0]
	v_mfma_scale_f32_16x16x128_f8f6f4 v[114:117], v[2:9], v[206:213], v[114:117], v1, v164 op_sel_hi:[0,0,0]
	v_mfma_scale_f32_16x16x128_f8f6f4 v[102:105], v[10:17], v[214:221], v[102:105], v1, v164 op_sel_hi:[0,0,0]
	v_mfma_scale_f32_16x16x128_f8f6f4 v[98:101], v[2:9], v[214:221], v[98:101], v1, v164 op_sel_hi:[0,0,0]
	s_setprio 0
	s_barrier
	ds_read_b128 v[190:193], v186 offset:16384
	ds_read_b128 v[194:197], v186 offset:17408
	ds_read_b128 v[198:201], v186 offset:18432
	ds_read_b128 v[202:205], v186 offset:19456
	ds_read_b128 v[206:209], v186 offset:20480
	ds_read_b128 v[210:213], v186 offset:21504
	ds_read_b128 v[214:217], v186 offset:22528
	ds_read_b128 v[218:221], v186 offset:23552
	s_mov_b32 m0, s55
	s_nop 0
	global_load_lds_dwordx4 v169, s[40:41]
	s_mov_b32 m0, s56
	s_nop 0
	global_load_lds_dwordx4 v170, s[40:41]
	s_add_u32 s74, s40, 0x40000
	s_addc_u32 s75, s41, 0
	s_mov_b32 m0, s57
	s_nop 0
	global_load_lds_dwordx4 v169, s[74:75]
	s_mov_b32 m0, s58
	s_nop 0
	global_load_lds_dwordx4 v170, s[74:75]
	s_mov_b32 m0, s54
	s_nop 0
	global_load_lds_dwordx4 v165, s[42:43]
	s_mov_b32 m0, s59
	s_nop 0
	global_load_lds_dwordx4 v166, s[42:43]
	s_waitcnt vmcnt(8)
	s_waitcnt lgkmcnt(0)
	s_barrier
	s_setprio 1
	s_waitcnt lgkmcnt(6)
	v_mfma_scale_f32_16x16x128_f8f6f4 v[94:97], v[26:33], v[190:197], v[94:97], v1, v164 op_sel_hi:[0,0,0]
	v_mfma_scale_f32_16x16x128_f8f6f4 v[90:93], v[18:25], v[190:197], v[90:93], v1, v164 op_sel_hi:[0,0,0]
	s_waitcnt lgkmcnt(4)
	v_mfma_scale_f32_16x16x128_f8f6f4 v[78:81], v[26:33], v[198:205], v[78:81], v1, v164 op_sel_hi:[0,0,0]
	v_mfma_scale_f32_16x16x128_f8f6f4 v[74:77], v[18:25], v[198:205], v[74:77], v1, v164 op_sel_hi:[0,0,0]
	s_waitcnt lgkmcnt(2)
	v_mfma_scale_f32_16x16x128_f8f6f4 v[62:65], v[26:33], v[206:213], v[62:65], v1, v164 op_sel_hi:[0,0,0]
	v_mfma_scale_f32_16x16x128_f8f6f4 v[58:61], v[18:25], v[206:213], v[58:61], v1, v164 op_sel_hi:[0,0,0]
	s_waitcnt lgkmcnt(0)
	v_mfma_scale_f32_16x16x128_f8f6f4 v[46:49], v[26:33], v[214:221], v[46:49], v1, v164 op_sel_hi:[0,0,0]
	v_mfma_scale_f32_16x16x128_f8f6f4 v[42:45], v[18:25], v[214:221], v[42:45], v1, v164 op_sel_hi:[0,0,0]
	s_setprio 0
	s_setprio 1
	v_mfma_scale_f32_16x16x128_f8f6f4 v[86:89], v[10:17], v[190:197], v[86:89], v1, v164 op_sel_hi:[0,0,0]
	v_mfma_scale_f32_16x16x128_f8f6f4 v[82:85], v[2:9], v[190:197], v[82:85], v1, v164 op_sel_hi:[0,0,0]
	v_mfma_scale_f32_16x16x128_f8f6f4 v[70:73], v[10:17], v[198:205], v[70:73], v1, v164 op_sel_hi:[0,0,0]
	v_mfma_scale_f32_16x16x128_f8f6f4 v[66:69], v[2:9], v[198:205], v[66:69], v1, v164 op_sel_hi:[0,0,0]
	v_mfma_scale_f32_16x16x128_f8f6f4 v[54:57], v[10:17], v[206:213], v[54:57], v1, v164 op_sel_hi:[0,0,0]
	v_mfma_scale_f32_16x16x128_f8f6f4 v[50:53], v[2:9], v[206:213], v[50:53], v1, v164 op_sel_hi:[0,0,0]
	v_mfma_scale_f32_16x16x128_f8f6f4 v[38:41], v[10:17], v[214:221], v[38:41], v1, v164 op_sel_hi:[0,0,0]
	v_mfma_scale_f32_16x16x128_f8f6f4 v[34:37], v[2:9], v[214:221], v[34:37], v1, v164 op_sel_hi:[0,0,0]
	s_setprio 0
	s_barrier
; #define LAS __attribute__((address_space(3)))
; #define PG8_STAGEB(bufoff, gbase) PG8_STAGE2(bufoff, gbase, voffB[0], voffB[1])
; #define PG8_STAGEA(bufoff, gbase, h) PG8_STAGE2(bufoff, gbase, voffA[h][0], voffA[h][1])
; #define PG8_STAGEAS(bufoff, gbase, h) PG8_STAGE2(bufoff, gbase, voffA[h][0], voffA[h][1])
; #define PG8_LDA(dst, b, h) do { _Pragma("unroll") for (int m = 0; m < 4; ++m) _Pragma("unroll") for (int k = 0; k < 2; ++k) dst[m][k] = *(const LAS bf16x8*)(lds + PG8_SA(b, h) + aoff + m * 2048 + k * 1024); } while (0)
; #define PG8_LDB(dst, b, h) do { _Pragma("unroll") for (int n = 0; n < 2; ++n) _Pragma("unroll") for (int k = 0; k < 2; ++k) dst[n][k] = *(const LAS bf16x8*)(lds + PG8_SB(b, h) + boff + n * 2048 + k * 1024); } while (0)
;     ...
;             const char* a1 = cA + (size_t)(t + 1) * kstep;
;             const char* a2 = last ? nA : cA + (size_t)(t + 2) * kstep; const char* b2 = last ? nB : cB + (size_t)(t + 2) * kstep;
;             const char* a3 = a2 + kstep; const char* b3 = b2 + kstep;
;             PG8_LDB(B0, 0, 0); PG8_LDB(B1, 0, 1); PG8_SCHED; PG8_LDA(At, 0, 0); if constexpr (!HM) PG8_STAGEA(PG8_SA(1, 1), a1, 1);
;             if constexpr (Sched::kGather) { if (last && has_next) { const u32x4 tn = *(const LAS u32x4*)(S.aux + tid * 16); voffA[0][0] = tn.x; voffA[0][1] = tn.y; voffA[1][0] = tn.z; voffA[1][1] = tn.w; } }
;             PG8_WAIT_K0(); PG8_WAIT_L(0); PG8_BAR; PG8_MMA(0, 0, At, B0); PG8_MMA(0, 1, At, B1); PG8_BAR; PG8_SCHED;
;             if constexpr (!HM) PG8_LDA(At, 0, 1);
;             PG8_STAGEB(PG8_SB(0, 0), b2); PG8_STAGEB(PG8_SB(0, 1), b2 + hstepB); PG8_STAGEAS(PG8_SA(0, 0), a2, 0);
;             PG8_WAIT_K0(); PG8_WAIT_L(0); PG8_BAR; if constexpr (!HM) { PG8_MMA(1, 0, At, B0); PG8_MMA(1, 1, At, B1); } PG8_BAR; PG8_SCHED;
;             PG8_LDB(B0, 1, 0); PG8_LDB(B1, 1, 1); PG8_SCHED; PG8_LDA(At, 1, 0); if constexpr (!HM) PG8_STAGEAS(PG8_SA(0, 1), a2, 1);
;             PG8_WAIT_K(); PG8_WAIT_L(0); PG8_BAR; PG8_MMA(0, 0, At, B0); PG8_MMA(0, 1, At, B1); PG8_BAR; PG8_SCHED;
;             if constexpr (!HM) PG8_LDA(At, 1, 1);
;             PG8_STAGEB(PG8_SB(1, 0), b3); PG8_STAGEB(PG8_SB(1, 1), b3 + hstepB); PG8_STAGEAS(PG8_SA(1, 0), a3, 0);
;             PG8_WAIT_K(); PG8_WAIT_L(0); PG8_BAR; if constexpr (!HM) { PG8_MMA(1, 0, At, B0); PG8_MMA(1, 1, At, B1); } PG8_BAR; PG8_SCHED;
	ds_read_b128 v[2:5], v187
	ds_read_b128 v[6:9], v187 offset:1024
	ds_read_b128 v[10:13], v187 offset:2048
	ds_read_b128 v[14:17], v187 offset:3072
	ds_read_b128 v[18:21], v188
	ds_read_b128 v[22:25], v188 offset:1024
	ds_read_b128 v[26:29], v188 offset:2048
	ds_read_b128 v[30:33], v188 offset:3072
	ds_read_b128 v[190:193], v186 offset:32768
	ds_read_b128 v[194:197], v186 offset:33792
	ds_read_b128 v[198:201], v186 offset:34816
	ds_read_b128 v[202:205], v186 offset:35840
	ds_read_b128 v[206:209], v186 offset:36864
	ds_read_b128 v[210:213], v186 offset:37888
	ds_read_b128 v[214:217], v186 offset:38912
	ds_read_b128 v[218:221], v186 offset:39936
	s_mov_b32 m0, s60
	s_nop 0
	global_load_lds_dwordx4 v167, s[42:43]
	s_mov_b32 m0, s61
	s_nop 0
	global_load_lds_dwordx4 v168, s[42:43]
	s_waitcnt vmcnt(8)
	s_waitcnt lgkmcnt(0)
	s_barrier
	s_setprio 1
	s_waitcnt lgkmcnt(6)
	v_mfma_scale_f32_16x16x128_f8f6f4 v[158:161], v[2:9], v[190:197], v[158:161], v1, v164 op_sel_hi:[0,0,0]
	v_mfma_scale_f32_16x16x128_f8f6f4 v[154:157], v[10:17], v[190:197], v[154:157], v1, v164 op_sel_hi:[0,0,0]
	s_waitcnt lgkmcnt(4)
	v_mfma_scale_f32_16x16x128_f8f6f4 v[142:145], v[2:9], v[198:205], v[142:145], v1, v164 op_sel_hi:[0,0,0]
	v_mfma_scale_f32_16x16x128_f8f6f4 v[138:141], v[10:17], v[198:205], v[138:141], v1, v164 op_sel_hi:[0,0,0]
	s_waitcnt lgkmcnt(2)
	v_mfma_scale_f32_16x16x128_f8f6f4 v[126:129], v[2:9], v[206:213], v[126:129], v1, v164 op_sel_hi:[0,0,0]
	v_mfma_scale_f32_16x16x128_f8f6f4 v[122:125], v[10:17], v[206:213], v[122:125], v1, v164 op_sel_hi:[0,0,0]
	s_waitcnt lgkmcnt(0)
	v_mfma_scale_f32_16x16x128_f8f6f4 v[110:113], v[2:9], v[214:221], v[110:113], v1, v164 op_sel_hi:[0,0,0]
	v_mfma_scale_f32_16x16x128_f8f6f4 v[106:109], v[10:17], v[214:221], v[106:109], v1, v164 op_sel_hi:[0,0,0]
	s_setprio 0
	s_setprio 1
	v_mfma_scale_f32_16x16x128_f8f6f4 v[150:153], v[18:25], v[190:197], v[150:153], v1, v164 op_sel_hi:[0,0,0]
	v_mfma_scale_f32_16x16x128_f8f6f4 v[146:149], v[26:33], v[190:197], v[146:149], v1, v164 op_sel_hi:[0,0,0]
	v_mfma_scale_f32_16x16x128_f8f6f4 v[134:137], v[18:25], v[198:205], v[134:137], v1, v164 op_sel_hi:[0,0,0]
	v_mfma_scale_f32_16x16x128_f8f6f4 v[130:133], v[26:33], v[198:205], v[130:133], v1, v164 op_sel_hi:[0,0,0]
	v_mfma_scale_f32_16x16x128_f8f6f4 v[118:121], v[18:25], v[206:213], v[118:121], v1, v164 op_sel_hi:[0,0,0]
	v_mfma_scale_f32_16x16x128_f8f6f4 v[114:117], v[26:33], v[206:213], v[114:117], v1, v164 op_sel_hi:[0,0,0]
	v_mfma_scale_f32_16x16x128_f8f6f4 v[102:105], v[18:25], v[214:221], v[102:105], v1, v164 op_sel_hi:[0,0,0]
	v_mfma_scale_f32_16x16x128_f8f6f4 v[98:101], v[26:33], v[214:221], v[98:101], v1, v164 op_sel_hi:[0,0,0]
	s_setprio 0
	s_barrier
	ds_read_b128 v[190:193], v186 offset:49152
	ds_read_b128 v[194:197], v186 offset:50176
	ds_read_b128 v[198:201], v186 offset:51200
	ds_read_b128 v[202:205], v186 offset:52224
	ds_read_b128 v[206:209], v186 offset:53248
	ds_read_b128 v[210:213], v186 offset:54272
	ds_read_b128 v[214:217], v186 offset:55296
	ds_read_b128 v[218:221], v186 offset:56320
	s_add_u32 s42, s40, 0x80
	s_addc_u32 s43, s41, 0
	s_mov_b32 m0, s62
	s_nop 0
	global_load_lds_dwordx4 v169, s[42:43]
	s_add_u32 s40, s40, 0x40080
	s_mov_b32 m0, s63
	s_nop 0
	global_load_lds_dwordx4 v170, s[42:43]
	s_addc_u32 s41, s41, 0
	s_mov_b32 m0, s66
	s_nop 0
	global_load_lds_dwordx4 v169, s[40:41]
	s_mov_b32 m0, s67
	s_nop 0
	global_load_lds_dwordx4 v170, s[40:41]
	s_mov_b32 m0, s64
	s_nop 0
	global_load_lds_dwordx4 v165, s[38:39]
	s_mov_b32 m0, s65
	s_nop 0
	global_load_lds_dwordx4 v166, s[38:39]
	s_waitcnt vmcnt(8)
	s_waitcnt lgkmcnt(0)
	s_barrier
	s_setprio 1
	s_waitcnt lgkmcnt(6)
	v_mfma_scale_f32_16x16x128_f8f6f4 v[94:97], v[2:9], v[190:197], v[94:97], v1, v164 op_sel_hi:[0,0,0]
	v_mfma_scale_f32_16x16x128_f8f6f4 v[90:93], v[10:17], v[190:197], v[90:93], v1, v164 op_sel_hi:[0,0,0]
	s_waitcnt lgkmcnt(4)
	v_mfma_scale_f32_16x16x128_f8f6f4 v[78:81], v[2:9], v[198:205], v[78:81], v1, v164 op_sel_hi:[0,0,0]
	v_mfma_scale_f32_16x16x128_f8f6f4 v[74:77], v[10:17], v[198:205], v[74:77], v1, v164 op_sel_hi:[0,0,0]
	s_waitcnt lgkmcnt(2)
	v_mfma_scale_f32_16x16x128_f8f6f4 v[62:65], v[2:9], v[206:213], v[62:65], v1, v164 op_sel_hi:[0,0,0]
	v_mfma_scale_f32_16x16x128_f8f6f4 v[58:61], v[10:17], v[206:213], v[58:61], v1, v164 op_sel_hi:[0,0,0]
	s_waitcnt lgkmcnt(0)
	v_mfma_scale_f32_16x16x128_f8f6f4 v[46:49], v[2:9], v[214:221], v[46:49], v1, v164 op_sel_hi:[0,0,0]
	v_mfma_scale_f32_16x16x128_f8f6f4 v[42:45], v[10:17], v[214:221], v[42:45], v1, v164 op_sel_hi:[0,0,0]
	s_setprio 0
	s_setprio 1
	v_mfma_scale_f32_16x16x128_f8f6f4 v[86:89], v[18:25], v[190:197], v[86:89], v1, v164 op_sel_hi:[0,0,0]
	v_mfma_scale_f32_16x16x128_f8f6f4 v[82:85], v[26:33], v[190:197], v[82:85], v1, v164 op_sel_hi:[0,0,0]
	v_mfma_scale_f32_16x16x128_f8f6f4 v[70:73], v[18:25], v[198:205], v[70:73], v1, v164 op_sel_hi:[0,0,0]
	v_mfma_scale_f32_16x16x128_f8f6f4 v[66:69], v[26:33], v[198:205], v[66:69], v1, v164 op_sel_hi:[0,0,0]
	v_mfma_scale_f32_16x16x128_f8f6f4 v[54:57], v[18:25], v[206:213], v[54:57], v1, v164 op_sel_hi:[0,0,0]
	v_mfma_scale_f32_16x16x128_f8f6f4 v[50:53], v[26:33], v[206:213], v[50:53], v1, v164 op_sel_hi:[0,0,0]
	v_mfma_scale_f32_16x16x128_f8f6f4 v[38:41], v[18:25], v[214:221], v[38:41], v1, v164 op_sel_hi:[0,0,0]
	v_mfma_scale_f32_16x16x128_f8f6f4 v[34:37], v[26:33], v[214:221], v[34:37], v1, v164 op_sel_hi:[0,0,0]
	s_setprio 0
	s_barrier
	s_add_i32 s73, s73, 2
	s_add_u32 s25, s25, 0x100
	s_addc_u32 s27, s27, 0
	s_add_u32 s29, s29, 0x100
	s_addc_u32 s72, s72, 0
	s_add_u32 s36, s36, 0x100
	s_addc_u32 s37, s37, 0
	s_cmp_gt_u32 s73, 13
	s_cbranch_scc0 .LBB0_1290
	s_and_b64 vcc, exec, s[20:21]
	s_cbranch_vccz .LBB0_1293
	s_barrier

;     __device__ __forceinline__ const char* bias_base(const pg8::Unit& u) const { return (const char*)(bgu + (size_t)u.e * 4096 + u.pn * 128); }
;     __device__ __forceinline__ unsigned bias_off(const pg8::Unit&, int wc, int lane) const { return (unsigned)(((lane >> 3) & 1) * 2048 + wc * 32 + (lane & 7) * 4) * 4u; }
; __device__ __forceinline__ unsigned row_base(unsigned lane, unsigned s) { return row_addr16(lane, 0, s); }
;     ...
;         if constexpr (Epi::kBiasDMA) { if (lane < 16) glds16(E.bias_base(cur), E.bias_off(cur, wc, lane), bias_lds); }
;         if constexpr (Epi::kRowDMA) { if (lane < 32) glds16(E.row_base(cur), E.row_off(cur, wr, lane), rowid_lds); }
;     __device__ __forceinline__ const char* bias_base(const pg8::Unit& u) const { return (const char*)(bdn + (size_t)u.e * D + u.pn * 256); }
;     __device__ __forceinline__ unsigned bias_off(const pg8::Unit&, int wc, int lane) const { return (unsigned)(wc * 64 + lane * 4) * 4u; }
;     __device__ __forceinline__ const char* row_base(const pg8::Unit& u) const { return (const char*)((const int*)(ws + WS_ROWTOK) + (size_t)u.e * T + u.mt * 256 + u.hx * 128); }
;     __device__ __forceinline__ unsigned row_off(const pg8::Unit&, int wr, int lane) const { return (unsigned)(((lane >> 4) & 1) * 128 + wr * 64 + (lane & 15) * 4) * 4u; }
.LBB0_1313:
	s_ashr_i32 s25, s24, 31
	s_lshl_b64 s[34:35], s[24:25], 13
	s_add_u32 s25, s14, s34
	s_addc_u32 s27, s15, s35
	s_lshl_b32 s34, s26, 8
	s_ashr_i32 s35, s34, 31
	s_lshl_b64 s[34:35], s[34:35], 2
	s_add_u32 s34, s25, s34
	s_addc_u32 s35, s27, s35
	s_mov_b32 m0, s52
	s_nop 0
	global_load_lds_dwordx4 v181, s[34:35]
	s_or_b64 exec, exec, s[10:11]
	s_and_saveexec_b64 s[10:11], s[8:9]
	s_cbranch_execz .LBB0_1312
.LBB0_1314:
	s_ashr_i32 s25, s24, 31
	s_lshl_b64 s[34:35], s[24:25], 16
	s_add_u32 s25, s46, s34
	s_addc_u32 s27, s47, s35
	s_lshl_b32 s34, s70, 8
	s_ashr_i32 s35, s34, 31
	s_lshl_b64 s[34:35], s[34:35], 2
	s_add_u32 s34, s25, s34
	s_addc_u32 s35, s27, s35
	s_mov_b32 m0, s53
	s_nop 0
	global_load_lds_dwordx4 v182, s[34:35]
	s_or_b64 exec, exec, s[10:11]
	s_andn2_b64 vcc, exec, s[18:19]
	s_cbranch_vccnz .LBB0_1279

;     __device__ __forceinline__ const char* a_base(const Unit& u) const { return (const char*)A + (size_t)u.pm * BM * lda * 2; }
;     __device__ __forceinline__ const char* b_base(const Unit& u) const { return (const char*)Bt + (size_t)u.pn * BM * K * 2; }
;     __device__ __forceinline__ const char* b_base(const Unit& u) const { return (const char*)Bt + ((size_t)u.e * NB + (size_t)u.pn * BM) * K * 2; }
; #define PG8_STAGEB(bufoff, gbase) PG8_STAGE2(bufoff, gbase, voffB[0], voffB[1])
; #define PG8_STAGEA(bufoff, gbase, h) PG8_STAGE2(bufoff, gbase, voffA[h][0], voffA[h][1])
; #define PG8_BAR __builtin_amdgcn_s_barrier()
;     __device__ __forceinline__ const char* bias_base(const pg8::Unit& u) const { return (const char*)(bgu + (size_t)u.e * 4096 + u.pn * 128); }
;     __device__ __forceinline__ unsigned bias_off(const pg8::Unit&, int wc, int lane) const { return (unsigned)(((lane >> 3) & 1) * 2048 + wc * 32 + (lane & 7) * 4) * 4u; }
;     ...
;     const char* cA = S.a_base(cur); const char* cB = S.b_base(cur);
;     const unsigned bias_lds = (unsigned)__builtin_amdgcn_readfirstlane((int)((unsigned)(size_t)lds + (unsigned)(AUX_OFF + 8192) + (unsigned)wid * 256u));
;     if constexpr (Epi::kBiasDMA) { if (lane < 16) glds16(E.bias_base(cur), E.bias_off(cur, wc, lane), bias_lds); }
;     const unsigned rowid_lds = (unsigned)__builtin_amdgcn_readfirstlane((int)((unsigned)(size_t)lds + (unsigned)AUX_OFF + (unsigned)wid * 512u));
;     if constexpr (Epi::kRowDMA) { if (lane < 32) glds16(E.row_base(cur), E.row_off(cur, wr, lane), rowid_lds); }
;     PG8_STAGEB(PG8_SB(0, 0), cB); PG8_STAGEB(PG8_SB(0, 1), cB + hstepB); PG8_STAGEA(PG8_SA(0, 0), cA, 0); if constexpr (!HM) PG8_STAGEA(PG8_SA(0, 1), cA, 1);
;     if (wr == 1) PG8_BAR;
;     __device__ __forceinline__ const char* bias_base(const pg8::Unit& u) const { return (const char*)(bdn + (size_t)u.e * D + u.pn * 256); }
;     __device__ __forceinline__ unsigned bias_off(const pg8::Unit&, int wc, int lane) const { return (unsigned)(wc * 64 + lane * 4) * 4u; }
;     __device__ __forceinline__ const char* row_base(const pg8::Unit& u) const { return (const char*)((const int*)(ws + WS_ROWTOK) + (size_t)u.e * T + u.mt * 256 + u.hx * 128); }
;     __device__ __forceinline__ unsigned row_off(const pg8::Unit&, int wr, int lane) const { return (unsigned)(((lane >> 4) & 1) * 128 + wr * 64 + (lane & 15) * 4) * 4u; }
.LBB0_1326:
	s_lshl_b32 s6, s20, 8
	v_and_b32_e32 v4, 63, v2
	s_add_i32 s43, s6, 0
	s_and_b32 s22, s20, 3
	s_waitcnt vmcnt(1)
	v_mov_b32_e32 v6, v0
	s_ashr_i32 s17, s16, 31
	s_add_i32 s43, s43, 0x22000
	v_cmp_gt_u32_e64 s[6:7], 16, v4
	v_lshlrev_b32_e32 v3, 4, v4
	s_and_saveexec_b64 s[8:9], s[6:7]
	s_cbranch_execz .LBB0_1328
	s_lshl_b32 s18, s26, 8
	s_ashr_i32 s19, s18, 31
	s_lshl_b64 s[24:25], s[16:17], 13
	s_add_u32 s21, s14, s24
	s_addc_u32 s24, s15, s25
	s_lshl_b64 s[18:19], s[18:19], 2
	s_add_u32 s18, s21, s18
	v_lshl_or_b32 v5, s22, 8, v3
	s_addc_u32 s19, s24, s19
	s_mov_b32 m0, s43
	s_nop 0
	global_load_lds_dwordx4 v5, s[18:19]
.LBB0_1328:
	s_or_b64 exec, exec, s[8:9]
	s_lshl_b32 s8, s20, 9
	s_ashr_i32 s21, s1, 8
	s_add_i32 s49, s8, 0
	s_lshl_b32 s24, s21, 6
	s_add_i32 s49, s49, 0x20000
	v_cmp_gt_u32_e64 s[8:9], 32, v4
	v_lshlrev_b32_e32 v5, 3, v4
	v_lshlrev_b32_e32 v4, 2, v4
	s_and_saveexec_b64 s[18:19], s[8:9]
	s_cbranch_execz .LBB0_1330
	s_lshl_b64 s[28:29], s[16:17], 16
	s_add_u32 s25, s46, s28
	s_addc_u32 s27, s47, s29
	s_lshl_b32 s28, s63, 8
	s_ashr_i32 s29, s28, 31
	v_and_b32_e32 v7, 0x80, v5
	s_lshl_b64 s[28:29], s[28:29], 2
	v_add_u32_e32 v7, s24, v7
	s_add_u32 s28, s25, s28
	v_and_or_b32 v7, v4, 60, v7
	s_addc_u32 s29, s27, s29
	v_lshlrev_b32_e32 v7, 2, v7
	s_mov_b32 m0, s49
	s_nop 0
	global_load_lds_dwordx4 v7, s[28:29]
.LBB0_1330:
	s_or_b64 exec, exec, s[18:19]
	v_ashrrev_i32_e32 v8, 31, v6
	v_lshrrev_b32_e32 v8, 26, v8
	v_lshlrev_b32_e32 v7, 4, v6
	v_add_u32_e32 v8, v6, v8
	v_bfe_i32 v6, v6, 27, 1
	v_lshrrev_b32_e32 v6, 22, v6
	v_add_u32_e32 v6, v7, v6
	v_and_b32_e32 v6, 0xfffffc00, v6
	v_sub_u32_e32 v6, v7, v6
	v_lshrrev_b32_e32 v9, 4, v6
	v_bitop3_b32 v6, v9, v6, 32 bitop3:0x6c
	v_ashrrev_i32_e32 v10, 31, v6
	v_lshrrev_b32_e32 v10, 26, v10
	v_add_u32_e32 v10, v6, v10
	v_ashrrev_i32_e32 v8, 6, v8
	v_lshrrev_b32_e32 v11, 6, v10
	v_and_b32_e32 v10, 0xc0, v10
	v_lshlrev_b32_e32 v9, 3, v8
	v_lshlrev_b32_e32 v8, 5, v8
	v_sub_u32_e32 v6, v6, v10
	v_mov_b32_e32 v10, 1
	v_and_b32_e32 v8, 32, v8
	v_ashrrev_i16_sdwa v6, v10, sext(v6) dst_sel:DWORD dst_unused:UNUSED_PAD src0_sel:DWORD src1_sel:BYTE_0
	v_add_u32_e32 v7, 0x2000, v7
	v_add_u32_sdwa v6, v8, sext(v6) dst_sel:DWORD dst_unused:UNUSED_PAD src0_sel:DWORD src1_sel:WORD_0
	v_ashrrev_i32_e32 v8, 31, v7
	v_lshrrev_b32_e32 v8, 22, v8
	v_add_u32_e32 v8, v7, v8
	v_ashrrev_i32_e32 v8, 10, v8
	v_mul_i32_i24_e32 v12, 0x400, v8
	v_sub_u32_e32 v7, v7, v12
	v_lshrrev_b32_e32 v12, 4, v7
	v_bitop3_b32 v7, v12, v7, 32 bitop3:0x6c
	v_ashrrev_i32_e32 v13, 31, v7
	v_lshrrev_b32_e32 v13, 26, v13
	v_add_u32_e32 v13, v7, v13
	s_waitcnt vmcnt(0)
	v_lshrrev_b32_e32 v14, 6, v13
	v_and_b32_e32 v13, 0xc0, v13
	v_lshlrev_b32_e32 v12, 3, v8
	v_lshlrev_b32_e32 v8, 5, v8
	v_sub_u32_e32 v7, v7, v13
	v_and_b32_e32 v9, 0x1ffff0, v9
	v_and_b32_e32 v8, 32, v8
	v_ashrrev_i16_sdwa v7, v10, sext(v7) dst_sel:DWORD dst_unused:UNUSED_PAD src0_sel:DWORD src1_sel:BYTE_0
	v_and_b32_e32 v12, 0x1ffff0, v12
	v_add_u32_sdwa v7, v8, sext(v7) dst_sel:DWORD dst_unused:UNUSED_PAD src0_sel:DWORD src1_sel:WORD_0
	v_add_lshl_u32 v8, v11, v9, 11
	v_lshl_add_u32 v87, v6, 1, v8
	v_add_lshl_u32 v6, v14, v12, 11
	v_bfe_i32 v8, v2, 27, 1
	v_lshl_add_u32 v88, v7, 1, v6
	v_lshlrev_b32_e32 v6, 4, v2
	v_lshrrev_b32_e32 v8, 22, v8
	v_add_u32_e32 v8, v6, v8
	v_and_b32_e32 v8, 0xfffffc00, v8
	v_sub_u32_e32 v8, v6, v8
	v_lshrrev_b32_e32 v9, 4, v8
	v_ashrrev_i32_e32 v7, 31, v2
	v_bitop3_b32 v8, v9, v8, 32 bitop3:0x6c
	v_lshrrev_b32_e32 v7, 26, v7
	v_ashrrev_i32_e32 v11, 31, v8
	v_add_u32_e32 v7, v2, v7
	v_lshrrev_b32_e32 v11, 26, v11
	v_ashrrev_i32_e32 v7, 6, v7
	v_add_u32_e32 v11, v8, v11
	v_lshlrev_b32_e32 v9, 3, v7
	v_lshrrev_b32_e32 v12, 6, v11
	v_and_b32_e32 v11, 0xc0, v11
	v_and_b32_e32 v9, 0x1ffff0, v9
	v_lshlrev_b32_e32 v7, 5, v7
	v_sub_u32_e32 v8, v8, v11
	v_add_u32_e32 v9, v12, v9
	v_and_b32_e32 v7, 32, v7
	v_ashrrev_i16_sdwa v8, v10, sext(v8) dst_sel:DWORD dst_unused:UNUSED_PAD src0_sel:DWORD src1_sel:BYTE_0
	v_bfe_i32 v8, v8, 0, 16
	v_lshl_or_b32 v7, v9, 10, v7
	v_add_u32_e32 v6, 0x2000, v6
	v_add_lshl_u32 v89, v7, v8, 1
	v_ashrrev_i32_e32 v7, 31, v6
	v_lshrrev_b32_e32 v7, 22, v7
	v_add_u32_e32 v7, v6, v7
	v_ashrrev_i32_e32 v7, 10, v7
	v_mul_i32_i24_e32 v8, 0x400, v7
	v_sub_u32_e32 v6, v6, v8
	s_add_u32 s36, s23, s10
	v_lshrrev_b32_e32 v8, 4, v6
	s_addc_u32 s37, s33, s11
	s_ashr_i32 s27, s26, 31
	v_bitop3_b32 v6, v8, v6, 32 bitop3:0x6c
	s_lshl_b64 s[10:11], s[26:27], 19
	s_lshl_b64 s[18:19], s[16:17], 22
	v_ashrrev_i32_e32 v9, 31, v6
	s_add_u32 s17, s44, s18
	v_lshrrev_b32_e32 v9, 26, v9
	s_addc_u32 s18, s45, s19
	v_add_u32_e32 v9, v6, v9
	s_add_u32 s38, s17, s10
	v_lshlrev_b32_e32 v8, 3, v7
	v_lshrrev_b32_e32 v11, 6, v9
	v_and_b32_e32 v9, 0xc0, v9
	s_addc_u32 s39, s18, s11
	v_and_b32_e32 v8, 0x1ffff0, v8
	v_lshlrev_b32_e32 v7, 5, v7
	v_sub_u32_e32 v6, v6, v9
	s_lshl_b32 s10, s20, 10
	v_add_u32_e32 v8, v11, v8
	v_and_b32_e32 v7, 32, v7
	v_ashrrev_i16_sdwa v6, v10, sext(v6) dst_sel:DWORD dst_unused:UNUSED_PAD src0_sel:DWORD src1_sel:BYTE_0
	s_add_i32 s50, s10, 0
	v_bfe_i32 v6, v6, 0, 16
	v_lshl_or_b32 v7, v8, 10, v7
	s_add_i32 s51, s50, 0x10000
	s_mov_b32 m0, s51
	s_nop 0
	global_load_lds_dwordx4 v89, s[38:39]
	v_add_lshl_u32 v90, v7, v6, 1
	s_add_i32 s52, s50, 0x12000
	s_mov_b32 m0, s52
	s_nop 0
	global_load_lds_dwordx4 v90, s[38:39]
	s_add_u32 s10, s38, 0x40000
	s_addc_u32 s11, s39, 0
	s_add_i32 s53, s50, 0x14000
	s_mov_b32 m0, s53
	s_nop 0
	global_load_lds_dwordx4 v89, s[10:11]
	s_add_i32 s54, s50, 0x16000
	s_mov_b32 m0, s54
	s_nop 0
	global_load_lds_dwordx4 v90, s[10:11]
	s_mov_b32 m0, s50
	s_nop 0
	global_load_lds_dwordx4 v87, s[36:37]
	s_add_i32 s55, s50, 0x2000
	s_mov_b32 m0, s55
	s_nop 0
	global_load_lds_dwordx4 v88, s[36:37]
	s_cmp_eq_u32 s21, 1
	s_mov_b32 s17, 0
	s_cselect_b64 s[18:19], -1, 0
	s_cmp_lg_u32 s21, 1
	s_cbranch_scc1 .LBB0_1332
	s_barrier
; #define PG8_STAGEB(bufoff, gbase) PG8_STAGE2(bufoff, gbase, voffB[0], voffB[1])
; #define PG8_STAGEA(bufoff, gbase, h) PG8_STAGE2(bufoff, gbase, voffA[h][0], voffA[h][1])
; #define PG8_WAIT_V(n) asm volatile("s_waitcnt vmcnt(" #n ")" ::: "memory")
; #define PG8_BAR __builtin_amdgcn_s_barrier()
;     ...
;     if (wr == 1) PG8_BAR;
;     if constexpr (HM) PG8_WAIT_V(0); else PG8_WAIT_V(2);
;     PG8_BAR;
;     PG8_STAGEB(PG8_SB(1, 0), cB + kstep); PG8_STAGEA(PG8_SA(1, 0), cA + kstep, 0); PG8_STAGEB(PG8_SB(1, 1), cB + hstepB + kstep);
;     PG8_WAIT_V(6); PG8_BAR;
.LBB0_1332:
	v_and_b32_e32 v6, 15, v2
	v_or_b32_e32 v91, s24, v6
	v_and_b32_e32 v2, 48, v2
	v_lshlrev_b32_e32 v7, 6, v91
	s_movk_i32 s10, 0x3c0
	v_lshlrev_b32_e32 v8, 2, v91
	v_and_or_b32 v7, v7, s10, v2
	s_lshl_b32 s10, s21, 13
	v_and_b32_e32 v8, 32, v8
	v_bitop3_b32 v7, v7, s10, v8 bitop3:0xde
	v_lshl_or_b32 v8, v6, 6, v2
	v_lshlrev_b32_e32 v6, 2, v6
	s_lshl_b32 s10, s22, 12
	v_and_b32_e32 v9, 32, v6
	v_bitop3_b32 v8, v8, s10, v9 bitop3:0xde
	s_add_u32 s10, s38, 0x80
	s_waitcnt vmcnt(0)
	s_barrier
	s_addc_u32 s11, s39, 0
	s_add_i32 s56, s50, 0x18000
	s_mov_b32 m0, s56
	s_nop 0
	global_load_lds_dwordx4 v89, s[10:11]
	s_add_i32 s57, s50, 0x1a000
	s_mov_b32 m0, s57
	s_nop 0
	global_load_lds_dwordx4 v90, s[10:11]
	s_add_u32 s10, s36, 0x80
	s_addc_u32 s11, s37, 0
	s_add_i32 s58, s50, 0x8000
	s_mov_b32 m0, s58
	s_nop 0
	global_load_lds_dwordx4 v87, s[10:11]
	s_add_i32 s59, s50, 0xa000
	s_mov_b32 m0, s59
	s_nop 0
	global_load_lds_dwordx4 v88, s[10:11]
	s_add_u32 s10, s38, 0x40080
	s_addc_u32 s11, s39, 0
	s_add_i32 s60, s50, 0x1c000
	s_mov_b32 m0, s60
	s_nop 0
	global_load_lds_dwordx4 v89, s[10:11]
	s_add_i32 s61, s50, 0x1e000
	s_mov_b32 m0, s61
	s_nop 0
	global_load_lds_dwordx4 v90, s[10:11]
	v_lshl_add_u32 v97, s22, 8, v3
	v_and_b32_e32 v3, 0x80, v5
	s_waitcnt vmcnt(6)
	s_cmpk_lt_u32 s1, 0x100
	v_add_u32_e32 v3, s24, v3
	s_cselect_b64 s[20:21], -1, 0
	v_lshl_add_u32 v92, v2, 2, s43
	v_and_or_b32 v3, v4, 60, v3
	s_ashr_i32 s1, s0, 31
	v_lshl_or_b32 v99, s22, 6, v2
	v_add_u32_e32 v2, 0, v8
	v_add_u32_e32 v93, s49, v6
	v_or_b32_e32 v94, 16, v91
	v_or_b32_e32 v95, 32, v91
	v_or_b32_e32 v96, 48, v91
	v_lshlrev_b32_e32 v98, 2, v3
	v_mov_b64_e32 v[66:67], s[0:1]
	s_add_i32 s62, 0, 0x23180
	v_add_u32_e32 v100, 0x10000, v2
	v_add_u32_e32 v101, 0x14000, v2
	v_add_u32_e32 v102, 0, v7
	v_add_u32_e32 v103, 0x18000, v2
	v_add_u32_e32 v104, 0x1c000, v2
	s_mov_b32 s22, 0x42000000
	s_mov_b32 s27, s16
	s_barrier
	s_branch .LBB0_1335

; #define LAS __attribute__((address_space(3)))
; #define PG8_STAGEB(bufoff, gbase) PG8_STAGE2(bufoff, gbase, voffB[0], voffB[1])
; #define PG8_STAGEA(bufoff, gbase, h) PG8_STAGE2(bufoff, gbase, voffA[h][0], voffA[h][1])
; #define PG8_STAGEAS(bufoff, gbase, h) PG8_STAGE2(bufoff, gbase, voffA[h][0], voffA[h][1])
; #define PG8_LDA(dst, b, h) do { _Pragma("unroll") for (int m = 0; m < 4; ++m) _Pragma("unroll") for (int k = 0; k < 2; ++k) dst[m][k] = *(const LAS bf16x8*)(lds + PG8_SA(b, h) + aoff + m * 2048 + k * 1024); } while (0)
; #define PG8_LDB(dst, b, h) do { _Pragma("unroll") for (int n = 0; n < 2; ++n) _Pragma("unroll") for (int k = 0; k < 2; ++k) dst[n][k] = *(const LAS bf16x8*)(lds + PG8_SB(b, h) + boff + n * 2048 + k * 1024); } while (0)
;     ...
;             const char* a1 = cA + (size_t)(t + 1) * kstep;
;             const char* a2 = last ? nA : cA + (size_t)(t + 2) * kstep; const char* b2 = last ? nB : cB + (size_t)(t + 2) * kstep;
;             const char* a3 = a2 + kstep; const char* b3 = b2 + kstep;
;             PG8_LDB(B0, 0, 0); PG8_LDB(B1, 0, 1); PG8_SCHED; PG8_LDA(At, 0, 0); if constexpr (!HM) PG8_STAGEA(PG8_SA(1, 1), a1, 1);
;             if constexpr (Sched::kGather) { if (last && has_next) { const u32x4 tn = *(const LAS u32x4*)(S.aux + tid * 16); voffA[0][0] = tn.x; voffA[0][1] = tn.y; voffA[1][0] = tn.z; voffA[1][1] = tn.w; } }
;             PG8_WAIT_K0(); PG8_WAIT_L(0); PG8_BAR; PG8_MMA(0, 0, At, B0); PG8_MMA(0, 1, At, B1); PG8_BAR; PG8_SCHED;
;             if constexpr (!HM) PG8_LDA(At, 0, 1);
;             PG8_STAGEB(PG8_SB(0, 0), b2); PG8_STAGEB(PG8_SB(0, 1), b2 + hstepB); PG8_STAGEAS(PG8_SA(0, 0), a2, 0);
;             PG8_WAIT_K0(); PG8_WAIT_L(0); PG8_BAR; if constexpr (!HM) { PG8_MMA(1, 0, At, B0); PG8_MMA(1, 1, At, B1); } PG8_BAR; PG8_SCHED;
;             PG8_LDB(B0, 1, 0); PG8_LDB(B1, 1, 1); PG8_SCHED; PG8_LDA(At, 1, 0); if constexpr (!HM) PG8_STAGEAS(PG8_SA(0, 1), a2, 1);
;             PG8_WAIT_K(); PG8_WAIT_L(0); PG8_BAR; PG8_MMA(0, 0, At, B0); PG8_MMA(0, 1, At, B1); PG8_BAR; PG8_SCHED;
;             if constexpr (!HM) PG8_LDA(At, 1, 1);
;             PG8_STAGEB(PG8_SB(1, 0), b3); PG8_STAGEB(PG8_SB(1, 1), b3 + hstepB); PG8_STAGEAS(PG8_SA(1, 0), a3, 0);
;             PG8_WAIT_K(); PG8_WAIT_L(0); PG8_BAR; if constexpr (!HM) { PG8_MMA(1, 0, At, B0); PG8_MMA(1, 1, At, B1); } PG8_BAR; PG8_SCHED;
.LBB0_1346:
	ds_read_b128 v[68:71], v100
	ds_read_b128 v[72:75], v100 offset:1024
	ds_read_b128 v[76:79], v100 offset:2048
	ds_read_b128 v[80:83], v100 offset:3072
	ds_read_b128 v[106:109], v101
	ds_read_b128 v[110:113], v101 offset:1024
	ds_read_b128 v[114:117], v101 offset:2048
	ds_read_b128 v[118:121], v101 offset:3072
	s_cmp_eq_u32 s66, 12
	s_cselect_b32 s40, s0, s25
	s_cselect_b32 s41, s1, s29
	s_cselect_b32 s38, s34, s31
	s_cselect_b32 s39, s35, s65
	s_add_u32 s36, s40, 0x80
	s_addc_u32 s37, s41, 0
	ds_read_b128 v[122:125], v102
	ds_read_b128 v[126:129], v102 offset:1024
	ds_read_b128 v[130:133], v102 offset:2048
	ds_read_b128 v[134:137], v102 offset:3072
	ds_read_b128 v[138:141], v102 offset:4096
	ds_read_b128 v[142:145], v102 offset:5120
	ds_read_b128 v[146:149], v102 offset:6144
	ds_read_b128 v[150:153], v102 offset:7168
	s_waitcnt vmcnt(6)
	s_waitcnt lgkmcnt(0)
	s_barrier
	s_setprio 1
	s_waitcnt lgkmcnt(6)
	v_mfma_scale_f32_16x16x128_f8f6f4 v[62:65], v[68:75], v[122:129], v[62:65], v1, v86 op_sel_hi:[0,0,0]
	v_mfma_scale_f32_16x16x128_f8f6f4 v[58:61], v[76:83], v[122:129], v[58:61], v1, v86 op_sel_hi:[0,0,0]
	s_waitcnt lgkmcnt(4)
	v_mfma_scale_f32_16x16x128_f8f6f4 v[46:49], v[68:75], v[130:137], v[46:49], v1, v86 op_sel_hi:[0,0,0]
	v_mfma_scale_f32_16x16x128_f8f6f4 v[42:45], v[76:83], v[130:137], v[42:45], v1, v86 op_sel_hi:[0,0,0]
	s_waitcnt lgkmcnt(2)
	v_mfma_scale_f32_16x16x128_f8f6f4 v[30:33], v[68:75], v[138:145], v[30:33], v1, v86 op_sel_hi:[0,0,0]
	v_mfma_scale_f32_16x16x128_f8f6f4 v[26:29], v[76:83], v[138:145], v[26:29], v1, v86 op_sel_hi:[0,0,0]
	s_waitcnt lgkmcnt(0)
	v_mfma_scale_f32_16x16x128_f8f6f4 v[14:17], v[68:75], v[146:153], v[14:17], v1, v86 op_sel_hi:[0,0,0]
	v_mfma_scale_f32_16x16x128_f8f6f4 v[10:13], v[76:83], v[146:153], v[10:13], v1, v86 op_sel_hi:[0,0,0]
	s_setprio 0
	s_setprio 1
	v_mfma_scale_f32_16x16x128_f8f6f4 v[54:57], v[106:113], v[122:129], v[54:57], v1, v86 op_sel_hi:[0,0,0]
	v_mfma_scale_f32_16x16x128_f8f6f4 v[50:53], v[114:121], v[122:129], v[50:53], v1, v86 op_sel_hi:[0,0,0]
	v_mfma_scale_f32_16x16x128_f8f6f4 v[38:41], v[106:113], v[130:137], v[38:41], v1, v86 op_sel_hi:[0,0,0]
	v_mfma_scale_f32_16x16x128_f8f6f4 v[34:37], v[114:121], v[130:137], v[34:37], v1, v86 op_sel_hi:[0,0,0]
	v_mfma_scale_f32_16x16x128_f8f6f4 v[22:25], v[106:113], v[138:145], v[22:25], v1, v86 op_sel_hi:[0,0,0]
	v_mfma_scale_f32_16x16x128_f8f6f4 v[18:21], v[114:121], v[138:145], v[18:21], v1, v86 op_sel_hi:[0,0,0]
	v_mfma_scale_f32_16x16x128_f8f6f4 v[6:9], v[106:113], v[146:153], v[6:9], v1, v86 op_sel_hi:[0,0,0]
	v_mfma_scale_f32_16x16x128_f8f6f4 v[2:5], v[114:121], v[146:153], v[2:5], v1, v86 op_sel_hi:[0,0,0]
	s_setprio 0
	s_barrier
	s_mov_b32 m0, s51
	s_nop 0
	global_load_lds_dwordx4 v89, s[38:39]
	s_add_u32 s68, s38, 0x40000
	s_mov_b32 m0, s52
	s_nop 0
	global_load_lds_dwordx4 v90, s[38:39]
	s_addc_u32 s69, s39, 0
	s_mov_b32 m0, s53
	s_nop 0
	global_load_lds_dwordx4 v89, s[68:69]
	s_mov_b32 m0, s54
	s_nop 0
	global_load_lds_dwordx4 v90, s[68:69]
	s_mov_b32 m0, s50
	s_nop 0
	global_load_lds_dwordx4 v87, s[40:41]
	s_mov_b32 m0, s55
	s_nop 0
	global_load_lds_dwordx4 v88, s[40:41]
	s_waitcnt vmcnt(6)
	s_waitcnt lgkmcnt(0)
	s_barrier
	s_barrier
	ds_read_b128 v[68:71], v103
	ds_read_b128 v[72:75], v103 offset:1024
	ds_read_b128 v[76:79], v103 offset:2048
	ds_read_b128 v[80:83], v103 offset:3072
	ds_read_b128 v[106:109], v104
	ds_read_b128 v[110:113], v104 offset:1024
	ds_read_b128 v[114:117], v104 offset:2048
	ds_read_b128 v[118:121], v104 offset:3072
	ds_read_b128 v[122:125], v102 offset:32768
	ds_read_b128 v[126:129], v102 offset:33792
	ds_read_b128 v[130:133], v102 offset:34816
	ds_read_b128 v[134:137], v102 offset:35840
	ds_read_b128 v[138:141], v102 offset:36864
	ds_read_b128 v[142:145], v102 offset:37888
	ds_read_b128 v[146:149], v102 offset:38912
	ds_read_b128 v[150:153], v102 offset:39936
	s_waitcnt vmcnt(6)
	s_waitcnt lgkmcnt(0)
	s_barrier
	s_setprio 1
	s_waitcnt lgkmcnt(6)
	v_mfma_scale_f32_16x16x128_f8f6f4 v[62:65], v[68:75], v[122:129], v[62:65], v1, v86 op_sel_hi:[0,0,0]
	v_mfma_scale_f32_16x16x128_f8f6f4 v[58:61], v[76:83], v[122:129], v[58:61], v1, v86 op_sel_hi:[0,0,0]
	s_waitcnt lgkmcnt(4)
	v_mfma_scale_f32_16x16x128_f8f6f4 v[46:49], v[68:75], v[130:137], v[46:49], v1, v86 op_sel_hi:[0,0,0]
	v_mfma_scale_f32_16x16x128_f8f6f4 v[42:45], v[76:83], v[130:137], v[42:45], v1, v86 op_sel_hi:[0,0,0]
	s_waitcnt lgkmcnt(2)
	v_mfma_scale_f32_16x16x128_f8f6f4 v[30:33], v[68:75], v[138:145], v[30:33], v1, v86 op_sel_hi:[0,0,0]
	v_mfma_scale_f32_16x16x128_f8f6f4 v[26:29], v[76:83], v[138:145], v[26:29], v1, v86 op_sel_hi:[0,0,0]
	s_waitcnt lgkmcnt(0)
	v_mfma_scale_f32_16x16x128_f8f6f4 v[14:17], v[68:75], v[146:153], v[14:17], v1, v86 op_sel_hi:[0,0,0]
	v_mfma_scale_f32_16x16x128_f8f6f4 v[10:13], v[76:83], v[146:153], v[10:13], v1, v86 op_sel_hi:[0,0,0]
	s_setprio 0
	s_setprio 1
	s_add_u32 s40, s38, 0x80
	v_mfma_scale_f32_16x16x128_f8f6f4 v[54:57], v[106:113], v[122:129], v[54:57], v1, v86 op_sel_hi:[0,0,0]
	v_mfma_scale_f32_16x16x128_f8f6f4 v[50:53], v[114:121], v[122:129], v[50:53], v1, v86 op_sel_hi:[0,0,0]
	v_mfma_scale_f32_16x16x128_f8f6f4 v[38:41], v[106:113], v[130:137], v[38:41], v1, v86 op_sel_hi:[0,0,0]
	v_mfma_scale_f32_16x16x128_f8f6f4 v[34:37], v[114:121], v[130:137], v[34:37], v1, v86 op_sel_hi:[0,0,0]
	v_mfma_scale_f32_16x16x128_f8f6f4 v[22:25], v[106:113], v[138:145], v[22:25], v1, v86 op_sel_hi:[0,0,0]
	v_mfma_scale_f32_16x16x128_f8f6f4 v[18:21], v[114:121], v[138:145], v[18:21], v1, v86 op_sel_hi:[0,0,0]
	v_mfma_scale_f32_16x16x128_f8f6f4 v[6:9], v[106:113], v[146:153], v[6:9], v1, v86 op_sel_hi:[0,0,0]
	v_mfma_scale_f32_16x16x128_f8f6f4 v[2:5], v[114:121], v[146:153], v[2:5], v1, v86 op_sel_hi:[0,0,0]
	s_addc_u32 s41, s39, 0
	s_setprio 0
	s_barrier
	s_mov_b32 m0, s56
	s_nop 0
	global_load_lds_dwordx4 v89, s[40:41]
	s_add_u32 s38, s38, 0x40080
	s_mov_b32 m0, s57
	s_nop 0
	global_load_lds_dwordx4 v90, s[40:41]
	s_addc_u32 s39, s39, 0
	s_mov_b32 m0, s60
	s_nop 0
	global_load_lds_dwordx4 v89, s[38:39]
	s_mov_b32 m0, s61
	s_nop 0
	global_load_lds_dwordx4 v90, s[38:39]
	s_mov_b32 m0, s58
	s_nop 0
	global_load_lds_dwordx4 v87, s[36:37]
	s_mov_b32 m0, s59
	s_nop 0
	global_load_lds_dwordx4 v88, s[36:37]
	s_waitcnt vmcnt(6)
	s_waitcnt lgkmcnt(0)
	s_barrier
	s_barrier
	s_add_i32 s66, s66, 2
	s_add_u32 s25, s25, 0x100
	s_addc_u32 s29, s29, 0
	s_add_u32 s31, s31, 0x100
	s_addc_u32 s65, s65, 0
	s_cmp_gt_u32 s66, 13
	s_cbranch_scc0 .LBB0_1346
	s_and_b64 vcc, exec, s[20:21]
	s_cbranch_vccz .LBB0_1349
	s_barrier

;     __device__ __forceinline__ const char* bias_base(const pg8::Unit& u) const { return (const char*)(bgu + (size_t)u.e * 4096 + u.pn * 128); }
;     __device__ __forceinline__ unsigned bias_off(const pg8::Unit&, int wc, int lane) const { return (unsigned)(((lane >> 3) & 1) * 2048 + wc * 32 + (lane & 7) * 4) * 4u; }
; __device__ __forceinline__ unsigned row_base(unsigned lane, unsigned s) { return row_addr16(lane, 0, s); }
;     ...
;         if constexpr (Epi::kBiasDMA) { if (lane < 16) glds16(E.bias_base(cur), E.bias_off(cur, wc, lane), bias_lds); }
;         if constexpr (Epi::kRowDMA) { if (lane < 32) glds16(E.row_base(cur), E.row_off(cur, wr, lane), rowid_lds); }
;     __device__ __forceinline__ const char* bias_base(const pg8::Unit& u) const { return (const char*)(bdn + (size_t)u.e * D + u.pn * 256); }
;     __device__ __forceinline__ unsigned bias_off(const pg8::Unit&, int wc, int lane) const { return (unsigned)(wc * 64 + lane * 4) * 4u; }
;     __device__ __forceinline__ const char* row_base(const pg8::Unit& u) const { return (const char*)((const int*)(ws + WS_ROWTOK) + (size_t)u.e * T + u.mt * 256 + u.hx * 128); }
;     __device__ __forceinline__ unsigned row_off(const pg8::Unit&, int wr, int lane) const { return (unsigned)(((lane >> 4) & 1) * 128 + wr * 64 + (lane & 15) * 4) * 4u; }
.LBB0_1361:
	s_ashr_i32 s25, s24, 31
	s_lshl_b64 s[26:27], s[24:25], 13
	s_add_u32 s25, s14, s26
	s_addc_u32 s29, s15, s27
	s_lshl_b32 s26, s28, 8
	s_ashr_i32 s27, s26, 31
	s_lshl_b64 s[26:27], s[26:27], 2
	s_add_u32 s26, s25, s26
	s_addc_u32 s27, s29, s27
	s_mov_b32 m0, s43
	s_nop 0
	global_load_lds_dwordx4 v97, s[26:27]
	s_or_b64 exec, exec, s[10:11]
	s_and_saveexec_b64 s[10:11], s[8:9]
	s_cbranch_execz .LBB0_1360
.LBB0_1362:
	s_ashr_i32 s25, s24, 31
	s_lshl_b64 s[26:27], s[24:25], 16
	s_add_u32 s25, s46, s26
	s_addc_u32 s29, s47, s27
	s_lshl_b32 s26, s64, 8
	s_ashr_i32 s27, s26, 31
	s_lshl_b64 s[26:27], s[26:27], 2
	s_add_u32 s26, s25, s26
	s_addc_u32 s27, s29, s27
	s_mov_b32 m0, s49
	s_nop 0
	global_load_lds_dwordx4 v98, s[26:27]
	s_or_b64 exec, exec, s[10:11]
	s_andn2_b64 vcc, exec, s[18:19]
	s_cbranch_vccnz .LBB0_1333
